# K-loop load segments: the s_nop between each m0 write and its LDS-DMA replaced by one of the segment's own ds_read_b128 (450 sites)
# baseline (speedup 1.0000x reference)
; #define PG8_STAGE(bufoff, gbase, voff) do { _Pragma("unroll") for (int _i = 0; _i < 2; ++_i) \
;         __builtin_amdgcn_global_load_lds((const unsigned*)((const char*)(gbase) + (voff)[_i]), (PG8_LAS unsigned*)(lds + (bufoff) + ldsw + _i * 8192), 16, 0, 0); } while (0)
; #define PG8_WAIT_V(n) asm volatile("s_waitcnt vmcnt(" #n ")" ::: "memory")
; #define PG8_WAIT_L(n) asm volatile("s_waitcnt lgkmcnt(" #n ")" ::: "memory")
; #define PG8_BAR __builtin_amdgcn_s_barrier()
;     __device__ __forceinline__ void operator()(const f32x4 (&acc)[2][2][4][2], const Unit& u, int wr, int wc, int fr, int fq) const {
;     ...
;         for (int n = 0; n < 2; ++n) { cg[n] = IN8 ? *(const f32x4*)(cstep + u.pn * BM + wc * 32 + 8 * fq + 4 * n) : (f32x4){1.f, 1.f, 1.f, 1.f}; cu[n] = IN8 ? *(const f32x4*)(cstep + u.pn * BM + HALF + wc * 32 + 8 * fq + 4 * n) : (f32x4){1.f, 1.f, 1.f, 1.f}; }
;     ...
;         for (int t = 0; t < nt; t += 2) {
;             const bool last = (t == nt - 2);
;             const char* a1 = cA + (size_t)(t + 1) * kstep;
;             const char* a2 = last ? nA : cA + (size_t)(t + 2) * kstep; const char* b2 = last ? nB : cB + (size_t)(t + 2) * kstep;
;             const char* a3 = a2 + kstep; const char* b3 = b2 + kstep;
;             if (last && has_next) S.a_ready(nxt);
;             if constexpr (SP2) {
;             PG8_LDB(B0, 0, 0); PG8_LDB(B1, 0, 1); PG8_SCHED; PG8_LDA(At, 0, 0); PG8_STAGE(PG8_SA(1, 1), a1 + hstepA, voffA);
;             PG8_WAIT_V(8); PG8_WAIT_L(0); PG8_BAR; PG8_MMA(0, 0, At, B0); PG8_MMA(0, 1, At, B1); PG8_BAR; PG8_SCHED;
;             PG8_LDA(At, 0, 1); PG8_STAGE(PG8_SB(0, 0), b2, voffB); PG8_STAGE(PG8_SB(0, 1), b2 + hstepB, voffB); PG8_STAGE(PG8_SA(0, 0), a2, voffA);
;             PG8_WAIT_V(8); PG8_WAIT_L(0); PG8_BAR; PG8_MMA(1, 0, At, B0); PG8_MMA(1, 1, At, B1); PG8_BAR; PG8_SCHED;
;             PG8_LDB(B0, 1, 0); PG8_LDB(B1, 1, 1); PG8_SCHED; PG8_LDA(At, 1, 0); PG8_STAGE(PG8_SA(0, 1), a2 + hstepA, voffA);
;             PG8_WAIT_V(8); PG8_WAIT_L(0); PG8_BAR; PG8_MMA(0, 0, At, B0); PG8_MMA(0, 1, At, B1); PG8_BAR; PG8_SCHED;
;             PG8_LDA(At, 1, 1); PG8_STAGE(PG8_SB(1, 0), b3, voffB); PG8_STAGE(PG8_SB(1, 1), b3 + hstepB, voffB); PG8_STAGE(PG8_SA(1, 0), a3, voffA);
;             PG8_WAIT_V(8); PG8_WAIT_L(0); PG8_BAR; PG8_MMA(1, 0, At, B0); PG8_MMA(1, 1, At, B1); PG8_BAR; PG8_SCHED;
.Lzs_1:
	s_cbranch_vccnz .LBB0_228
	s_and_b64 s[28:29], s[0:1], exec
	s_cselect_b32 s15, s19, s27
	s_cselect_b32 s17, s18, s26
	s_cselect_b32 s64, s21, s25
	s_cselect_b32 s65, s20, s24
	s_add_u32 s66, s24, 0x100
	s_addc_u32 s67, s25, 0
	s_add_u32 s24, s26, 0x40080
	s_addc_u32 s25, s27, 0
	s_mov_b32 s26, 0
	s_lshl_b32 s98, s63, 8
	s_ashr_i32 s99, s98, 31
	v_lshl_add_u64 v[242:243], s[98:99], 2, v[154:155]
	global_load_dwordx4 v[226:229], v[242:243], off
	global_load_dwordx4 v[230:233], v[242:243], off offset:512
	global_load_dwordx4 v[234:237], v[242:243], off offset:16
	global_load_dwordx4 v[238:241], v[242:243], off offset:528
	v_add_u32_e32 v142, s35, v164
	v_add_u32_e32 v180, s36, v164
	ds_read_b128 v[130:133], v142
	ds_read_b128 v[134:137], v142 offset:1024
	ds_read_b128 v[138:141], v142 offset:2048
	ds_read_b128 v[142:145], v142 offset:3072
	ds_read_b128 v[168:171], v180
	ds_read_b128 v[172:175], v180 offset:1024
	ds_read_b128 v[176:179], v180 offset:2048
	ds_read_b128 v[180:183], v180 offset:3072
	s_add_i32 s68, s26, 2
	s_add_u32 s27, s24, 0xfffc0080
	s_addc_u32 s28, s25, -1
	s_cmp_eq_u32 s61, s26
	s_cselect_b32 s26, s65, s66
	s_cselect_b32 s29, s15, s28
	s_cselect_b32 s28, s17, s27
	s_cselect_b32 s27, s64, s67
	s_add_i32 m0, s46, 0xc000
	ds_read_b128 v[184:187], v167
	ds_read_b128 v[188:191], v167 offset:1024
	ds_read_b128 v[192:195], v167 offset:2048
	ds_read_b128 v[196:199], v167 offset:3072
	ds_read_b128 v[200:203], v167 offset:4096
	ds_read_b128 v[204:207], v167 offset:5120
	ds_read_b128 v[208:211], v167 offset:6144
	ds_read_b128 v[212:215], v167 offset:7168
	global_load_lds_dwordx4 v158, s[24:25]
	s_add_i32 m0, s46, 0xe000
	s_nop 0
	global_load_lds_dwordx4 v156, s[24:25]
	s_waitcnt vmcnt(8) lgkmcnt(0)
	s_barrier
	s_setprio 1
	v_mfma_i32_16x16x64_i8 v[126:129], v[130:133], v[184:187], 0
	v_mfma_i32_16x16x64_i8 v[118:121], v[138:141], v[184:187], 0
	v_mfma_i32_16x16x64_i8 v[110:113], v[130:133], v[192:195], 0
	v_mfma_i32_16x16x64_i8 v[102:105], v[138:141], v[192:195], 0
	v_mfma_i32_16x16x64_i8 v[94:97], v[130:133], v[200:203], 0
	v_mfma_i32_16x16x64_i8 v[86:89], v[138:141], v[200:203], 0
	v_mfma_i32_16x16x64_i8 v[78:81], v[130:133], v[208:211], 0
	v_mfma_i32_16x16x64_i8 v[70:73], v[138:141], v[208:211], 0
	v_mfma_i32_16x16x64_i8 v[126:129], v[134:137], v[188:191], v[126:129]
	v_mfma_i32_16x16x64_i8 v[118:121], v[142:145], v[188:191], v[118:121]
	v_mfma_i32_16x16x64_i8 v[110:113], v[134:137], v[196:199], v[110:113]
	v_mfma_i32_16x16x64_i8 v[102:105], v[142:145], v[196:199], v[102:105]
	v_mfma_i32_16x16x64_i8 v[94:97], v[134:137], v[204:207], v[94:97]
	v_mfma_i32_16x16x64_i8 v[86:89], v[142:145], v[204:207], v[86:89]
	v_mfma_i32_16x16x64_i8 v[78:81], v[134:137], v[212:215], v[78:81]
	v_mfma_i32_16x16x64_i8 v[70:73], v[142:145], v[212:215], v[70:73]
	s_setprio 0
	s_setprio 1
	v_mfma_i32_16x16x64_i8 v[122:125], v[168:171], v[184:187], 0
	v_mfma_i32_16x16x64_i8 v[114:117], v[176:179], v[184:187], 0
	v_mfma_i32_16x16x64_i8 v[106:109], v[168:171], v[192:195], 0
	v_mfma_i32_16x16x64_i8 v[98:101], v[176:179], v[192:195], 0
	v_mfma_i32_16x16x64_i8 v[90:93], v[168:171], v[200:203], 0
	v_mfma_i32_16x16x64_i8 v[82:85], v[176:179], v[200:203], 0
	v_mfma_i32_16x16x64_i8 v[74:77], v[168:171], v[208:211], 0
	v_mfma_i32_16x16x64_i8 v[66:69], v[176:179], v[208:211], 0
	v_mfma_i32_16x16x64_i8 v[122:125], v[172:175], v[188:191], v[122:125]
	v_mfma_i32_16x16x64_i8 v[114:117], v[180:183], v[188:191], v[114:117]
	v_mfma_i32_16x16x64_i8 v[106:109], v[172:175], v[196:199], v[106:109]
	v_mfma_i32_16x16x64_i8 v[98:101], v[180:183], v[196:199], v[98:101]
	v_mfma_i32_16x16x64_i8 v[90:93], v[172:175], v[204:207], v[90:93]
	v_mfma_i32_16x16x64_i8 v[82:85], v[180:183], v[204:207], v[82:85]
	v_mfma_i32_16x16x64_i8 v[74:77], v[172:175], v[212:215], v[74:77]
	v_mfma_i32_16x16x64_i8 v[66:69], v[180:183], v[212:215], v[66:69]
	s_setprio 0
	s_barrier
	s_mov_b32 m0, s23
	s_add_u32 s98, s26, 0x80
	s_addc_u32 s99, s27, 0
	s_add_u32 s70, s26, 0x40000
	ds_read_b128 v[184:187], v167 offset:16384
	ds_read_b128 v[188:191], v167 offset:17408
	ds_read_b128 v[192:195], v167 offset:18432
	ds_read_b128 v[196:199], v167 offset:19456
	global_load_lds_dwordx4 v148, s[26:27]
	s_mov_b32 m0, s43
	s_addc_u32 s71, s27, 0
	global_load_lds_dwordx4 v152, s[26:27]
	s_mov_b32 m0, s44
	ds_read_b128 v[212:215], v167 offset:23552
	global_load_lds_dwordx4 v148, s[70:71]
	s_mov_b32 m0, s45
	ds_read_b128 v[208:211], v167 offset:22528
	global_load_lds_dwordx4 v152, s[70:71]
	s_add_u32 s100, s28, 0x80
	s_addc_u32 s101, s29, 0
	s_mov_b32 m0, s46
	ds_read_b128 v[204:207], v167 offset:21504
	global_load_lds_dwordx4 v146, s[28:29]
	s_mov_b32 m0, s47
	ds_read_b128 v[200:203], v167 offset:20480
	global_load_lds_dwordx4 v150, s[28:29]
	s_waitcnt vmcnt(8) lgkmcnt(0)
	s_barrier
; #define PG8_STAGE(bufoff, gbase, voff) do { _Pragma("unroll") for (int _i = 0; _i < 2; ++_i) \
;         __builtin_amdgcn_global_load_lds((const unsigned*)((const char*)(gbase) + (voff)[_i]), (PG8_LAS unsigned*)(lds + (bufoff) + ldsw + _i * 8192), 16, 0, 0); } while (0)
; #define PG8_LDA(dst, b, h) do { if constexpr (DT != 1) { _Pragma("unroll") for (int m = 0; m < 4; ++m) _Pragma("unroll") for (int k = 0; k < 2; ++k) dst[m][k] = *(const PG8_LAS bf16x8*)(lds + PG8_SA(b, h) + aoff + m * 2048 + k * 1024); } \
;         else { _Pragma("unroll") for (int m = 0; m < 4; ++m) dst##8[m] = ld32(lds + PG8_SA(b, h) + aoff + m * 2048); } } while (0)
; #define PG8_LDB(dst, b, h) do { if constexpr (DT != 1) { _Pragma("unroll") for (int n = 0; n < 2; ++n) _Pragma("unroll") for (int k = 0; k < 2; ++k) dst[n][k] = *(const PG8_LAS bf16x8*)(lds + PG8_SB(b, h) + boff + n * 2048 + k * 1024); } \
;         else { _Pragma("unroll") for (int n = 0; n < 2; ++n) dst##8[n] = ld32(lds + PG8_SB(b, h) + boff + n * 2048); } } while (0)
; #define PG8_WAIT_V(n) asm volatile("s_waitcnt vmcnt(" #n ")" ::: "memory")
; #define PG8_WAIT_L(n) asm volatile("s_waitcnt lgkmcnt(" #n ")" ::: "memory")
; #define PG8_BAR __builtin_amdgcn_s_barrier()
; #define PG8_SCHED __builtin_amdgcn_sched_barrier(0)
;     ...
;             if constexpr (SP2) {
;             PG8_LDB(B0, 0, 0); PG8_LDB(B1, 0, 1); PG8_SCHED; PG8_LDA(At, 0, 0); PG8_STAGE(PG8_SA(1, 1), a1 + hstepA, voffA);
;             PG8_WAIT_V(8); PG8_WAIT_L(0); PG8_BAR; PG8_MMA(0, 0, At, B0); PG8_MMA(0, 1, At, B1); PG8_BAR; PG8_SCHED;
;             PG8_LDA(At, 0, 1); PG8_STAGE(PG8_SB(0, 0), b2, voffB); PG8_STAGE(PG8_SB(0, 1), b2 + hstepB, voffB); PG8_STAGE(PG8_SA(0, 0), a2, voffA);
;             PG8_WAIT_V(8); PG8_WAIT_L(0); PG8_BAR; PG8_MMA(1, 0, At, B0); PG8_MMA(1, 1, At, B1); PG8_BAR; PG8_SCHED;
;             PG8_LDB(B0, 1, 0); PG8_LDB(B1, 1, 1); PG8_SCHED; PG8_LDA(At, 1, 0); PG8_STAGE(PG8_SA(0, 1), a2 + hstepA, voffA);
;             PG8_WAIT_V(8); PG8_WAIT_L(0); PG8_BAR; PG8_MMA(0, 0, At, B0); PG8_MMA(0, 1, At, B1); PG8_BAR; PG8_SCHED;
;             PG8_LDA(At, 1, 1); PG8_STAGE(PG8_SB(1, 0), b3, voffB); PG8_STAGE(PG8_SB(1, 1), b3 + hstepB, voffB); PG8_STAGE(PG8_SA(1, 0), a3, voffA);
;             PG8_WAIT_V(8); PG8_WAIT_L(0); PG8_BAR; PG8_MMA(1, 0, At, B0); PG8_MMA(1, 1, At, B1); PG8_BAR; PG8_SCHED;
	s_setprio 1
	v_mfma_i32_16x16x64_i8 v[62:65], v[130:133], v[184:187], 0
	v_mfma_i32_16x16x64_i8 v[54:57], v[138:141], v[184:187], 0
	v_mfma_i32_16x16x64_i8 v[46:49], v[130:133], v[192:195], 0
	v_mfma_i32_16x16x64_i8 v[38:41], v[138:141], v[192:195], 0
	v_mfma_i32_16x16x64_i8 v[30:33], v[130:133], v[200:203], 0
	v_mfma_i32_16x16x64_i8 v[22:25], v[138:141], v[200:203], 0
	v_mfma_i32_16x16x64_i8 v[14:17], v[130:133], v[208:211], 0
	v_mfma_i32_16x16x64_i8 v[6:9], v[138:141], v[208:211], 0
	v_mfma_i32_16x16x64_i8 v[62:65], v[134:137], v[188:191], v[62:65]
	v_mfma_i32_16x16x64_i8 v[54:57], v[142:145], v[188:191], v[54:57]
	v_mfma_i32_16x16x64_i8 v[46:49], v[134:137], v[196:199], v[46:49]
	v_mfma_i32_16x16x64_i8 v[38:41], v[142:145], v[196:199], v[38:41]
	v_mfma_i32_16x16x64_i8 v[30:33], v[134:137], v[204:207], v[30:33]
	v_mfma_i32_16x16x64_i8 v[22:25], v[142:145], v[204:207], v[22:25]
	v_mfma_i32_16x16x64_i8 v[14:17], v[134:137], v[212:215], v[14:17]
	v_mfma_i32_16x16x64_i8 v[6:9], v[142:145], v[212:215], v[6:9]
	s_setprio 0
	s_setprio 1
	v_mfma_i32_16x16x64_i8 v[58:61], v[168:171], v[184:187], 0
	v_mfma_i32_16x16x64_i8 v[50:53], v[176:179], v[184:187], 0
	v_mfma_i32_16x16x64_i8 v[42:45], v[168:171], v[192:195], 0
	v_mfma_i32_16x16x64_i8 v[34:37], v[176:179], v[192:195], 0
	v_mfma_i32_16x16x64_i8 v[26:29], v[168:171], v[200:203], 0
	v_mfma_i32_16x16x64_i8 v[18:21], v[176:179], v[200:203], 0
	v_mfma_i32_16x16x64_i8 v[10:13], v[168:171], v[208:211], 0
	v_mfma_i32_16x16x64_i8 v[2:5], v[176:179], v[208:211], 0
	v_mfma_i32_16x16x64_i8 v[58:61], v[172:175], v[188:191], v[58:61]
	v_mfma_i32_16x16x64_i8 v[50:53], v[180:183], v[188:191], v[50:53]
	v_mfma_i32_16x16x64_i8 v[42:45], v[172:175], v[196:199], v[42:45]
	v_mfma_i32_16x16x64_i8 v[34:37], v[180:183], v[196:199], v[34:37]
	v_mfma_i32_16x16x64_i8 v[26:29], v[172:175], v[204:207], v[26:29]
	v_mfma_i32_16x16x64_i8 v[18:21], v[180:183], v[204:207], v[18:21]
	v_mfma_i32_16x16x64_i8 v[10:13], v[172:175], v[212:215], v[10:13]
	v_mfma_i32_16x16x64_i8 v[2:5], v[180:183], v[212:215], v[2:5]
	s_setprio 0
	s_barrier
	v_add_u32_e32 v142, s51, v164
	v_add_u32_e32 v180, s52, v164
	ds_read_b128 v[130:133], v142
	ds_read_b128 v[134:137], v142 offset:1024
	ds_read_b128 v[138:141], v142 offset:2048
	ds_read_b128 v[142:145], v142 offset:3072
	ds_read_b128 v[168:171], v180
	ds_read_b128 v[172:175], v180 offset:1024
	ds_read_b128 v[176:179], v180 offset:2048
	ds_read_b128 v[180:183], v180 offset:3072
	s_add_u32 s28, s28, 0x40000
	s_addc_u32 s29, s29, 0
	s_mov_b32 m0, s48
	ds_read_b128 v[184:187], v167 offset:32768
	ds_read_b128 v[188:191], v167 offset:33792
	ds_read_b128 v[192:195], v167 offset:34816
	ds_read_b128 v[196:199], v167 offset:35840
	ds_read_b128 v[200:203], v167 offset:36864
	ds_read_b128 v[204:207], v167 offset:37888
	ds_read_b128 v[208:211], v167 offset:38912
	global_load_lds_dwordx4 v146, s[28:29]
	s_mov_b32 m0, s49
	ds_read_b128 v[212:215], v167 offset:39936
	global_load_lds_dwordx4 v150, s[28:29]
	s_waitcnt vmcnt(8) lgkmcnt(0)
	s_barrier
	s_setprio 1
	v_mfma_i32_16x16x64_i8 v[126:129], v[130:133], v[184:187], v[126:129]
	v_mfma_i32_16x16x64_i8 v[118:121], v[138:141], v[184:187], v[118:121]
	v_mfma_i32_16x16x64_i8 v[110:113], v[130:133], v[192:195], v[110:113]
	v_mfma_i32_16x16x64_i8 v[102:105], v[138:141], v[192:195], v[102:105]
	v_mfma_i32_16x16x64_i8 v[94:97], v[130:133], v[200:203], v[94:97]
	v_mfma_i32_16x16x64_i8 v[86:89], v[138:141], v[200:203], v[86:89]
	v_mfma_i32_16x16x64_i8 v[78:81], v[130:133], v[208:211], v[78:81]
	v_mfma_i32_16x16x64_i8 v[70:73], v[138:141], v[208:211], v[70:73]
	v_mfma_i32_16x16x64_i8 v[126:129], v[134:137], v[188:191], v[126:129]
	v_mfma_i32_16x16x64_i8 v[118:121], v[142:145], v[188:191], v[118:121]
	v_mfma_i32_16x16x64_i8 v[110:113], v[134:137], v[196:199], v[110:113]
	v_mfma_i32_16x16x64_i8 v[102:105], v[142:145], v[196:199], v[102:105]
	v_mfma_i32_16x16x64_i8 v[94:97], v[134:137], v[204:207], v[94:97]
	v_mfma_i32_16x16x64_i8 v[86:89], v[142:145], v[204:207], v[86:89]
	v_mfma_i32_16x16x64_i8 v[78:81], v[134:137], v[212:215], v[78:81]
	v_mfma_i32_16x16x64_i8 v[70:73], v[142:145], v[212:215], v[70:73]
	s_setprio 0
	s_setprio 1
	v_mfma_i32_16x16x64_i8 v[122:125], v[168:171], v[184:187], v[122:125]
	v_mfma_i32_16x16x64_i8 v[114:117], v[176:179], v[184:187], v[114:117]
	v_mfma_i32_16x16x64_i8 v[106:109], v[168:171], v[192:195], v[106:109]
	v_mfma_i32_16x16x64_i8 v[98:101], v[176:179], v[192:195], v[98:101]
	v_mfma_i32_16x16x64_i8 v[90:93], v[168:171], v[200:203], v[90:93]
	v_mfma_i32_16x16x64_i8 v[82:85], v[176:179], v[200:203], v[82:85]
	v_mfma_i32_16x16x64_i8 v[74:77], v[168:171], v[208:211], v[74:77]
	v_mfma_i32_16x16x64_i8 v[66:69], v[176:179], v[208:211], v[66:69]
	v_mfma_i32_16x16x64_i8 v[122:125], v[172:175], v[188:191], v[122:125]
	v_mfma_i32_16x16x64_i8 v[114:117], v[180:183], v[188:191], v[114:117]
	v_mfma_i32_16x16x64_i8 v[106:109], v[172:175], v[196:199], v[106:109]
	v_mfma_i32_16x16x64_i8 v[98:101], v[180:183], v[196:199], v[98:101]
	v_mfma_i32_16x16x64_i8 v[90:93], v[172:175], v[204:207], v[90:93]
	v_mfma_i32_16x16x64_i8 v[82:85], v[180:183], v[204:207], v[82:85]
	v_mfma_i32_16x16x64_i8 v[74:77], v[172:175], v[212:215], v[74:77]
	v_mfma_i32_16x16x64_i8 v[66:69], v[180:183], v[212:215], v[66:69]
	s_setprio 0
	s_barrier
; #define PG8_STAGE(bufoff, gbase, voff) do { _Pragma("unroll") for (int _i = 0; _i < 2; ++_i) \
;         __builtin_amdgcn_global_load_lds((const unsigned*)((const char*)(gbase) + (voff)[_i]), (PG8_LAS unsigned*)(lds + (bufoff) + ldsw + _i * 8192), 16, 0, 0); } while (0)
; #define PG8_LDA(dst, b, h) do { if constexpr (DT != 1) { _Pragma("unroll") for (int m = 0; m < 4; ++m) _Pragma("unroll") for (int k = 0; k < 2; ++k) dst[m][k] = *(const PG8_LAS bf16x8*)(lds + PG8_SA(b, h) + aoff + m * 2048 + k * 1024); } \
;         else { _Pragma("unroll") for (int m = 0; m < 4; ++m) dst##8[m] = ld32(lds + PG8_SA(b, h) + aoff + m * 2048); } } while (0)
; #define PG8_WAIT_V(n) asm volatile("s_waitcnt vmcnt(" #n ")" ::: "memory")
; #define PG8_WAIT_L(n) asm volatile("s_waitcnt lgkmcnt(" #n ")" ::: "memory")
; #define PG8_BAR __builtin_amdgcn_s_barrier()
; #define PG8_SCHED __builtin_amdgcn_sched_barrier(0)
;     ...
;         for (int t = 0; t < nt; t += 2) {
;             const bool last = (t == nt - 2);
;             const char* a1 = cA + (size_t)(t + 1) * kstep;
;             const char* a2 = last ? nA : cA + (size_t)(t + 2) * kstep; const char* b2 = last ? nB : cB + (size_t)(t + 2) * kstep;
;             const char* a3 = a2 + kstep; const char* b3 = b2 + kstep;
;             if (last && has_next) S.a_ready(nxt);
;             if constexpr (SP2) {
;             PG8_LDB(B0, 0, 0); PG8_LDB(B1, 0, 1); PG8_SCHED; PG8_LDA(At, 0, 0); PG8_STAGE(PG8_SA(1, 1), a1 + hstepA, voffA);
;             PG8_WAIT_V(8); PG8_WAIT_L(0); PG8_BAR; PG8_MMA(0, 0, At, B0); PG8_MMA(0, 1, At, B1); PG8_BAR; PG8_SCHED;
;             PG8_LDA(At, 0, 1); PG8_STAGE(PG8_SB(0, 0), b2, voffB); PG8_STAGE(PG8_SB(0, 1), b2 + hstepB, voffB); PG8_STAGE(PG8_SA(0, 0), a2, voffA);
;             PG8_WAIT_V(8); PG8_WAIT_L(0); PG8_BAR; PG8_MMA(1, 0, At, B0); PG8_MMA(1, 1, At, B1); PG8_BAR; PG8_SCHED;
;             PG8_LDB(B0, 1, 0); PG8_LDB(B1, 1, 1); PG8_SCHED; PG8_LDA(At, 1, 0); PG8_STAGE(PG8_SA(0, 1), a2 + hstepA, voffA);
;             PG8_WAIT_V(8); PG8_WAIT_L(0); PG8_BAR; PG8_MMA(0, 0, At, B0); PG8_MMA(0, 1, At, B1); PG8_BAR; PG8_SCHED;
;             PG8_LDA(At, 1, 1); PG8_STAGE(PG8_SB(1, 0), b3, voffB); PG8_STAGE(PG8_SB(1, 1), b3 + hstepB, voffB); PG8_STAGE(PG8_SA(1, 0), a3, voffA);
;             PG8_WAIT_V(8); PG8_WAIT_L(0); PG8_BAR; PG8_MMA(1, 0, At, B0); PG8_MMA(1, 1, At, B1); PG8_BAR; PG8_SCHED;
	s_mov_b32 m0, s55
	s_add_u32 s26, s26, 0x40080
	ds_read_b128 v[184:187], v167 offset:49152
	ds_read_b128 v[188:191], v167 offset:50176
	ds_read_b128 v[192:195], v167 offset:51200
	ds_read_b128 v[196:199], v167 offset:52224
	global_load_lds_dwordx4 v148, s[98:99]
	s_mov_b32 m0, s56
	s_addc_u32 s27, s27, 0
	global_load_lds_dwordx4 v152, s[98:99]
	s_mov_b32 m0, s59
	ds_read_b128 v[212:215], v167 offset:56320
	global_load_lds_dwordx4 v148, s[26:27]
	s_mov_b32 m0, s60
	ds_read_b128 v[208:211], v167 offset:55296
	global_load_lds_dwordx4 v152, s[26:27]
	s_mov_b32 m0, s57
	ds_read_b128 v[204:207], v167 offset:54272
	global_load_lds_dwordx4 v146, s[100:101]
	s_mov_b32 m0, s58
	ds_read_b128 v[200:203], v167 offset:53248
	global_load_lds_dwordx4 v150, s[100:101]
	s_waitcnt vmcnt(8) lgkmcnt(0)
	s_barrier
	s_setprio 1
	v_mfma_i32_16x16x64_i8 v[62:65], v[130:133], v[184:187], v[62:65]
	v_mfma_i32_16x16x64_i8 v[54:57], v[138:141], v[184:187], v[54:57]
	v_mfma_i32_16x16x64_i8 v[46:49], v[130:133], v[192:195], v[46:49]
	v_mfma_i32_16x16x64_i8 v[38:41], v[138:141], v[192:195], v[38:41]
	v_mfma_i32_16x16x64_i8 v[30:33], v[130:133], v[200:203], v[30:33]
	v_mfma_i32_16x16x64_i8 v[22:25], v[138:141], v[200:203], v[22:25]
	v_mfma_i32_16x16x64_i8 v[14:17], v[130:133], v[208:211], v[14:17]
	v_mfma_i32_16x16x64_i8 v[6:9], v[138:141], v[208:211], v[6:9]
	v_mfma_i32_16x16x64_i8 v[62:65], v[134:137], v[188:191], v[62:65]
	v_mfma_i32_16x16x64_i8 v[54:57], v[142:145], v[188:191], v[54:57]
	v_mfma_i32_16x16x64_i8 v[46:49], v[134:137], v[196:199], v[46:49]
	v_mfma_i32_16x16x64_i8 v[38:41], v[142:145], v[196:199], v[38:41]
	v_mfma_i32_16x16x64_i8 v[30:33], v[134:137], v[204:207], v[30:33]
	v_mfma_i32_16x16x64_i8 v[22:25], v[142:145], v[204:207], v[22:25]
	v_mfma_i32_16x16x64_i8 v[14:17], v[134:137], v[212:215], v[14:17]
	v_mfma_i32_16x16x64_i8 v[6:9], v[142:145], v[212:215], v[6:9]
	s_setprio 0
	s_setprio 1
	v_mfma_i32_16x16x64_i8 v[58:61], v[168:171], v[184:187], v[58:61]
	v_mfma_i32_16x16x64_i8 v[50:53], v[176:179], v[184:187], v[50:53]
	v_mfma_i32_16x16x64_i8 v[42:45], v[168:171], v[192:195], v[42:45]
	v_mfma_i32_16x16x64_i8 v[34:37], v[176:179], v[192:195], v[34:37]
	v_mfma_i32_16x16x64_i8 v[26:29], v[168:171], v[200:203], v[26:29]
	v_mfma_i32_16x16x64_i8 v[18:21], v[176:179], v[200:203], v[18:21]
	v_mfma_i32_16x16x64_i8 v[10:13], v[168:171], v[208:211], v[10:13]
	v_mfma_i32_16x16x64_i8 v[2:5], v[176:179], v[208:211], v[2:5]
	v_mfma_i32_16x16x64_i8 v[58:61], v[172:175], v[188:191], v[58:61]
	v_mfma_i32_16x16x64_i8 v[50:53], v[180:183], v[188:191], v[50:53]
	v_mfma_i32_16x16x64_i8 v[42:45], v[172:175], v[196:199], v[42:45]
	v_mfma_i32_16x16x64_i8 v[34:37], v[180:183], v[196:199], v[34:37]
	v_mfma_i32_16x16x64_i8 v[26:29], v[172:175], v[204:207], v[26:29]
	v_mfma_i32_16x16x64_i8 v[18:21], v[180:183], v[204:207], v[18:21]
	v_mfma_i32_16x16x64_i8 v[10:13], v[172:175], v[212:215], v[10:13]
	v_mfma_i32_16x16x64_i8 v[2:5], v[180:183], v[212:215], v[2:5]
	s_setprio 0
	s_barrier
	s_add_u32 s66, s66, 0x100
	s_addc_u32 s67, s67, 0
	s_add_u32 s24, s24, 0x100
	s_addc_u32 s25, s25, 0
	s_cmp_ge_i32 s68, s54
	s_mov_b32 s26, s68
	s_cbranch_scc0 .LBB0_227
	s_branch .LBB0_228
.LBB0_227:
	v_add_u32_e32 v142, s35, v164
	v_add_u32_e32 v180, s36, v164
	ds_read_b128 v[130:133], v142
	ds_read_b128 v[134:137], v142 offset:1024
	ds_read_b128 v[138:141], v142 offset:2048
	ds_read_b128 v[142:145], v142 offset:3072
	ds_read_b128 v[168:171], v180
	ds_read_b128 v[172:175], v180 offset:1024
	ds_read_b128 v[176:179], v180 offset:2048
	ds_read_b128 v[180:183], v180 offset:3072
	s_add_i32 s68, s26, 2
	s_add_u32 s27, s24, 0xfffc0080
	s_addc_u32 s28, s25, -1
	s_cmp_eq_u32 s61, s26
	s_cselect_b32 s26, s65, s66
	s_cselect_b32 s29, s15, s28
	s_cselect_b32 s28, s17, s27
	s_cselect_b32 s27, s64, s67
	s_add_i32 m0, s46, 0xc000
	ds_read_b128 v[184:187], v167
	ds_read_b128 v[188:191], v167 offset:1024
	ds_read_b128 v[192:195], v167 offset:2048
	ds_read_b128 v[196:199], v167 offset:3072
	ds_read_b128 v[200:203], v167 offset:4096
	ds_read_b128 v[204:207], v167 offset:5120
	ds_read_b128 v[208:211], v167 offset:6144
	ds_read_b128 v[212:215], v167 offset:7168
	global_load_lds_dwordx4 v158, s[24:25]
	s_add_i32 m0, s46, 0xe000
	s_nop 0
	global_load_lds_dwordx4 v156, s[24:25]
	s_waitcnt vmcnt(8) lgkmcnt(0)
	s_barrier
	s_setprio 1
	v_mfma_i32_16x16x64_i8 v[126:129], v[130:133], v[184:187], v[126:129]
	v_mfma_i32_16x16x64_i8 v[118:121], v[138:141], v[184:187], v[118:121]
	v_mfma_i32_16x16x64_i8 v[110:113], v[130:133], v[192:195], v[110:113]
	v_mfma_i32_16x16x64_i8 v[102:105], v[138:141], v[192:195], v[102:105]
	v_mfma_i32_16x16x64_i8 v[94:97], v[130:133], v[200:203], v[94:97]
	v_mfma_i32_16x16x64_i8 v[86:89], v[138:141], v[200:203], v[86:89]
	v_mfma_i32_16x16x64_i8 v[78:81], v[130:133], v[208:211], v[78:81]
	v_mfma_i32_16x16x64_i8 v[70:73], v[138:141], v[208:211], v[70:73]
	v_mfma_i32_16x16x64_i8 v[126:129], v[134:137], v[188:191], v[126:129]
	v_mfma_i32_16x16x64_i8 v[118:121], v[142:145], v[188:191], v[118:121]
	v_mfma_i32_16x16x64_i8 v[110:113], v[134:137], v[196:199], v[110:113]
	v_mfma_i32_16x16x64_i8 v[102:105], v[142:145], v[196:199], v[102:105]
	v_mfma_i32_16x16x64_i8 v[94:97], v[134:137], v[204:207], v[94:97]
	v_mfma_i32_16x16x64_i8 v[86:89], v[142:145], v[204:207], v[86:89]
	v_mfma_i32_16x16x64_i8 v[78:81], v[134:137], v[212:215], v[78:81]
	v_mfma_i32_16x16x64_i8 v[70:73], v[142:145], v[212:215], v[70:73]
	s_setprio 0
	s_setprio 1
	v_mfma_i32_16x16x64_i8 v[122:125], v[168:171], v[184:187], v[122:125]
	v_mfma_i32_16x16x64_i8 v[114:117], v[176:179], v[184:187], v[114:117]
	v_mfma_i32_16x16x64_i8 v[106:109], v[168:171], v[192:195], v[106:109]
	v_mfma_i32_16x16x64_i8 v[98:101], v[176:179], v[192:195], v[98:101]
	v_mfma_i32_16x16x64_i8 v[90:93], v[168:171], v[200:203], v[90:93]
	v_mfma_i32_16x16x64_i8 v[82:85], v[176:179], v[200:203], v[82:85]
	v_mfma_i32_16x16x64_i8 v[74:77], v[168:171], v[208:211], v[74:77]
	v_mfma_i32_16x16x64_i8 v[66:69], v[176:179], v[208:211], v[66:69]
	v_mfma_i32_16x16x64_i8 v[122:125], v[172:175], v[188:191], v[122:125]
	v_mfma_i32_16x16x64_i8 v[114:117], v[180:183], v[188:191], v[114:117]
	v_mfma_i32_16x16x64_i8 v[106:109], v[172:175], v[196:199], v[106:109]
	v_mfma_i32_16x16x64_i8 v[98:101], v[180:183], v[196:199], v[98:101]
	v_mfma_i32_16x16x64_i8 v[90:93], v[172:175], v[204:207], v[90:93]
	v_mfma_i32_16x16x64_i8 v[82:85], v[180:183], v[204:207], v[82:85]
	v_mfma_i32_16x16x64_i8 v[74:77], v[172:175], v[212:215], v[74:77]
	v_mfma_i32_16x16x64_i8 v[66:69], v[180:183], v[212:215], v[66:69]
	s_setprio 0
	s_barrier
; #define PG8_STAGE(bufoff, gbase, voff) do { _Pragma("unroll") for (int _i = 0; _i < 2; ++_i) \
;         __builtin_amdgcn_global_load_lds((const unsigned*)((const char*)(gbase) + (voff)[_i]), (PG8_LAS unsigned*)(lds + (bufoff) + ldsw + _i * 8192), 16, 0, 0); } while (0)
; #define PG8_LDA(dst, b, h) do { if constexpr (DT != 1) { _Pragma("unroll") for (int m = 0; m < 4; ++m) _Pragma("unroll") for (int k = 0; k < 2; ++k) dst[m][k] = *(const PG8_LAS bf16x8*)(lds + PG8_SA(b, h) + aoff + m * 2048 + k * 1024); } \
;         else { _Pragma("unroll") for (int m = 0; m < 4; ++m) dst##8[m] = ld32(lds + PG8_SA(b, h) + aoff + m * 2048); } } while (0)
; #define PG8_LDB(dst, b, h) do { if constexpr (DT != 1) { _Pragma("unroll") for (int n = 0; n < 2; ++n) _Pragma("unroll") for (int k = 0; k < 2; ++k) dst[n][k] = *(const PG8_LAS bf16x8*)(lds + PG8_SB(b, h) + boff + n * 2048 + k * 1024); } \
;         else { _Pragma("unroll") for (int n = 0; n < 2; ++n) dst##8[n] = ld32(lds + PG8_SB(b, h) + boff + n * 2048); } } while (0)
; #define PG8_WAIT_V(n) asm volatile("s_waitcnt vmcnt(" #n ")" ::: "memory")
; #define PG8_WAIT_L(n) asm volatile("s_waitcnt lgkmcnt(" #n ")" ::: "memory")
; #define PG8_BAR __builtin_amdgcn_s_barrier()
; #define PG8_SCHED __builtin_amdgcn_sched_barrier(0)
;     ...
;             if constexpr (SP2) {
;             PG8_LDB(B0, 0, 0); PG8_LDB(B1, 0, 1); PG8_SCHED; PG8_LDA(At, 0, 0); PG8_STAGE(PG8_SA(1, 1), a1 + hstepA, voffA);
;             PG8_WAIT_V(8); PG8_WAIT_L(0); PG8_BAR; PG8_MMA(0, 0, At, B0); PG8_MMA(0, 1, At, B1); PG8_BAR; PG8_SCHED;
;             PG8_LDA(At, 0, 1); PG8_STAGE(PG8_SB(0, 0), b2, voffB); PG8_STAGE(PG8_SB(0, 1), b2 + hstepB, voffB); PG8_STAGE(PG8_SA(0, 0), a2, voffA);
;             PG8_WAIT_V(8); PG8_WAIT_L(0); PG8_BAR; PG8_MMA(1, 0, At, B0); PG8_MMA(1, 1, At, B1); PG8_BAR; PG8_SCHED;
;             PG8_LDB(B0, 1, 0); PG8_LDB(B1, 1, 1); PG8_SCHED; PG8_LDA(At, 1, 0); PG8_STAGE(PG8_SA(0, 1), a2 + hstepA, voffA);
;             PG8_WAIT_V(8); PG8_WAIT_L(0); PG8_BAR; PG8_MMA(0, 0, At, B0); PG8_MMA(0, 1, At, B1); PG8_BAR; PG8_SCHED;
;             PG8_LDA(At, 1, 1); PG8_STAGE(PG8_SB(1, 0), b3, voffB); PG8_STAGE(PG8_SB(1, 1), b3 + hstepB, voffB); PG8_STAGE(PG8_SA(1, 0), a3, voffA);
;             PG8_WAIT_V(8); PG8_WAIT_L(0); PG8_BAR; PG8_MMA(1, 0, At, B0); PG8_MMA(1, 1, At, B1); PG8_BAR; PG8_SCHED;
	s_mov_b32 m0, s23
	s_add_u32 s98, s26, 0x80
	s_addc_u32 s99, s27, 0
	s_add_u32 s70, s26, 0x40000
	ds_read_b128 v[184:187], v167 offset:16384
	ds_read_b128 v[188:191], v167 offset:17408
	ds_read_b128 v[192:195], v167 offset:18432
	ds_read_b128 v[196:199], v167 offset:19456
	global_load_lds_dwordx4 v148, s[26:27]
	s_mov_b32 m0, s43
	s_addc_u32 s71, s27, 0
	global_load_lds_dwordx4 v152, s[26:27]
	s_mov_b32 m0, s44
	ds_read_b128 v[212:215], v167 offset:23552
	global_load_lds_dwordx4 v148, s[70:71]
	s_mov_b32 m0, s45
	ds_read_b128 v[208:211], v167 offset:22528
	global_load_lds_dwordx4 v152, s[70:71]
	s_add_u32 s100, s28, 0x80
	s_addc_u32 s101, s29, 0
	s_mov_b32 m0, s46
	ds_read_b128 v[204:207], v167 offset:21504
	global_load_lds_dwordx4 v146, s[28:29]
	s_mov_b32 m0, s47
	ds_read_b128 v[200:203], v167 offset:20480
	global_load_lds_dwordx4 v150, s[28:29]
	s_waitcnt vmcnt(8) lgkmcnt(0)
	s_barrier
	s_setprio 1
	v_mfma_i32_16x16x64_i8 v[62:65], v[130:133], v[184:187], v[62:65]
	v_mfma_i32_16x16x64_i8 v[54:57], v[138:141], v[184:187], v[54:57]
	v_mfma_i32_16x16x64_i8 v[46:49], v[130:133], v[192:195], v[46:49]
	v_mfma_i32_16x16x64_i8 v[38:41], v[138:141], v[192:195], v[38:41]
	v_mfma_i32_16x16x64_i8 v[30:33], v[130:133], v[200:203], v[30:33]
	v_mfma_i32_16x16x64_i8 v[22:25], v[138:141], v[200:203], v[22:25]
	v_mfma_i32_16x16x64_i8 v[14:17], v[130:133], v[208:211], v[14:17]
	v_mfma_i32_16x16x64_i8 v[6:9], v[138:141], v[208:211], v[6:9]
	v_mfma_i32_16x16x64_i8 v[62:65], v[134:137], v[188:191], v[62:65]
	v_mfma_i32_16x16x64_i8 v[54:57], v[142:145], v[188:191], v[54:57]
	v_mfma_i32_16x16x64_i8 v[46:49], v[134:137], v[196:199], v[46:49]
	v_mfma_i32_16x16x64_i8 v[38:41], v[142:145], v[196:199], v[38:41]
	v_mfma_i32_16x16x64_i8 v[30:33], v[134:137], v[204:207], v[30:33]
	v_mfma_i32_16x16x64_i8 v[22:25], v[142:145], v[204:207], v[22:25]
	v_mfma_i32_16x16x64_i8 v[14:17], v[134:137], v[212:215], v[14:17]
	v_mfma_i32_16x16x64_i8 v[6:9], v[142:145], v[212:215], v[6:9]
	s_setprio 0
	s_setprio 1
	v_mfma_i32_16x16x64_i8 v[58:61], v[168:171], v[184:187], v[58:61]
	v_mfma_i32_16x16x64_i8 v[50:53], v[176:179], v[184:187], v[50:53]
	v_mfma_i32_16x16x64_i8 v[42:45], v[168:171], v[192:195], v[42:45]
	v_mfma_i32_16x16x64_i8 v[34:37], v[176:179], v[192:195], v[34:37]
	v_mfma_i32_16x16x64_i8 v[26:29], v[168:171], v[200:203], v[26:29]
	v_mfma_i32_16x16x64_i8 v[18:21], v[176:179], v[200:203], v[18:21]
	v_mfma_i32_16x16x64_i8 v[10:13], v[168:171], v[208:211], v[10:13]
	v_mfma_i32_16x16x64_i8 v[2:5], v[176:179], v[208:211], v[2:5]
	v_mfma_i32_16x16x64_i8 v[58:61], v[172:175], v[188:191], v[58:61]
	v_mfma_i32_16x16x64_i8 v[50:53], v[180:183], v[188:191], v[50:53]
	v_mfma_i32_16x16x64_i8 v[42:45], v[172:175], v[196:199], v[42:45]
	v_mfma_i32_16x16x64_i8 v[34:37], v[180:183], v[196:199], v[34:37]
	v_mfma_i32_16x16x64_i8 v[26:29], v[172:175], v[204:207], v[26:29]
	v_mfma_i32_16x16x64_i8 v[18:21], v[180:183], v[204:207], v[18:21]
	v_mfma_i32_16x16x64_i8 v[10:13], v[172:175], v[212:215], v[10:13]
	v_mfma_i32_16x16x64_i8 v[2:5], v[180:183], v[212:215], v[2:5]
	s_setprio 0
	s_barrier
	v_add_u32_e32 v142, s51, v164
	v_add_u32_e32 v180, s52, v164
	ds_read_b128 v[130:133], v142
	ds_read_b128 v[134:137], v142 offset:1024
	ds_read_b128 v[138:141], v142 offset:2048
	ds_read_b128 v[142:145], v142 offset:3072
	ds_read_b128 v[168:171], v180
	ds_read_b128 v[172:175], v180 offset:1024
	ds_read_b128 v[176:179], v180 offset:2048
	ds_read_b128 v[180:183], v180 offset:3072
	s_add_u32 s28, s28, 0x40000
	s_addc_u32 s29, s29, 0
	s_mov_b32 m0, s48
	ds_read_b128 v[184:187], v167 offset:32768
	ds_read_b128 v[188:191], v167 offset:33792
	ds_read_b128 v[192:195], v167 offset:34816
	ds_read_b128 v[196:199], v167 offset:35840
	ds_read_b128 v[200:203], v167 offset:36864
	ds_read_b128 v[204:207], v167 offset:37888
	ds_read_b128 v[208:211], v167 offset:38912
	global_load_lds_dwordx4 v146, s[28:29]
	s_mov_b32 m0, s49
	ds_read_b128 v[212:215], v167 offset:39936
	global_load_lds_dwordx4 v150, s[28:29]
	s_waitcnt vmcnt(8) lgkmcnt(0)
	s_barrier
; #define PG8_STAGE(bufoff, gbase, voff) do { _Pragma("unroll") for (int _i = 0; _i < 2; ++_i) \
;         __builtin_amdgcn_global_load_lds((const unsigned*)((const char*)(gbase) + (voff)[_i]), (PG8_LAS unsigned*)(lds + (bufoff) + ldsw + _i * 8192), 16, 0, 0); } while (0)
; #define PG8_LDA(dst, b, h) do { if constexpr (DT != 1) { _Pragma("unroll") for (int m = 0; m < 4; ++m) _Pragma("unroll") for (int k = 0; k < 2; ++k) dst[m][k] = *(const PG8_LAS bf16x8*)(lds + PG8_SA(b, h) + aoff + m * 2048 + k * 1024); } \
;         else { _Pragma("unroll") for (int m = 0; m < 4; ++m) dst##8[m] = ld32(lds + PG8_SA(b, h) + aoff + m * 2048); } } while (0)
; #define PG8_LDB(dst, b, h) do { if constexpr (DT != 1) { _Pragma("unroll") for (int n = 0; n < 2; ++n) _Pragma("unroll") for (int k = 0; k < 2; ++k) dst[n][k] = *(const PG8_LAS bf16x8*)(lds + PG8_SB(b, h) + boff + n * 2048 + k * 1024); } \
;         else { _Pragma("unroll") for (int n = 0; n < 2; ++n) dst##8[n] = ld32(lds + PG8_SB(b, h) + boff + n * 2048); } } while (0)
; #define PG8_WAIT_V(n) asm volatile("s_waitcnt vmcnt(" #n ")" ::: "memory")
; #define PG8_WAIT_L(n) asm volatile("s_waitcnt lgkmcnt(" #n ")" ::: "memory")
; #define PG8_BAR __builtin_amdgcn_s_barrier()
; #define PG8_SCHED __builtin_amdgcn_sched_barrier(0)
;     ...
;             if constexpr (SP2) {
;             PG8_LDB(B0, 0, 0); PG8_LDB(B1, 0, 1); PG8_SCHED; PG8_LDA(At, 0, 0); PG8_STAGE(PG8_SA(1, 1), a1 + hstepA, voffA);
;             PG8_WAIT_V(8); PG8_WAIT_L(0); PG8_BAR; PG8_MMA(0, 0, At, B0); PG8_MMA(0, 1, At, B1); PG8_BAR; PG8_SCHED;
;             PG8_LDA(At, 0, 1); PG8_STAGE(PG8_SB(0, 0), b2, voffB); PG8_STAGE(PG8_SB(0, 1), b2 + hstepB, voffB); PG8_STAGE(PG8_SA(0, 0), a2, voffA);
;             PG8_WAIT_V(8); PG8_WAIT_L(0); PG8_BAR; PG8_MMA(1, 0, At, B0); PG8_MMA(1, 1, At, B1); PG8_BAR; PG8_SCHED;
;             PG8_LDB(B0, 1, 0); PG8_LDB(B1, 1, 1); PG8_SCHED; PG8_LDA(At, 1, 0); PG8_STAGE(PG8_SA(0, 1), a2 + hstepA, voffA);
;             PG8_WAIT_V(8); PG8_WAIT_L(0); PG8_BAR; PG8_MMA(0, 0, At, B0); PG8_MMA(0, 1, At, B1); PG8_BAR; PG8_SCHED;
;             PG8_LDA(At, 1, 1); PG8_STAGE(PG8_SB(1, 0), b3, voffB); PG8_STAGE(PG8_SB(1, 1), b3 + hstepB, voffB); PG8_STAGE(PG8_SA(1, 0), a3, voffA);
;             PG8_WAIT_V(8); PG8_WAIT_L(0); PG8_BAR; PG8_MMA(1, 0, At, B0); PG8_MMA(1, 1, At, B1); PG8_BAR; PG8_SCHED;
	s_setprio 1
	v_mfma_i32_16x16x64_i8 v[126:129], v[130:133], v[184:187], v[126:129]
	v_mfma_i32_16x16x64_i8 v[118:121], v[138:141], v[184:187], v[118:121]
	v_mfma_i32_16x16x64_i8 v[110:113], v[130:133], v[192:195], v[110:113]
	v_mfma_i32_16x16x64_i8 v[102:105], v[138:141], v[192:195], v[102:105]
	v_mfma_i32_16x16x64_i8 v[94:97], v[130:133], v[200:203], v[94:97]
	v_mfma_i32_16x16x64_i8 v[86:89], v[138:141], v[200:203], v[86:89]
	v_mfma_i32_16x16x64_i8 v[78:81], v[130:133], v[208:211], v[78:81]
	v_mfma_i32_16x16x64_i8 v[70:73], v[138:141], v[208:211], v[70:73]
	v_mfma_i32_16x16x64_i8 v[126:129], v[134:137], v[188:191], v[126:129]
	v_mfma_i32_16x16x64_i8 v[118:121], v[142:145], v[188:191], v[118:121]
	v_mfma_i32_16x16x64_i8 v[110:113], v[134:137], v[196:199], v[110:113]
	v_mfma_i32_16x16x64_i8 v[102:105], v[142:145], v[196:199], v[102:105]
	v_mfma_i32_16x16x64_i8 v[94:97], v[134:137], v[204:207], v[94:97]
	v_mfma_i32_16x16x64_i8 v[86:89], v[142:145], v[204:207], v[86:89]
	v_mfma_i32_16x16x64_i8 v[78:81], v[134:137], v[212:215], v[78:81]
	v_mfma_i32_16x16x64_i8 v[70:73], v[142:145], v[212:215], v[70:73]
	s_setprio 0
	s_setprio 1
	v_mfma_i32_16x16x64_i8 v[122:125], v[168:171], v[184:187], v[122:125]
	v_mfma_i32_16x16x64_i8 v[114:117], v[176:179], v[184:187], v[114:117]
	v_mfma_i32_16x16x64_i8 v[106:109], v[168:171], v[192:195], v[106:109]
	v_mfma_i32_16x16x64_i8 v[98:101], v[176:179], v[192:195], v[98:101]
	v_mfma_i32_16x16x64_i8 v[90:93], v[168:171], v[200:203], v[90:93]
	v_mfma_i32_16x16x64_i8 v[82:85], v[176:179], v[200:203], v[82:85]
	v_mfma_i32_16x16x64_i8 v[74:77], v[168:171], v[208:211], v[74:77]
	v_mfma_i32_16x16x64_i8 v[66:69], v[176:179], v[208:211], v[66:69]
	v_mfma_i32_16x16x64_i8 v[122:125], v[172:175], v[188:191], v[122:125]
	v_mfma_i32_16x16x64_i8 v[114:117], v[180:183], v[188:191], v[114:117]
	v_mfma_i32_16x16x64_i8 v[106:109], v[172:175], v[196:199], v[106:109]
	v_mfma_i32_16x16x64_i8 v[98:101], v[180:183], v[196:199], v[98:101]
	v_mfma_i32_16x16x64_i8 v[90:93], v[172:175], v[204:207], v[90:93]
	v_mfma_i32_16x16x64_i8 v[82:85], v[180:183], v[204:207], v[82:85]
	v_mfma_i32_16x16x64_i8 v[74:77], v[172:175], v[212:215], v[74:77]
	v_mfma_i32_16x16x64_i8 v[66:69], v[180:183], v[212:215], v[66:69]
	s_setprio 0
	s_barrier
	s_mov_b32 m0, s55
	s_add_u32 s26, s26, 0x40080
	ds_read_b128 v[184:187], v167 offset:49152
	ds_read_b128 v[188:191], v167 offset:50176
	ds_read_b128 v[192:195], v167 offset:51200
	ds_read_b128 v[196:199], v167 offset:52224
	global_load_lds_dwordx4 v148, s[98:99]
	s_mov_b32 m0, s56
	s_addc_u32 s27, s27, 0
	global_load_lds_dwordx4 v152, s[98:99]
	s_mov_b32 m0, s59
	ds_read_b128 v[212:215], v167 offset:56320
	global_load_lds_dwordx4 v148, s[26:27]
	s_mov_b32 m0, s60
	ds_read_b128 v[208:211], v167 offset:55296
	global_load_lds_dwordx4 v152, s[26:27]
	s_mov_b32 m0, s57
	ds_read_b128 v[204:207], v167 offset:54272
	global_load_lds_dwordx4 v146, s[100:101]
	s_mov_b32 m0, s58
	ds_read_b128 v[200:203], v167 offset:53248
	global_load_lds_dwordx4 v150, s[100:101]
	s_waitcnt vmcnt(8) lgkmcnt(0)
	s_barrier
	s_setprio 1
	v_mfma_i32_16x16x64_i8 v[62:65], v[130:133], v[184:187], v[62:65]
	v_mfma_i32_16x16x64_i8 v[54:57], v[138:141], v[184:187], v[54:57]
	v_mfma_i32_16x16x64_i8 v[46:49], v[130:133], v[192:195], v[46:49]
	v_mfma_i32_16x16x64_i8 v[38:41], v[138:141], v[192:195], v[38:41]
	v_mfma_i32_16x16x64_i8 v[30:33], v[130:133], v[200:203], v[30:33]
	v_mfma_i32_16x16x64_i8 v[22:25], v[138:141], v[200:203], v[22:25]
	v_mfma_i32_16x16x64_i8 v[14:17], v[130:133], v[208:211], v[14:17]
	v_mfma_i32_16x16x64_i8 v[6:9], v[138:141], v[208:211], v[6:9]
	v_mfma_i32_16x16x64_i8 v[62:65], v[134:137], v[188:191], v[62:65]
	v_mfma_i32_16x16x64_i8 v[54:57], v[142:145], v[188:191], v[54:57]
	v_mfma_i32_16x16x64_i8 v[46:49], v[134:137], v[196:199], v[46:49]
	v_mfma_i32_16x16x64_i8 v[38:41], v[142:145], v[196:199], v[38:41]
	v_mfma_i32_16x16x64_i8 v[30:33], v[134:137], v[204:207], v[30:33]
	v_mfma_i32_16x16x64_i8 v[22:25], v[142:145], v[204:207], v[22:25]
	v_mfma_i32_16x16x64_i8 v[14:17], v[134:137], v[212:215], v[14:17]
	v_mfma_i32_16x16x64_i8 v[6:9], v[142:145], v[212:215], v[6:9]
	s_setprio 0
	s_setprio 1
	v_mfma_i32_16x16x64_i8 v[58:61], v[168:171], v[184:187], v[58:61]
	v_mfma_i32_16x16x64_i8 v[50:53], v[176:179], v[184:187], v[50:53]
	v_mfma_i32_16x16x64_i8 v[42:45], v[168:171], v[192:195], v[42:45]
	v_mfma_i32_16x16x64_i8 v[34:37], v[176:179], v[192:195], v[34:37]
	v_mfma_i32_16x16x64_i8 v[26:29], v[168:171], v[200:203], v[26:29]
	v_mfma_i32_16x16x64_i8 v[18:21], v[176:179], v[200:203], v[18:21]
	v_mfma_i32_16x16x64_i8 v[10:13], v[168:171], v[208:211], v[10:13]
	v_mfma_i32_16x16x64_i8 v[2:5], v[176:179], v[208:211], v[2:5]
	v_mfma_i32_16x16x64_i8 v[58:61], v[172:175], v[188:191], v[58:61]
	v_mfma_i32_16x16x64_i8 v[50:53], v[180:183], v[188:191], v[50:53]
	v_mfma_i32_16x16x64_i8 v[42:45], v[172:175], v[196:199], v[42:45]
	v_mfma_i32_16x16x64_i8 v[34:37], v[180:183], v[196:199], v[34:37]
	v_mfma_i32_16x16x64_i8 v[26:29], v[172:175], v[204:207], v[26:29]
	v_mfma_i32_16x16x64_i8 v[18:21], v[180:183], v[204:207], v[18:21]
	v_mfma_i32_16x16x64_i8 v[10:13], v[172:175], v[212:215], v[10:13]
	v_mfma_i32_16x16x64_i8 v[2:5], v[180:183], v[212:215], v[2:5]
	s_setprio 0
	s_barrier
	s_add_u32 s66, s66, 0x100
	s_addc_u32 s67, s67, 0
	s_add_u32 s24, s24, 0x100
	s_addc_u32 s25, s25, 0
	s_cmp_ge_i32 s68, s54
	s_mov_b32 s26, s68
	s_cbranch_scc0 .LBB0_227

; #define PG8_STAGE(bufoff, gbase, voff) do { _Pragma("unroll") for (int _i = 0; _i < 2; ++_i) \
;         __builtin_amdgcn_global_load_lds((const unsigned*)((const char*)(gbase) + (voff)[_i]), (PG8_LAS unsigned*)(lds + (bufoff) + ldsw + _i * 8192), 16, 0, 0); } while (0)
; #define PG8_LDA(dst, b, h) do { if constexpr (DT != 1) { _Pragma("unroll") for (int m = 0; m < 4; ++m) _Pragma("unroll") for (int k = 0; k < 2; ++k) dst[m][k] = *(const PG8_LAS bf16x8*)(lds + PG8_SA(b, h) + aoff + m * 2048 + k * 1024); } \
;         else { _Pragma("unroll") for (int m = 0; m < 4; ++m) dst##8[m] = ld32(lds + PG8_SA(b, h) + aoff + m * 2048); } } while (0)
; #define PG8_WAIT_V(n) asm volatile("s_waitcnt vmcnt(" #n ")" ::: "memory")
; #define PG8_WAIT_L(n) asm volatile("s_waitcnt lgkmcnt(" #n ")" ::: "memory")
; #define PG8_BAR __builtin_amdgcn_s_barrier()
; #define PG8_SCHED __builtin_amdgcn_sched_barrier(0)
;     ...
;         for (int t = 0; t < nt; t += 2) {
;             const bool last = (t == nt - 2);
;             const char* a1 = cA + (size_t)(t + 1) * kstep;
;             const char* a2 = last ? nA : cA + (size_t)(t + 2) * kstep; const char* b2 = last ? nB : cB + (size_t)(t + 2) * kstep;
;             const char* a3 = a2 + kstep; const char* b3 = b2 + kstep;
;             if (last && has_next) S.a_ready(nxt);
;             if constexpr (SP2) {
;             PG8_LDB(B0, 0, 0); PG8_LDB(B1, 0, 1); PG8_SCHED; PG8_LDA(At, 0, 0); PG8_STAGE(PG8_SA(1, 1), a1 + hstepA, voffA);
;             PG8_WAIT_V(8); PG8_WAIT_L(0); PG8_BAR; PG8_MMA(0, 0, At, B0); PG8_MMA(0, 1, At, B1); PG8_BAR; PG8_SCHED;
;             PG8_LDA(At, 0, 1); PG8_STAGE(PG8_SB(0, 0), b2, voffB); PG8_STAGE(PG8_SB(0, 1), b2 + hstepB, voffB); PG8_STAGE(PG8_SA(0, 0), a2, voffA);
;             PG8_WAIT_V(8); PG8_WAIT_L(0); PG8_BAR; PG8_MMA(1, 0, At, B0); PG8_MMA(1, 1, At, B1); PG8_BAR; PG8_SCHED;
;             PG8_LDB(B0, 1, 0); PG8_LDB(B1, 1, 1); PG8_SCHED; PG8_LDA(At, 1, 0); PG8_STAGE(PG8_SA(0, 1), a2 + hstepA, voffA);
;             PG8_WAIT_V(8); PG8_WAIT_L(0); PG8_BAR; PG8_MMA(0, 0, At, B0); PG8_MMA(0, 1, At, B1); PG8_BAR; PG8_SCHED;
;             PG8_LDA(At, 1, 1); PG8_STAGE(PG8_SB(1, 0), b3, voffB); PG8_STAGE(PG8_SB(1, 1), b3 + hstepB, voffB); PG8_STAGE(PG8_SA(1, 0), a3, voffA);
;             PG8_WAIT_V(8); PG8_WAIT_L(0); PG8_BAR; PG8_MMA(1, 0, At, B0); PG8_MMA(1, 1, At, B1); PG8_BAR; PG8_SCHED;
.Lzt_1:
	s_cbranch_vccnz .LBB0_305
	s_add_u32 s67, s30, 0x100
	s_addc_u32 s68, s31, 0
	s_mov_b32 s34, 0
	ds_read_b128 v[146:149], v159
	ds_read_b128 v[150:153], v159 offset:1024
	ds_read_b128 v[154:157], v159 offset:2048
	ds_read_b128 v[164:167], v159 offset:3072
	ds_read_b128 v[168:171], v160
	ds_read_b128 v[172:175], v160 offset:1024
	ds_read_b128 v[176:179], v160 offset:2048
	ds_read_b128 v[180:183], v160 offset:3072
	s_add_i32 s69, s34, 2
	s_add_u32 s30, s28, 0x100
	s_addc_u32 s31, s29, 0
	s_cmp_eq_u32 s60, s34
	s_cselect_b32 s34, s26, s67
	s_cselect_b32 s37, s3, s31
	s_cselect_b32 s36, s2, s30
	s_cselect_b32 s35, s27, s68
	v_lshl_add_u64 v[216:217], s[28:29], 0, v[140:141]
	s_add_i32 m0, s48, 0xc000
	ds_read_b128 v[184:187], v161
	ds_read_b128 v[188:191], v161 offset:1024
	ds_read_b128 v[192:195], v161 offset:2048
	ds_read_b128 v[196:199], v161 offset:3072
	ds_read_b128 v[200:203], v161 offset:4096
	ds_read_b128 v[204:207], v161 offset:5120
	ds_read_b128 v[208:211], v161 offset:6144
	ds_read_b128 v[212:215], v161 offset:7168
	global_load_lds_dwordx4 v[216:217], off
	v_lshl_add_u64 v[216:217], s[28:29], 0, v[138:139]
	s_add_i32 m0, s48, 0xe000
	s_nop 0
	global_load_lds_dwordx4 v[216:217], off
	s_waitcnt vmcnt(8) lgkmcnt(0)
	s_barrier
	s_setprio 1
	v_mfma_f32_16x16x32_bf16 v[126:129], v[146:149], v[184:187], 0
	v_mfma_f32_16x16x32_bf16 v[122:125], v[154:157], v[184:187], 0
	v_mfma_f32_16x16x32_bf16 v[118:121], v[146:149], v[192:195], 0
	v_mfma_f32_16x16x32_bf16 v[114:117], v[154:157], v[192:195], 0
	v_mfma_f32_16x16x32_bf16 v[106:109], v[146:149], v[200:203], 0
	v_mfma_f32_16x16x32_bf16 v[98:101], v[154:157], v[200:203], 0
	v_mfma_f32_16x16x32_bf16 v[90:93], v[146:149], v[208:211], 0
	v_mfma_f32_16x16x32_bf16 v[82:85], v[154:157], v[208:211], 0
	v_mfma_f32_16x16x32_bf16 v[126:129], v[150:153], v[188:191], v[126:129]
	v_mfma_f32_16x16x32_bf16 v[122:125], v[164:167], v[188:191], v[122:125]
	v_mfma_f32_16x16x32_bf16 v[118:121], v[150:153], v[196:199], v[118:121]
	v_mfma_f32_16x16x32_bf16 v[114:117], v[164:167], v[196:199], v[114:117]
	v_mfma_f32_16x16x32_bf16 v[106:109], v[150:153], v[204:207], v[106:109]
	v_mfma_f32_16x16x32_bf16 v[98:101], v[164:167], v[204:207], v[98:101]
	v_mfma_f32_16x16x32_bf16 v[90:93], v[150:153], v[212:215], v[90:93]
	v_mfma_f32_16x16x32_bf16 v[82:85], v[164:167], v[212:215], v[82:85]
	s_setprio 0
	s_setprio 1
	v_mfma_f32_16x16x32_bf16 v[110:113], v[168:171], v[184:187], 0
	v_mfma_f32_16x16x32_bf16 v[102:105], v[176:179], v[184:187], 0
	v_mfma_f32_16x16x32_bf16 v[94:97], v[168:171], v[192:195], 0
	v_mfma_f32_16x16x32_bf16 v[86:89], v[176:179], v[192:195], 0
	v_mfma_f32_16x16x32_bf16 v[78:81], v[168:171], v[200:203], 0
	v_mfma_f32_16x16x32_bf16 v[74:77], v[176:179], v[200:203], 0
	v_mfma_f32_16x16x32_bf16 v[70:73], v[168:171], v[208:211], 0
	v_mfma_f32_16x16x32_bf16 v[66:69], v[176:179], v[208:211], 0
	v_mfma_f32_16x16x32_bf16 v[110:113], v[172:175], v[188:191], v[110:113]
	v_mfma_f32_16x16x32_bf16 v[102:105], v[180:183], v[188:191], v[102:105]
	v_mfma_f32_16x16x32_bf16 v[94:97], v[172:175], v[196:199], v[94:97]
	v_mfma_f32_16x16x32_bf16 v[86:89], v[180:183], v[196:199], v[86:89]
	v_mfma_f32_16x16x32_bf16 v[78:81], v[172:175], v[204:207], v[78:81]
	v_mfma_f32_16x16x32_bf16 v[74:77], v[180:183], v[204:207], v[74:77]
	v_mfma_f32_16x16x32_bf16 v[70:73], v[172:175], v[212:215], v[70:73]
	v_mfma_f32_16x16x32_bf16 v[66:69], v[180:183], v[212:215], v[66:69]
	s_setprio 0
	s_barrier
	s_mov_b32 m0, s44
	s_add_u32 s98, s34, 0x80
	s_addc_u32 s99, s35, 0
	s_add_u32 s28, s34, 0x160000
	ds_read_b128 v[184:187], v161 offset:16384
	ds_read_b128 v[188:191], v161 offset:17408
	ds_read_b128 v[192:195], v161 offset:18432
	ds_read_b128 v[196:199], v161 offset:19456
	global_load_lds_dwordx4 v132, s[34:35]
	s_mov_b32 m0, s45
	s_addc_u32 s29, s35, 0
	global_load_lds_dwordx4 v136, s[34:35]
	s_mov_b32 m0, s46
	ds_read_b128 v[212:215], v161 offset:23552
	global_load_lds_dwordx4 v132, s[28:29]
	s_mov_b32 m0, s47
	ds_read_b128 v[208:211], v161 offset:22528
	global_load_lds_dwordx4 v136, s[28:29]
	s_add_u32 s100, s36, 0x80
	s_addc_u32 s101, s37, 0
	s_mov_b32 m0, s48
	ds_read_b128 v[204:207], v161 offset:21504
	global_load_lds_dwordx4 v130, s[36:37]
	s_mov_b32 m0, s49
	ds_read_b128 v[200:203], v161 offset:20480
	global_load_lds_dwordx4 v134, s[36:37]
	s_waitcnt vmcnt(8) lgkmcnt(0)
	s_barrier
	s_setprio 1
	v_mfma_f32_16x16x32_bf16 v[62:65], v[146:149], v[184:187], 0
	v_mfma_f32_16x16x32_bf16 v[58:61], v[154:157], v[184:187], 0
	v_mfma_f32_16x16x32_bf16 v[54:57], v[146:149], v[192:195], 0
	v_mfma_f32_16x16x32_bf16 v[50:53], v[154:157], v[192:195], 0
	v_mfma_f32_16x16x32_bf16 v[42:45], v[146:149], v[200:203], 0
	v_mfma_f32_16x16x32_bf16 v[34:37], v[154:157], v[200:203], 0
	v_mfma_f32_16x16x32_bf16 v[26:29], v[146:149], v[208:211], 0
	v_mfma_f32_16x16x32_bf16 v[18:21], v[154:157], v[208:211], 0
	v_mfma_f32_16x16x32_bf16 v[62:65], v[150:153], v[188:191], v[62:65]
	v_mfma_f32_16x16x32_bf16 v[58:61], v[164:167], v[188:191], v[58:61]
	v_mfma_f32_16x16x32_bf16 v[54:57], v[150:153], v[196:199], v[54:57]
	v_mfma_f32_16x16x32_bf16 v[50:53], v[164:167], v[196:199], v[50:53]
	v_mfma_f32_16x16x32_bf16 v[42:45], v[150:153], v[204:207], v[42:45]
	v_mfma_f32_16x16x32_bf16 v[34:37], v[164:167], v[204:207], v[34:37]
	v_mfma_f32_16x16x32_bf16 v[26:29], v[150:153], v[212:215], v[26:29]
	v_mfma_f32_16x16x32_bf16 v[18:21], v[164:167], v[212:215], v[18:21]
	s_setprio 0
	s_setprio 1
	v_mfma_f32_16x16x32_bf16 v[46:49], v[168:171], v[184:187], 0
	v_mfma_f32_16x16x32_bf16 v[38:41], v[176:179], v[184:187], 0
	v_mfma_f32_16x16x32_bf16 v[30:33], v[168:171], v[192:195], 0
	v_mfma_f32_16x16x32_bf16 v[22:25], v[176:179], v[192:195], 0
	v_mfma_f32_16x16x32_bf16 v[14:17], v[168:171], v[200:203], 0
	v_mfma_f32_16x16x32_bf16 v[10:13], v[176:179], v[200:203], 0
	v_mfma_f32_16x16x32_bf16 v[6:9], v[168:171], v[208:211], 0
	v_mfma_f32_16x16x32_bf16 v[2:5], v[176:179], v[208:211], 0
	v_mfma_f32_16x16x32_bf16 v[46:49], v[172:175], v[188:191], v[46:49]
	v_mfma_f32_16x16x32_bf16 v[38:41], v[180:183], v[188:191], v[38:41]
	v_mfma_f32_16x16x32_bf16 v[30:33], v[172:175], v[196:199], v[30:33]
	v_mfma_f32_16x16x32_bf16 v[22:25], v[180:183], v[196:199], v[22:25]
	v_mfma_f32_16x16x32_bf16 v[14:17], v[172:175], v[204:207], v[14:17]
	v_mfma_f32_16x16x32_bf16 v[10:13], v[180:183], v[204:207], v[10:13]
	v_mfma_f32_16x16x32_bf16 v[6:9], v[172:175], v[212:215], v[6:9]
	v_mfma_f32_16x16x32_bf16 v[2:5], v[180:183], v[212:215], v[2:5]
	s_setprio 0
	s_barrier
; #define PG8_STAGE(bufoff, gbase, voff) do { _Pragma("unroll") for (int _i = 0; _i < 2; ++_i) \
;         __builtin_amdgcn_global_load_lds((const unsigned*)((const char*)(gbase) + (voff)[_i]), (PG8_LAS unsigned*)(lds + (bufoff) + ldsw + _i * 8192), 16, 0, 0); } while (0)
; #define PG8_LDA(dst, b, h) do { if constexpr (DT != 1) { _Pragma("unroll") for (int m = 0; m < 4; ++m) _Pragma("unroll") for (int k = 0; k < 2; ++k) dst[m][k] = *(const PG8_LAS bf16x8*)(lds + PG8_SA(b, h) + aoff + m * 2048 + k * 1024); } \
;         else { _Pragma("unroll") for (int m = 0; m < 4; ++m) dst##8[m] = ld32(lds + PG8_SA(b, h) + aoff + m * 2048); } } while (0)
; #define PG8_LDB(dst, b, h) do { if constexpr (DT != 1) { _Pragma("unroll") for (int n = 0; n < 2; ++n) _Pragma("unroll") for (int k = 0; k < 2; ++k) dst[n][k] = *(const PG8_LAS bf16x8*)(lds + PG8_SB(b, h) + boff + n * 2048 + k * 1024); } \
;         else { _Pragma("unroll") for (int n = 0; n < 2; ++n) dst##8[n] = ld32(lds + PG8_SB(b, h) + boff + n * 2048); } } while (0)
; #define PG8_WAIT_V(n) asm volatile("s_waitcnt vmcnt(" #n ")" ::: "memory")
; #define PG8_WAIT_L(n) asm volatile("s_waitcnt lgkmcnt(" #n ")" ::: "memory")
; #define PG8_BAR __builtin_amdgcn_s_barrier()
; #define PG8_SCHED __builtin_amdgcn_sched_barrier(0)
;     ...
;             if constexpr (SP2) {
;             PG8_LDB(B0, 0, 0); PG8_LDB(B1, 0, 1); PG8_SCHED; PG8_LDA(At, 0, 0); PG8_STAGE(PG8_SA(1, 1), a1 + hstepA, voffA);
;             PG8_WAIT_V(8); PG8_WAIT_L(0); PG8_BAR; PG8_MMA(0, 0, At, B0); PG8_MMA(0, 1, At, B1); PG8_BAR; PG8_SCHED;
;             PG8_LDA(At, 0, 1); PG8_STAGE(PG8_SB(0, 0), b2, voffB); PG8_STAGE(PG8_SB(0, 1), b2 + hstepB, voffB); PG8_STAGE(PG8_SA(0, 0), a2, voffA);
;             PG8_WAIT_V(8); PG8_WAIT_L(0); PG8_BAR; PG8_MMA(1, 0, At, B0); PG8_MMA(1, 1, At, B1); PG8_BAR; PG8_SCHED;
;             PG8_LDB(B0, 1, 0); PG8_LDB(B1, 1, 1); PG8_SCHED; PG8_LDA(At, 1, 0); PG8_STAGE(PG8_SA(0, 1), a2 + hstepA, voffA);
;             PG8_WAIT_V(8); PG8_WAIT_L(0); PG8_BAR; PG8_MMA(0, 0, At, B0); PG8_MMA(0, 1, At, B1); PG8_BAR; PG8_SCHED;
;             PG8_LDA(At, 1, 1); PG8_STAGE(PG8_SB(1, 0), b3, voffB); PG8_STAGE(PG8_SB(1, 1), b3 + hstepB, voffB); PG8_STAGE(PG8_SA(1, 0), a3, voffA);
;             PG8_WAIT_V(8); PG8_WAIT_L(0); PG8_BAR; PG8_MMA(1, 0, At, B0); PG8_MMA(1, 1, At, B1); PG8_BAR; PG8_SCHED;
	ds_read_b128 v[146:149], v162
	ds_read_b128 v[150:153], v162 offset:1024
	ds_read_b128 v[154:157], v162 offset:2048
	ds_read_b128 v[164:167], v162 offset:3072
	ds_read_b128 v[168:171], v163
	ds_read_b128 v[172:175], v163 offset:1024
	ds_read_b128 v[176:179], v163 offset:2048
	ds_read_b128 v[180:183], v163 offset:3072
	s_add_u32 s28, s36, 0x160000
	s_addc_u32 s29, s37, 0
	s_mov_b32 m0, s50
	ds_read_b128 v[184:187], v161 offset:32768
	ds_read_b128 v[188:191], v161 offset:33792
	ds_read_b128 v[192:195], v161 offset:34816
	ds_read_b128 v[196:199], v161 offset:35840
	ds_read_b128 v[200:203], v161 offset:36864
	ds_read_b128 v[204:207], v161 offset:37888
	ds_read_b128 v[208:211], v161 offset:38912
	global_load_lds_dwordx4 v130, s[28:29]
	s_mov_b32 m0, s51
	ds_read_b128 v[212:215], v161 offset:39936
	global_load_lds_dwordx4 v134, s[28:29]
	s_waitcnt vmcnt(8) lgkmcnt(0)
	s_barrier
	s_setprio 1
	v_mfma_f32_16x16x32_bf16 v[126:129], v[146:149], v[184:187], v[126:129]
	v_mfma_f32_16x16x32_bf16 v[122:125], v[154:157], v[184:187], v[122:125]
	v_mfma_f32_16x16x32_bf16 v[118:121], v[146:149], v[192:195], v[118:121]
	v_mfma_f32_16x16x32_bf16 v[114:117], v[154:157], v[192:195], v[114:117]
	v_mfma_f32_16x16x32_bf16 v[106:109], v[146:149], v[200:203], v[106:109]
	v_mfma_f32_16x16x32_bf16 v[98:101], v[154:157], v[200:203], v[98:101]
	v_mfma_f32_16x16x32_bf16 v[90:93], v[146:149], v[208:211], v[90:93]
	v_mfma_f32_16x16x32_bf16 v[82:85], v[154:157], v[208:211], v[82:85]
	v_mfma_f32_16x16x32_bf16 v[126:129], v[150:153], v[188:191], v[126:129]
	v_mfma_f32_16x16x32_bf16 v[122:125], v[164:167], v[188:191], v[122:125]
	v_mfma_f32_16x16x32_bf16 v[118:121], v[150:153], v[196:199], v[118:121]
	v_mfma_f32_16x16x32_bf16 v[114:117], v[164:167], v[196:199], v[114:117]
	v_mfma_f32_16x16x32_bf16 v[106:109], v[150:153], v[204:207], v[106:109]
	v_mfma_f32_16x16x32_bf16 v[98:101], v[164:167], v[204:207], v[98:101]
	v_mfma_f32_16x16x32_bf16 v[90:93], v[150:153], v[212:215], v[90:93]
	v_mfma_f32_16x16x32_bf16 v[82:85], v[164:167], v[212:215], v[82:85]
	s_setprio 0
	s_setprio 1
	v_mfma_f32_16x16x32_bf16 v[110:113], v[168:171], v[184:187], v[110:113]
	v_mfma_f32_16x16x32_bf16 v[102:105], v[176:179], v[184:187], v[102:105]
	v_mfma_f32_16x16x32_bf16 v[94:97], v[168:171], v[192:195], v[94:97]
	v_mfma_f32_16x16x32_bf16 v[86:89], v[176:179], v[192:195], v[86:89]
	v_mfma_f32_16x16x32_bf16 v[78:81], v[168:171], v[200:203], v[78:81]
	v_mfma_f32_16x16x32_bf16 v[74:77], v[176:179], v[200:203], v[74:77]
	v_mfma_f32_16x16x32_bf16 v[70:73], v[168:171], v[208:211], v[70:73]
	v_mfma_f32_16x16x32_bf16 v[66:69], v[176:179], v[208:211], v[66:69]
	v_mfma_f32_16x16x32_bf16 v[110:113], v[172:175], v[188:191], v[110:113]
	v_mfma_f32_16x16x32_bf16 v[102:105], v[180:183], v[188:191], v[102:105]
	v_mfma_f32_16x16x32_bf16 v[94:97], v[172:175], v[196:199], v[94:97]
	v_mfma_f32_16x16x32_bf16 v[86:89], v[180:183], v[196:199], v[86:89]
	v_mfma_f32_16x16x32_bf16 v[78:81], v[172:175], v[204:207], v[78:81]
	v_mfma_f32_16x16x32_bf16 v[74:77], v[180:183], v[204:207], v[74:77]
	v_mfma_f32_16x16x32_bf16 v[70:73], v[172:175], v[212:215], v[70:73]
	v_mfma_f32_16x16x32_bf16 v[66:69], v[180:183], v[212:215], v[66:69]
	s_setprio 0
	s_barrier
	s_mov_b32 m0, s54
	s_add_u32 s28, s34, 0x160080
	ds_read_b128 v[184:187], v161 offset:49152
	ds_read_b128 v[188:191], v161 offset:50176
	ds_read_b128 v[192:195], v161 offset:51200
	ds_read_b128 v[196:199], v161 offset:52224
	global_load_lds_dwordx4 v132, s[98:99]
	s_mov_b32 m0, s55
	s_addc_u32 s29, s35, 0
	global_load_lds_dwordx4 v136, s[98:99]
	s_mov_b32 m0, s58
	ds_read_b128 v[212:215], v161 offset:56320
	global_load_lds_dwordx4 v132, s[28:29]
	s_mov_b32 m0, s59
	ds_read_b128 v[208:211], v161 offset:55296
	global_load_lds_dwordx4 v136, s[28:29]
	s_mov_b32 m0, s56
	ds_read_b128 v[204:207], v161 offset:54272
	global_load_lds_dwordx4 v130, s[100:101]
	s_mov_b32 m0, s57
	ds_read_b128 v[200:203], v161 offset:53248
	global_load_lds_dwordx4 v134, s[100:101]
	s_waitcnt vmcnt(8) lgkmcnt(0)
	s_barrier
	s_setprio 1
	v_mfma_f32_16x16x32_bf16 v[62:65], v[146:149], v[184:187], v[62:65]
	v_mfma_f32_16x16x32_bf16 v[58:61], v[154:157], v[184:187], v[58:61]
	v_mfma_f32_16x16x32_bf16 v[54:57], v[146:149], v[192:195], v[54:57]
	v_mfma_f32_16x16x32_bf16 v[50:53], v[154:157], v[192:195], v[50:53]
	v_mfma_f32_16x16x32_bf16 v[42:45], v[146:149], v[200:203], v[42:45]
	v_mfma_f32_16x16x32_bf16 v[34:37], v[154:157], v[200:203], v[34:37]
	v_mfma_f32_16x16x32_bf16 v[26:29], v[146:149], v[208:211], v[26:29]
	v_mfma_f32_16x16x32_bf16 v[18:21], v[154:157], v[208:211], v[18:21]
	v_mfma_f32_16x16x32_bf16 v[62:65], v[150:153], v[188:191], v[62:65]
	v_mfma_f32_16x16x32_bf16 v[58:61], v[164:167], v[188:191], v[58:61]
	v_mfma_f32_16x16x32_bf16 v[54:57], v[150:153], v[196:199], v[54:57]
	v_mfma_f32_16x16x32_bf16 v[50:53], v[164:167], v[196:199], v[50:53]
	v_mfma_f32_16x16x32_bf16 v[42:45], v[150:153], v[204:207], v[42:45]
	v_mfma_f32_16x16x32_bf16 v[34:37], v[164:167], v[204:207], v[34:37]
	v_mfma_f32_16x16x32_bf16 v[26:29], v[150:153], v[212:215], v[26:29]
	v_mfma_f32_16x16x32_bf16 v[18:21], v[164:167], v[212:215], v[18:21]
	s_setprio 0
	s_setprio 1
	v_mfma_f32_16x16x32_bf16 v[46:49], v[168:171], v[184:187], v[46:49]
	v_mfma_f32_16x16x32_bf16 v[38:41], v[176:179], v[184:187], v[38:41]
	v_mfma_f32_16x16x32_bf16 v[30:33], v[168:171], v[192:195], v[30:33]
	v_mfma_f32_16x16x32_bf16 v[22:25], v[176:179], v[192:195], v[22:25]
	v_mfma_f32_16x16x32_bf16 v[14:17], v[168:171], v[200:203], v[14:17]
	v_mfma_f32_16x16x32_bf16 v[10:13], v[176:179], v[200:203], v[10:13]
	v_mfma_f32_16x16x32_bf16 v[6:9], v[168:171], v[208:211], v[6:9]
	v_mfma_f32_16x16x32_bf16 v[2:5], v[176:179], v[208:211], v[2:5]
	v_mfma_f32_16x16x32_bf16 v[46:49], v[172:175], v[188:191], v[46:49]
	v_mfma_f32_16x16x32_bf16 v[38:41], v[180:183], v[188:191], v[38:41]
	v_mfma_f32_16x16x32_bf16 v[30:33], v[172:175], v[196:199], v[30:33]
	v_mfma_f32_16x16x32_bf16 v[22:25], v[180:183], v[196:199], v[22:25]
	v_mfma_f32_16x16x32_bf16 v[14:17], v[172:175], v[204:207], v[14:17]
	v_mfma_f32_16x16x32_bf16 v[10:13], v[180:183], v[204:207], v[10:13]
	v_mfma_f32_16x16x32_bf16 v[6:9], v[172:175], v[212:215], v[6:9]
	v_mfma_f32_16x16x32_bf16 v[2:5], v[180:183], v[212:215], v[2:5]
	s_setprio 0
	s_barrier
	s_add_u32 s67, s67, 0x100
	s_addc_u32 s68, s68, 0
	s_cmp_ge_i32 s69, s53
	s_mov_b64 s[28:29], s[30:31]
	s_mov_b32 s34, s69
	s_cbranch_scc0 .LBB0_303
	s_branch .Lpx_1
; #define PG8_STAGE(bufoff, gbase, voff) do { _Pragma("unroll") for (int _i = 0; _i < 2; ++_i) \
;         __builtin_amdgcn_global_load_lds((const unsigned*)((const char*)(gbase) + (voff)[_i]), (PG8_LAS unsigned*)(lds + (bufoff) + ldsw + _i * 8192), 16, 0, 0); } while (0)
; #define PG8_LDA(dst, b, h) do { if constexpr (DT != 1) { _Pragma("unroll") for (int m = 0; m < 4; ++m) _Pragma("unroll") for (int k = 0; k < 2; ++k) dst[m][k] = *(const PG8_LAS bf16x8*)(lds + PG8_SA(b, h) + aoff + m * 2048 + k * 1024); } \
;         else { _Pragma("unroll") for (int m = 0; m < 4; ++m) dst##8[m] = ld32(lds + PG8_SA(b, h) + aoff + m * 2048); } } while (0)
; #define PG8_LDB(dst, b, h) do { if constexpr (DT != 1) { _Pragma("unroll") for (int n = 0; n < 2; ++n) _Pragma("unroll") for (int k = 0; k < 2; ++k) dst[n][k] = *(const PG8_LAS bf16x8*)(lds + PG8_SB(b, h) + boff + n * 2048 + k * 1024); } \
;         else { _Pragma("unroll") for (int n = 0; n < 2; ++n) dst##8[n] = ld32(lds + PG8_SB(b, h) + boff + n * 2048); } } while (0)
; #define PG8_WAIT_V(n) asm volatile("s_waitcnt vmcnt(" #n ")" ::: "memory")
; #define PG8_WAIT_L(n) asm volatile("s_waitcnt lgkmcnt(" #n ")" ::: "memory")
; #define PG8_BAR __builtin_amdgcn_s_barrier()
; #define PG8_SCHED __builtin_amdgcn_sched_barrier(0)
;     ...
;             if constexpr (SP2) {
;             PG8_LDB(B0, 0, 0); PG8_LDB(B1, 0, 1); PG8_SCHED; PG8_LDA(At, 0, 0); PG8_STAGE(PG8_SA(1, 1), a1 + hstepA, voffA);
;             PG8_WAIT_V(8); PG8_WAIT_L(0); PG8_BAR; PG8_MMA(0, 0, At, B0); PG8_MMA(0, 1, At, B1); PG8_BAR; PG8_SCHED;
;             PG8_LDA(At, 0, 1); PG8_STAGE(PG8_SB(0, 0), b2, voffB); PG8_STAGE(PG8_SB(0, 1), b2 + hstepB, voffB); PG8_STAGE(PG8_SA(0, 0), a2, voffA);
;             PG8_WAIT_V(8); PG8_WAIT_L(0); PG8_BAR; PG8_MMA(1, 0, At, B0); PG8_MMA(1, 1, At, B1); PG8_BAR; PG8_SCHED;
;             PG8_LDB(B0, 1, 0); PG8_LDB(B1, 1, 1); PG8_SCHED; PG8_LDA(At, 1, 0); PG8_STAGE(PG8_SA(0, 1), a2 + hstepA, voffA);
;             PG8_WAIT_V(8); PG8_WAIT_L(0); PG8_BAR; PG8_MMA(0, 0, At, B0); PG8_MMA(0, 1, At, B1); PG8_BAR; PG8_SCHED;
;             PG8_LDA(At, 1, 1); PG8_STAGE(PG8_SB(1, 0), b3, voffB); PG8_STAGE(PG8_SB(1, 1), b3 + hstepB, voffB); PG8_STAGE(PG8_SA(1, 0), a3, voffA);
;             PG8_WAIT_V(8); PG8_WAIT_L(0); PG8_BAR; PG8_MMA(1, 0, At, B0); PG8_MMA(1, 1, At, B1); PG8_BAR; PG8_SCHED;
.LBB0_303:
	ds_read_b128 v[146:149], v159
	ds_read_b128 v[150:153], v159 offset:1024
	ds_read_b128 v[154:157], v159 offset:2048
	ds_read_b128 v[164:167], v159 offset:3072
	ds_read_b128 v[168:171], v160
	ds_read_b128 v[172:175], v160 offset:1024
	ds_read_b128 v[176:179], v160 offset:2048
	ds_read_b128 v[180:183], v160 offset:3072
	s_add_i32 s69, s34, 2
	s_add_u32 s30, s28, 0x100
	s_addc_u32 s31, s29, 0
	s_cmp_eq_u32 s60, s34
	s_cselect_b32 s34, s26, s67
	s_cselect_b32 s37, s3, s31
	s_cselect_b32 s36, s2, s30
	s_cselect_b32 s35, s27, s68
	v_lshl_add_u64 v[216:217], s[28:29], 0, v[140:141]
	s_add_i32 m0, s48, 0xc000
	ds_read_b128 v[184:187], v161
	ds_read_b128 v[188:191], v161 offset:1024
	ds_read_b128 v[192:195], v161 offset:2048
	ds_read_b128 v[196:199], v161 offset:3072
	ds_read_b128 v[200:203], v161 offset:4096
	ds_read_b128 v[204:207], v161 offset:5120
	ds_read_b128 v[208:211], v161 offset:6144
	ds_read_b128 v[212:215], v161 offset:7168
	global_load_lds_dwordx4 v[216:217], off
	v_lshl_add_u64 v[216:217], s[28:29], 0, v[138:139]
	s_add_i32 m0, s48, 0xe000
	s_nop 0
	global_load_lds_dwordx4 v[216:217], off
	s_waitcnt vmcnt(8) lgkmcnt(0)
	s_barrier
	s_setprio 1
	v_mfma_f32_16x16x32_bf16 v[126:129], v[146:149], v[184:187], v[126:129]
	v_mfma_f32_16x16x32_bf16 v[122:125], v[154:157], v[184:187], v[122:125]
	v_mfma_f32_16x16x32_bf16 v[118:121], v[146:149], v[192:195], v[118:121]
	v_mfma_f32_16x16x32_bf16 v[114:117], v[154:157], v[192:195], v[114:117]
	v_mfma_f32_16x16x32_bf16 v[106:109], v[146:149], v[200:203], v[106:109]
	v_mfma_f32_16x16x32_bf16 v[98:101], v[154:157], v[200:203], v[98:101]
	v_mfma_f32_16x16x32_bf16 v[90:93], v[146:149], v[208:211], v[90:93]
	v_mfma_f32_16x16x32_bf16 v[82:85], v[154:157], v[208:211], v[82:85]
	v_mfma_f32_16x16x32_bf16 v[126:129], v[150:153], v[188:191], v[126:129]
	v_mfma_f32_16x16x32_bf16 v[122:125], v[164:167], v[188:191], v[122:125]
	v_mfma_f32_16x16x32_bf16 v[118:121], v[150:153], v[196:199], v[118:121]
	v_mfma_f32_16x16x32_bf16 v[114:117], v[164:167], v[196:199], v[114:117]
	v_mfma_f32_16x16x32_bf16 v[106:109], v[150:153], v[204:207], v[106:109]
	v_mfma_f32_16x16x32_bf16 v[98:101], v[164:167], v[204:207], v[98:101]
	v_mfma_f32_16x16x32_bf16 v[90:93], v[150:153], v[212:215], v[90:93]
	v_mfma_f32_16x16x32_bf16 v[82:85], v[164:167], v[212:215], v[82:85]
	s_setprio 0
	s_setprio 1
	v_mfma_f32_16x16x32_bf16 v[110:113], v[168:171], v[184:187], v[110:113]
	v_mfma_f32_16x16x32_bf16 v[102:105], v[176:179], v[184:187], v[102:105]
	v_mfma_f32_16x16x32_bf16 v[94:97], v[168:171], v[192:195], v[94:97]
	v_mfma_f32_16x16x32_bf16 v[86:89], v[176:179], v[192:195], v[86:89]
	v_mfma_f32_16x16x32_bf16 v[78:81], v[168:171], v[200:203], v[78:81]
	v_mfma_f32_16x16x32_bf16 v[74:77], v[176:179], v[200:203], v[74:77]
	v_mfma_f32_16x16x32_bf16 v[70:73], v[168:171], v[208:211], v[70:73]
	v_mfma_f32_16x16x32_bf16 v[66:69], v[176:179], v[208:211], v[66:69]
	v_mfma_f32_16x16x32_bf16 v[110:113], v[172:175], v[188:191], v[110:113]
	v_mfma_f32_16x16x32_bf16 v[102:105], v[180:183], v[188:191], v[102:105]
	v_mfma_f32_16x16x32_bf16 v[94:97], v[172:175], v[196:199], v[94:97]
	v_mfma_f32_16x16x32_bf16 v[86:89], v[180:183], v[196:199], v[86:89]
	v_mfma_f32_16x16x32_bf16 v[78:81], v[172:175], v[204:207], v[78:81]
	v_mfma_f32_16x16x32_bf16 v[74:77], v[180:183], v[204:207], v[74:77]
	v_mfma_f32_16x16x32_bf16 v[70:73], v[172:175], v[212:215], v[70:73]
	v_mfma_f32_16x16x32_bf16 v[66:69], v[180:183], v[212:215], v[66:69]
	s_setprio 0
	s_barrier
	s_mov_b32 m0, s44
	s_add_u32 s98, s34, 0x80
	s_addc_u32 s99, s35, 0
	s_add_u32 s28, s34, 0x160000
	ds_read_b128 v[184:187], v161 offset:16384
	ds_read_b128 v[188:191], v161 offset:17408
	ds_read_b128 v[192:195], v161 offset:18432
	ds_read_b128 v[196:199], v161 offset:19456
	global_load_lds_dwordx4 v132, s[34:35]
	s_mov_b32 m0, s45
	s_addc_u32 s29, s35, 0
	global_load_lds_dwordx4 v136, s[34:35]
	s_mov_b32 m0, s46
	ds_read_b128 v[212:215], v161 offset:23552
	global_load_lds_dwordx4 v132, s[28:29]
	s_mov_b32 m0, s47
	ds_read_b128 v[208:211], v161 offset:22528
	global_load_lds_dwordx4 v136, s[28:29]
	s_add_u32 s100, s36, 0x80
	s_addc_u32 s101, s37, 0
	s_mov_b32 m0, s48
	ds_read_b128 v[204:207], v161 offset:21504
	global_load_lds_dwordx4 v130, s[36:37]
	s_mov_b32 m0, s49
	ds_read_b128 v[200:203], v161 offset:20480
	global_load_lds_dwordx4 v134, s[36:37]
	s_waitcnt vmcnt(8) lgkmcnt(0)
	s_barrier
	s_setprio 1
	v_mfma_f32_16x16x32_bf16 v[62:65], v[146:149], v[184:187], v[62:65]
	v_mfma_f32_16x16x32_bf16 v[58:61], v[154:157], v[184:187], v[58:61]
	v_mfma_f32_16x16x32_bf16 v[54:57], v[146:149], v[192:195], v[54:57]
	v_mfma_f32_16x16x32_bf16 v[50:53], v[154:157], v[192:195], v[50:53]
	v_mfma_f32_16x16x32_bf16 v[42:45], v[146:149], v[200:203], v[42:45]
	v_mfma_f32_16x16x32_bf16 v[34:37], v[154:157], v[200:203], v[34:37]
	v_mfma_f32_16x16x32_bf16 v[26:29], v[146:149], v[208:211], v[26:29]
	v_mfma_f32_16x16x32_bf16 v[18:21], v[154:157], v[208:211], v[18:21]
	v_mfma_f32_16x16x32_bf16 v[62:65], v[150:153], v[188:191], v[62:65]
	v_mfma_f32_16x16x32_bf16 v[58:61], v[164:167], v[188:191], v[58:61]
	v_mfma_f32_16x16x32_bf16 v[54:57], v[150:153], v[196:199], v[54:57]
	v_mfma_f32_16x16x32_bf16 v[50:53], v[164:167], v[196:199], v[50:53]
	v_mfma_f32_16x16x32_bf16 v[42:45], v[150:153], v[204:207], v[42:45]
	v_mfma_f32_16x16x32_bf16 v[34:37], v[164:167], v[204:207], v[34:37]
	v_mfma_f32_16x16x32_bf16 v[26:29], v[150:153], v[212:215], v[26:29]
	v_mfma_f32_16x16x32_bf16 v[18:21], v[164:167], v[212:215], v[18:21]
	s_setprio 0
	s_setprio 1
	v_mfma_f32_16x16x32_bf16 v[46:49], v[168:171], v[184:187], v[46:49]
	v_mfma_f32_16x16x32_bf16 v[38:41], v[176:179], v[184:187], v[38:41]
	v_mfma_f32_16x16x32_bf16 v[30:33], v[168:171], v[192:195], v[30:33]
	v_mfma_f32_16x16x32_bf16 v[22:25], v[176:179], v[192:195], v[22:25]
	v_mfma_f32_16x16x32_bf16 v[14:17], v[168:171], v[200:203], v[14:17]
	v_mfma_f32_16x16x32_bf16 v[10:13], v[176:179], v[200:203], v[10:13]
	v_mfma_f32_16x16x32_bf16 v[6:9], v[168:171], v[208:211], v[6:9]
	v_mfma_f32_16x16x32_bf16 v[2:5], v[176:179], v[208:211], v[2:5]
	v_mfma_f32_16x16x32_bf16 v[46:49], v[172:175], v[188:191], v[46:49]
	v_mfma_f32_16x16x32_bf16 v[38:41], v[180:183], v[188:191], v[38:41]
	v_mfma_f32_16x16x32_bf16 v[30:33], v[172:175], v[196:199], v[30:33]
	v_mfma_f32_16x16x32_bf16 v[22:25], v[180:183], v[196:199], v[22:25]
	v_mfma_f32_16x16x32_bf16 v[14:17], v[172:175], v[204:207], v[14:17]
	v_mfma_f32_16x16x32_bf16 v[10:13], v[180:183], v[204:207], v[10:13]
	v_mfma_f32_16x16x32_bf16 v[6:9], v[172:175], v[212:215], v[6:9]
	v_mfma_f32_16x16x32_bf16 v[2:5], v[180:183], v[212:215], v[2:5]
	s_setprio 0
	s_barrier
; #define PG8_STAGE(bufoff, gbase, voff) do { _Pragma("unroll") for (int _i = 0; _i < 2; ++_i) \
;         __builtin_amdgcn_global_load_lds((const unsigned*)((const char*)(gbase) + (voff)[_i]), (PG8_LAS unsigned*)(lds + (bufoff) + ldsw + _i * 8192), 16, 0, 0); } while (0)
; #define PG8_LDA(dst, b, h) do { if constexpr (DT != 1) { _Pragma("unroll") for (int m = 0; m < 4; ++m) _Pragma("unroll") for (int k = 0; k < 2; ++k) dst[m][k] = *(const PG8_LAS bf16x8*)(lds + PG8_SA(b, h) + aoff + m * 2048 + k * 1024); } \
;         else { _Pragma("unroll") for (int m = 0; m < 4; ++m) dst##8[m] = ld32(lds + PG8_SA(b, h) + aoff + m * 2048); } } while (0)
; #define PG8_LDB(dst, b, h) do { if constexpr (DT != 1) { _Pragma("unroll") for (int n = 0; n < 2; ++n) _Pragma("unroll") for (int k = 0; k < 2; ++k) dst[n][k] = *(const PG8_LAS bf16x8*)(lds + PG8_SB(b, h) + boff + n * 2048 + k * 1024); } \
;         else { _Pragma("unroll") for (int n = 0; n < 2; ++n) dst##8[n] = ld32(lds + PG8_SB(b, h) + boff + n * 2048); } } while (0)
; #define PG8_WAIT_V(n) asm volatile("s_waitcnt vmcnt(" #n ")" ::: "memory")
; #define PG8_WAIT_L(n) asm volatile("s_waitcnt lgkmcnt(" #n ")" ::: "memory")
; #define PG8_BAR __builtin_amdgcn_s_barrier()
; #define PG8_SCHED __builtin_amdgcn_sched_barrier(0)
;     ...
;             if constexpr (SP2) {
;             PG8_LDB(B0, 0, 0); PG8_LDB(B1, 0, 1); PG8_SCHED; PG8_LDA(At, 0, 0); PG8_STAGE(PG8_SA(1, 1), a1 + hstepA, voffA);
;             PG8_WAIT_V(8); PG8_WAIT_L(0); PG8_BAR; PG8_MMA(0, 0, At, B0); PG8_MMA(0, 1, At, B1); PG8_BAR; PG8_SCHED;
;             PG8_LDA(At, 0, 1); PG8_STAGE(PG8_SB(0, 0), b2, voffB); PG8_STAGE(PG8_SB(0, 1), b2 + hstepB, voffB); PG8_STAGE(PG8_SA(0, 0), a2, voffA);
;             PG8_WAIT_V(8); PG8_WAIT_L(0); PG8_BAR; PG8_MMA(1, 0, At, B0); PG8_MMA(1, 1, At, B1); PG8_BAR; PG8_SCHED;
;             PG8_LDB(B0, 1, 0); PG8_LDB(B1, 1, 1); PG8_SCHED; PG8_LDA(At, 1, 0); PG8_STAGE(PG8_SA(0, 1), a2 + hstepA, voffA);
;             PG8_WAIT_V(8); PG8_WAIT_L(0); PG8_BAR; PG8_MMA(0, 0, At, B0); PG8_MMA(0, 1, At, B1); PG8_BAR; PG8_SCHED;
;             PG8_LDA(At, 1, 1); PG8_STAGE(PG8_SB(1, 0), b3, voffB); PG8_STAGE(PG8_SB(1, 1), b3 + hstepB, voffB); PG8_STAGE(PG8_SA(1, 0), a3, voffA);
;             PG8_WAIT_V(8); PG8_WAIT_L(0); PG8_BAR; PG8_MMA(1, 0, At, B0); PG8_MMA(1, 1, At, B1); PG8_BAR; PG8_SCHED;
	ds_read_b128 v[146:149], v162
	ds_read_b128 v[150:153], v162 offset:1024
	ds_read_b128 v[154:157], v162 offset:2048
	ds_read_b128 v[164:167], v162 offset:3072
	ds_read_b128 v[168:171], v163
	ds_read_b128 v[172:175], v163 offset:1024
	ds_read_b128 v[176:179], v163 offset:2048
	ds_read_b128 v[180:183], v163 offset:3072
	s_add_u32 s28, s36, 0x160000
	s_addc_u32 s29, s37, 0
	s_mov_b32 m0, s50
	ds_read_b128 v[184:187], v161 offset:32768
	ds_read_b128 v[188:191], v161 offset:33792
	ds_read_b128 v[192:195], v161 offset:34816
	ds_read_b128 v[196:199], v161 offset:35840
	ds_read_b128 v[200:203], v161 offset:36864
	ds_read_b128 v[204:207], v161 offset:37888
	ds_read_b128 v[208:211], v161 offset:38912
	global_load_lds_dwordx4 v130, s[28:29]
	s_mov_b32 m0, s51
	ds_read_b128 v[212:215], v161 offset:39936
	global_load_lds_dwordx4 v134, s[28:29]
	s_waitcnt vmcnt(8) lgkmcnt(0)
	s_barrier
	s_setprio 1
	v_mfma_f32_16x16x32_bf16 v[126:129], v[146:149], v[184:187], v[126:129]
	v_mfma_f32_16x16x32_bf16 v[122:125], v[154:157], v[184:187], v[122:125]
	v_mfma_f32_16x16x32_bf16 v[118:121], v[146:149], v[192:195], v[118:121]
	v_mfma_f32_16x16x32_bf16 v[114:117], v[154:157], v[192:195], v[114:117]
	v_mfma_f32_16x16x32_bf16 v[106:109], v[146:149], v[200:203], v[106:109]
	v_mfma_f32_16x16x32_bf16 v[98:101], v[154:157], v[200:203], v[98:101]
	v_mfma_f32_16x16x32_bf16 v[90:93], v[146:149], v[208:211], v[90:93]
	v_mfma_f32_16x16x32_bf16 v[82:85], v[154:157], v[208:211], v[82:85]
	v_mfma_f32_16x16x32_bf16 v[126:129], v[150:153], v[188:191], v[126:129]
	v_mfma_f32_16x16x32_bf16 v[122:125], v[164:167], v[188:191], v[122:125]
	v_mfma_f32_16x16x32_bf16 v[118:121], v[150:153], v[196:199], v[118:121]
	v_mfma_f32_16x16x32_bf16 v[114:117], v[164:167], v[196:199], v[114:117]
	v_mfma_f32_16x16x32_bf16 v[106:109], v[150:153], v[204:207], v[106:109]
	v_mfma_f32_16x16x32_bf16 v[98:101], v[164:167], v[204:207], v[98:101]
	v_mfma_f32_16x16x32_bf16 v[90:93], v[150:153], v[212:215], v[90:93]
	v_mfma_f32_16x16x32_bf16 v[82:85], v[164:167], v[212:215], v[82:85]
	s_setprio 0
	s_setprio 1
	v_mfma_f32_16x16x32_bf16 v[110:113], v[168:171], v[184:187], v[110:113]
	v_mfma_f32_16x16x32_bf16 v[102:105], v[176:179], v[184:187], v[102:105]
	v_mfma_f32_16x16x32_bf16 v[94:97], v[168:171], v[192:195], v[94:97]
	v_mfma_f32_16x16x32_bf16 v[86:89], v[176:179], v[192:195], v[86:89]
	v_mfma_f32_16x16x32_bf16 v[78:81], v[168:171], v[200:203], v[78:81]
	v_mfma_f32_16x16x32_bf16 v[74:77], v[176:179], v[200:203], v[74:77]
	v_mfma_f32_16x16x32_bf16 v[70:73], v[168:171], v[208:211], v[70:73]
	v_mfma_f32_16x16x32_bf16 v[66:69], v[176:179], v[208:211], v[66:69]
	v_mfma_f32_16x16x32_bf16 v[110:113], v[172:175], v[188:191], v[110:113]
	v_mfma_f32_16x16x32_bf16 v[102:105], v[180:183], v[188:191], v[102:105]
	v_mfma_f32_16x16x32_bf16 v[94:97], v[172:175], v[196:199], v[94:97]
	v_mfma_f32_16x16x32_bf16 v[86:89], v[180:183], v[196:199], v[86:89]
	v_mfma_f32_16x16x32_bf16 v[78:81], v[172:175], v[204:207], v[78:81]
	v_mfma_f32_16x16x32_bf16 v[74:77], v[180:183], v[204:207], v[74:77]
	v_mfma_f32_16x16x32_bf16 v[70:73], v[172:175], v[212:215], v[70:73]
	v_mfma_f32_16x16x32_bf16 v[66:69], v[180:183], v[212:215], v[66:69]
	s_setprio 0
	s_barrier
	s_mov_b32 m0, s54
	s_add_u32 s28, s34, 0x160080
	ds_read_b128 v[184:187], v161 offset:49152
	ds_read_b128 v[188:191], v161 offset:50176
	ds_read_b128 v[192:195], v161 offset:51200
	ds_read_b128 v[196:199], v161 offset:52224
	global_load_lds_dwordx4 v132, s[98:99]
	s_mov_b32 m0, s55
	s_addc_u32 s29, s35, 0
	global_load_lds_dwordx4 v136, s[98:99]
	s_mov_b32 m0, s58
	ds_read_b128 v[212:215], v161 offset:56320
	global_load_lds_dwordx4 v132, s[28:29]
	s_mov_b32 m0, s59
	ds_read_b128 v[208:211], v161 offset:55296
	global_load_lds_dwordx4 v136, s[28:29]
	s_mov_b32 m0, s56
	ds_read_b128 v[204:207], v161 offset:54272
	global_load_lds_dwordx4 v130, s[100:101]
	s_mov_b32 m0, s57
	ds_read_b128 v[200:203], v161 offset:53248
	global_load_lds_dwordx4 v134, s[100:101]
	s_waitcnt vmcnt(8) lgkmcnt(0)
	s_barrier
	s_setprio 1
	v_mfma_f32_16x16x32_bf16 v[62:65], v[146:149], v[184:187], v[62:65]
	v_mfma_f32_16x16x32_bf16 v[58:61], v[154:157], v[184:187], v[58:61]
	v_mfma_f32_16x16x32_bf16 v[54:57], v[146:149], v[192:195], v[54:57]
	v_mfma_f32_16x16x32_bf16 v[50:53], v[154:157], v[192:195], v[50:53]
	v_mfma_f32_16x16x32_bf16 v[42:45], v[146:149], v[200:203], v[42:45]
	v_mfma_f32_16x16x32_bf16 v[34:37], v[154:157], v[200:203], v[34:37]
	v_mfma_f32_16x16x32_bf16 v[26:29], v[146:149], v[208:211], v[26:29]
	v_mfma_f32_16x16x32_bf16 v[18:21], v[154:157], v[208:211], v[18:21]
	v_mfma_f32_16x16x32_bf16 v[62:65], v[150:153], v[188:191], v[62:65]
	v_mfma_f32_16x16x32_bf16 v[58:61], v[164:167], v[188:191], v[58:61]
	v_mfma_f32_16x16x32_bf16 v[54:57], v[150:153], v[196:199], v[54:57]
	v_mfma_f32_16x16x32_bf16 v[50:53], v[164:167], v[196:199], v[50:53]
	v_mfma_f32_16x16x32_bf16 v[42:45], v[150:153], v[204:207], v[42:45]
	v_mfma_f32_16x16x32_bf16 v[34:37], v[164:167], v[204:207], v[34:37]
	v_mfma_f32_16x16x32_bf16 v[26:29], v[150:153], v[212:215], v[26:29]
	v_mfma_f32_16x16x32_bf16 v[18:21], v[164:167], v[212:215], v[18:21]
	s_setprio 0
	s_setprio 1
	v_mfma_f32_16x16x32_bf16 v[46:49], v[168:171], v[184:187], v[46:49]
	v_mfma_f32_16x16x32_bf16 v[38:41], v[176:179], v[184:187], v[38:41]
	v_mfma_f32_16x16x32_bf16 v[30:33], v[168:171], v[192:195], v[30:33]
	v_mfma_f32_16x16x32_bf16 v[22:25], v[176:179], v[192:195], v[22:25]
	v_mfma_f32_16x16x32_bf16 v[14:17], v[168:171], v[200:203], v[14:17]
	v_mfma_f32_16x16x32_bf16 v[10:13], v[176:179], v[200:203], v[10:13]
	v_mfma_f32_16x16x32_bf16 v[6:9], v[168:171], v[208:211], v[6:9]
	v_mfma_f32_16x16x32_bf16 v[2:5], v[176:179], v[208:211], v[2:5]
	v_mfma_f32_16x16x32_bf16 v[46:49], v[172:175], v[188:191], v[46:49]
	v_mfma_f32_16x16x32_bf16 v[38:41], v[180:183], v[188:191], v[38:41]
	v_mfma_f32_16x16x32_bf16 v[30:33], v[172:175], v[196:199], v[30:33]
	v_mfma_f32_16x16x32_bf16 v[22:25], v[180:183], v[196:199], v[22:25]
	v_mfma_f32_16x16x32_bf16 v[14:17], v[172:175], v[204:207], v[14:17]
	v_mfma_f32_16x16x32_bf16 v[10:13], v[180:183], v[204:207], v[10:13]
	v_mfma_f32_16x16x32_bf16 v[6:9], v[172:175], v[212:215], v[6:9]
	v_mfma_f32_16x16x32_bf16 v[2:5], v[180:183], v[212:215], v[2:5]
	s_setprio 0
	s_barrier
	s_add_u32 s67, s67, 0x100
	s_addc_u32 s68, s68, 0
	s_cmp_ge_i32 s69, s53
	s_mov_b64 s[28:29], s[30:31]
	s_mov_b32 s34, s69
	s_cbranch_scc0 .LBB0_303

; #define PG8_STAGE(bufoff, gbase, voff) do { _Pragma("unroll") for (int _i = 0; _i < 2; ++_i) \
;         __builtin_amdgcn_global_load_lds((const unsigned*)((const char*)(gbase) + (voff)[_i]), (PG8_LAS unsigned*)(lds + (bufoff) + ldsw + _i * 8192), 16, 0, 0); } while (0)
; #define PG8_LDA(dst, b, h) do { if constexpr (DT != 1) { _Pragma("unroll") for (int m = 0; m < 4; ++m) _Pragma("unroll") for (int k = 0; k < 2; ++k) dst[m][k] = *(const PG8_LAS bf16x8*)(lds + PG8_SA(b, h) + aoff + m * 2048 + k * 1024); } \
;         else { _Pragma("unroll") for (int m = 0; m < 4; ++m) dst##8[m] = ld32(lds + PG8_SA(b, h) + aoff + m * 2048); } } while (0)
; #define PG8_WAIT_V(n) asm volatile("s_waitcnt vmcnt(" #n ")" ::: "memory")
; #define PG8_WAIT_L(n) asm volatile("s_waitcnt lgkmcnt(" #n ")" ::: "memory")
; #define PG8_BAR __builtin_amdgcn_s_barrier()
; #define PG8_SCHED __builtin_amdgcn_sched_barrier(0)
;     ...
;         for (int t = 0; t < nt; t += 2) {
;             const bool last = (t == nt - 2);
;             const char* a1 = cA + (size_t)(t + 1) * kstep;
;             const char* a2 = last ? nA : cA + (size_t)(t + 2) * kstep; const char* b2 = last ? nB : cB + (size_t)(t + 2) * kstep;
;             const char* a3 = a2 + kstep; const char* b3 = b2 + kstep;
;             if (last && has_next) S.a_ready(nxt);
;             if constexpr (SP2) {
;             PG8_LDB(B0, 0, 0); PG8_LDB(B1, 0, 1); PG8_SCHED; PG8_LDA(At, 0, 0); PG8_STAGE(PG8_SA(1, 1), a1 + hstepA, voffA);
;             PG8_WAIT_V(8); PG8_WAIT_L(0); PG8_BAR; PG8_MMA(0, 0, At, B0); PG8_MMA(0, 1, At, B1); PG8_BAR; PG8_SCHED;
;             PG8_LDA(At, 0, 1); PG8_STAGE(PG8_SB(0, 0), b2, voffB); PG8_STAGE(PG8_SB(0, 1), b2 + hstepB, voffB); PG8_STAGE(PG8_SA(0, 0), a2, voffA);
;             PG8_WAIT_V(8); PG8_WAIT_L(0); PG8_BAR; PG8_MMA(1, 0, At, B0); PG8_MMA(1, 1, At, B1); PG8_BAR; PG8_SCHED;
;             PG8_LDB(B0, 1, 0); PG8_LDB(B1, 1, 1); PG8_SCHED; PG8_LDA(At, 1, 0); PG8_STAGE(PG8_SA(0, 1), a2 + hstepA, voffA);
;             PG8_WAIT_V(8); PG8_WAIT_L(0); PG8_BAR; PG8_MMA(0, 0, At, B0); PG8_MMA(0, 1, At, B1); PG8_BAR; PG8_SCHED;
;             PG8_LDA(At, 1, 1); PG8_STAGE(PG8_SB(1, 0), b3, voffB); PG8_STAGE(PG8_SB(1, 1), b3 + hstepB, voffB); PG8_STAGE(PG8_SA(1, 0), a3, voffA);
;             PG8_WAIT_V(8); PG8_WAIT_L(0); PG8_BAR; PG8_MMA(1, 0, At, B0); PG8_MMA(1, 1, At, B1); PG8_BAR; PG8_SCHED;
.Lzs_2:
	s_cbranch_vccnz .LBB0_419
	s_and_b64 s[30:31], s[0:1], exec
	s_cselect_b32 s19, s23, s29
	s_cselect_b32 s21, s22, s28
	s_cselect_b32 s61, s25, s27
	s_cselect_b32 s62, s24, s26
	s_add_u32 s63, s26, 0x100
	s_addc_u32 s64, s27, 0
	s_add_u32 s26, s28, 0x80080
	s_addc_u32 s27, s29, 0
	s_mov_b32 s28, 0
	ds_read_b128 v[156:159], v150
	ds_read_b128 v[160:163], v150 offset:1024
	ds_read_b128 v[164:167], v150 offset:2048
	ds_read_b128 v[168:171], v150 offset:3072
	ds_read_b128 v[172:175], v151
	ds_read_b128 v[176:179], v151 offset:1024
	ds_read_b128 v[180:183], v151 offset:2048
	ds_read_b128 v[184:187], v151 offset:3072
	s_add_i32 s65, s28, 2
	s_add_u32 s29, s26, 0xfff80080
	s_addc_u32 s30, s27, -1
	s_cmp_eq_u32 s59, s28
	s_cselect_b32 s28, s62, s63
	s_cselect_b32 s31, s19, s30
	s_cselect_b32 s30, s21, s29
	s_cselect_b32 s29, s61, s64
	s_add_i32 m0, s45, 0xc000
	ds_read_b128 v[188:191], v152
	ds_read_b128 v[192:195], v152 offset:1024
	ds_read_b128 v[196:199], v152 offset:2048
	ds_read_b128 v[200:203], v152 offset:3072
	ds_read_b128 v[204:207], v152 offset:4096
	ds_read_b128 v[208:211], v152 offset:5120
	ds_read_b128 v[212:215], v152 offset:6144
	ds_read_b128 v[216:219], v152 offset:7168
	global_load_lds_dwordx4 v144, s[26:27]
	s_add_i32 m0, s45, 0xe000
	s_nop 0
	global_load_lds_dwordx4 v142, s[26:27]
	s_waitcnt vmcnt(8) lgkmcnt(0)
	s_barrier
	s_setprio 1
	v_mfma_f32_16x16x32_bf16 v[122:125], v[156:159], v[188:191], 0
	v_mfma_f32_16x16x32_bf16 v[126:129], v[164:167], v[188:191], 0
	v_mfma_f32_16x16x32_bf16 v[110:113], v[156:159], v[196:199], 0
	v_mfma_f32_16x16x32_bf16 v[106:109], v[164:167], v[196:199], 0
	v_mfma_f32_16x16x32_bf16 v[94:97], v[156:159], v[204:207], 0
	v_mfma_f32_16x16x32_bf16 v[90:93], v[164:167], v[204:207], 0
	v_mfma_f32_16x16x32_bf16 v[78:81], v[156:159], v[212:215], 0
	v_mfma_f32_16x16x32_bf16 v[74:77], v[164:167], v[212:215], 0
	v_mfma_f32_16x16x32_bf16 v[122:125], v[160:163], v[192:195], v[122:125]
	v_mfma_f32_16x16x32_bf16 v[126:129], v[168:171], v[192:195], v[126:129]
	v_mfma_f32_16x16x32_bf16 v[110:113], v[160:163], v[200:203], v[110:113]
	v_mfma_f32_16x16x32_bf16 v[106:109], v[168:171], v[200:203], v[106:109]
	v_mfma_f32_16x16x32_bf16 v[94:97], v[160:163], v[208:211], v[94:97]
	v_mfma_f32_16x16x32_bf16 v[90:93], v[168:171], v[208:211], v[90:93]
	v_mfma_f32_16x16x32_bf16 v[78:81], v[160:163], v[216:219], v[78:81]
	v_mfma_f32_16x16x32_bf16 v[74:77], v[168:171], v[216:219], v[74:77]
	s_setprio 0
	s_setprio 1
	v_mfma_f32_16x16x32_bf16 v[118:121], v[172:175], v[188:191], 0
	v_mfma_f32_16x16x32_bf16 v[114:117], v[180:183], v[188:191], 0
	v_mfma_f32_16x16x32_bf16 v[102:105], v[172:175], v[196:199], 0
	v_mfma_f32_16x16x32_bf16 v[98:101], v[180:183], v[196:199], 0
	v_mfma_f32_16x16x32_bf16 v[86:89], v[172:175], v[204:207], 0
	v_mfma_f32_16x16x32_bf16 v[82:85], v[180:183], v[204:207], 0
	v_mfma_f32_16x16x32_bf16 v[70:73], v[172:175], v[212:215], 0
	v_mfma_f32_16x16x32_bf16 v[66:69], v[180:183], v[212:215], 0
	v_mfma_f32_16x16x32_bf16 v[118:121], v[176:179], v[192:195], v[118:121]
	v_mfma_f32_16x16x32_bf16 v[114:117], v[184:187], v[192:195], v[114:117]
	v_mfma_f32_16x16x32_bf16 v[102:105], v[176:179], v[200:203], v[102:105]
	v_mfma_f32_16x16x32_bf16 v[98:101], v[184:187], v[200:203], v[98:101]
	v_mfma_f32_16x16x32_bf16 v[86:89], v[176:179], v[208:211], v[86:89]
	v_mfma_f32_16x16x32_bf16 v[82:85], v[184:187], v[208:211], v[82:85]
	v_mfma_f32_16x16x32_bf16 v[70:73], v[176:179], v[216:219], v[70:73]
	v_mfma_f32_16x16x32_bf16 v[66:69], v[184:187], v[216:219], v[66:69]
	s_setprio 0
	s_barrier
	s_mov_b32 m0, s41
	s_add_u32 s98, s28, 0x80
	s_addc_u32 s99, s29, 0
	s_add_u32 s66, s28, 0x80000
	ds_read_b128 v[188:191], v152 offset:16384
	ds_read_b128 v[192:195], v152 offset:17408
	ds_read_b128 v[196:199], v152 offset:18432
	ds_read_b128 v[200:203], v152 offset:19456
	global_load_lds_dwordx4 v132, s[28:29]
	s_mov_b32 m0, s42
	s_addc_u32 s67, s29, 0
	global_load_lds_dwordx4 v136, s[28:29]
	s_mov_b32 m0, s43
	ds_read_b128 v[216:219], v152 offset:23552
	global_load_lds_dwordx4 v132, s[66:67]
	s_mov_b32 m0, s44
	ds_read_b128 v[212:215], v152 offset:22528
	global_load_lds_dwordx4 v136, s[66:67]
	s_add_u32 s100, s30, 0x80
	s_addc_u32 s101, s31, 0
	s_mov_b32 m0, s45
	ds_read_b128 v[208:211], v152 offset:21504
	global_load_lds_dwordx4 v130, s[30:31]
	s_mov_b32 m0, s46
	ds_read_b128 v[204:207], v152 offset:20480
	global_load_lds_dwordx4 v134, s[30:31]
	s_waitcnt vmcnt(8) lgkmcnt(0)
	s_barrier
	s_setprio 1
	v_mfma_f32_16x16x32_bf16 v[62:65], v[156:159], v[188:191], 0
	v_mfma_f32_16x16x32_bf16 v[58:61], v[164:167], v[188:191], 0
	v_mfma_f32_16x16x32_bf16 v[46:49], v[156:159], v[196:199], 0
	v_mfma_f32_16x16x32_bf16 v[42:45], v[164:167], v[196:199], 0
	v_mfma_f32_16x16x32_bf16 v[30:33], v[156:159], v[204:207], 0
	v_mfma_f32_16x16x32_bf16 v[26:29], v[164:167], v[204:207], 0
	v_mfma_f32_16x16x32_bf16 v[14:17], v[156:159], v[212:215], 0
	v_mfma_f32_16x16x32_bf16 v[10:13], v[164:167], v[212:215], 0
	v_mfma_f32_16x16x32_bf16 v[62:65], v[160:163], v[192:195], v[62:65]
	v_mfma_f32_16x16x32_bf16 v[58:61], v[168:171], v[192:195], v[58:61]
	v_mfma_f32_16x16x32_bf16 v[46:49], v[160:163], v[200:203], v[46:49]
	v_mfma_f32_16x16x32_bf16 v[42:45], v[168:171], v[200:203], v[42:45]
	v_mfma_f32_16x16x32_bf16 v[30:33], v[160:163], v[208:211], v[30:33]
	v_mfma_f32_16x16x32_bf16 v[26:29], v[168:171], v[208:211], v[26:29]
	v_mfma_f32_16x16x32_bf16 v[14:17], v[160:163], v[216:219], v[14:17]
	v_mfma_f32_16x16x32_bf16 v[10:13], v[168:171], v[216:219], v[10:13]
	s_setprio 0
	s_setprio 1
	v_mfma_f32_16x16x32_bf16 v[54:57], v[172:175], v[188:191], 0
	v_mfma_f32_16x16x32_bf16 v[50:53], v[180:183], v[188:191], 0
	v_mfma_f32_16x16x32_bf16 v[38:41], v[172:175], v[196:199], 0
	v_mfma_f32_16x16x32_bf16 v[34:37], v[180:183], v[196:199], 0
	v_mfma_f32_16x16x32_bf16 v[22:25], v[172:175], v[204:207], 0
	v_mfma_f32_16x16x32_bf16 v[18:21], v[180:183], v[204:207], 0
	v_mfma_f32_16x16x32_bf16 v[6:9], v[172:175], v[212:215], 0
	v_mfma_f32_16x16x32_bf16 v[2:5], v[180:183], v[212:215], 0
	v_mfma_f32_16x16x32_bf16 v[54:57], v[176:179], v[192:195], v[54:57]
	v_mfma_f32_16x16x32_bf16 v[50:53], v[184:187], v[192:195], v[50:53]
	v_mfma_f32_16x16x32_bf16 v[38:41], v[176:179], v[200:203], v[38:41]
	v_mfma_f32_16x16x32_bf16 v[34:37], v[184:187], v[200:203], v[34:37]
	v_mfma_f32_16x16x32_bf16 v[22:25], v[176:179], v[208:211], v[22:25]
	v_mfma_f32_16x16x32_bf16 v[18:21], v[184:187], v[208:211], v[18:21]
	v_mfma_f32_16x16x32_bf16 v[6:9], v[176:179], v[216:219], v[6:9]
	v_mfma_f32_16x16x32_bf16 v[2:5], v[184:187], v[216:219], v[2:5]
	s_setprio 0
	s_barrier
; #define PG8_STAGE(bufoff, gbase, voff) do { _Pragma("unroll") for (int _i = 0; _i < 2; ++_i) \
;         __builtin_amdgcn_global_load_lds((const unsigned*)((const char*)(gbase) + (voff)[_i]), (PG8_LAS unsigned*)(lds + (bufoff) + ldsw + _i * 8192), 16, 0, 0); } while (0)
; #define PG8_LDA(dst, b, h) do { if constexpr (DT != 1) { _Pragma("unroll") for (int m = 0; m < 4; ++m) _Pragma("unroll") for (int k = 0; k < 2; ++k) dst[m][k] = *(const PG8_LAS bf16x8*)(lds + PG8_SA(b, h) + aoff + m * 2048 + k * 1024); } \
;         else { _Pragma("unroll") for (int m = 0; m < 4; ++m) dst##8[m] = ld32(lds + PG8_SA(b, h) + aoff + m * 2048); } } while (0)
; #define PG8_LDB(dst, b, h) do { if constexpr (DT != 1) { _Pragma("unroll") for (int n = 0; n < 2; ++n) _Pragma("unroll") for (int k = 0; k < 2; ++k) dst[n][k] = *(const PG8_LAS bf16x8*)(lds + PG8_SB(b, h) + boff + n * 2048 + k * 1024); } \
;         else { _Pragma("unroll") for (int n = 0; n < 2; ++n) dst##8[n] = ld32(lds + PG8_SB(b, h) + boff + n * 2048); } } while (0)
; #define PG8_WAIT_V(n) asm volatile("s_waitcnt vmcnt(" #n ")" ::: "memory")
; #define PG8_WAIT_L(n) asm volatile("s_waitcnt lgkmcnt(" #n ")" ::: "memory")
; #define PG8_BAR __builtin_amdgcn_s_barrier()
; #define PG8_SCHED __builtin_amdgcn_sched_barrier(0)
;     ...
;             if constexpr (SP2) {
;             PG8_LDB(B0, 0, 0); PG8_LDB(B1, 0, 1); PG8_SCHED; PG8_LDA(At, 0, 0); PG8_STAGE(PG8_SA(1, 1), a1 + hstepA, voffA);
;             PG8_WAIT_V(8); PG8_WAIT_L(0); PG8_BAR; PG8_MMA(0, 0, At, B0); PG8_MMA(0, 1, At, B1); PG8_BAR; PG8_SCHED;
;             PG8_LDA(At, 0, 1); PG8_STAGE(PG8_SB(0, 0), b2, voffB); PG8_STAGE(PG8_SB(0, 1), b2 + hstepB, voffB); PG8_STAGE(PG8_SA(0, 0), a2, voffA);
;             PG8_WAIT_V(8); PG8_WAIT_L(0); PG8_BAR; PG8_MMA(1, 0, At, B0); PG8_MMA(1, 1, At, B1); PG8_BAR; PG8_SCHED;
;             PG8_LDB(B0, 1, 0); PG8_LDB(B1, 1, 1); PG8_SCHED; PG8_LDA(At, 1, 0); PG8_STAGE(PG8_SA(0, 1), a2 + hstepA, voffA);
;             PG8_WAIT_V(8); PG8_WAIT_L(0); PG8_BAR; PG8_MMA(0, 0, At, B0); PG8_MMA(0, 1, At, B1); PG8_BAR; PG8_SCHED;
;             PG8_LDA(At, 1, 1); PG8_STAGE(PG8_SB(1, 0), b3, voffB); PG8_STAGE(PG8_SB(1, 1), b3 + hstepB, voffB); PG8_STAGE(PG8_SA(1, 0), a3, voffA);
;             PG8_WAIT_V(8); PG8_WAIT_L(0); PG8_BAR; PG8_MMA(1, 0, At, B0); PG8_MMA(1, 1, At, B1); PG8_BAR; PG8_SCHED;
	ds_read_b128 v[156:159], v153
	ds_read_b128 v[160:163], v153 offset:1024
	ds_read_b128 v[164:167], v153 offset:2048
	ds_read_b128 v[168:171], v153 offset:3072
	ds_read_b128 v[172:175], v154
	ds_read_b128 v[176:179], v154 offset:1024
	ds_read_b128 v[180:183], v154 offset:2048
	ds_read_b128 v[184:187], v154 offset:3072
	s_add_u32 s30, s30, 0x80000
	s_addc_u32 s31, s31, 0
	s_mov_b32 m0, s47
	ds_read_b128 v[188:191], v152 offset:32768
	ds_read_b128 v[192:195], v152 offset:33792
	ds_read_b128 v[196:199], v152 offset:34816
	ds_read_b128 v[200:203], v152 offset:35840
	ds_read_b128 v[204:207], v152 offset:36864
	ds_read_b128 v[208:211], v152 offset:37888
	ds_read_b128 v[212:215], v152 offset:38912
	global_load_lds_dwordx4 v130, s[30:31]
	s_mov_b32 m0, s48
	ds_read_b128 v[216:219], v152 offset:39936
	global_load_lds_dwordx4 v134, s[30:31]
	s_waitcnt vmcnt(8) lgkmcnt(0)
	s_barrier
	s_setprio 1
	v_mfma_f32_16x16x32_bf16 v[122:125], v[156:159], v[188:191], v[122:125]
	v_mfma_f32_16x16x32_bf16 v[126:129], v[164:167], v[188:191], v[126:129]
	v_mfma_f32_16x16x32_bf16 v[110:113], v[156:159], v[196:199], v[110:113]
	v_mfma_f32_16x16x32_bf16 v[106:109], v[164:167], v[196:199], v[106:109]
	v_mfma_f32_16x16x32_bf16 v[94:97], v[156:159], v[204:207], v[94:97]
	v_mfma_f32_16x16x32_bf16 v[90:93], v[164:167], v[204:207], v[90:93]
	v_mfma_f32_16x16x32_bf16 v[78:81], v[156:159], v[212:215], v[78:81]
	v_mfma_f32_16x16x32_bf16 v[74:77], v[164:167], v[212:215], v[74:77]
	v_mfma_f32_16x16x32_bf16 v[122:125], v[160:163], v[192:195], v[122:125]
	v_mfma_f32_16x16x32_bf16 v[126:129], v[168:171], v[192:195], v[126:129]
	v_mfma_f32_16x16x32_bf16 v[110:113], v[160:163], v[200:203], v[110:113]
	v_mfma_f32_16x16x32_bf16 v[106:109], v[168:171], v[200:203], v[106:109]
	v_mfma_f32_16x16x32_bf16 v[94:97], v[160:163], v[208:211], v[94:97]
	v_mfma_f32_16x16x32_bf16 v[90:93], v[168:171], v[208:211], v[90:93]
	v_mfma_f32_16x16x32_bf16 v[78:81], v[160:163], v[216:219], v[78:81]
	v_mfma_f32_16x16x32_bf16 v[74:77], v[168:171], v[216:219], v[74:77]
	s_setprio 0
	s_setprio 1
	v_mfma_f32_16x16x32_bf16 v[118:121], v[172:175], v[188:191], v[118:121]
	v_mfma_f32_16x16x32_bf16 v[114:117], v[180:183], v[188:191], v[114:117]
	v_mfma_f32_16x16x32_bf16 v[102:105], v[172:175], v[196:199], v[102:105]
	v_mfma_f32_16x16x32_bf16 v[98:101], v[180:183], v[196:199], v[98:101]
	v_mfma_f32_16x16x32_bf16 v[86:89], v[172:175], v[204:207], v[86:89]
	v_mfma_f32_16x16x32_bf16 v[82:85], v[180:183], v[204:207], v[82:85]
	v_mfma_f32_16x16x32_bf16 v[70:73], v[172:175], v[212:215], v[70:73]
	v_mfma_f32_16x16x32_bf16 v[66:69], v[180:183], v[212:215], v[66:69]
	v_mfma_f32_16x16x32_bf16 v[118:121], v[176:179], v[192:195], v[118:121]
	v_mfma_f32_16x16x32_bf16 v[114:117], v[184:187], v[192:195], v[114:117]
	v_mfma_f32_16x16x32_bf16 v[102:105], v[176:179], v[200:203], v[102:105]
	v_mfma_f32_16x16x32_bf16 v[98:101], v[184:187], v[200:203], v[98:101]
	v_mfma_f32_16x16x32_bf16 v[86:89], v[176:179], v[208:211], v[86:89]
	v_mfma_f32_16x16x32_bf16 v[82:85], v[184:187], v[208:211], v[82:85]
	v_mfma_f32_16x16x32_bf16 v[70:73], v[176:179], v[216:219], v[70:73]
	v_mfma_f32_16x16x32_bf16 v[66:69], v[184:187], v[216:219], v[66:69]
	s_setprio 0
	s_barrier
	s_mov_b32 m0, s50
	s_add_u32 s28, s28, 0x80080
	ds_read_b128 v[188:191], v152 offset:49152
	ds_read_b128 v[192:195], v152 offset:50176
	ds_read_b128 v[196:199], v152 offset:51200
	ds_read_b128 v[200:203], v152 offset:52224
	global_load_lds_dwordx4 v132, s[98:99]
	s_mov_b32 m0, s51
	s_addc_u32 s29, s29, 0
	global_load_lds_dwordx4 v136, s[98:99]
	s_mov_b32 m0, s54
	ds_read_b128 v[216:219], v152 offset:56320
	global_load_lds_dwordx4 v132, s[28:29]
	s_mov_b32 m0, s55
	ds_read_b128 v[212:215], v152 offset:55296
	global_load_lds_dwordx4 v136, s[28:29]
	s_mov_b32 m0, s52
	ds_read_b128 v[208:211], v152 offset:54272
	global_load_lds_dwordx4 v130, s[100:101]
	s_mov_b32 m0, s53
	ds_read_b128 v[204:207], v152 offset:53248
	global_load_lds_dwordx4 v134, s[100:101]
	s_waitcnt vmcnt(8) lgkmcnt(0)
	s_barrier
	s_setprio 1
	v_mfma_f32_16x16x32_bf16 v[62:65], v[156:159], v[188:191], v[62:65]
	v_mfma_f32_16x16x32_bf16 v[58:61], v[164:167], v[188:191], v[58:61]
	v_mfma_f32_16x16x32_bf16 v[46:49], v[156:159], v[196:199], v[46:49]
	v_mfma_f32_16x16x32_bf16 v[42:45], v[164:167], v[196:199], v[42:45]
	v_mfma_f32_16x16x32_bf16 v[30:33], v[156:159], v[204:207], v[30:33]
	v_mfma_f32_16x16x32_bf16 v[26:29], v[164:167], v[204:207], v[26:29]
	v_mfma_f32_16x16x32_bf16 v[14:17], v[156:159], v[212:215], v[14:17]
	v_mfma_f32_16x16x32_bf16 v[10:13], v[164:167], v[212:215], v[10:13]
	v_mfma_f32_16x16x32_bf16 v[62:65], v[160:163], v[192:195], v[62:65]
	v_mfma_f32_16x16x32_bf16 v[58:61], v[168:171], v[192:195], v[58:61]
	v_mfma_f32_16x16x32_bf16 v[46:49], v[160:163], v[200:203], v[46:49]
	v_mfma_f32_16x16x32_bf16 v[42:45], v[168:171], v[200:203], v[42:45]
	v_mfma_f32_16x16x32_bf16 v[30:33], v[160:163], v[208:211], v[30:33]
	v_mfma_f32_16x16x32_bf16 v[26:29], v[168:171], v[208:211], v[26:29]
	v_mfma_f32_16x16x32_bf16 v[14:17], v[160:163], v[216:219], v[14:17]
	v_mfma_f32_16x16x32_bf16 v[10:13], v[168:171], v[216:219], v[10:13]
	s_setprio 0
	s_setprio 1
	v_mfma_f32_16x16x32_bf16 v[54:57], v[172:175], v[188:191], v[54:57]
	v_mfma_f32_16x16x32_bf16 v[50:53], v[180:183], v[188:191], v[50:53]
	v_mfma_f32_16x16x32_bf16 v[38:41], v[172:175], v[196:199], v[38:41]
	v_mfma_f32_16x16x32_bf16 v[34:37], v[180:183], v[196:199], v[34:37]
	v_mfma_f32_16x16x32_bf16 v[22:25], v[172:175], v[204:207], v[22:25]
	v_mfma_f32_16x16x32_bf16 v[18:21], v[180:183], v[204:207], v[18:21]
	v_mfma_f32_16x16x32_bf16 v[6:9], v[172:175], v[212:215], v[6:9]
	v_mfma_f32_16x16x32_bf16 v[2:5], v[180:183], v[212:215], v[2:5]
	v_mfma_f32_16x16x32_bf16 v[54:57], v[176:179], v[192:195], v[54:57]
	v_mfma_f32_16x16x32_bf16 v[50:53], v[184:187], v[192:195], v[50:53]
	v_mfma_f32_16x16x32_bf16 v[38:41], v[176:179], v[200:203], v[38:41]
	v_mfma_f32_16x16x32_bf16 v[34:37], v[184:187], v[200:203], v[34:37]
	v_mfma_f32_16x16x32_bf16 v[22:25], v[176:179], v[208:211], v[22:25]
	v_mfma_f32_16x16x32_bf16 v[18:21], v[184:187], v[208:211], v[18:21]
	v_mfma_f32_16x16x32_bf16 v[6:9], v[176:179], v[216:219], v[6:9]
	v_mfma_f32_16x16x32_bf16 v[2:5], v[184:187], v[216:219], v[2:5]
	s_setprio 0
	s_barrier
	s_add_u32 s63, s63, 0x100
	s_addc_u32 s64, s64, 0
	s_add_u32 s26, s26, 0x100
	s_addc_u32 s27, s27, 0
	s_cmp_ge_i32 s65, s49
	s_mov_b32 s28, s65
	s_cbranch_scc0 .LBB0_418
	s_branch .LBB0_419
; #define PG8_STAGE(bufoff, gbase, voff) do { _Pragma("unroll") for (int _i = 0; _i < 2; ++_i) \
;         __builtin_amdgcn_global_load_lds((const unsigned*)((const char*)(gbase) + (voff)[_i]), (PG8_LAS unsigned*)(lds + (bufoff) + ldsw + _i * 8192), 16, 0, 0); } while (0)
; #define PG8_LDA(dst, b, h) do { if constexpr (DT != 1) { _Pragma("unroll") for (int m = 0; m < 4; ++m) _Pragma("unroll") for (int k = 0; k < 2; ++k) dst[m][k] = *(const PG8_LAS bf16x8*)(lds + PG8_SA(b, h) + aoff + m * 2048 + k * 1024); } \
;         else { _Pragma("unroll") for (int m = 0; m < 4; ++m) dst##8[m] = ld32(lds + PG8_SA(b, h) + aoff + m * 2048); } } while (0)
; #define PG8_LDB(dst, b, h) do { if constexpr (DT != 1) { _Pragma("unroll") for (int n = 0; n < 2; ++n) _Pragma("unroll") for (int k = 0; k < 2; ++k) dst[n][k] = *(const PG8_LAS bf16x8*)(lds + PG8_SB(b, h) + boff + n * 2048 + k * 1024); } \
;         else { _Pragma("unroll") for (int n = 0; n < 2; ++n) dst##8[n] = ld32(lds + PG8_SB(b, h) + boff + n * 2048); } } while (0)
; #define PG8_WAIT_V(n) asm volatile("s_waitcnt vmcnt(" #n ")" ::: "memory")
; #define PG8_WAIT_L(n) asm volatile("s_waitcnt lgkmcnt(" #n ")" ::: "memory")
; #define PG8_BAR __builtin_amdgcn_s_barrier()
; #define PG8_SCHED __builtin_amdgcn_sched_barrier(0)
;     ...
;             if constexpr (SP2) {
;             PG8_LDB(B0, 0, 0); PG8_LDB(B1, 0, 1); PG8_SCHED; PG8_LDA(At, 0, 0); PG8_STAGE(PG8_SA(1, 1), a1 + hstepA, voffA);
;             PG8_WAIT_V(8); PG8_WAIT_L(0); PG8_BAR; PG8_MMA(0, 0, At, B0); PG8_MMA(0, 1, At, B1); PG8_BAR; PG8_SCHED;
;             PG8_LDA(At, 0, 1); PG8_STAGE(PG8_SB(0, 0), b2, voffB); PG8_STAGE(PG8_SB(0, 1), b2 + hstepB, voffB); PG8_STAGE(PG8_SA(0, 0), a2, voffA);
;             PG8_WAIT_V(8); PG8_WAIT_L(0); PG8_BAR; PG8_MMA(1, 0, At, B0); PG8_MMA(1, 1, At, B1); PG8_BAR; PG8_SCHED;
;             PG8_LDB(B0, 1, 0); PG8_LDB(B1, 1, 1); PG8_SCHED; PG8_LDA(At, 1, 0); PG8_STAGE(PG8_SA(0, 1), a2 + hstepA, voffA);
;             PG8_WAIT_V(8); PG8_WAIT_L(0); PG8_BAR; PG8_MMA(0, 0, At, B0); PG8_MMA(0, 1, At, B1); PG8_BAR; PG8_SCHED;
;             PG8_LDA(At, 1, 1); PG8_STAGE(PG8_SB(1, 0), b3, voffB); PG8_STAGE(PG8_SB(1, 1), b3 + hstepB, voffB); PG8_STAGE(PG8_SA(1, 0), a3, voffA);
;             PG8_WAIT_V(8); PG8_WAIT_L(0); PG8_BAR; PG8_MMA(1, 0, At, B0); PG8_MMA(1, 1, At, B1); PG8_BAR; PG8_SCHED;
.LBB0_418:
	ds_read_b128 v[156:159], v150
	ds_read_b128 v[160:163], v150 offset:1024
	ds_read_b128 v[164:167], v150 offset:2048
	ds_read_b128 v[168:171], v150 offset:3072
	ds_read_b128 v[172:175], v151
	ds_read_b128 v[176:179], v151 offset:1024
	ds_read_b128 v[180:183], v151 offset:2048
	ds_read_b128 v[184:187], v151 offset:3072
	s_add_i32 s65, s28, 2
	s_add_u32 s29, s26, 0xfff80080
	s_addc_u32 s30, s27, -1
	s_cmp_eq_u32 s59, s28
	s_cselect_b32 s28, s62, s63
	s_cselect_b32 s31, s19, s30
	s_cselect_b32 s30, s21, s29
	s_cselect_b32 s29, s61, s64
	s_add_i32 m0, s45, 0xc000
	ds_read_b128 v[188:191], v152
	ds_read_b128 v[192:195], v152 offset:1024
	ds_read_b128 v[196:199], v152 offset:2048
	ds_read_b128 v[200:203], v152 offset:3072
	ds_read_b128 v[204:207], v152 offset:4096
	ds_read_b128 v[208:211], v152 offset:5120
	ds_read_b128 v[212:215], v152 offset:6144
	ds_read_b128 v[216:219], v152 offset:7168
	global_load_lds_dwordx4 v144, s[26:27]
	s_add_i32 m0, s45, 0xe000
	s_nop 0
	global_load_lds_dwordx4 v142, s[26:27]
	s_waitcnt vmcnt(8) lgkmcnt(0)
	s_barrier
	s_setprio 1
	v_mfma_f32_16x16x32_bf16 v[122:125], v[156:159], v[188:191], v[122:125]
	v_mfma_f32_16x16x32_bf16 v[126:129], v[164:167], v[188:191], v[126:129]
	v_mfma_f32_16x16x32_bf16 v[110:113], v[156:159], v[196:199], v[110:113]
	v_mfma_f32_16x16x32_bf16 v[106:109], v[164:167], v[196:199], v[106:109]
	v_mfma_f32_16x16x32_bf16 v[94:97], v[156:159], v[204:207], v[94:97]
	v_mfma_f32_16x16x32_bf16 v[90:93], v[164:167], v[204:207], v[90:93]
	v_mfma_f32_16x16x32_bf16 v[78:81], v[156:159], v[212:215], v[78:81]
	v_mfma_f32_16x16x32_bf16 v[74:77], v[164:167], v[212:215], v[74:77]
	v_mfma_f32_16x16x32_bf16 v[122:125], v[160:163], v[192:195], v[122:125]
	v_mfma_f32_16x16x32_bf16 v[126:129], v[168:171], v[192:195], v[126:129]
	v_mfma_f32_16x16x32_bf16 v[110:113], v[160:163], v[200:203], v[110:113]
	v_mfma_f32_16x16x32_bf16 v[106:109], v[168:171], v[200:203], v[106:109]
	v_mfma_f32_16x16x32_bf16 v[94:97], v[160:163], v[208:211], v[94:97]
	v_mfma_f32_16x16x32_bf16 v[90:93], v[168:171], v[208:211], v[90:93]
	v_mfma_f32_16x16x32_bf16 v[78:81], v[160:163], v[216:219], v[78:81]
	v_mfma_f32_16x16x32_bf16 v[74:77], v[168:171], v[216:219], v[74:77]
	s_setprio 0
	s_setprio 1
	v_mfma_f32_16x16x32_bf16 v[118:121], v[172:175], v[188:191], v[118:121]
	v_mfma_f32_16x16x32_bf16 v[114:117], v[180:183], v[188:191], v[114:117]
	v_mfma_f32_16x16x32_bf16 v[102:105], v[172:175], v[196:199], v[102:105]
	v_mfma_f32_16x16x32_bf16 v[98:101], v[180:183], v[196:199], v[98:101]
	v_mfma_f32_16x16x32_bf16 v[86:89], v[172:175], v[204:207], v[86:89]
	v_mfma_f32_16x16x32_bf16 v[82:85], v[180:183], v[204:207], v[82:85]
	v_mfma_f32_16x16x32_bf16 v[70:73], v[172:175], v[212:215], v[70:73]
	v_mfma_f32_16x16x32_bf16 v[66:69], v[180:183], v[212:215], v[66:69]
	v_mfma_f32_16x16x32_bf16 v[118:121], v[176:179], v[192:195], v[118:121]
	v_mfma_f32_16x16x32_bf16 v[114:117], v[184:187], v[192:195], v[114:117]
	v_mfma_f32_16x16x32_bf16 v[102:105], v[176:179], v[200:203], v[102:105]
	v_mfma_f32_16x16x32_bf16 v[98:101], v[184:187], v[200:203], v[98:101]
	v_mfma_f32_16x16x32_bf16 v[86:89], v[176:179], v[208:211], v[86:89]
	v_mfma_f32_16x16x32_bf16 v[82:85], v[184:187], v[208:211], v[82:85]
	v_mfma_f32_16x16x32_bf16 v[70:73], v[176:179], v[216:219], v[70:73]
	v_mfma_f32_16x16x32_bf16 v[66:69], v[184:187], v[216:219], v[66:69]
	s_setprio 0
	s_barrier
	s_mov_b32 m0, s41
	s_add_u32 s98, s28, 0x80
	s_addc_u32 s99, s29, 0
	s_add_u32 s66, s28, 0x80000
	ds_read_b128 v[188:191], v152 offset:16384
	ds_read_b128 v[192:195], v152 offset:17408
	ds_read_b128 v[196:199], v152 offset:18432
	ds_read_b128 v[200:203], v152 offset:19456
	global_load_lds_dwordx4 v132, s[28:29]
	s_mov_b32 m0, s42
	s_addc_u32 s67, s29, 0
	global_load_lds_dwordx4 v136, s[28:29]
	s_mov_b32 m0, s43
	ds_read_b128 v[216:219], v152 offset:23552
	global_load_lds_dwordx4 v132, s[66:67]
	s_mov_b32 m0, s44
	ds_read_b128 v[212:215], v152 offset:22528
	global_load_lds_dwordx4 v136, s[66:67]
	s_add_u32 s100, s30, 0x80
	s_addc_u32 s101, s31, 0
	s_mov_b32 m0, s45
	ds_read_b128 v[208:211], v152 offset:21504
	global_load_lds_dwordx4 v130, s[30:31]
	s_mov_b32 m0, s46
	ds_read_b128 v[204:207], v152 offset:20480
	global_load_lds_dwordx4 v134, s[30:31]
	s_waitcnt vmcnt(8) lgkmcnt(0)
	s_barrier
	s_setprio 1
	v_mfma_f32_16x16x32_bf16 v[62:65], v[156:159], v[188:191], v[62:65]
	v_mfma_f32_16x16x32_bf16 v[58:61], v[164:167], v[188:191], v[58:61]
	v_mfma_f32_16x16x32_bf16 v[46:49], v[156:159], v[196:199], v[46:49]
	v_mfma_f32_16x16x32_bf16 v[42:45], v[164:167], v[196:199], v[42:45]
	v_mfma_f32_16x16x32_bf16 v[30:33], v[156:159], v[204:207], v[30:33]
	v_mfma_f32_16x16x32_bf16 v[26:29], v[164:167], v[204:207], v[26:29]
	v_mfma_f32_16x16x32_bf16 v[14:17], v[156:159], v[212:215], v[14:17]
	v_mfma_f32_16x16x32_bf16 v[10:13], v[164:167], v[212:215], v[10:13]
	v_mfma_f32_16x16x32_bf16 v[62:65], v[160:163], v[192:195], v[62:65]
	v_mfma_f32_16x16x32_bf16 v[58:61], v[168:171], v[192:195], v[58:61]
	v_mfma_f32_16x16x32_bf16 v[46:49], v[160:163], v[200:203], v[46:49]
	v_mfma_f32_16x16x32_bf16 v[42:45], v[168:171], v[200:203], v[42:45]
	v_mfma_f32_16x16x32_bf16 v[30:33], v[160:163], v[208:211], v[30:33]
	v_mfma_f32_16x16x32_bf16 v[26:29], v[168:171], v[208:211], v[26:29]
	v_mfma_f32_16x16x32_bf16 v[14:17], v[160:163], v[216:219], v[14:17]
	v_mfma_f32_16x16x32_bf16 v[10:13], v[168:171], v[216:219], v[10:13]
	s_setprio 0
	s_setprio 1
	v_mfma_f32_16x16x32_bf16 v[54:57], v[172:175], v[188:191], v[54:57]
	v_mfma_f32_16x16x32_bf16 v[50:53], v[180:183], v[188:191], v[50:53]
	v_mfma_f32_16x16x32_bf16 v[38:41], v[172:175], v[196:199], v[38:41]
	v_mfma_f32_16x16x32_bf16 v[34:37], v[180:183], v[196:199], v[34:37]
	v_mfma_f32_16x16x32_bf16 v[22:25], v[172:175], v[204:207], v[22:25]
	v_mfma_f32_16x16x32_bf16 v[18:21], v[180:183], v[204:207], v[18:21]
	v_mfma_f32_16x16x32_bf16 v[6:9], v[172:175], v[212:215], v[6:9]
	v_mfma_f32_16x16x32_bf16 v[2:5], v[180:183], v[212:215], v[2:5]
	v_mfma_f32_16x16x32_bf16 v[54:57], v[176:179], v[192:195], v[54:57]
	v_mfma_f32_16x16x32_bf16 v[50:53], v[184:187], v[192:195], v[50:53]
	v_mfma_f32_16x16x32_bf16 v[38:41], v[176:179], v[200:203], v[38:41]
	v_mfma_f32_16x16x32_bf16 v[34:37], v[184:187], v[200:203], v[34:37]
	v_mfma_f32_16x16x32_bf16 v[22:25], v[176:179], v[208:211], v[22:25]
	v_mfma_f32_16x16x32_bf16 v[18:21], v[184:187], v[208:211], v[18:21]
	v_mfma_f32_16x16x32_bf16 v[6:9], v[176:179], v[216:219], v[6:9]
	v_mfma_f32_16x16x32_bf16 v[2:5], v[184:187], v[216:219], v[2:5]
	s_setprio 0
	s_barrier
; #define PG8_STAGE(bufoff, gbase, voff) do { _Pragma("unroll") for (int _i = 0; _i < 2; ++_i) \
;         __builtin_amdgcn_global_load_lds((const unsigned*)((const char*)(gbase) + (voff)[_i]), (PG8_LAS unsigned*)(lds + (bufoff) + ldsw + _i * 8192), 16, 0, 0); } while (0)
; #define PG8_LDA(dst, b, h) do { if constexpr (DT != 1) { _Pragma("unroll") for (int m = 0; m < 4; ++m) _Pragma("unroll") for (int k = 0; k < 2; ++k) dst[m][k] = *(const PG8_LAS bf16x8*)(lds + PG8_SA(b, h) + aoff + m * 2048 + k * 1024); } \
;         else { _Pragma("unroll") for (int m = 0; m < 4; ++m) dst##8[m] = ld32(lds + PG8_SA(b, h) + aoff + m * 2048); } } while (0)
; #define PG8_LDB(dst, b, h) do { if constexpr (DT != 1) { _Pragma("unroll") for (int n = 0; n < 2; ++n) _Pragma("unroll") for (int k = 0; k < 2; ++k) dst[n][k] = *(const PG8_LAS bf16x8*)(lds + PG8_SB(b, h) + boff + n * 2048 + k * 1024); } \
;         else { _Pragma("unroll") for (int n = 0; n < 2; ++n) dst##8[n] = ld32(lds + PG8_SB(b, h) + boff + n * 2048); } } while (0)
; #define PG8_WAIT_V(n) asm volatile("s_waitcnt vmcnt(" #n ")" ::: "memory")
; #define PG8_WAIT_L(n) asm volatile("s_waitcnt lgkmcnt(" #n ")" ::: "memory")
; #define PG8_BAR __builtin_amdgcn_s_barrier()
; #define PG8_SCHED __builtin_amdgcn_sched_barrier(0)
;     ...
;             if constexpr (SP2) {
;             PG8_LDB(B0, 0, 0); PG8_LDB(B1, 0, 1); PG8_SCHED; PG8_LDA(At, 0, 0); PG8_STAGE(PG8_SA(1, 1), a1 + hstepA, voffA);
;             PG8_WAIT_V(8); PG8_WAIT_L(0); PG8_BAR; PG8_MMA(0, 0, At, B0); PG8_MMA(0, 1, At, B1); PG8_BAR; PG8_SCHED;
;             PG8_LDA(At, 0, 1); PG8_STAGE(PG8_SB(0, 0), b2, voffB); PG8_STAGE(PG8_SB(0, 1), b2 + hstepB, voffB); PG8_STAGE(PG8_SA(0, 0), a2, voffA);
;             PG8_WAIT_V(8); PG8_WAIT_L(0); PG8_BAR; PG8_MMA(1, 0, At, B0); PG8_MMA(1, 1, At, B1); PG8_BAR; PG8_SCHED;
;             PG8_LDB(B0, 1, 0); PG8_LDB(B1, 1, 1); PG8_SCHED; PG8_LDA(At, 1, 0); PG8_STAGE(PG8_SA(0, 1), a2 + hstepA, voffA);
;             PG8_WAIT_V(8); PG8_WAIT_L(0); PG8_BAR; PG8_MMA(0, 0, At, B0); PG8_MMA(0, 1, At, B1); PG8_BAR; PG8_SCHED;
;             PG8_LDA(At, 1, 1); PG8_STAGE(PG8_SB(1, 0), b3, voffB); PG8_STAGE(PG8_SB(1, 1), b3 + hstepB, voffB); PG8_STAGE(PG8_SA(1, 0), a3, voffA);
;             PG8_WAIT_V(8); PG8_WAIT_L(0); PG8_BAR; PG8_MMA(1, 0, At, B0); PG8_MMA(1, 1, At, B1); PG8_BAR; PG8_SCHED;
	ds_read_b128 v[156:159], v153
	ds_read_b128 v[160:163], v153 offset:1024
	ds_read_b128 v[164:167], v153 offset:2048
	ds_read_b128 v[168:171], v153 offset:3072
	ds_read_b128 v[172:175], v154
	ds_read_b128 v[176:179], v154 offset:1024
	ds_read_b128 v[180:183], v154 offset:2048
	ds_read_b128 v[184:187], v154 offset:3072
	s_add_u32 s30, s30, 0x80000
	s_addc_u32 s31, s31, 0
	s_mov_b32 m0, s47
	ds_read_b128 v[188:191], v152 offset:32768
	ds_read_b128 v[192:195], v152 offset:33792
	ds_read_b128 v[196:199], v152 offset:34816
	ds_read_b128 v[200:203], v152 offset:35840
	ds_read_b128 v[204:207], v152 offset:36864
	ds_read_b128 v[208:211], v152 offset:37888
	ds_read_b128 v[212:215], v152 offset:38912
	global_load_lds_dwordx4 v130, s[30:31]
	s_mov_b32 m0, s48
	ds_read_b128 v[216:219], v152 offset:39936
	global_load_lds_dwordx4 v134, s[30:31]
	s_waitcnt vmcnt(8) lgkmcnt(0)
	s_barrier
	s_setprio 1
	v_mfma_f32_16x16x32_bf16 v[122:125], v[156:159], v[188:191], v[122:125]
	v_mfma_f32_16x16x32_bf16 v[126:129], v[164:167], v[188:191], v[126:129]
	v_mfma_f32_16x16x32_bf16 v[110:113], v[156:159], v[196:199], v[110:113]
	v_mfma_f32_16x16x32_bf16 v[106:109], v[164:167], v[196:199], v[106:109]
	v_mfma_f32_16x16x32_bf16 v[94:97], v[156:159], v[204:207], v[94:97]
	v_mfma_f32_16x16x32_bf16 v[90:93], v[164:167], v[204:207], v[90:93]
	v_mfma_f32_16x16x32_bf16 v[78:81], v[156:159], v[212:215], v[78:81]
	v_mfma_f32_16x16x32_bf16 v[74:77], v[164:167], v[212:215], v[74:77]
	v_mfma_f32_16x16x32_bf16 v[122:125], v[160:163], v[192:195], v[122:125]
	v_mfma_f32_16x16x32_bf16 v[126:129], v[168:171], v[192:195], v[126:129]
	v_mfma_f32_16x16x32_bf16 v[110:113], v[160:163], v[200:203], v[110:113]
	v_mfma_f32_16x16x32_bf16 v[106:109], v[168:171], v[200:203], v[106:109]
	v_mfma_f32_16x16x32_bf16 v[94:97], v[160:163], v[208:211], v[94:97]
	v_mfma_f32_16x16x32_bf16 v[90:93], v[168:171], v[208:211], v[90:93]
	v_mfma_f32_16x16x32_bf16 v[78:81], v[160:163], v[216:219], v[78:81]
	v_mfma_f32_16x16x32_bf16 v[74:77], v[168:171], v[216:219], v[74:77]
	s_setprio 0
	s_setprio 1
	v_mfma_f32_16x16x32_bf16 v[118:121], v[172:175], v[188:191], v[118:121]
	v_mfma_f32_16x16x32_bf16 v[114:117], v[180:183], v[188:191], v[114:117]
	v_mfma_f32_16x16x32_bf16 v[102:105], v[172:175], v[196:199], v[102:105]
	v_mfma_f32_16x16x32_bf16 v[98:101], v[180:183], v[196:199], v[98:101]
	v_mfma_f32_16x16x32_bf16 v[86:89], v[172:175], v[204:207], v[86:89]
	v_mfma_f32_16x16x32_bf16 v[82:85], v[180:183], v[204:207], v[82:85]
	v_mfma_f32_16x16x32_bf16 v[70:73], v[172:175], v[212:215], v[70:73]
	v_mfma_f32_16x16x32_bf16 v[66:69], v[180:183], v[212:215], v[66:69]
	v_mfma_f32_16x16x32_bf16 v[118:121], v[176:179], v[192:195], v[118:121]
	v_mfma_f32_16x16x32_bf16 v[114:117], v[184:187], v[192:195], v[114:117]
	v_mfma_f32_16x16x32_bf16 v[102:105], v[176:179], v[200:203], v[102:105]
	v_mfma_f32_16x16x32_bf16 v[98:101], v[184:187], v[200:203], v[98:101]
	v_mfma_f32_16x16x32_bf16 v[86:89], v[176:179], v[208:211], v[86:89]
	v_mfma_f32_16x16x32_bf16 v[82:85], v[184:187], v[208:211], v[82:85]
	v_mfma_f32_16x16x32_bf16 v[70:73], v[176:179], v[216:219], v[70:73]
	v_mfma_f32_16x16x32_bf16 v[66:69], v[184:187], v[216:219], v[66:69]
	s_setprio 0
	s_barrier
	s_mov_b32 m0, s50
	s_add_u32 s28, s28, 0x80080
	ds_read_b128 v[188:191], v152 offset:49152
	ds_read_b128 v[192:195], v152 offset:50176
	ds_read_b128 v[196:199], v152 offset:51200
	ds_read_b128 v[200:203], v152 offset:52224
	global_load_lds_dwordx4 v132, s[98:99]
	s_mov_b32 m0, s51
	s_addc_u32 s29, s29, 0
	global_load_lds_dwordx4 v136, s[98:99]
	s_mov_b32 m0, s54
	ds_read_b128 v[216:219], v152 offset:56320
	global_load_lds_dwordx4 v132, s[28:29]
	s_mov_b32 m0, s55
	ds_read_b128 v[212:215], v152 offset:55296
	global_load_lds_dwordx4 v136, s[28:29]
	s_mov_b32 m0, s52
	ds_read_b128 v[208:211], v152 offset:54272
	global_load_lds_dwordx4 v130, s[100:101]
	s_mov_b32 m0, s53
	ds_read_b128 v[204:207], v152 offset:53248
	global_load_lds_dwordx4 v134, s[100:101]
	s_waitcnt vmcnt(8) lgkmcnt(0)
	s_barrier
	s_setprio 1
	v_mfma_f32_16x16x32_bf16 v[62:65], v[156:159], v[188:191], v[62:65]
	v_mfma_f32_16x16x32_bf16 v[58:61], v[164:167], v[188:191], v[58:61]
	v_mfma_f32_16x16x32_bf16 v[46:49], v[156:159], v[196:199], v[46:49]
	v_mfma_f32_16x16x32_bf16 v[42:45], v[164:167], v[196:199], v[42:45]
	v_mfma_f32_16x16x32_bf16 v[30:33], v[156:159], v[204:207], v[30:33]
	v_mfma_f32_16x16x32_bf16 v[26:29], v[164:167], v[204:207], v[26:29]
	v_mfma_f32_16x16x32_bf16 v[14:17], v[156:159], v[212:215], v[14:17]
	v_mfma_f32_16x16x32_bf16 v[10:13], v[164:167], v[212:215], v[10:13]
	v_mfma_f32_16x16x32_bf16 v[62:65], v[160:163], v[192:195], v[62:65]
	v_mfma_f32_16x16x32_bf16 v[58:61], v[168:171], v[192:195], v[58:61]
	v_mfma_f32_16x16x32_bf16 v[46:49], v[160:163], v[200:203], v[46:49]
	v_mfma_f32_16x16x32_bf16 v[42:45], v[168:171], v[200:203], v[42:45]
	v_mfma_f32_16x16x32_bf16 v[30:33], v[160:163], v[208:211], v[30:33]
	v_mfma_f32_16x16x32_bf16 v[26:29], v[168:171], v[208:211], v[26:29]
	v_mfma_f32_16x16x32_bf16 v[14:17], v[160:163], v[216:219], v[14:17]
	v_mfma_f32_16x16x32_bf16 v[10:13], v[168:171], v[216:219], v[10:13]
	s_setprio 0
	s_setprio 1
	v_mfma_f32_16x16x32_bf16 v[54:57], v[172:175], v[188:191], v[54:57]
	v_mfma_f32_16x16x32_bf16 v[50:53], v[180:183], v[188:191], v[50:53]
	v_mfma_f32_16x16x32_bf16 v[38:41], v[172:175], v[196:199], v[38:41]
	v_mfma_f32_16x16x32_bf16 v[34:37], v[180:183], v[196:199], v[34:37]
	v_mfma_f32_16x16x32_bf16 v[22:25], v[172:175], v[204:207], v[22:25]
	v_mfma_f32_16x16x32_bf16 v[18:21], v[180:183], v[204:207], v[18:21]
	v_mfma_f32_16x16x32_bf16 v[6:9], v[172:175], v[212:215], v[6:9]
	v_mfma_f32_16x16x32_bf16 v[2:5], v[180:183], v[212:215], v[2:5]
	v_mfma_f32_16x16x32_bf16 v[54:57], v[176:179], v[192:195], v[54:57]
	v_mfma_f32_16x16x32_bf16 v[50:53], v[184:187], v[192:195], v[50:53]
	v_mfma_f32_16x16x32_bf16 v[38:41], v[176:179], v[200:203], v[38:41]
	v_mfma_f32_16x16x32_bf16 v[34:37], v[184:187], v[200:203], v[34:37]
	v_mfma_f32_16x16x32_bf16 v[22:25], v[176:179], v[208:211], v[22:25]
	v_mfma_f32_16x16x32_bf16 v[18:21], v[184:187], v[208:211], v[18:21]
	v_mfma_f32_16x16x32_bf16 v[6:9], v[176:179], v[216:219], v[6:9]
	v_mfma_f32_16x16x32_bf16 v[2:5], v[184:187], v[216:219], v[2:5]
	s_setprio 0
	s_barrier
	s_add_u32 s63, s63, 0x100
	s_addc_u32 s64, s64, 0
	s_add_u32 s26, s26, 0x100
	s_addc_u32 s27, s27, 0
	s_cmp_ge_i32 s65, s49
	s_mov_b32 s28, s65
	s_cbranch_scc0 .LBB0_418

; #define PG8_STAGE(bufoff, gbase, voff) do { _Pragma("unroll") for (int _i = 0; _i < 2; ++_i) \
;         __builtin_amdgcn_global_load_lds((const unsigned*)((const char*)(gbase) + (voff)[_i]), (PG8_LAS unsigned*)(lds + (bufoff) + ldsw + _i * 8192), 16, 0, 0); } while (0)
; #define PG8_LDA(dst, b, h) do { if constexpr (DT != 1) { _Pragma("unroll") for (int m = 0; m < 4; ++m) _Pragma("unroll") for (int k = 0; k < 2; ++k) dst[m][k] = *(const PG8_LAS bf16x8*)(lds + PG8_SA(b, h) + aoff + m * 2048 + k * 1024); } \
;         else { _Pragma("unroll") for (int m = 0; m < 4; ++m) dst##8[m] = ld32(lds + PG8_SA(b, h) + aoff + m * 2048); } } while (0)
; #define PG8_WAIT_V(n) asm volatile("s_waitcnt vmcnt(" #n ")" ::: "memory")
; #define PG8_WAIT_L(n) asm volatile("s_waitcnt lgkmcnt(" #n ")" ::: "memory")
; #define PG8_BAR __builtin_amdgcn_s_barrier()
; #define PG8_SCHED __builtin_amdgcn_sched_barrier(0)
;     ...
;         for (int t = 0; t < nt; t += 2) {
;             const bool last = (t == nt - 2);
;             const char* a1 = cA + (size_t)(t + 1) * kstep;
;             const char* a2 = last ? nA : cA + (size_t)(t + 2) * kstep; const char* b2 = last ? nB : cB + (size_t)(t + 2) * kstep;
;             const char* a3 = a2 + kstep; const char* b3 = b2 + kstep;
;             if (last && has_next) S.a_ready(nxt);
;             if constexpr (SP2) {
;             PG8_LDB(B0, 0, 0); PG8_LDB(B1, 0, 1); PG8_SCHED; PG8_LDA(At, 0, 0); PG8_STAGE(PG8_SA(1, 1), a1 + hstepA, voffA);
;             PG8_WAIT_V(8); PG8_WAIT_L(0); PG8_BAR; PG8_MMA(0, 0, At, B0); PG8_MMA(0, 1, At, B1); PG8_BAR; PG8_SCHED;
;             PG8_LDA(At, 0, 1); PG8_STAGE(PG8_SB(0, 0), b2, voffB); PG8_STAGE(PG8_SB(0, 1), b2 + hstepB, voffB); PG8_STAGE(PG8_SA(0, 0), a2, voffA);
;             PG8_WAIT_V(8); PG8_WAIT_L(0); PG8_BAR; PG8_MMA(1, 0, At, B0); PG8_MMA(1, 1, At, B1); PG8_BAR; PG8_SCHED;
;             PG8_LDB(B0, 1, 0); PG8_LDB(B1, 1, 1); PG8_SCHED; PG8_LDA(At, 1, 0); PG8_STAGE(PG8_SA(0, 1), a2 + hstepA, voffA);
;             PG8_WAIT_V(8); PG8_WAIT_L(0); PG8_BAR; PG8_MMA(0, 0, At, B0); PG8_MMA(0, 1, At, B1); PG8_BAR; PG8_SCHED;
;             PG8_LDA(At, 1, 1); PG8_STAGE(PG8_SB(1, 0), b3, voffB); PG8_STAGE(PG8_SB(1, 1), b3 + hstepB, voffB); PG8_STAGE(PG8_SA(1, 0), a3, voffA);
;             PG8_WAIT_V(8); PG8_WAIT_L(0); PG8_BAR; PG8_MMA(1, 0, At, B0); PG8_MMA(1, 1, At, B1); PG8_BAR; PG8_SCHED;
.Lzs_3:
	s_cbranch_vccnz .LBB0_714
	s_and_b64 s[38:39], s[0:1], exec
	s_cselect_b32 s23, s27, s37
	s_cselect_b32 s25, s26, s36
	s_cselect_b32 s65, s29, s35
	s_cselect_b32 s66, s28, s34
	s_add_u32 s67, s34, 0x100
	s_addc_u32 s68, s35, 0
	s_add_u32 s34, s36, 0x80080
	s_addc_u32 s35, s37, 0
	s_mov_b32 s36, 0
	ds_read_b128 v[130:133], v173
	ds_read_b128 v[134:137], v173 offset:1024
	ds_read_b128 v[138:141], v173 offset:2048
	ds_read_b128 v[142:145], v173 offset:3072
	ds_read_b128 v[162:165], v174
	ds_read_b128 v[166:169], v174 offset:1024
	ds_read_b128 v[178:181], v174 offset:2048
	ds_read_b128 v[182:185], v174 offset:3072
	s_add_i32 s69, s36, 2
	s_add_u32 s37, s34, 0xfff80080
	s_addc_u32 s38, s35, -1
	s_cmp_eq_u32 s61, s36
	s_cselect_b32 s36, s66, s67
	s_cselect_b32 s39, s23, s38
	s_cselect_b32 s38, s25, s37
	s_cselect_b32 s37, s65, s68
	s_add_i32 m0, s49, 0xc000
	ds_read_b128 v[186:189], v175
	ds_read_b128 v[190:193], v175 offset:1024
	ds_read_b128 v[194:197], v175 offset:2048
	ds_read_b128 v[198:201], v175 offset:3072
	ds_read_b128 v[202:205], v175 offset:4096
	ds_read_b128 v[206:209], v175 offset:5120
	ds_read_b128 v[210:213], v175 offset:6144
	ds_read_b128 v[214:217], v175 offset:7168
	global_load_lds_dwordx4 v156, s[34:35]
	s_add_i32 m0, s49, 0xe000
	s_nop 0
	global_load_lds_dwordx4 v154, s[34:35]
	s_waitcnt vmcnt(8) lgkmcnt(0)
	s_barrier
	s_setprio 1
	v_mfma_f32_16x16x32_bf16 v[122:125], v[130:133], v[186:189], 0
	v_mfma_f32_16x16x32_bf16 v[126:129], v[138:141], v[186:189], 0
	v_mfma_f32_16x16x32_bf16 v[110:113], v[130:133], v[194:197], 0
	v_mfma_f32_16x16x32_bf16 v[106:109], v[138:141], v[194:197], 0
	v_mfma_f32_16x16x32_bf16 v[94:97], v[130:133], v[202:205], 0
	v_mfma_f32_16x16x32_bf16 v[90:93], v[138:141], v[202:205], 0
	v_mfma_f32_16x16x32_bf16 v[78:81], v[130:133], v[210:213], 0
	v_mfma_f32_16x16x32_bf16 v[74:77], v[138:141], v[210:213], 0
	v_mfma_f32_16x16x32_bf16 v[122:125], v[134:137], v[190:193], v[122:125]
	v_mfma_f32_16x16x32_bf16 v[126:129], v[142:145], v[190:193], v[126:129]
	v_mfma_f32_16x16x32_bf16 v[110:113], v[134:137], v[198:201], v[110:113]
	v_mfma_f32_16x16x32_bf16 v[106:109], v[142:145], v[198:201], v[106:109]
	v_mfma_f32_16x16x32_bf16 v[94:97], v[134:137], v[206:209], v[94:97]
	v_mfma_f32_16x16x32_bf16 v[90:93], v[142:145], v[206:209], v[90:93]
	v_mfma_f32_16x16x32_bf16 v[78:81], v[134:137], v[214:217], v[78:81]
	v_mfma_f32_16x16x32_bf16 v[74:77], v[142:145], v[214:217], v[74:77]
	s_setprio 0
	s_setprio 1
	v_mfma_f32_16x16x32_bf16 v[118:121], v[162:165], v[186:189], 0
	v_mfma_f32_16x16x32_bf16 v[114:117], v[178:181], v[186:189], 0
	v_mfma_f32_16x16x32_bf16 v[102:105], v[162:165], v[194:197], 0
	v_mfma_f32_16x16x32_bf16 v[98:101], v[178:181], v[194:197], 0
	v_mfma_f32_16x16x32_bf16 v[86:89], v[162:165], v[202:205], 0
	v_mfma_f32_16x16x32_bf16 v[82:85], v[178:181], v[202:205], 0
	v_mfma_f32_16x16x32_bf16 v[70:73], v[162:165], v[210:213], 0
	v_mfma_f32_16x16x32_bf16 v[66:69], v[178:181], v[210:213], 0
	v_mfma_f32_16x16x32_bf16 v[118:121], v[166:169], v[190:193], v[118:121]
	v_mfma_f32_16x16x32_bf16 v[114:117], v[182:185], v[190:193], v[114:117]
	v_mfma_f32_16x16x32_bf16 v[102:105], v[166:169], v[198:201], v[102:105]
	v_mfma_f32_16x16x32_bf16 v[98:101], v[182:185], v[198:201], v[98:101]
	v_mfma_f32_16x16x32_bf16 v[86:89], v[166:169], v[206:209], v[86:89]
	v_mfma_f32_16x16x32_bf16 v[82:85], v[182:185], v[206:209], v[82:85]
	v_mfma_f32_16x16x32_bf16 v[70:73], v[166:169], v[214:217], v[70:73]
	v_mfma_f32_16x16x32_bf16 v[66:69], v[182:185], v[214:217], v[66:69]
	s_setprio 0
	s_barrier
	s_mov_b32 m0, s31
	s_add_u32 s98, s36, 0x80
	s_addc_u32 s99, s37, 0
	s_add_u32 s70, s36, 0x80000
	ds_read_b128 v[186:189], v175 offset:16384
	ds_read_b128 v[190:193], v175 offset:17408
	ds_read_b128 v[194:197], v175 offset:18432
	ds_read_b128 v[198:201], v175 offset:19456
	global_load_lds_dwordx4 v148, s[36:37]
	s_mov_b32 m0, s46
	s_addc_u32 s71, s37, 0
	global_load_lds_dwordx4 v152, s[36:37]
	s_mov_b32 m0, s47
	ds_read_b128 v[214:217], v175 offset:23552
	global_load_lds_dwordx4 v148, s[70:71]
	s_mov_b32 m0, s48
	ds_read_b128 v[210:213], v175 offset:22528
	global_load_lds_dwordx4 v152, s[70:71]
	s_add_u32 s100, s38, 0x80
	s_addc_u32 s101, s39, 0
	s_mov_b32 m0, s49
	ds_read_b128 v[206:209], v175 offset:21504
	global_load_lds_dwordx4 v146, s[38:39]
	s_mov_b32 m0, s50
	ds_read_b128 v[202:205], v175 offset:20480
	global_load_lds_dwordx4 v150, s[38:39]
	s_waitcnt vmcnt(8) lgkmcnt(0)
	s_barrier
	s_setprio 1
	v_mfma_f32_16x16x32_bf16 v[62:65], v[130:133], v[186:189], 0
	v_mfma_f32_16x16x32_bf16 v[58:61], v[138:141], v[186:189], 0
	v_mfma_f32_16x16x32_bf16 v[46:49], v[130:133], v[194:197], 0
	v_mfma_f32_16x16x32_bf16 v[42:45], v[138:141], v[194:197], 0
	v_mfma_f32_16x16x32_bf16 v[30:33], v[130:133], v[202:205], 0
	v_mfma_f32_16x16x32_bf16 v[26:29], v[138:141], v[202:205], 0
	v_mfma_f32_16x16x32_bf16 v[14:17], v[130:133], v[210:213], 0
	v_mfma_f32_16x16x32_bf16 v[10:13], v[138:141], v[210:213], 0
	v_mfma_f32_16x16x32_bf16 v[62:65], v[134:137], v[190:193], v[62:65]
	v_mfma_f32_16x16x32_bf16 v[58:61], v[142:145], v[190:193], v[58:61]
	v_mfma_f32_16x16x32_bf16 v[46:49], v[134:137], v[198:201], v[46:49]
	v_mfma_f32_16x16x32_bf16 v[42:45], v[142:145], v[198:201], v[42:45]
	v_mfma_f32_16x16x32_bf16 v[30:33], v[134:137], v[206:209], v[30:33]
	v_mfma_f32_16x16x32_bf16 v[26:29], v[142:145], v[206:209], v[26:29]
	v_mfma_f32_16x16x32_bf16 v[14:17], v[134:137], v[214:217], v[14:17]
	v_mfma_f32_16x16x32_bf16 v[10:13], v[142:145], v[214:217], v[10:13]
	s_setprio 0
	s_setprio 1
	v_mfma_f32_16x16x32_bf16 v[54:57], v[162:165], v[186:189], 0
	v_mfma_f32_16x16x32_bf16 v[50:53], v[178:181], v[186:189], 0
	v_mfma_f32_16x16x32_bf16 v[38:41], v[162:165], v[194:197], 0
	v_mfma_f32_16x16x32_bf16 v[34:37], v[178:181], v[194:197], 0
	v_mfma_f32_16x16x32_bf16 v[22:25], v[162:165], v[202:205], 0
	v_mfma_f32_16x16x32_bf16 v[18:21], v[178:181], v[202:205], 0
	v_mfma_f32_16x16x32_bf16 v[6:9], v[162:165], v[210:213], 0
	v_mfma_f32_16x16x32_bf16 v[2:5], v[178:181], v[210:213], 0
	v_mfma_f32_16x16x32_bf16 v[54:57], v[166:169], v[190:193], v[54:57]
	v_mfma_f32_16x16x32_bf16 v[50:53], v[182:185], v[190:193], v[50:53]
	v_mfma_f32_16x16x32_bf16 v[38:41], v[166:169], v[198:201], v[38:41]
	v_mfma_f32_16x16x32_bf16 v[34:37], v[182:185], v[198:201], v[34:37]
	v_mfma_f32_16x16x32_bf16 v[22:25], v[166:169], v[206:209], v[22:25]
	v_mfma_f32_16x16x32_bf16 v[18:21], v[182:185], v[206:209], v[18:21]
	v_mfma_f32_16x16x32_bf16 v[6:9], v[166:169], v[214:217], v[6:9]
	v_mfma_f32_16x16x32_bf16 v[2:5], v[182:185], v[214:217], v[2:5]
	s_setprio 0
	s_barrier
; #define PG8_STAGE(bufoff, gbase, voff) do { _Pragma("unroll") for (int _i = 0; _i < 2; ++_i) \
;         __builtin_amdgcn_global_load_lds((const unsigned*)((const char*)(gbase) + (voff)[_i]), (PG8_LAS unsigned*)(lds + (bufoff) + ldsw + _i * 8192), 16, 0, 0); } while (0)
; #define PG8_LDA(dst, b, h) do { if constexpr (DT != 1) { _Pragma("unroll") for (int m = 0; m < 4; ++m) _Pragma("unroll") for (int k = 0; k < 2; ++k) dst[m][k] = *(const PG8_LAS bf16x8*)(lds + PG8_SA(b, h) + aoff + m * 2048 + k * 1024); } \
;         else { _Pragma("unroll") for (int m = 0; m < 4; ++m) dst##8[m] = ld32(lds + PG8_SA(b, h) + aoff + m * 2048); } } while (0)
; #define PG8_LDB(dst, b, h) do { if constexpr (DT != 1) { _Pragma("unroll") for (int n = 0; n < 2; ++n) _Pragma("unroll") for (int k = 0; k < 2; ++k) dst[n][k] = *(const PG8_LAS bf16x8*)(lds + PG8_SB(b, h) + boff + n * 2048 + k * 1024); } \
;         else { _Pragma("unroll") for (int n = 0; n < 2; ++n) dst##8[n] = ld32(lds + PG8_SB(b, h) + boff + n * 2048); } } while (0)
; #define PG8_WAIT_V(n) asm volatile("s_waitcnt vmcnt(" #n ")" ::: "memory")
; #define PG8_WAIT_L(n) asm volatile("s_waitcnt lgkmcnt(" #n ")" ::: "memory")
; #define PG8_BAR __builtin_amdgcn_s_barrier()
; #define PG8_SCHED __builtin_amdgcn_sched_barrier(0)
;     ...
;             if constexpr (SP2) {
;             PG8_LDB(B0, 0, 0); PG8_LDB(B1, 0, 1); PG8_SCHED; PG8_LDA(At, 0, 0); PG8_STAGE(PG8_SA(1, 1), a1 + hstepA, voffA);
;             PG8_WAIT_V(8); PG8_WAIT_L(0); PG8_BAR; PG8_MMA(0, 0, At, B0); PG8_MMA(0, 1, At, B1); PG8_BAR; PG8_SCHED;
;             PG8_LDA(At, 0, 1); PG8_STAGE(PG8_SB(0, 0), b2, voffB); PG8_STAGE(PG8_SB(0, 1), b2 + hstepB, voffB); PG8_STAGE(PG8_SA(0, 0), a2, voffA);
;             PG8_WAIT_V(8); PG8_WAIT_L(0); PG8_BAR; PG8_MMA(1, 0, At, B0); PG8_MMA(1, 1, At, B1); PG8_BAR; PG8_SCHED;
;             PG8_LDB(B0, 1, 0); PG8_LDB(B1, 1, 1); PG8_SCHED; PG8_LDA(At, 1, 0); PG8_STAGE(PG8_SA(0, 1), a2 + hstepA, voffA);
;             PG8_WAIT_V(8); PG8_WAIT_L(0); PG8_BAR; PG8_MMA(0, 0, At, B0); PG8_MMA(0, 1, At, B1); PG8_BAR; PG8_SCHED;
;             PG8_LDA(At, 1, 1); PG8_STAGE(PG8_SB(1, 0), b3, voffB); PG8_STAGE(PG8_SB(1, 1), b3 + hstepB, voffB); PG8_STAGE(PG8_SA(1, 0), a3, voffA);
;             PG8_WAIT_V(8); PG8_WAIT_L(0); PG8_BAR; PG8_MMA(1, 0, At, B0); PG8_MMA(1, 1, At, B1); PG8_BAR; PG8_SCHED;
	ds_read_b128 v[130:133], v176
	ds_read_b128 v[134:137], v176 offset:1024
	ds_read_b128 v[138:141], v176 offset:2048
	ds_read_b128 v[142:145], v176 offset:3072
	ds_read_b128 v[162:165], v177
	ds_read_b128 v[166:169], v177 offset:1024
	ds_read_b128 v[178:181], v177 offset:2048
	ds_read_b128 v[182:185], v177 offset:3072
	s_add_u32 s38, s38, 0x80000
	s_addc_u32 s39, s39, 0
	s_mov_b32 m0, s51
	ds_read_b128 v[186:189], v175 offset:32768
	ds_read_b128 v[190:193], v175 offset:33792
	ds_read_b128 v[194:197], v175 offset:34816
	ds_read_b128 v[198:201], v175 offset:35840
	ds_read_b128 v[202:205], v175 offset:36864
	ds_read_b128 v[206:209], v175 offset:37888
	ds_read_b128 v[210:213], v175 offset:38912
	global_load_lds_dwordx4 v146, s[38:39]
	s_mov_b32 m0, s52
	ds_read_b128 v[214:217], v175 offset:39936
	global_load_lds_dwordx4 v150, s[38:39]
	s_waitcnt vmcnt(8) lgkmcnt(0)
	s_barrier
	s_setprio 1
	v_mfma_f32_16x16x32_bf16 v[122:125], v[130:133], v[186:189], v[122:125]
	v_mfma_f32_16x16x32_bf16 v[126:129], v[138:141], v[186:189], v[126:129]
	v_mfma_f32_16x16x32_bf16 v[110:113], v[130:133], v[194:197], v[110:113]
	v_mfma_f32_16x16x32_bf16 v[106:109], v[138:141], v[194:197], v[106:109]
	v_mfma_f32_16x16x32_bf16 v[94:97], v[130:133], v[202:205], v[94:97]
	v_mfma_f32_16x16x32_bf16 v[90:93], v[138:141], v[202:205], v[90:93]
	v_mfma_f32_16x16x32_bf16 v[78:81], v[130:133], v[210:213], v[78:81]
	v_mfma_f32_16x16x32_bf16 v[74:77], v[138:141], v[210:213], v[74:77]
	v_mfma_f32_16x16x32_bf16 v[122:125], v[134:137], v[190:193], v[122:125]
	v_mfma_f32_16x16x32_bf16 v[126:129], v[142:145], v[190:193], v[126:129]
	v_mfma_f32_16x16x32_bf16 v[110:113], v[134:137], v[198:201], v[110:113]
	v_mfma_f32_16x16x32_bf16 v[106:109], v[142:145], v[198:201], v[106:109]
	v_mfma_f32_16x16x32_bf16 v[94:97], v[134:137], v[206:209], v[94:97]
	v_mfma_f32_16x16x32_bf16 v[90:93], v[142:145], v[206:209], v[90:93]
	v_mfma_f32_16x16x32_bf16 v[78:81], v[134:137], v[214:217], v[78:81]
	v_mfma_f32_16x16x32_bf16 v[74:77], v[142:145], v[214:217], v[74:77]
	s_setprio 0
	s_setprio 1
	v_mfma_f32_16x16x32_bf16 v[118:121], v[162:165], v[186:189], v[118:121]
	v_mfma_f32_16x16x32_bf16 v[114:117], v[178:181], v[186:189], v[114:117]
	v_mfma_f32_16x16x32_bf16 v[102:105], v[162:165], v[194:197], v[102:105]
	v_mfma_f32_16x16x32_bf16 v[98:101], v[178:181], v[194:197], v[98:101]
	v_mfma_f32_16x16x32_bf16 v[86:89], v[162:165], v[202:205], v[86:89]
	v_mfma_f32_16x16x32_bf16 v[82:85], v[178:181], v[202:205], v[82:85]
	v_mfma_f32_16x16x32_bf16 v[70:73], v[162:165], v[210:213], v[70:73]
	v_mfma_f32_16x16x32_bf16 v[66:69], v[178:181], v[210:213], v[66:69]
	v_mfma_f32_16x16x32_bf16 v[118:121], v[166:169], v[190:193], v[118:121]
	v_mfma_f32_16x16x32_bf16 v[114:117], v[182:185], v[190:193], v[114:117]
	v_mfma_f32_16x16x32_bf16 v[102:105], v[166:169], v[198:201], v[102:105]
	v_mfma_f32_16x16x32_bf16 v[98:101], v[182:185], v[198:201], v[98:101]
	v_mfma_f32_16x16x32_bf16 v[86:89], v[166:169], v[206:209], v[86:89]
	v_mfma_f32_16x16x32_bf16 v[82:85], v[182:185], v[206:209], v[82:85]
	v_mfma_f32_16x16x32_bf16 v[70:73], v[166:169], v[214:217], v[70:73]
	v_mfma_f32_16x16x32_bf16 v[66:69], v[182:185], v[214:217], v[66:69]
	s_setprio 0
	s_barrier
	s_mov_b32 m0, s55
	s_add_u32 s36, s36, 0x80080
	ds_read_b128 v[186:189], v175 offset:49152
	ds_read_b128 v[190:193], v175 offset:50176
	ds_read_b128 v[194:197], v175 offset:51200
	ds_read_b128 v[198:201], v175 offset:52224
	global_load_lds_dwordx4 v148, s[98:99]
	s_mov_b32 m0, s56
	s_addc_u32 s37, s37, 0
	global_load_lds_dwordx4 v152, s[98:99]
	s_mov_b32 m0, s59
	ds_read_b128 v[214:217], v175 offset:56320
	global_load_lds_dwordx4 v148, s[36:37]
	s_mov_b32 m0, s60
	ds_read_b128 v[210:213], v175 offset:55296
	global_load_lds_dwordx4 v152, s[36:37]
	s_mov_b32 m0, s57
	ds_read_b128 v[206:209], v175 offset:54272
	global_load_lds_dwordx4 v146, s[100:101]
	s_mov_b32 m0, s58
	ds_read_b128 v[202:205], v175 offset:53248
	global_load_lds_dwordx4 v150, s[100:101]
	s_waitcnt vmcnt(8) lgkmcnt(0)
	s_barrier
	s_setprio 1
	v_mfma_f32_16x16x32_bf16 v[62:65], v[130:133], v[186:189], v[62:65]
	v_mfma_f32_16x16x32_bf16 v[58:61], v[138:141], v[186:189], v[58:61]
	v_mfma_f32_16x16x32_bf16 v[46:49], v[130:133], v[194:197], v[46:49]
	v_mfma_f32_16x16x32_bf16 v[42:45], v[138:141], v[194:197], v[42:45]
	v_mfma_f32_16x16x32_bf16 v[30:33], v[130:133], v[202:205], v[30:33]
	v_mfma_f32_16x16x32_bf16 v[26:29], v[138:141], v[202:205], v[26:29]
	v_mfma_f32_16x16x32_bf16 v[14:17], v[130:133], v[210:213], v[14:17]
	v_mfma_f32_16x16x32_bf16 v[10:13], v[138:141], v[210:213], v[10:13]
	v_mfma_f32_16x16x32_bf16 v[62:65], v[134:137], v[190:193], v[62:65]
	v_mfma_f32_16x16x32_bf16 v[58:61], v[142:145], v[190:193], v[58:61]
	v_mfma_f32_16x16x32_bf16 v[46:49], v[134:137], v[198:201], v[46:49]
	v_mfma_f32_16x16x32_bf16 v[42:45], v[142:145], v[198:201], v[42:45]
	v_mfma_f32_16x16x32_bf16 v[30:33], v[134:137], v[206:209], v[30:33]
	v_mfma_f32_16x16x32_bf16 v[26:29], v[142:145], v[206:209], v[26:29]
	v_mfma_f32_16x16x32_bf16 v[14:17], v[134:137], v[214:217], v[14:17]
	v_mfma_f32_16x16x32_bf16 v[10:13], v[142:145], v[214:217], v[10:13]
	s_setprio 0
	s_setprio 1
	v_mfma_f32_16x16x32_bf16 v[54:57], v[162:165], v[186:189], v[54:57]
	v_mfma_f32_16x16x32_bf16 v[50:53], v[178:181], v[186:189], v[50:53]
	v_mfma_f32_16x16x32_bf16 v[38:41], v[162:165], v[194:197], v[38:41]
	v_mfma_f32_16x16x32_bf16 v[34:37], v[178:181], v[194:197], v[34:37]
	v_mfma_f32_16x16x32_bf16 v[22:25], v[162:165], v[202:205], v[22:25]
	v_mfma_f32_16x16x32_bf16 v[18:21], v[178:181], v[202:205], v[18:21]
	v_mfma_f32_16x16x32_bf16 v[6:9], v[162:165], v[210:213], v[6:9]
	v_mfma_f32_16x16x32_bf16 v[2:5], v[178:181], v[210:213], v[2:5]
	v_mfma_f32_16x16x32_bf16 v[54:57], v[166:169], v[190:193], v[54:57]
	v_mfma_f32_16x16x32_bf16 v[50:53], v[182:185], v[190:193], v[50:53]
	v_mfma_f32_16x16x32_bf16 v[38:41], v[166:169], v[198:201], v[38:41]
	v_mfma_f32_16x16x32_bf16 v[34:37], v[182:185], v[198:201], v[34:37]
	v_mfma_f32_16x16x32_bf16 v[22:25], v[166:169], v[206:209], v[22:25]
	v_mfma_f32_16x16x32_bf16 v[18:21], v[182:185], v[206:209], v[18:21]
	v_mfma_f32_16x16x32_bf16 v[6:9], v[166:169], v[214:217], v[6:9]
	v_mfma_f32_16x16x32_bf16 v[2:5], v[182:185], v[214:217], v[2:5]
	s_setprio 0
	s_barrier
	s_add_u32 s67, s67, 0x100
	s_addc_u32 s68, s68, 0
	s_add_u32 s34, s34, 0x100
	s_addc_u32 s35, s35, 0
	s_cmp_ge_i32 s69, s54
	s_mov_b32 s36, s69
	s_cbranch_scc0 .LBB0_713
	s_branch .LBB0_714
; #define PG8_STAGE(bufoff, gbase, voff) do { _Pragma("unroll") for (int _i = 0; _i < 2; ++_i) \
;         __builtin_amdgcn_global_load_lds((const unsigned*)((const char*)(gbase) + (voff)[_i]), (PG8_LAS unsigned*)(lds + (bufoff) + ldsw + _i * 8192), 16, 0, 0); } while (0)
; #define PG8_LDA(dst, b, h) do { if constexpr (DT != 1) { _Pragma("unroll") for (int m = 0; m < 4; ++m) _Pragma("unroll") for (int k = 0; k < 2; ++k) dst[m][k] = *(const PG8_LAS bf16x8*)(lds + PG8_SA(b, h) + aoff + m * 2048 + k * 1024); } \
;         else { _Pragma("unroll") for (int m = 0; m < 4; ++m) dst##8[m] = ld32(lds + PG8_SA(b, h) + aoff + m * 2048); } } while (0)
; #define PG8_LDB(dst, b, h) do { if constexpr (DT != 1) { _Pragma("unroll") for (int n = 0; n < 2; ++n) _Pragma("unroll") for (int k = 0; k < 2; ++k) dst[n][k] = *(const PG8_LAS bf16x8*)(lds + PG8_SB(b, h) + boff + n * 2048 + k * 1024); } \
;         else { _Pragma("unroll") for (int n = 0; n < 2; ++n) dst##8[n] = ld32(lds + PG8_SB(b, h) + boff + n * 2048); } } while (0)
; #define PG8_WAIT_V(n) asm volatile("s_waitcnt vmcnt(" #n ")" ::: "memory")
; #define PG8_WAIT_L(n) asm volatile("s_waitcnt lgkmcnt(" #n ")" ::: "memory")
; #define PG8_BAR __builtin_amdgcn_s_barrier()
; #define PG8_SCHED __builtin_amdgcn_sched_barrier(0)
;     ...
;             if constexpr (SP2) {
;             PG8_LDB(B0, 0, 0); PG8_LDB(B1, 0, 1); PG8_SCHED; PG8_LDA(At, 0, 0); PG8_STAGE(PG8_SA(1, 1), a1 + hstepA, voffA);
;             PG8_WAIT_V(8); PG8_WAIT_L(0); PG8_BAR; PG8_MMA(0, 0, At, B0); PG8_MMA(0, 1, At, B1); PG8_BAR; PG8_SCHED;
;             PG8_LDA(At, 0, 1); PG8_STAGE(PG8_SB(0, 0), b2, voffB); PG8_STAGE(PG8_SB(0, 1), b2 + hstepB, voffB); PG8_STAGE(PG8_SA(0, 0), a2, voffA);
;             PG8_WAIT_V(8); PG8_WAIT_L(0); PG8_BAR; PG8_MMA(1, 0, At, B0); PG8_MMA(1, 1, At, B1); PG8_BAR; PG8_SCHED;
;             PG8_LDB(B0, 1, 0); PG8_LDB(B1, 1, 1); PG8_SCHED; PG8_LDA(At, 1, 0); PG8_STAGE(PG8_SA(0, 1), a2 + hstepA, voffA);
;             PG8_WAIT_V(8); PG8_WAIT_L(0); PG8_BAR; PG8_MMA(0, 0, At, B0); PG8_MMA(0, 1, At, B1); PG8_BAR; PG8_SCHED;
;             PG8_LDA(At, 1, 1); PG8_STAGE(PG8_SB(1, 0), b3, voffB); PG8_STAGE(PG8_SB(1, 1), b3 + hstepB, voffB); PG8_STAGE(PG8_SA(1, 0), a3, voffA);
;             PG8_WAIT_V(8); PG8_WAIT_L(0); PG8_BAR; PG8_MMA(1, 0, At, B0); PG8_MMA(1, 1, At, B1); PG8_BAR; PG8_SCHED;
.LBB0_713:
	ds_read_b128 v[130:133], v173
	ds_read_b128 v[134:137], v173 offset:1024
	ds_read_b128 v[138:141], v173 offset:2048
	ds_read_b128 v[142:145], v173 offset:3072
	ds_read_b128 v[162:165], v174
	ds_read_b128 v[166:169], v174 offset:1024
	ds_read_b128 v[178:181], v174 offset:2048
	ds_read_b128 v[182:185], v174 offset:3072
	s_add_i32 s69, s36, 2
	s_add_u32 s37, s34, 0xfff80080
	s_addc_u32 s38, s35, -1
	s_cmp_eq_u32 s61, s36
	s_cselect_b32 s36, s66, s67
	s_cselect_b32 s39, s23, s38
	s_cselect_b32 s38, s25, s37
	s_cselect_b32 s37, s65, s68
	s_add_i32 m0, s49, 0xc000
	ds_read_b128 v[186:189], v175
	ds_read_b128 v[190:193], v175 offset:1024
	ds_read_b128 v[194:197], v175 offset:2048
	ds_read_b128 v[198:201], v175 offset:3072
	ds_read_b128 v[202:205], v175 offset:4096
	ds_read_b128 v[206:209], v175 offset:5120
	ds_read_b128 v[210:213], v175 offset:6144
	ds_read_b128 v[214:217], v175 offset:7168
	global_load_lds_dwordx4 v156, s[34:35]
	s_add_i32 m0, s49, 0xe000
	s_nop 0
	global_load_lds_dwordx4 v154, s[34:35]
	s_waitcnt vmcnt(8) lgkmcnt(0)
	s_barrier
	s_setprio 1
	v_mfma_f32_16x16x32_bf16 v[122:125], v[130:133], v[186:189], v[122:125]
	v_mfma_f32_16x16x32_bf16 v[126:129], v[138:141], v[186:189], v[126:129]
	v_mfma_f32_16x16x32_bf16 v[110:113], v[130:133], v[194:197], v[110:113]
	v_mfma_f32_16x16x32_bf16 v[106:109], v[138:141], v[194:197], v[106:109]
	v_mfma_f32_16x16x32_bf16 v[94:97], v[130:133], v[202:205], v[94:97]
	v_mfma_f32_16x16x32_bf16 v[90:93], v[138:141], v[202:205], v[90:93]
	v_mfma_f32_16x16x32_bf16 v[78:81], v[130:133], v[210:213], v[78:81]
	v_mfma_f32_16x16x32_bf16 v[74:77], v[138:141], v[210:213], v[74:77]
	v_mfma_f32_16x16x32_bf16 v[122:125], v[134:137], v[190:193], v[122:125]
	v_mfma_f32_16x16x32_bf16 v[126:129], v[142:145], v[190:193], v[126:129]
	v_mfma_f32_16x16x32_bf16 v[110:113], v[134:137], v[198:201], v[110:113]
	v_mfma_f32_16x16x32_bf16 v[106:109], v[142:145], v[198:201], v[106:109]
	v_mfma_f32_16x16x32_bf16 v[94:97], v[134:137], v[206:209], v[94:97]
	v_mfma_f32_16x16x32_bf16 v[90:93], v[142:145], v[206:209], v[90:93]
	v_mfma_f32_16x16x32_bf16 v[78:81], v[134:137], v[214:217], v[78:81]
	v_mfma_f32_16x16x32_bf16 v[74:77], v[142:145], v[214:217], v[74:77]
	s_setprio 0
	s_setprio 1
	v_mfma_f32_16x16x32_bf16 v[118:121], v[162:165], v[186:189], v[118:121]
	v_mfma_f32_16x16x32_bf16 v[114:117], v[178:181], v[186:189], v[114:117]
	v_mfma_f32_16x16x32_bf16 v[102:105], v[162:165], v[194:197], v[102:105]
	v_mfma_f32_16x16x32_bf16 v[98:101], v[178:181], v[194:197], v[98:101]
	v_mfma_f32_16x16x32_bf16 v[86:89], v[162:165], v[202:205], v[86:89]
	v_mfma_f32_16x16x32_bf16 v[82:85], v[178:181], v[202:205], v[82:85]
	v_mfma_f32_16x16x32_bf16 v[70:73], v[162:165], v[210:213], v[70:73]
	v_mfma_f32_16x16x32_bf16 v[66:69], v[178:181], v[210:213], v[66:69]
	v_mfma_f32_16x16x32_bf16 v[118:121], v[166:169], v[190:193], v[118:121]
	v_mfma_f32_16x16x32_bf16 v[114:117], v[182:185], v[190:193], v[114:117]
	v_mfma_f32_16x16x32_bf16 v[102:105], v[166:169], v[198:201], v[102:105]
	v_mfma_f32_16x16x32_bf16 v[98:101], v[182:185], v[198:201], v[98:101]
	v_mfma_f32_16x16x32_bf16 v[86:89], v[166:169], v[206:209], v[86:89]
	v_mfma_f32_16x16x32_bf16 v[82:85], v[182:185], v[206:209], v[82:85]
	v_mfma_f32_16x16x32_bf16 v[70:73], v[166:169], v[214:217], v[70:73]
	v_mfma_f32_16x16x32_bf16 v[66:69], v[182:185], v[214:217], v[66:69]
	s_setprio 0
	s_barrier
	s_mov_b32 m0, s31
	s_add_u32 s98, s36, 0x80
	s_addc_u32 s99, s37, 0
	s_add_u32 s70, s36, 0x80000
	ds_read_b128 v[186:189], v175 offset:16384
	ds_read_b128 v[190:193], v175 offset:17408
	ds_read_b128 v[194:197], v175 offset:18432
	ds_read_b128 v[198:201], v175 offset:19456
	global_load_lds_dwordx4 v148, s[36:37]
	s_mov_b32 m0, s46
	s_addc_u32 s71, s37, 0
	global_load_lds_dwordx4 v152, s[36:37]
	s_mov_b32 m0, s47
	ds_read_b128 v[214:217], v175 offset:23552
	global_load_lds_dwordx4 v148, s[70:71]
	s_mov_b32 m0, s48
	ds_read_b128 v[210:213], v175 offset:22528
	global_load_lds_dwordx4 v152, s[70:71]
	s_add_u32 s100, s38, 0x80
	s_addc_u32 s101, s39, 0
	s_mov_b32 m0, s49
	ds_read_b128 v[206:209], v175 offset:21504
	global_load_lds_dwordx4 v146, s[38:39]
	s_mov_b32 m0, s50
	ds_read_b128 v[202:205], v175 offset:20480
	global_load_lds_dwordx4 v150, s[38:39]
	s_waitcnt vmcnt(8) lgkmcnt(0)
	s_barrier
	s_setprio 1
	v_mfma_f32_16x16x32_bf16 v[62:65], v[130:133], v[186:189], v[62:65]
	v_mfma_f32_16x16x32_bf16 v[58:61], v[138:141], v[186:189], v[58:61]
	v_mfma_f32_16x16x32_bf16 v[46:49], v[130:133], v[194:197], v[46:49]
	v_mfma_f32_16x16x32_bf16 v[42:45], v[138:141], v[194:197], v[42:45]
	v_mfma_f32_16x16x32_bf16 v[30:33], v[130:133], v[202:205], v[30:33]
	v_mfma_f32_16x16x32_bf16 v[26:29], v[138:141], v[202:205], v[26:29]
	v_mfma_f32_16x16x32_bf16 v[14:17], v[130:133], v[210:213], v[14:17]
	v_mfma_f32_16x16x32_bf16 v[10:13], v[138:141], v[210:213], v[10:13]
	v_mfma_f32_16x16x32_bf16 v[62:65], v[134:137], v[190:193], v[62:65]
	v_mfma_f32_16x16x32_bf16 v[58:61], v[142:145], v[190:193], v[58:61]
	v_mfma_f32_16x16x32_bf16 v[46:49], v[134:137], v[198:201], v[46:49]
	v_mfma_f32_16x16x32_bf16 v[42:45], v[142:145], v[198:201], v[42:45]
	v_mfma_f32_16x16x32_bf16 v[30:33], v[134:137], v[206:209], v[30:33]
	v_mfma_f32_16x16x32_bf16 v[26:29], v[142:145], v[206:209], v[26:29]
	v_mfma_f32_16x16x32_bf16 v[14:17], v[134:137], v[214:217], v[14:17]
	v_mfma_f32_16x16x32_bf16 v[10:13], v[142:145], v[214:217], v[10:13]
	s_setprio 0
	s_setprio 1
	v_mfma_f32_16x16x32_bf16 v[54:57], v[162:165], v[186:189], v[54:57]
	v_mfma_f32_16x16x32_bf16 v[50:53], v[178:181], v[186:189], v[50:53]
	v_mfma_f32_16x16x32_bf16 v[38:41], v[162:165], v[194:197], v[38:41]
	v_mfma_f32_16x16x32_bf16 v[34:37], v[178:181], v[194:197], v[34:37]
	v_mfma_f32_16x16x32_bf16 v[22:25], v[162:165], v[202:205], v[22:25]
	v_mfma_f32_16x16x32_bf16 v[18:21], v[178:181], v[202:205], v[18:21]
	v_mfma_f32_16x16x32_bf16 v[6:9], v[162:165], v[210:213], v[6:9]
	v_mfma_f32_16x16x32_bf16 v[2:5], v[178:181], v[210:213], v[2:5]
	v_mfma_f32_16x16x32_bf16 v[54:57], v[166:169], v[190:193], v[54:57]
	v_mfma_f32_16x16x32_bf16 v[50:53], v[182:185], v[190:193], v[50:53]
	v_mfma_f32_16x16x32_bf16 v[38:41], v[166:169], v[198:201], v[38:41]
	v_mfma_f32_16x16x32_bf16 v[34:37], v[182:185], v[198:201], v[34:37]
	v_mfma_f32_16x16x32_bf16 v[22:25], v[166:169], v[206:209], v[22:25]
	v_mfma_f32_16x16x32_bf16 v[18:21], v[182:185], v[206:209], v[18:21]
	v_mfma_f32_16x16x32_bf16 v[6:9], v[166:169], v[214:217], v[6:9]
	v_mfma_f32_16x16x32_bf16 v[2:5], v[182:185], v[214:217], v[2:5]
	s_setprio 0
	s_barrier
; #define PG8_STAGE(bufoff, gbase, voff) do { _Pragma("unroll") for (int _i = 0; _i < 2; ++_i) \
;         __builtin_amdgcn_global_load_lds((const unsigned*)((const char*)(gbase) + (voff)[_i]), (PG8_LAS unsigned*)(lds + (bufoff) + ldsw + _i * 8192), 16, 0, 0); } while (0)
; #define PG8_LDA(dst, b, h) do { if constexpr (DT != 1) { _Pragma("unroll") for (int m = 0; m < 4; ++m) _Pragma("unroll") for (int k = 0; k < 2; ++k) dst[m][k] = *(const PG8_LAS bf16x8*)(lds + PG8_SA(b, h) + aoff + m * 2048 + k * 1024); } \
;         else { _Pragma("unroll") for (int m = 0; m < 4; ++m) dst##8[m] = ld32(lds + PG8_SA(b, h) + aoff + m * 2048); } } while (0)
; #define PG8_LDB(dst, b, h) do { if constexpr (DT != 1) { _Pragma("unroll") for (int n = 0; n < 2; ++n) _Pragma("unroll") for (int k = 0; k < 2; ++k) dst[n][k] = *(const PG8_LAS bf16x8*)(lds + PG8_SB(b, h) + boff + n * 2048 + k * 1024); } \
;         else { _Pragma("unroll") for (int n = 0; n < 2; ++n) dst##8[n] = ld32(lds + PG8_SB(b, h) + boff + n * 2048); } } while (0)
; #define PG8_WAIT_V(n) asm volatile("s_waitcnt vmcnt(" #n ")" ::: "memory")
; #define PG8_WAIT_L(n) asm volatile("s_waitcnt lgkmcnt(" #n ")" ::: "memory")
; #define PG8_BAR __builtin_amdgcn_s_barrier()
; #define PG8_SCHED __builtin_amdgcn_sched_barrier(0)
;     ...
;             if constexpr (SP2) {
;             PG8_LDB(B0, 0, 0); PG8_LDB(B1, 0, 1); PG8_SCHED; PG8_LDA(At, 0, 0); PG8_STAGE(PG8_SA(1, 1), a1 + hstepA, voffA);
;             PG8_WAIT_V(8); PG8_WAIT_L(0); PG8_BAR; PG8_MMA(0, 0, At, B0); PG8_MMA(0, 1, At, B1); PG8_BAR; PG8_SCHED;
;             PG8_LDA(At, 0, 1); PG8_STAGE(PG8_SB(0, 0), b2, voffB); PG8_STAGE(PG8_SB(0, 1), b2 + hstepB, voffB); PG8_STAGE(PG8_SA(0, 0), a2, voffA);
;             PG8_WAIT_V(8); PG8_WAIT_L(0); PG8_BAR; PG8_MMA(1, 0, At, B0); PG8_MMA(1, 1, At, B1); PG8_BAR; PG8_SCHED;
;             PG8_LDB(B0, 1, 0); PG8_LDB(B1, 1, 1); PG8_SCHED; PG8_LDA(At, 1, 0); PG8_STAGE(PG8_SA(0, 1), a2 + hstepA, voffA);
;             PG8_WAIT_V(8); PG8_WAIT_L(0); PG8_BAR; PG8_MMA(0, 0, At, B0); PG8_MMA(0, 1, At, B1); PG8_BAR; PG8_SCHED;
;             PG8_LDA(At, 1, 1); PG8_STAGE(PG8_SB(1, 0), b3, voffB); PG8_STAGE(PG8_SB(1, 1), b3 + hstepB, voffB); PG8_STAGE(PG8_SA(1, 0), a3, voffA);
;             PG8_WAIT_V(8); PG8_WAIT_L(0); PG8_BAR; PG8_MMA(1, 0, At, B0); PG8_MMA(1, 1, At, B1); PG8_BAR; PG8_SCHED;
	ds_read_b128 v[130:133], v176
	ds_read_b128 v[134:137], v176 offset:1024
	ds_read_b128 v[138:141], v176 offset:2048
	ds_read_b128 v[142:145], v176 offset:3072
	ds_read_b128 v[162:165], v177
	ds_read_b128 v[166:169], v177 offset:1024
	ds_read_b128 v[178:181], v177 offset:2048
	ds_read_b128 v[182:185], v177 offset:3072
	s_add_u32 s38, s38, 0x80000
	s_addc_u32 s39, s39, 0
	s_mov_b32 m0, s51
	ds_read_b128 v[186:189], v175 offset:32768
	ds_read_b128 v[190:193], v175 offset:33792
	ds_read_b128 v[194:197], v175 offset:34816
	ds_read_b128 v[198:201], v175 offset:35840
	ds_read_b128 v[202:205], v175 offset:36864
	ds_read_b128 v[206:209], v175 offset:37888
	ds_read_b128 v[210:213], v175 offset:38912
	global_load_lds_dwordx4 v146, s[38:39]
	s_mov_b32 m0, s52
	ds_read_b128 v[214:217], v175 offset:39936
	global_load_lds_dwordx4 v150, s[38:39]
	s_waitcnt vmcnt(8) lgkmcnt(0)
	s_barrier
	s_setprio 1
	v_mfma_f32_16x16x32_bf16 v[122:125], v[130:133], v[186:189], v[122:125]
	v_mfma_f32_16x16x32_bf16 v[126:129], v[138:141], v[186:189], v[126:129]
	v_mfma_f32_16x16x32_bf16 v[110:113], v[130:133], v[194:197], v[110:113]
	v_mfma_f32_16x16x32_bf16 v[106:109], v[138:141], v[194:197], v[106:109]
	v_mfma_f32_16x16x32_bf16 v[94:97], v[130:133], v[202:205], v[94:97]
	v_mfma_f32_16x16x32_bf16 v[90:93], v[138:141], v[202:205], v[90:93]
	v_mfma_f32_16x16x32_bf16 v[78:81], v[130:133], v[210:213], v[78:81]
	v_mfma_f32_16x16x32_bf16 v[74:77], v[138:141], v[210:213], v[74:77]
	v_mfma_f32_16x16x32_bf16 v[122:125], v[134:137], v[190:193], v[122:125]
	v_mfma_f32_16x16x32_bf16 v[126:129], v[142:145], v[190:193], v[126:129]
	v_mfma_f32_16x16x32_bf16 v[110:113], v[134:137], v[198:201], v[110:113]
	v_mfma_f32_16x16x32_bf16 v[106:109], v[142:145], v[198:201], v[106:109]
	v_mfma_f32_16x16x32_bf16 v[94:97], v[134:137], v[206:209], v[94:97]
	v_mfma_f32_16x16x32_bf16 v[90:93], v[142:145], v[206:209], v[90:93]
	v_mfma_f32_16x16x32_bf16 v[78:81], v[134:137], v[214:217], v[78:81]
	v_mfma_f32_16x16x32_bf16 v[74:77], v[142:145], v[214:217], v[74:77]
	s_setprio 0
	s_setprio 1
	v_mfma_f32_16x16x32_bf16 v[118:121], v[162:165], v[186:189], v[118:121]
	v_mfma_f32_16x16x32_bf16 v[114:117], v[178:181], v[186:189], v[114:117]
	v_mfma_f32_16x16x32_bf16 v[102:105], v[162:165], v[194:197], v[102:105]
	v_mfma_f32_16x16x32_bf16 v[98:101], v[178:181], v[194:197], v[98:101]
	v_mfma_f32_16x16x32_bf16 v[86:89], v[162:165], v[202:205], v[86:89]
	v_mfma_f32_16x16x32_bf16 v[82:85], v[178:181], v[202:205], v[82:85]
	v_mfma_f32_16x16x32_bf16 v[70:73], v[162:165], v[210:213], v[70:73]
	v_mfma_f32_16x16x32_bf16 v[66:69], v[178:181], v[210:213], v[66:69]
	v_mfma_f32_16x16x32_bf16 v[118:121], v[166:169], v[190:193], v[118:121]
	v_mfma_f32_16x16x32_bf16 v[114:117], v[182:185], v[190:193], v[114:117]
	v_mfma_f32_16x16x32_bf16 v[102:105], v[166:169], v[198:201], v[102:105]
	v_mfma_f32_16x16x32_bf16 v[98:101], v[182:185], v[198:201], v[98:101]
	v_mfma_f32_16x16x32_bf16 v[86:89], v[166:169], v[206:209], v[86:89]
	v_mfma_f32_16x16x32_bf16 v[82:85], v[182:185], v[206:209], v[82:85]
	v_mfma_f32_16x16x32_bf16 v[70:73], v[166:169], v[214:217], v[70:73]
	v_mfma_f32_16x16x32_bf16 v[66:69], v[182:185], v[214:217], v[66:69]
	s_setprio 0
	s_barrier
	s_mov_b32 m0, s55
	s_add_u32 s36, s36, 0x80080
	ds_read_b128 v[186:189], v175 offset:49152
	ds_read_b128 v[190:193], v175 offset:50176
	ds_read_b128 v[194:197], v175 offset:51200
	ds_read_b128 v[198:201], v175 offset:52224
	global_load_lds_dwordx4 v148, s[98:99]
	s_mov_b32 m0, s56
	s_addc_u32 s37, s37, 0
	global_load_lds_dwordx4 v152, s[98:99]
	s_mov_b32 m0, s59
	ds_read_b128 v[214:217], v175 offset:56320
	global_load_lds_dwordx4 v148, s[36:37]
	s_mov_b32 m0, s60
	ds_read_b128 v[210:213], v175 offset:55296
	global_load_lds_dwordx4 v152, s[36:37]
	s_mov_b32 m0, s57
	ds_read_b128 v[206:209], v175 offset:54272
	global_load_lds_dwordx4 v146, s[100:101]
	s_mov_b32 m0, s58
	ds_read_b128 v[202:205], v175 offset:53248
	global_load_lds_dwordx4 v150, s[100:101]
	s_waitcnt vmcnt(8) lgkmcnt(0)
	s_barrier
	s_setprio 1
	v_mfma_f32_16x16x32_bf16 v[62:65], v[130:133], v[186:189], v[62:65]
	v_mfma_f32_16x16x32_bf16 v[58:61], v[138:141], v[186:189], v[58:61]
	v_mfma_f32_16x16x32_bf16 v[46:49], v[130:133], v[194:197], v[46:49]
	v_mfma_f32_16x16x32_bf16 v[42:45], v[138:141], v[194:197], v[42:45]
	v_mfma_f32_16x16x32_bf16 v[30:33], v[130:133], v[202:205], v[30:33]
	v_mfma_f32_16x16x32_bf16 v[26:29], v[138:141], v[202:205], v[26:29]
	v_mfma_f32_16x16x32_bf16 v[14:17], v[130:133], v[210:213], v[14:17]
	v_mfma_f32_16x16x32_bf16 v[10:13], v[138:141], v[210:213], v[10:13]
	v_mfma_f32_16x16x32_bf16 v[62:65], v[134:137], v[190:193], v[62:65]
	v_mfma_f32_16x16x32_bf16 v[58:61], v[142:145], v[190:193], v[58:61]
	v_mfma_f32_16x16x32_bf16 v[46:49], v[134:137], v[198:201], v[46:49]
	v_mfma_f32_16x16x32_bf16 v[42:45], v[142:145], v[198:201], v[42:45]
	v_mfma_f32_16x16x32_bf16 v[30:33], v[134:137], v[206:209], v[30:33]
	v_mfma_f32_16x16x32_bf16 v[26:29], v[142:145], v[206:209], v[26:29]
	v_mfma_f32_16x16x32_bf16 v[14:17], v[134:137], v[214:217], v[14:17]
	v_mfma_f32_16x16x32_bf16 v[10:13], v[142:145], v[214:217], v[10:13]
	s_setprio 0
	s_setprio 1
	v_mfma_f32_16x16x32_bf16 v[54:57], v[162:165], v[186:189], v[54:57]
	v_mfma_f32_16x16x32_bf16 v[50:53], v[178:181], v[186:189], v[50:53]
	v_mfma_f32_16x16x32_bf16 v[38:41], v[162:165], v[194:197], v[38:41]
	v_mfma_f32_16x16x32_bf16 v[34:37], v[178:181], v[194:197], v[34:37]
	v_mfma_f32_16x16x32_bf16 v[22:25], v[162:165], v[202:205], v[22:25]
	v_mfma_f32_16x16x32_bf16 v[18:21], v[178:181], v[202:205], v[18:21]
	v_mfma_f32_16x16x32_bf16 v[6:9], v[162:165], v[210:213], v[6:9]
	v_mfma_f32_16x16x32_bf16 v[2:5], v[178:181], v[210:213], v[2:5]
	v_mfma_f32_16x16x32_bf16 v[54:57], v[166:169], v[190:193], v[54:57]
	v_mfma_f32_16x16x32_bf16 v[50:53], v[182:185], v[190:193], v[50:53]
	v_mfma_f32_16x16x32_bf16 v[38:41], v[166:169], v[198:201], v[38:41]
	v_mfma_f32_16x16x32_bf16 v[34:37], v[182:185], v[198:201], v[34:37]
	v_mfma_f32_16x16x32_bf16 v[22:25], v[166:169], v[206:209], v[22:25]
	v_mfma_f32_16x16x32_bf16 v[18:21], v[182:185], v[206:209], v[18:21]
	v_mfma_f32_16x16x32_bf16 v[6:9], v[166:169], v[214:217], v[6:9]
	v_mfma_f32_16x16x32_bf16 v[2:5], v[182:185], v[214:217], v[2:5]
	s_setprio 0
	s_barrier
	s_add_u32 s67, s67, 0x100
	s_addc_u32 s68, s68, 0
	s_add_u32 s34, s34, 0x100
	s_addc_u32 s35, s35, 0
	s_cmp_ge_i32 s69, s54
	s_mov_b32 s36, s69
	s_cbranch_scc0 .LBB0_713

; #define PG8_STAGE(bufoff, gbase, voff) do { _Pragma("unroll") for (int _i = 0; _i < 2; ++_i) \
;         __builtin_amdgcn_global_load_lds((const unsigned*)((const char*)(gbase) + (voff)[_i]), (PG8_LAS unsigned*)(lds + (bufoff) + ldsw + _i * 8192), 16, 0, 0); } while (0)
; #define PG8_LDA(dst, b, h) do { if constexpr (DT != 1) { _Pragma("unroll") for (int m = 0; m < 4; ++m) _Pragma("unroll") for (int k = 0; k < 2; ++k) dst[m][k] = *(const PG8_LAS bf16x8*)(lds + PG8_SA(b, h) + aoff + m * 2048 + k * 1024); } \
;         else { _Pragma("unroll") for (int m = 0; m < 4; ++m) dst##8[m] = ld32(lds + PG8_SA(b, h) + aoff + m * 2048); } } while (0)
; #define PG8_WAIT_V(n) asm volatile("s_waitcnt vmcnt(" #n ")" ::: "memory")
; #define PG8_WAIT_L(n) asm volatile("s_waitcnt lgkmcnt(" #n ")" ::: "memory")
; #define PG8_BAR __builtin_amdgcn_s_barrier()
; #define PG8_SCHED __builtin_amdgcn_sched_barrier(0)
;     ...
;         for (int t = 0; t < nt; t += 2) {
;             const bool last = (t == nt - 2);
;             const char* a1 = cA + (size_t)(t + 1) * kstep;
;             const char* a2 = last ? nA : cA + (size_t)(t + 2) * kstep; const char* b2 = last ? nB : cB + (size_t)(t + 2) * kstep;
;             const char* a3 = a2 + kstep; const char* b3 = b2 + kstep;
;             if (last && has_next) S.a_ready(nxt);
;             if constexpr (SP2) {
;             PG8_LDB(B0, 0, 0); PG8_LDB(B1, 0, 1); PG8_SCHED; PG8_LDA(At, 0, 0); PG8_STAGE(PG8_SA(1, 1), a1 + hstepA, voffA);
;             PG8_WAIT_V(8); PG8_WAIT_L(0); PG8_BAR; PG8_MMA(0, 0, At, B0); PG8_MMA(0, 1, At, B1); PG8_BAR; PG8_SCHED;
;             PG8_LDA(At, 0, 1); PG8_STAGE(PG8_SB(0, 0), b2, voffB); PG8_STAGE(PG8_SB(0, 1), b2 + hstepB, voffB); PG8_STAGE(PG8_SA(0, 0), a2, voffA);
;             PG8_WAIT_V(8); PG8_WAIT_L(0); PG8_BAR; PG8_MMA(1, 0, At, B0); PG8_MMA(1, 1, At, B1); PG8_BAR; PG8_SCHED;
;             PG8_LDB(B0, 1, 0); PG8_LDB(B1, 1, 1); PG8_SCHED; PG8_LDA(At, 1, 0); PG8_STAGE(PG8_SA(0, 1), a2 + hstepA, voffA);
;             PG8_WAIT_V(8); PG8_WAIT_L(0); PG8_BAR; PG8_MMA(0, 0, At, B0); PG8_MMA(0, 1, At, B1); PG8_BAR; PG8_SCHED;
;             PG8_LDA(At, 1, 1); PG8_STAGE(PG8_SB(1, 0), b3, voffB); PG8_STAGE(PG8_SB(1, 1), b3 + hstepB, voffB); PG8_STAGE(PG8_SA(1, 0), a3, voffA);
;             PG8_WAIT_V(8); PG8_WAIT_L(0); PG8_BAR; PG8_MMA(1, 0, At, B0); PG8_MMA(1, 1, At, B1); PG8_BAR; PG8_SCHED;
.Lzt_2:
	s_cbranch_vccnz .LBB0_924
	s_add_u32 s65, s28, 0x100
	s_addc_u32 s66, s29, 0
	s_mov_b32 s30, 0
	ds_read_b128 v[146:149], v173
	ds_read_b128 v[150:153], v173 offset:1024
	ds_read_b128 v[154:157], v173 offset:2048
	ds_read_b128 v[158:161], v173 offset:3072
	ds_read_b128 v[162:165], v174
	ds_read_b128 v[166:169], v174 offset:1024
	ds_read_b128 v[178:181], v174 offset:2048
	ds_read_b128 v[182:185], v174 offset:3072
	s_add_i32 s67, s30, 2
	s_add_u32 s28, s26, 0x100
	s_addc_u32 s29, s27, 0
	s_cmp_eq_u32 s58, s30
	s_cselect_b32 s30, s24, s65
	s_cselect_b32 s35, s3, s29
	s_cselect_b32 s34, s2, s28
	s_cselect_b32 s31, s25, s66
	v_lshl_add_u64 v[170:171], s[26:27], 0, v[140:141]
	s_add_i32 m0, s46, 0xc000
	ds_read_b128 v[186:189], v175
	ds_read_b128 v[190:193], v175 offset:1024
	ds_read_b128 v[194:197], v175 offset:2048
	ds_read_b128 v[198:201], v175 offset:3072
	ds_read_b128 v[202:205], v175 offset:4096
	ds_read_b128 v[206:209], v175 offset:5120
	ds_read_b128 v[210:213], v175 offset:6144
	ds_read_b128 v[214:217], v175 offset:7168
	global_load_lds_dwordx4 v[170:171], off
	v_lshl_add_u64 v[170:171], s[26:27], 0, v[138:139]
	s_add_i32 m0, s46, 0xe000
	s_nop 0
	global_load_lds_dwordx4 v[170:171], off
	s_waitcnt vmcnt(8) lgkmcnt(0)
	s_barrier
	s_setprio 1
	v_mfma_f32_16x16x32_bf16 v[126:129], v[146:149], v[186:189], 0
	v_mfma_f32_16x16x32_bf16 v[122:125], v[154:157], v[186:189], 0
	v_mfma_f32_16x16x32_bf16 v[118:121], v[146:149], v[194:197], 0
	v_mfma_f32_16x16x32_bf16 v[114:117], v[154:157], v[194:197], 0
	v_mfma_f32_16x16x32_bf16 v[106:109], v[146:149], v[202:205], 0
	v_mfma_f32_16x16x32_bf16 v[98:101], v[154:157], v[202:205], 0
	v_mfma_f32_16x16x32_bf16 v[90:93], v[146:149], v[210:213], 0
	v_mfma_f32_16x16x32_bf16 v[82:85], v[154:157], v[210:213], 0
	v_mfma_f32_16x16x32_bf16 v[126:129], v[150:153], v[190:193], v[126:129]
	v_mfma_f32_16x16x32_bf16 v[122:125], v[158:161], v[190:193], v[122:125]
	v_mfma_f32_16x16x32_bf16 v[118:121], v[150:153], v[198:201], v[118:121]
	v_mfma_f32_16x16x32_bf16 v[114:117], v[158:161], v[198:201], v[114:117]
	v_mfma_f32_16x16x32_bf16 v[106:109], v[150:153], v[206:209], v[106:109]
	v_mfma_f32_16x16x32_bf16 v[98:101], v[158:161], v[206:209], v[98:101]
	v_mfma_f32_16x16x32_bf16 v[90:93], v[150:153], v[214:217], v[90:93]
	v_mfma_f32_16x16x32_bf16 v[82:85], v[158:161], v[214:217], v[82:85]
	s_setprio 0
	s_setprio 1
	v_mfma_f32_16x16x32_bf16 v[110:113], v[162:165], v[186:189], 0
	v_mfma_f32_16x16x32_bf16 v[102:105], v[178:181], v[186:189], 0
	v_mfma_f32_16x16x32_bf16 v[94:97], v[162:165], v[194:197], 0
	v_mfma_f32_16x16x32_bf16 v[86:89], v[178:181], v[194:197], 0
	v_mfma_f32_16x16x32_bf16 v[78:81], v[162:165], v[202:205], 0
	v_mfma_f32_16x16x32_bf16 v[74:77], v[178:181], v[202:205], 0
	v_mfma_f32_16x16x32_bf16 v[70:73], v[162:165], v[210:213], 0
	v_mfma_f32_16x16x32_bf16 v[66:69], v[178:181], v[210:213], 0
	v_mfma_f32_16x16x32_bf16 v[110:113], v[166:169], v[190:193], v[110:113]
	v_mfma_f32_16x16x32_bf16 v[102:105], v[182:185], v[190:193], v[102:105]
	v_mfma_f32_16x16x32_bf16 v[94:97], v[166:169], v[198:201], v[94:97]
	v_mfma_f32_16x16x32_bf16 v[86:89], v[182:185], v[198:201], v[86:89]
	v_mfma_f32_16x16x32_bf16 v[78:81], v[166:169], v[206:209], v[78:81]
	v_mfma_f32_16x16x32_bf16 v[74:77], v[182:185], v[206:209], v[74:77]
	v_mfma_f32_16x16x32_bf16 v[70:73], v[166:169], v[214:217], v[70:73]
	v_mfma_f32_16x16x32_bf16 v[66:69], v[182:185], v[214:217], v[66:69]
	s_setprio 0
	s_barrier
	s_mov_b32 m0, s42
	s_add_u32 s98, s30, 0x80
	s_addc_u32 s99, s31, 0
	s_add_u32 s26, s30, 0x160000
	ds_read_b128 v[186:189], v175 offset:16384
	ds_read_b128 v[190:193], v175 offset:17408
	ds_read_b128 v[194:197], v175 offset:18432
	ds_read_b128 v[198:201], v175 offset:19456
	global_load_lds_dwordx4 v132, s[30:31]
	s_mov_b32 m0, s43
	s_addc_u32 s27, s31, 0
	global_load_lds_dwordx4 v136, s[30:31]
	s_mov_b32 m0, s44
	ds_read_b128 v[214:217], v175 offset:23552
	global_load_lds_dwordx4 v132, s[26:27]
	s_mov_b32 m0, s45
	ds_read_b128 v[210:213], v175 offset:22528
	global_load_lds_dwordx4 v136, s[26:27]
	s_add_u32 s100, s34, 0x80
	s_addc_u32 s101, s35, 0
	s_mov_b32 m0, s46
	ds_read_b128 v[206:209], v175 offset:21504
	global_load_lds_dwordx4 v130, s[34:35]
	s_mov_b32 m0, s47
	ds_read_b128 v[202:205], v175 offset:20480
	global_load_lds_dwordx4 v134, s[34:35]
	s_waitcnt vmcnt(8) lgkmcnt(0)
	s_barrier
	s_setprio 1
	v_mfma_f32_16x16x32_bf16 v[62:65], v[146:149], v[186:189], 0
	v_mfma_f32_16x16x32_bf16 v[58:61], v[154:157], v[186:189], 0
	v_mfma_f32_16x16x32_bf16 v[54:57], v[146:149], v[194:197], 0
	v_mfma_f32_16x16x32_bf16 v[50:53], v[154:157], v[194:197], 0
	v_mfma_f32_16x16x32_bf16 v[42:45], v[146:149], v[202:205], 0
	v_mfma_f32_16x16x32_bf16 v[34:37], v[154:157], v[202:205], 0
	v_mfma_f32_16x16x32_bf16 v[26:29], v[146:149], v[210:213], 0
	v_mfma_f32_16x16x32_bf16 v[18:21], v[154:157], v[210:213], 0
	v_mfma_f32_16x16x32_bf16 v[62:65], v[150:153], v[190:193], v[62:65]
	v_mfma_f32_16x16x32_bf16 v[58:61], v[158:161], v[190:193], v[58:61]
	v_mfma_f32_16x16x32_bf16 v[54:57], v[150:153], v[198:201], v[54:57]
	v_mfma_f32_16x16x32_bf16 v[50:53], v[158:161], v[198:201], v[50:53]
	v_mfma_f32_16x16x32_bf16 v[42:45], v[150:153], v[206:209], v[42:45]
	v_mfma_f32_16x16x32_bf16 v[34:37], v[158:161], v[206:209], v[34:37]
	v_mfma_f32_16x16x32_bf16 v[26:29], v[150:153], v[214:217], v[26:29]
	v_mfma_f32_16x16x32_bf16 v[18:21], v[158:161], v[214:217], v[18:21]
	s_setprio 0
	s_setprio 1
	v_mfma_f32_16x16x32_bf16 v[46:49], v[162:165], v[186:189], 0
	v_mfma_f32_16x16x32_bf16 v[38:41], v[178:181], v[186:189], 0
	v_mfma_f32_16x16x32_bf16 v[30:33], v[162:165], v[194:197], 0
	v_mfma_f32_16x16x32_bf16 v[22:25], v[178:181], v[194:197], 0
	v_mfma_f32_16x16x32_bf16 v[14:17], v[162:165], v[202:205], 0
	v_mfma_f32_16x16x32_bf16 v[10:13], v[178:181], v[202:205], 0
	v_mfma_f32_16x16x32_bf16 v[6:9], v[162:165], v[210:213], 0
	v_mfma_f32_16x16x32_bf16 v[2:5], v[178:181], v[210:213], 0
	v_mfma_f32_16x16x32_bf16 v[46:49], v[166:169], v[190:193], v[46:49]
	v_mfma_f32_16x16x32_bf16 v[38:41], v[182:185], v[190:193], v[38:41]
	v_mfma_f32_16x16x32_bf16 v[30:33], v[166:169], v[198:201], v[30:33]
	v_mfma_f32_16x16x32_bf16 v[22:25], v[182:185], v[198:201], v[22:25]
	v_mfma_f32_16x16x32_bf16 v[14:17], v[166:169], v[206:209], v[14:17]
	v_mfma_f32_16x16x32_bf16 v[10:13], v[182:185], v[206:209], v[10:13]
	v_mfma_f32_16x16x32_bf16 v[6:9], v[166:169], v[214:217], v[6:9]
	v_mfma_f32_16x16x32_bf16 v[2:5], v[182:185], v[214:217], v[2:5]
	s_setprio 0
	s_barrier
; #define PG8_STAGE(bufoff, gbase, voff) do { _Pragma("unroll") for (int _i = 0; _i < 2; ++_i) \
;         __builtin_amdgcn_global_load_lds((const unsigned*)((const char*)(gbase) + (voff)[_i]), (PG8_LAS unsigned*)(lds + (bufoff) + ldsw + _i * 8192), 16, 0, 0); } while (0)
; #define PG8_LDA(dst, b, h) do { if constexpr (DT != 1) { _Pragma("unroll") for (int m = 0; m < 4; ++m) _Pragma("unroll") for (int k = 0; k < 2; ++k) dst[m][k] = *(const PG8_LAS bf16x8*)(lds + PG8_SA(b, h) + aoff + m * 2048 + k * 1024); } \
;         else { _Pragma("unroll") for (int m = 0; m < 4; ++m) dst##8[m] = ld32(lds + PG8_SA(b, h) + aoff + m * 2048); } } while (0)
; #define PG8_LDB(dst, b, h) do { if constexpr (DT != 1) { _Pragma("unroll") for (int n = 0; n < 2; ++n) _Pragma("unroll") for (int k = 0; k < 2; ++k) dst[n][k] = *(const PG8_LAS bf16x8*)(lds + PG8_SB(b, h) + boff + n * 2048 + k * 1024); } \
;         else { _Pragma("unroll") for (int n = 0; n < 2; ++n) dst##8[n] = ld32(lds + PG8_SB(b, h) + boff + n * 2048); } } while (0)
; #define PG8_WAIT_V(n) asm volatile("s_waitcnt vmcnt(" #n ")" ::: "memory")
; #define PG8_WAIT_L(n) asm volatile("s_waitcnt lgkmcnt(" #n ")" ::: "memory")
; #define PG8_BAR __builtin_amdgcn_s_barrier()
; #define PG8_SCHED __builtin_amdgcn_sched_barrier(0)
;     ...
;             PG8_LDB(B0, 0, 0); PG8_LDB(B1, 0, 1); PG8_SCHED; PG8_LDA(At, 0, 0); PG8_STAGE(PG8_SA(1, 1), a1 + hstepA, voffA);
;             PG8_WAIT_V(8); PG8_WAIT_L(0); PG8_BAR; PG8_MMA(0, 0, At, B0); PG8_MMA(0, 1, At, B1); PG8_BAR; PG8_SCHED;
;             PG8_LDA(At, 0, 1); PG8_STAGE(PG8_SB(0, 0), b2, voffB); PG8_STAGE(PG8_SB(0, 1), b2 + hstepB, voffB); PG8_STAGE(PG8_SA(0, 0), a2, voffA);
;             PG8_WAIT_V(8); PG8_WAIT_L(0); PG8_BAR; PG8_MMA(1, 0, At, B0); PG8_MMA(1, 1, At, B1); PG8_BAR; PG8_SCHED;
;             PG8_LDB(B0, 1, 0); PG8_LDB(B1, 1, 1); PG8_SCHED; PG8_LDA(At, 1, 0); PG8_STAGE(PG8_SA(0, 1), a2 + hstepA, voffA);
;             PG8_WAIT_V(8); PG8_WAIT_L(0); PG8_BAR; PG8_MMA(0, 0, At, B0); PG8_MMA(0, 1, At, B1); PG8_BAR; PG8_SCHED;
;             PG8_LDA(At, 1, 1); PG8_STAGE(PG8_SB(1, 0), b3, voffB); PG8_STAGE(PG8_SB(1, 1), b3 + hstepB, voffB); PG8_STAGE(PG8_SA(1, 0), a3, voffA);
;             PG8_WAIT_V(8); PG8_WAIT_L(0); PG8_BAR; PG8_MMA(1, 0, At, B0); PG8_MMA(1, 1, At, B1); PG8_BAR; PG8_SCHED;
	ds_read_b128 v[146:149], v176
	ds_read_b128 v[150:153], v176 offset:1024
	ds_read_b128 v[154:157], v176 offset:2048
	ds_read_b128 v[158:161], v176 offset:3072
	ds_read_b128 v[162:165], v177
	ds_read_b128 v[166:169], v177 offset:1024
	ds_read_b128 v[178:181], v177 offset:2048
	ds_read_b128 v[182:185], v177 offset:3072
	s_add_u32 s26, s34, 0x160000
	s_addc_u32 s27, s35, 0
	s_mov_b32 m0, s48
	ds_read_b128 v[186:189], v175 offset:32768
	ds_read_b128 v[190:193], v175 offset:33792
	ds_read_b128 v[194:197], v175 offset:34816
	ds_read_b128 v[198:201], v175 offset:35840
	ds_read_b128 v[202:205], v175 offset:36864
	ds_read_b128 v[206:209], v175 offset:37888
	ds_read_b128 v[210:213], v175 offset:38912
	global_load_lds_dwordx4 v130, s[26:27]
	s_mov_b32 m0, s49
	ds_read_b128 v[214:217], v175 offset:39936
	global_load_lds_dwordx4 v134, s[26:27]
	s_waitcnt vmcnt(8) lgkmcnt(0)
	s_barrier
	s_setprio 1
	v_mfma_f32_16x16x32_bf16 v[126:129], v[146:149], v[186:189], v[126:129]
	v_mfma_f32_16x16x32_bf16 v[122:125], v[154:157], v[186:189], v[122:125]
	v_mfma_f32_16x16x32_bf16 v[118:121], v[146:149], v[194:197], v[118:121]
	v_mfma_f32_16x16x32_bf16 v[114:117], v[154:157], v[194:197], v[114:117]
	v_mfma_f32_16x16x32_bf16 v[106:109], v[146:149], v[202:205], v[106:109]
	v_mfma_f32_16x16x32_bf16 v[98:101], v[154:157], v[202:205], v[98:101]
	v_mfma_f32_16x16x32_bf16 v[90:93], v[146:149], v[210:213], v[90:93]
	v_mfma_f32_16x16x32_bf16 v[82:85], v[154:157], v[210:213], v[82:85]
	v_mfma_f32_16x16x32_bf16 v[126:129], v[150:153], v[190:193], v[126:129]
	v_mfma_f32_16x16x32_bf16 v[122:125], v[158:161], v[190:193], v[122:125]
	v_mfma_f32_16x16x32_bf16 v[118:121], v[150:153], v[198:201], v[118:121]
	v_mfma_f32_16x16x32_bf16 v[114:117], v[158:161], v[198:201], v[114:117]
	v_mfma_f32_16x16x32_bf16 v[106:109], v[150:153], v[206:209], v[106:109]
	v_mfma_f32_16x16x32_bf16 v[98:101], v[158:161], v[206:209], v[98:101]
	v_mfma_f32_16x16x32_bf16 v[90:93], v[150:153], v[214:217], v[90:93]
	v_mfma_f32_16x16x32_bf16 v[82:85], v[158:161], v[214:217], v[82:85]
	s_setprio 0
	s_setprio 1
	v_mfma_f32_16x16x32_bf16 v[110:113], v[162:165], v[186:189], v[110:113]
	v_mfma_f32_16x16x32_bf16 v[102:105], v[178:181], v[186:189], v[102:105]
	v_mfma_f32_16x16x32_bf16 v[94:97], v[162:165], v[194:197], v[94:97]
	v_mfma_f32_16x16x32_bf16 v[86:89], v[178:181], v[194:197], v[86:89]
	v_mfma_f32_16x16x32_bf16 v[78:81], v[162:165], v[202:205], v[78:81]
	v_mfma_f32_16x16x32_bf16 v[74:77], v[178:181], v[202:205], v[74:77]
	v_mfma_f32_16x16x32_bf16 v[70:73], v[162:165], v[210:213], v[70:73]
	v_mfma_f32_16x16x32_bf16 v[66:69], v[178:181], v[210:213], v[66:69]
	v_mfma_f32_16x16x32_bf16 v[110:113], v[166:169], v[190:193], v[110:113]
	v_mfma_f32_16x16x32_bf16 v[102:105], v[182:185], v[190:193], v[102:105]
	v_mfma_f32_16x16x32_bf16 v[94:97], v[166:169], v[198:201], v[94:97]
	v_mfma_f32_16x16x32_bf16 v[86:89], v[182:185], v[198:201], v[86:89]
	v_mfma_f32_16x16x32_bf16 v[78:81], v[166:169], v[206:209], v[78:81]
	v_mfma_f32_16x16x32_bf16 v[74:77], v[182:185], v[206:209], v[74:77]
	v_mfma_f32_16x16x32_bf16 v[70:73], v[166:169], v[214:217], v[70:73]
	v_mfma_f32_16x16x32_bf16 v[66:69], v[182:185], v[214:217], v[66:69]
	s_setprio 0
	s_barrier
	s_mov_b32 m0, s52
	s_add_u32 s26, s30, 0x160080
	ds_read_b128 v[186:189], v175 offset:49152
	ds_read_b128 v[190:193], v175 offset:50176
	ds_read_b128 v[194:197], v175 offset:51200
	ds_read_b128 v[198:201], v175 offset:52224
	global_load_lds_dwordx4 v132, s[98:99]
	s_mov_b32 m0, s53
	s_addc_u32 s27, s31, 0
	global_load_lds_dwordx4 v136, s[98:99]
	s_mov_b32 m0, s56
	ds_read_b128 v[214:217], v175 offset:56320
	global_load_lds_dwordx4 v132, s[26:27]
	s_mov_b32 m0, s57
	ds_read_b128 v[210:213], v175 offset:55296
	global_load_lds_dwordx4 v136, s[26:27]
	s_mov_b32 m0, s54
	ds_read_b128 v[206:209], v175 offset:54272
	global_load_lds_dwordx4 v130, s[100:101]
	s_mov_b32 m0, s55
	ds_read_b128 v[202:205], v175 offset:53248
	global_load_lds_dwordx4 v134, s[100:101]
	s_waitcnt vmcnt(8) lgkmcnt(0)
	s_barrier
	s_setprio 1
	v_mfma_f32_16x16x32_bf16 v[62:65], v[146:149], v[186:189], v[62:65]
	v_mfma_f32_16x16x32_bf16 v[58:61], v[154:157], v[186:189], v[58:61]
	v_mfma_f32_16x16x32_bf16 v[54:57], v[146:149], v[194:197], v[54:57]
	v_mfma_f32_16x16x32_bf16 v[50:53], v[154:157], v[194:197], v[50:53]
	v_mfma_f32_16x16x32_bf16 v[42:45], v[146:149], v[202:205], v[42:45]
	v_mfma_f32_16x16x32_bf16 v[34:37], v[154:157], v[202:205], v[34:37]
	v_mfma_f32_16x16x32_bf16 v[26:29], v[146:149], v[210:213], v[26:29]
	v_mfma_f32_16x16x32_bf16 v[18:21], v[154:157], v[210:213], v[18:21]
	v_mfma_f32_16x16x32_bf16 v[62:65], v[150:153], v[190:193], v[62:65]
	v_mfma_f32_16x16x32_bf16 v[58:61], v[158:161], v[190:193], v[58:61]
	v_mfma_f32_16x16x32_bf16 v[54:57], v[150:153], v[198:201], v[54:57]
	v_mfma_f32_16x16x32_bf16 v[50:53], v[158:161], v[198:201], v[50:53]
	v_mfma_f32_16x16x32_bf16 v[42:45], v[150:153], v[206:209], v[42:45]
	v_mfma_f32_16x16x32_bf16 v[34:37], v[158:161], v[206:209], v[34:37]
	v_mfma_f32_16x16x32_bf16 v[26:29], v[150:153], v[214:217], v[26:29]
	v_mfma_f32_16x16x32_bf16 v[18:21], v[158:161], v[214:217], v[18:21]
	s_setprio 0
	s_setprio 1
	v_mfma_f32_16x16x32_bf16 v[46:49], v[162:165], v[186:189], v[46:49]
	v_mfma_f32_16x16x32_bf16 v[38:41], v[178:181], v[186:189], v[38:41]
	v_mfma_f32_16x16x32_bf16 v[30:33], v[162:165], v[194:197], v[30:33]
	v_mfma_f32_16x16x32_bf16 v[22:25], v[178:181], v[194:197], v[22:25]
	v_mfma_f32_16x16x32_bf16 v[14:17], v[162:165], v[202:205], v[14:17]
	v_mfma_f32_16x16x32_bf16 v[10:13], v[178:181], v[202:205], v[10:13]
	v_mfma_f32_16x16x32_bf16 v[6:9], v[162:165], v[210:213], v[6:9]
	v_mfma_f32_16x16x32_bf16 v[2:5], v[178:181], v[210:213], v[2:5]
	v_mfma_f32_16x16x32_bf16 v[46:49], v[166:169], v[190:193], v[46:49]
	v_mfma_f32_16x16x32_bf16 v[38:41], v[182:185], v[190:193], v[38:41]
	v_mfma_f32_16x16x32_bf16 v[30:33], v[166:169], v[198:201], v[30:33]
	v_mfma_f32_16x16x32_bf16 v[22:25], v[182:185], v[198:201], v[22:25]
	v_mfma_f32_16x16x32_bf16 v[14:17], v[166:169], v[206:209], v[14:17]
	v_mfma_f32_16x16x32_bf16 v[10:13], v[182:185], v[206:209], v[10:13]
	v_mfma_f32_16x16x32_bf16 v[6:9], v[166:169], v[214:217], v[6:9]
	v_mfma_f32_16x16x32_bf16 v[2:5], v[182:185], v[214:217], v[2:5]
	s_setprio 0
	s_barrier
	s_add_u32 s65, s65, 0x100
	s_addc_u32 s66, s66, 0
	s_cmp_ge_i32 s67, s51
	s_mov_b64 s[26:27], s[28:29]
	s_mov_b32 s30, s67
	s_cbranch_scc0 .LBB0_922
	s_branch .Lpx_5
; #define PG8_STAGE(bufoff, gbase, voff) do { _Pragma("unroll") for (int _i = 0; _i < 2; ++_i) \
;         __builtin_amdgcn_global_load_lds((const unsigned*)((const char*)(gbase) + (voff)[_i]), (PG8_LAS unsigned*)(lds + (bufoff) + ldsw + _i * 8192), 16, 0, 0); } while (0)
; #define PG8_LDA(dst, b, h) do { if constexpr (DT != 1) { _Pragma("unroll") for (int m = 0; m < 4; ++m) _Pragma("unroll") for (int k = 0; k < 2; ++k) dst[m][k] = *(const PG8_LAS bf16x8*)(lds + PG8_SA(b, h) + aoff + m * 2048 + k * 1024); } \
;         else { _Pragma("unroll") for (int m = 0; m < 4; ++m) dst##8[m] = ld32(lds + PG8_SA(b, h) + aoff + m * 2048); } } while (0)
; #define PG8_WAIT_V(n) asm volatile("s_waitcnt vmcnt(" #n ")" ::: "memory")
;     ...
;         const char* nA = has_next ? (const char*)g.A + (size_t)nxt.pm * tstepA : cA; const char* nB = has_next ? (const char*)g.Bt + (size_t)nxt.pn * tstepB : cB;
;         for (int t = 0; t < nt; t += 2) {
;             const bool last = (t == nt - 2);
;             const char* a1 = cA + (size_t)(t + 1) * kstep;
;             const char* a2 = last ? nA : cA + (size_t)(t + 2) * kstep; const char* b2 = last ? nB : cB + (size_t)(t + 2) * kstep;
;             const char* a3 = a2 + kstep; const char* b3 = b2 + kstep;
;             if (last && has_next) S.a_ready(nxt);
;             if constexpr (SP2) {
;             PG8_LDB(B0, 0, 0); PG8_LDB(B1, 0, 1); PG8_SCHED; PG8_LDA(At, 0, 0); PG8_STAGE(PG8_SA(1, 1), a1 + hstepA, voffA);
;             PG8_WAIT_V(8); PG8_WAIT_L(0); PG8_BAR; PG8_MMA(0, 0, At, B0); PG8_MMA(0, 1, At, B1); PG8_BAR; PG8_SCHED;
;             PG8_LDA(At, 0, 1); PG8_STAGE(PG8_SB(0, 0), b2, voffB); PG8_STAGE(PG8_SB(0, 1), b2 + hstepB, voffB); PG8_STAGE(PG8_SA(0, 0), a2, voffA);
;             PG8_WAIT_V(8); PG8_WAIT_L(0); PG8_BAR; PG8_MMA(1, 0, At, B0); PG8_MMA(1, 1, At, B1); PG8_BAR; PG8_SCHED;
;             PG8_LDB(B0, 1, 0); PG8_LDB(B1, 1, 1); PG8_SCHED; PG8_LDA(At, 1, 0); PG8_STAGE(PG8_SA(0, 1), a2 + hstepA, voffA);
;             PG8_WAIT_V(8); PG8_WAIT_L(0); PG8_BAR; PG8_MMA(0, 0, At, B0); PG8_MMA(0, 1, At, B1); PG8_BAR; PG8_SCHED;
;             PG8_LDA(At, 1, 1); PG8_STAGE(PG8_SB(1, 0), b3, voffB); PG8_STAGE(PG8_SB(1, 1), b3 + hstepB, voffB); PG8_STAGE(PG8_SA(1, 0), a3, voffA);
;             PG8_WAIT_V(8); PG8_WAIT_L(0); PG8_BAR; PG8_MMA(1, 0, At, B0); PG8_MMA(1, 1, At, B1); PG8_BAR; PG8_SCHED;
.LBB0_922:
	ds_read_b128 v[146:149], v173
	ds_read_b128 v[150:153], v173 offset:1024
	ds_read_b128 v[154:157], v173 offset:2048
	ds_read_b128 v[158:161], v173 offset:3072
	ds_read_b128 v[162:165], v174
	ds_read_b128 v[166:169], v174 offset:1024
	ds_read_b128 v[178:181], v174 offset:2048
	ds_read_b128 v[182:185], v174 offset:3072
	s_add_i32 s67, s30, 2
	s_add_u32 s28, s26, 0x100
	s_addc_u32 s29, s27, 0
	s_cmp_eq_u32 s58, s30
	s_cselect_b32 s30, s24, s65
	s_cselect_b32 s35, s3, s29
	s_cselect_b32 s34, s2, s28
	s_cselect_b32 s31, s25, s66
	v_lshl_add_u64 v[170:171], s[26:27], 0, v[140:141]
	s_add_i32 m0, s46, 0xc000
	ds_read_b128 v[186:189], v175
	ds_read_b128 v[190:193], v175 offset:1024
	ds_read_b128 v[194:197], v175 offset:2048
	ds_read_b128 v[198:201], v175 offset:3072
	ds_read_b128 v[202:205], v175 offset:4096
	ds_read_b128 v[206:209], v175 offset:5120
	ds_read_b128 v[210:213], v175 offset:6144
	ds_read_b128 v[214:217], v175 offset:7168
	global_load_lds_dwordx4 v[170:171], off
	v_lshl_add_u64 v[170:171], s[26:27], 0, v[138:139]
	s_add_i32 m0, s46, 0xe000
	s_nop 0
	global_load_lds_dwordx4 v[170:171], off
	s_waitcnt vmcnt(8) lgkmcnt(0)
	s_barrier
	s_setprio 1
	v_mfma_f32_16x16x32_bf16 v[126:129], v[146:149], v[186:189], v[126:129]
	v_mfma_f32_16x16x32_bf16 v[122:125], v[154:157], v[186:189], v[122:125]
	v_mfma_f32_16x16x32_bf16 v[118:121], v[146:149], v[194:197], v[118:121]
	v_mfma_f32_16x16x32_bf16 v[114:117], v[154:157], v[194:197], v[114:117]
	v_mfma_f32_16x16x32_bf16 v[106:109], v[146:149], v[202:205], v[106:109]
	v_mfma_f32_16x16x32_bf16 v[98:101], v[154:157], v[202:205], v[98:101]
	v_mfma_f32_16x16x32_bf16 v[90:93], v[146:149], v[210:213], v[90:93]
	v_mfma_f32_16x16x32_bf16 v[82:85], v[154:157], v[210:213], v[82:85]
	v_mfma_f32_16x16x32_bf16 v[126:129], v[150:153], v[190:193], v[126:129]
	v_mfma_f32_16x16x32_bf16 v[122:125], v[158:161], v[190:193], v[122:125]
	v_mfma_f32_16x16x32_bf16 v[118:121], v[150:153], v[198:201], v[118:121]
	v_mfma_f32_16x16x32_bf16 v[114:117], v[158:161], v[198:201], v[114:117]
	v_mfma_f32_16x16x32_bf16 v[106:109], v[150:153], v[206:209], v[106:109]
	v_mfma_f32_16x16x32_bf16 v[98:101], v[158:161], v[206:209], v[98:101]
	v_mfma_f32_16x16x32_bf16 v[90:93], v[150:153], v[214:217], v[90:93]
	v_mfma_f32_16x16x32_bf16 v[82:85], v[158:161], v[214:217], v[82:85]
	s_setprio 0
	s_setprio 1
	v_mfma_f32_16x16x32_bf16 v[110:113], v[162:165], v[186:189], v[110:113]
	v_mfma_f32_16x16x32_bf16 v[102:105], v[178:181], v[186:189], v[102:105]
	v_mfma_f32_16x16x32_bf16 v[94:97], v[162:165], v[194:197], v[94:97]
	v_mfma_f32_16x16x32_bf16 v[86:89], v[178:181], v[194:197], v[86:89]
	v_mfma_f32_16x16x32_bf16 v[78:81], v[162:165], v[202:205], v[78:81]
	v_mfma_f32_16x16x32_bf16 v[74:77], v[178:181], v[202:205], v[74:77]
	v_mfma_f32_16x16x32_bf16 v[70:73], v[162:165], v[210:213], v[70:73]
	v_mfma_f32_16x16x32_bf16 v[66:69], v[178:181], v[210:213], v[66:69]
	v_mfma_f32_16x16x32_bf16 v[110:113], v[166:169], v[190:193], v[110:113]
	v_mfma_f32_16x16x32_bf16 v[102:105], v[182:185], v[190:193], v[102:105]
	v_mfma_f32_16x16x32_bf16 v[94:97], v[166:169], v[198:201], v[94:97]
	v_mfma_f32_16x16x32_bf16 v[86:89], v[182:185], v[198:201], v[86:89]
	v_mfma_f32_16x16x32_bf16 v[78:81], v[166:169], v[206:209], v[78:81]
	v_mfma_f32_16x16x32_bf16 v[74:77], v[182:185], v[206:209], v[74:77]
	v_mfma_f32_16x16x32_bf16 v[70:73], v[166:169], v[214:217], v[70:73]
	v_mfma_f32_16x16x32_bf16 v[66:69], v[182:185], v[214:217], v[66:69]
	s_setprio 0
	s_barrier
	s_mov_b32 m0, s42
	s_add_u32 s98, s30, 0x80
	s_addc_u32 s99, s31, 0
	s_add_u32 s26, s30, 0x160000
	ds_read_b128 v[186:189], v175 offset:16384
	ds_read_b128 v[190:193], v175 offset:17408
	ds_read_b128 v[194:197], v175 offset:18432
	ds_read_b128 v[198:201], v175 offset:19456
	global_load_lds_dwordx4 v132, s[30:31]
	s_mov_b32 m0, s43
	s_addc_u32 s27, s31, 0
	global_load_lds_dwordx4 v136, s[30:31]
	s_mov_b32 m0, s44
	ds_read_b128 v[214:217], v175 offset:23552
	global_load_lds_dwordx4 v132, s[26:27]
	s_mov_b32 m0, s45
	ds_read_b128 v[210:213], v175 offset:22528
	global_load_lds_dwordx4 v136, s[26:27]
	s_add_u32 s100, s34, 0x80
	s_addc_u32 s101, s35, 0
	s_mov_b32 m0, s46
	ds_read_b128 v[206:209], v175 offset:21504
	global_load_lds_dwordx4 v130, s[34:35]
	s_mov_b32 m0, s47
	ds_read_b128 v[202:205], v175 offset:20480
	global_load_lds_dwordx4 v134, s[34:35]
	s_waitcnt vmcnt(8) lgkmcnt(0)
	s_barrier
	s_setprio 1
	v_mfma_f32_16x16x32_bf16 v[62:65], v[146:149], v[186:189], v[62:65]
	v_mfma_f32_16x16x32_bf16 v[58:61], v[154:157], v[186:189], v[58:61]
	v_mfma_f32_16x16x32_bf16 v[54:57], v[146:149], v[194:197], v[54:57]
	v_mfma_f32_16x16x32_bf16 v[50:53], v[154:157], v[194:197], v[50:53]
	v_mfma_f32_16x16x32_bf16 v[42:45], v[146:149], v[202:205], v[42:45]
	v_mfma_f32_16x16x32_bf16 v[34:37], v[154:157], v[202:205], v[34:37]
	v_mfma_f32_16x16x32_bf16 v[26:29], v[146:149], v[210:213], v[26:29]
	v_mfma_f32_16x16x32_bf16 v[18:21], v[154:157], v[210:213], v[18:21]
	v_mfma_f32_16x16x32_bf16 v[62:65], v[150:153], v[190:193], v[62:65]
	v_mfma_f32_16x16x32_bf16 v[58:61], v[158:161], v[190:193], v[58:61]
	v_mfma_f32_16x16x32_bf16 v[54:57], v[150:153], v[198:201], v[54:57]
	v_mfma_f32_16x16x32_bf16 v[50:53], v[158:161], v[198:201], v[50:53]
	v_mfma_f32_16x16x32_bf16 v[42:45], v[150:153], v[206:209], v[42:45]
	v_mfma_f32_16x16x32_bf16 v[34:37], v[158:161], v[206:209], v[34:37]
	v_mfma_f32_16x16x32_bf16 v[26:29], v[150:153], v[214:217], v[26:29]
	v_mfma_f32_16x16x32_bf16 v[18:21], v[158:161], v[214:217], v[18:21]
	s_setprio 0
	s_setprio 1
	v_mfma_f32_16x16x32_bf16 v[46:49], v[162:165], v[186:189], v[46:49]
	v_mfma_f32_16x16x32_bf16 v[38:41], v[178:181], v[186:189], v[38:41]
	v_mfma_f32_16x16x32_bf16 v[30:33], v[162:165], v[194:197], v[30:33]
	v_mfma_f32_16x16x32_bf16 v[22:25], v[178:181], v[194:197], v[22:25]
	v_mfma_f32_16x16x32_bf16 v[14:17], v[162:165], v[202:205], v[14:17]
	v_mfma_f32_16x16x32_bf16 v[10:13], v[178:181], v[202:205], v[10:13]
	v_mfma_f32_16x16x32_bf16 v[6:9], v[162:165], v[210:213], v[6:9]
	v_mfma_f32_16x16x32_bf16 v[2:5], v[178:181], v[210:213], v[2:5]
	v_mfma_f32_16x16x32_bf16 v[46:49], v[166:169], v[190:193], v[46:49]
	v_mfma_f32_16x16x32_bf16 v[38:41], v[182:185], v[190:193], v[38:41]
	v_mfma_f32_16x16x32_bf16 v[30:33], v[166:169], v[198:201], v[30:33]
	v_mfma_f32_16x16x32_bf16 v[22:25], v[182:185], v[198:201], v[22:25]
	v_mfma_f32_16x16x32_bf16 v[14:17], v[166:169], v[206:209], v[14:17]
	v_mfma_f32_16x16x32_bf16 v[10:13], v[182:185], v[206:209], v[10:13]
	v_mfma_f32_16x16x32_bf16 v[6:9], v[166:169], v[214:217], v[6:9]
	v_mfma_f32_16x16x32_bf16 v[2:5], v[182:185], v[214:217], v[2:5]
	s_setprio 0
	s_barrier
; #define PG8_STAGE(bufoff, gbase, voff) do { _Pragma("unroll") for (int _i = 0; _i < 2; ++_i) \
;         __builtin_amdgcn_global_load_lds((const unsigned*)((const char*)(gbase) + (voff)[_i]), (PG8_LAS unsigned*)(lds + (bufoff) + ldsw + _i * 8192), 16, 0, 0); } while (0)
; #define PG8_LDA(dst, b, h) do { if constexpr (DT != 1) { _Pragma("unroll") for (int m = 0; m < 4; ++m) _Pragma("unroll") for (int k = 0; k < 2; ++k) dst[m][k] = *(const PG8_LAS bf16x8*)(lds + PG8_SA(b, h) + aoff + m * 2048 + k * 1024); } \
;         else { _Pragma("unroll") for (int m = 0; m < 4; ++m) dst##8[m] = ld32(lds + PG8_SA(b, h) + aoff + m * 2048); } } while (0)
; #define PG8_LDB(dst, b, h) do { if constexpr (DT != 1) { _Pragma("unroll") for (int n = 0; n < 2; ++n) _Pragma("unroll") for (int k = 0; k < 2; ++k) dst[n][k] = *(const PG8_LAS bf16x8*)(lds + PG8_SB(b, h) + boff + n * 2048 + k * 1024); } \
;         else { _Pragma("unroll") for (int n = 0; n < 2; ++n) dst##8[n] = ld32(lds + PG8_SB(b, h) + boff + n * 2048); } } while (0)
; #define PG8_WAIT_V(n) asm volatile("s_waitcnt vmcnt(" #n ")" ::: "memory")
; #define PG8_WAIT_L(n) asm volatile("s_waitcnt lgkmcnt(" #n ")" ::: "memory")
; #define PG8_BAR __builtin_amdgcn_s_barrier()
; #define PG8_SCHED __builtin_amdgcn_sched_barrier(0)
;     ...
;             PG8_LDB(B0, 0, 0); PG8_LDB(B1, 0, 1); PG8_SCHED; PG8_LDA(At, 0, 0); PG8_STAGE(PG8_SA(1, 1), a1 + hstepA, voffA);
;             PG8_WAIT_V(8); PG8_WAIT_L(0); PG8_BAR; PG8_MMA(0, 0, At, B0); PG8_MMA(0, 1, At, B1); PG8_BAR; PG8_SCHED;
;             PG8_LDA(At, 0, 1); PG8_STAGE(PG8_SB(0, 0), b2, voffB); PG8_STAGE(PG8_SB(0, 1), b2 + hstepB, voffB); PG8_STAGE(PG8_SA(0, 0), a2, voffA);
;             PG8_WAIT_V(8); PG8_WAIT_L(0); PG8_BAR; PG8_MMA(1, 0, At, B0); PG8_MMA(1, 1, At, B1); PG8_BAR; PG8_SCHED;
;             PG8_LDB(B0, 1, 0); PG8_LDB(B1, 1, 1); PG8_SCHED; PG8_LDA(At, 1, 0); PG8_STAGE(PG8_SA(0, 1), a2 + hstepA, voffA);
;             PG8_WAIT_V(8); PG8_WAIT_L(0); PG8_BAR; PG8_MMA(0, 0, At, B0); PG8_MMA(0, 1, At, B1); PG8_BAR; PG8_SCHED;
;             PG8_LDA(At, 1, 1); PG8_STAGE(PG8_SB(1, 0), b3, voffB); PG8_STAGE(PG8_SB(1, 1), b3 + hstepB, voffB); PG8_STAGE(PG8_SA(1, 0), a3, voffA);
;             PG8_WAIT_V(8); PG8_WAIT_L(0); PG8_BAR; PG8_MMA(1, 0, At, B0); PG8_MMA(1, 1, At, B1); PG8_BAR; PG8_SCHED;
	ds_read_b128 v[146:149], v176
	ds_read_b128 v[150:153], v176 offset:1024
	ds_read_b128 v[154:157], v176 offset:2048
	ds_read_b128 v[158:161], v176 offset:3072
	ds_read_b128 v[162:165], v177
	ds_read_b128 v[166:169], v177 offset:1024
	ds_read_b128 v[178:181], v177 offset:2048
	ds_read_b128 v[182:185], v177 offset:3072
	s_add_u32 s26, s34, 0x160000
	s_addc_u32 s27, s35, 0
	s_mov_b32 m0, s48
	ds_read_b128 v[186:189], v175 offset:32768
	ds_read_b128 v[190:193], v175 offset:33792
	ds_read_b128 v[194:197], v175 offset:34816
	ds_read_b128 v[198:201], v175 offset:35840
	ds_read_b128 v[202:205], v175 offset:36864
	ds_read_b128 v[206:209], v175 offset:37888
	ds_read_b128 v[210:213], v175 offset:38912
	global_load_lds_dwordx4 v130, s[26:27]
	s_mov_b32 m0, s49
	ds_read_b128 v[214:217], v175 offset:39936
	global_load_lds_dwordx4 v134, s[26:27]
	s_waitcnt vmcnt(8) lgkmcnt(0)
	s_barrier
	s_setprio 1
	v_mfma_f32_16x16x32_bf16 v[126:129], v[146:149], v[186:189], v[126:129]
	v_mfma_f32_16x16x32_bf16 v[122:125], v[154:157], v[186:189], v[122:125]
	v_mfma_f32_16x16x32_bf16 v[118:121], v[146:149], v[194:197], v[118:121]
	v_mfma_f32_16x16x32_bf16 v[114:117], v[154:157], v[194:197], v[114:117]
	v_mfma_f32_16x16x32_bf16 v[106:109], v[146:149], v[202:205], v[106:109]
	v_mfma_f32_16x16x32_bf16 v[98:101], v[154:157], v[202:205], v[98:101]
	v_mfma_f32_16x16x32_bf16 v[90:93], v[146:149], v[210:213], v[90:93]
	v_mfma_f32_16x16x32_bf16 v[82:85], v[154:157], v[210:213], v[82:85]
	v_mfma_f32_16x16x32_bf16 v[126:129], v[150:153], v[190:193], v[126:129]
	v_mfma_f32_16x16x32_bf16 v[122:125], v[158:161], v[190:193], v[122:125]
	v_mfma_f32_16x16x32_bf16 v[118:121], v[150:153], v[198:201], v[118:121]
	v_mfma_f32_16x16x32_bf16 v[114:117], v[158:161], v[198:201], v[114:117]
	v_mfma_f32_16x16x32_bf16 v[106:109], v[150:153], v[206:209], v[106:109]
	v_mfma_f32_16x16x32_bf16 v[98:101], v[158:161], v[206:209], v[98:101]
	v_mfma_f32_16x16x32_bf16 v[90:93], v[150:153], v[214:217], v[90:93]
	v_mfma_f32_16x16x32_bf16 v[82:85], v[158:161], v[214:217], v[82:85]
	s_setprio 0
	s_setprio 1
	v_mfma_f32_16x16x32_bf16 v[110:113], v[162:165], v[186:189], v[110:113]
	v_mfma_f32_16x16x32_bf16 v[102:105], v[178:181], v[186:189], v[102:105]
	v_mfma_f32_16x16x32_bf16 v[94:97], v[162:165], v[194:197], v[94:97]
	v_mfma_f32_16x16x32_bf16 v[86:89], v[178:181], v[194:197], v[86:89]
	v_mfma_f32_16x16x32_bf16 v[78:81], v[162:165], v[202:205], v[78:81]
	v_mfma_f32_16x16x32_bf16 v[74:77], v[178:181], v[202:205], v[74:77]
	v_mfma_f32_16x16x32_bf16 v[70:73], v[162:165], v[210:213], v[70:73]
	v_mfma_f32_16x16x32_bf16 v[66:69], v[178:181], v[210:213], v[66:69]
	v_mfma_f32_16x16x32_bf16 v[110:113], v[166:169], v[190:193], v[110:113]
	v_mfma_f32_16x16x32_bf16 v[102:105], v[182:185], v[190:193], v[102:105]
	v_mfma_f32_16x16x32_bf16 v[94:97], v[166:169], v[198:201], v[94:97]
	v_mfma_f32_16x16x32_bf16 v[86:89], v[182:185], v[198:201], v[86:89]
	v_mfma_f32_16x16x32_bf16 v[78:81], v[166:169], v[206:209], v[78:81]
	v_mfma_f32_16x16x32_bf16 v[74:77], v[182:185], v[206:209], v[74:77]
	v_mfma_f32_16x16x32_bf16 v[70:73], v[166:169], v[214:217], v[70:73]
	v_mfma_f32_16x16x32_bf16 v[66:69], v[182:185], v[214:217], v[66:69]
	s_setprio 0
	s_barrier
	s_mov_b32 m0, s52
	s_add_u32 s26, s30, 0x160080
	ds_read_b128 v[186:189], v175 offset:49152
	ds_read_b128 v[190:193], v175 offset:50176
	ds_read_b128 v[194:197], v175 offset:51200
	ds_read_b128 v[198:201], v175 offset:52224
	global_load_lds_dwordx4 v132, s[98:99]
	s_mov_b32 m0, s53
	s_addc_u32 s27, s31, 0
	global_load_lds_dwordx4 v136, s[98:99]
	s_mov_b32 m0, s56
	ds_read_b128 v[214:217], v175 offset:56320
	global_load_lds_dwordx4 v132, s[26:27]
	s_mov_b32 m0, s57
	ds_read_b128 v[210:213], v175 offset:55296
	global_load_lds_dwordx4 v136, s[26:27]
	s_mov_b32 m0, s54
	ds_read_b128 v[206:209], v175 offset:54272
	global_load_lds_dwordx4 v130, s[100:101]
	s_mov_b32 m0, s55
	ds_read_b128 v[202:205], v175 offset:53248
	global_load_lds_dwordx4 v134, s[100:101]
	s_waitcnt vmcnt(8) lgkmcnt(0)
	s_barrier
	s_setprio 1
	v_mfma_f32_16x16x32_bf16 v[62:65], v[146:149], v[186:189], v[62:65]
	v_mfma_f32_16x16x32_bf16 v[58:61], v[154:157], v[186:189], v[58:61]
	v_mfma_f32_16x16x32_bf16 v[54:57], v[146:149], v[194:197], v[54:57]
	v_mfma_f32_16x16x32_bf16 v[50:53], v[154:157], v[194:197], v[50:53]
	v_mfma_f32_16x16x32_bf16 v[42:45], v[146:149], v[202:205], v[42:45]
	v_mfma_f32_16x16x32_bf16 v[34:37], v[154:157], v[202:205], v[34:37]
	v_mfma_f32_16x16x32_bf16 v[26:29], v[146:149], v[210:213], v[26:29]
	v_mfma_f32_16x16x32_bf16 v[18:21], v[154:157], v[210:213], v[18:21]
	v_mfma_f32_16x16x32_bf16 v[62:65], v[150:153], v[190:193], v[62:65]
	v_mfma_f32_16x16x32_bf16 v[58:61], v[158:161], v[190:193], v[58:61]
	v_mfma_f32_16x16x32_bf16 v[54:57], v[150:153], v[198:201], v[54:57]
	v_mfma_f32_16x16x32_bf16 v[50:53], v[158:161], v[198:201], v[50:53]
	v_mfma_f32_16x16x32_bf16 v[42:45], v[150:153], v[206:209], v[42:45]
	v_mfma_f32_16x16x32_bf16 v[34:37], v[158:161], v[206:209], v[34:37]
	v_mfma_f32_16x16x32_bf16 v[26:29], v[150:153], v[214:217], v[26:29]
	v_mfma_f32_16x16x32_bf16 v[18:21], v[158:161], v[214:217], v[18:21]
	s_setprio 0
	s_setprio 1
	v_mfma_f32_16x16x32_bf16 v[46:49], v[162:165], v[186:189], v[46:49]
	v_mfma_f32_16x16x32_bf16 v[38:41], v[178:181], v[186:189], v[38:41]
	v_mfma_f32_16x16x32_bf16 v[30:33], v[162:165], v[194:197], v[30:33]
	v_mfma_f32_16x16x32_bf16 v[22:25], v[178:181], v[194:197], v[22:25]
	v_mfma_f32_16x16x32_bf16 v[14:17], v[162:165], v[202:205], v[14:17]
	v_mfma_f32_16x16x32_bf16 v[10:13], v[178:181], v[202:205], v[10:13]
	v_mfma_f32_16x16x32_bf16 v[6:9], v[162:165], v[210:213], v[6:9]
	v_mfma_f32_16x16x32_bf16 v[2:5], v[178:181], v[210:213], v[2:5]
	v_mfma_f32_16x16x32_bf16 v[46:49], v[166:169], v[190:193], v[46:49]
	v_mfma_f32_16x16x32_bf16 v[38:41], v[182:185], v[190:193], v[38:41]
	v_mfma_f32_16x16x32_bf16 v[30:33], v[166:169], v[198:201], v[30:33]
	v_mfma_f32_16x16x32_bf16 v[22:25], v[182:185], v[198:201], v[22:25]
	v_mfma_f32_16x16x32_bf16 v[14:17], v[166:169], v[206:209], v[14:17]
	v_mfma_f32_16x16x32_bf16 v[10:13], v[182:185], v[206:209], v[10:13]
	v_mfma_f32_16x16x32_bf16 v[6:9], v[166:169], v[214:217], v[6:9]
	v_mfma_f32_16x16x32_bf16 v[2:5], v[182:185], v[214:217], v[2:5]
	s_setprio 0
	s_barrier
	s_add_u32 s65, s65, 0x100
	s_addc_u32 s66, s66, 0
	s_cmp_ge_i32 s67, s51
	s_mov_b64 s[26:27], s[28:29]
	s_mov_b32 s30, s67
	s_cbranch_scc0 .LBB0_922

; #define PG8_STAGE(bufoff, gbase, voff) do { _Pragma("unroll") for (int _i = 0; _i < 2; ++_i) \
;         __builtin_amdgcn_global_load_lds((const unsigned*)((const char*)(gbase) + (voff)[_i]), (PG8_LAS unsigned*)(lds + (bufoff) + ldsw + _i * 8192), 16, 0, 0); } while (0)
; #define PG8_LDA(dst, b, h) do { if constexpr (DT != 1) { _Pragma("unroll") for (int m = 0; m < 4; ++m) _Pragma("unroll") for (int k = 0; k < 2; ++k) dst[m][k] = *(const PG8_LAS bf16x8*)(lds + PG8_SA(b, h) + aoff + m * 2048 + k * 1024); } \
;         else { _Pragma("unroll") for (int m = 0; m < 4; ++m) dst##8[m] = ld32(lds + PG8_SA(b, h) + aoff + m * 2048); } } while (0)
; #define PG8_WAIT_V(n) asm volatile("s_waitcnt vmcnt(" #n ")" ::: "memory")
;     ...
;         const char* nA = has_next ? (const char*)g.A + (size_t)nxt.pm * tstepA : cA; const char* nB = has_next ? (const char*)g.Bt + (size_t)nxt.pn * tstepB : cB;
;         for (int t = 0; t < nt; t += 2) {
;             const bool last = (t == nt - 2);
;             const char* a1 = cA + (size_t)(t + 1) * kstep;
;             const char* a2 = last ? nA : cA + (size_t)(t + 2) * kstep; const char* b2 = last ? nB : cB + (size_t)(t + 2) * kstep;
;             const char* a3 = a2 + kstep; const char* b3 = b2 + kstep;
;             if (last && has_next) S.a_ready(nxt);
;             if constexpr (SP2) {
;             PG8_LDB(B0, 0, 0); PG8_LDB(B1, 0, 1); PG8_SCHED; PG8_LDA(At, 0, 0); PG8_STAGE(PG8_SA(1, 1), a1 + hstepA, voffA);
;             PG8_WAIT_V(8); PG8_WAIT_L(0); PG8_BAR; PG8_MMA(0, 0, At, B0); PG8_MMA(0, 1, At, B1); PG8_BAR; PG8_SCHED;
;             PG8_LDA(At, 0, 1); PG8_STAGE(PG8_SB(0, 0), b2, voffB); PG8_STAGE(PG8_SB(0, 1), b2 + hstepB, voffB); PG8_STAGE(PG8_SA(0, 0), a2, voffA);
;             PG8_WAIT_V(8); PG8_WAIT_L(0); PG8_BAR; PG8_MMA(1, 0, At, B0); PG8_MMA(1, 1, At, B1); PG8_BAR; PG8_SCHED;
;             PG8_LDB(B0, 1, 0); PG8_LDB(B1, 1, 1); PG8_SCHED; PG8_LDA(At, 1, 0); PG8_STAGE(PG8_SA(0, 1), a2 + hstepA, voffA);
;             PG8_WAIT_V(8); PG8_WAIT_L(0); PG8_BAR; PG8_MMA(0, 0, At, B0); PG8_MMA(0, 1, At, B1); PG8_BAR; PG8_SCHED;
;             PG8_LDA(At, 1, 1); PG8_STAGE(PG8_SB(1, 0), b3, voffB); PG8_STAGE(PG8_SB(1, 1), b3 + hstepB, voffB); PG8_STAGE(PG8_SA(1, 0), a3, voffA);
;             PG8_WAIT_V(8); PG8_WAIT_L(0); PG8_BAR; PG8_MMA(1, 0, At, B0); PG8_MMA(1, 1, At, B1); PG8_BAR; PG8_SCHED;
.Lzt_4:
	s_cbranch_vccnz .LBB0_1414
	s_and_b64 s[28:29], s[0:1], exec
	s_cselect_b32 s15, s19, s27
	s_cselect_b32 s17, s18, s26
	s_cselect_b32 s64, s21, s25
	s_cselect_b32 s65, s20, s24
	s_add_u32 s66, s24, 0x100
	s_addc_u32 s67, s25, 0
	s_add_u32 s24, s26, 0x40080
	s_addc_u32 s25, s27, 0
	s_mov_b32 s26, 0
	v_add_u32_e32 v162, s35, v168
	v_add_u32_e32 v166, s36, v168
	ds_read_b128 v[150:153], v162
	ds_read_b128 v[154:157], v162 offset:1024
	ds_read_b128 v[158:161], v162 offset:2048
	ds_read_b128 v[162:165], v162 offset:3072
	ds_read_b128 v[178:181], v166
	ds_read_b128 v[182:185], v166 offset:1024
	ds_read_b128 v[186:189], v166 offset:2048
	ds_read_b128 v[190:193], v166 offset:3072
	s_add_i32 s68, s26, 2
	s_add_u32 s27, s24, 0xfffc0080
	s_addc_u32 s28, s25, -1
	s_cmp_eq_u32 s61, s26
	s_cselect_b32 s26, s65, s66
	s_cselect_b32 s29, s15, s28
	s_cselect_b32 s28, s17, s27
	s_cselect_b32 s27, s64, s67
	s_add_i32 m0, s46, 0xc000
	ds_read_b128 v[194:197], v177
	ds_read_b128 v[198:201], v177 offset:1024
	ds_read_b128 v[202:205], v177 offset:2048
	ds_read_b128 v[206:209], v177 offset:3072
	ds_read_b128 v[210:213], v177 offset:4096
	ds_read_b128 v[214:217], v177 offset:5120
	ds_read_b128 v[218:221], v177 offset:6144
	ds_read_b128 v[222:225], v177 offset:7168
	global_load_lds_dwordx4 v144, s[24:25]
	s_add_i32 m0, s46, 0xe000
	s_nop 0
	global_load_lds_dwordx4 v142, s[24:25]
	s_waitcnt vmcnt(8) lgkmcnt(0)
	s_barrier
	s_setprio 1
	v_mfma_i32_16x16x64_i8 v[126:129], v[150:153], v[194:197], 0
	v_mfma_i32_16x16x64_i8 v[122:125], v[158:161], v[194:197], 0
	v_mfma_i32_16x16x64_i8 v[118:121], v[150:153], v[202:205], 0
	v_mfma_i32_16x16x64_i8 v[114:117], v[158:161], v[202:205], 0
	v_mfma_i32_16x16x64_i8 v[106:109], v[150:153], v[210:213], 0
	v_mfma_i32_16x16x64_i8 v[98:101], v[158:161], v[210:213], 0
	v_mfma_i32_16x16x64_i8 v[90:93], v[150:153], v[218:221], 0
	v_mfma_i32_16x16x64_i8 v[82:85], v[158:161], v[218:221], 0
	v_mfma_i32_16x16x64_i8 v[126:129], v[154:157], v[198:201], v[126:129]
	v_mfma_i32_16x16x64_i8 v[122:125], v[162:165], v[198:201], v[122:125]
	v_mfma_i32_16x16x64_i8 v[118:121], v[154:157], v[206:209], v[118:121]
	v_mfma_i32_16x16x64_i8 v[114:117], v[162:165], v[206:209], v[114:117]
	v_mfma_i32_16x16x64_i8 v[106:109], v[154:157], v[214:217], v[106:109]
	v_mfma_i32_16x16x64_i8 v[98:101], v[162:165], v[214:217], v[98:101]
	v_mfma_i32_16x16x64_i8 v[90:93], v[154:157], v[222:225], v[90:93]
	v_mfma_i32_16x16x64_i8 v[82:85], v[162:165], v[222:225], v[82:85]
	s_setprio 0
	s_setprio 1
	v_mfma_i32_16x16x64_i8 v[110:113], v[178:181], v[194:197], 0
	v_mfma_i32_16x16x64_i8 v[102:105], v[186:189], v[194:197], 0
	v_mfma_i32_16x16x64_i8 v[94:97], v[178:181], v[202:205], 0
	v_mfma_i32_16x16x64_i8 v[86:89], v[186:189], v[202:205], 0
	v_mfma_i32_16x16x64_i8 v[78:81], v[178:181], v[210:213], 0
	v_mfma_i32_16x16x64_i8 v[74:77], v[186:189], v[210:213], 0
	v_mfma_i32_16x16x64_i8 v[70:73], v[178:181], v[218:221], 0
	v_mfma_i32_16x16x64_i8 v[66:69], v[186:189], v[218:221], 0
	v_mfma_i32_16x16x64_i8 v[110:113], v[182:185], v[198:201], v[110:113]
	v_mfma_i32_16x16x64_i8 v[102:105], v[190:193], v[198:201], v[102:105]
	v_mfma_i32_16x16x64_i8 v[94:97], v[182:185], v[206:209], v[94:97]
	v_mfma_i32_16x16x64_i8 v[86:89], v[190:193], v[206:209], v[86:89]
	v_mfma_i32_16x16x64_i8 v[78:81], v[182:185], v[214:217], v[78:81]
	v_mfma_i32_16x16x64_i8 v[74:77], v[190:193], v[214:217], v[74:77]
	v_mfma_i32_16x16x64_i8 v[70:73], v[182:185], v[222:225], v[70:73]
	v_mfma_i32_16x16x64_i8 v[66:69], v[190:193], v[222:225], v[66:69]
	s_setprio 0
	s_barrier
	s_mov_b32 m0, s23
	s_add_u32 s98, s26, 0x80
	s_addc_u32 s99, s27, 0
	s_add_u32 s70, s26, 0x40000
	ds_read_b128 v[194:197], v177 offset:16384
	ds_read_b128 v[198:201], v177 offset:17408
	ds_read_b128 v[202:205], v177 offset:18432
	ds_read_b128 v[206:209], v177 offset:19456
	global_load_lds_dwordx4 v132, s[26:27]
	s_mov_b32 m0, s43
	s_addc_u32 s71, s27, 0
	global_load_lds_dwordx4 v136, s[26:27]
	s_mov_b32 m0, s44
	ds_read_b128 v[222:225], v177 offset:23552
	global_load_lds_dwordx4 v132, s[70:71]
	s_mov_b32 m0, s45
	ds_read_b128 v[218:221], v177 offset:22528
	global_load_lds_dwordx4 v136, s[70:71]
	s_add_u32 s100, s28, 0x80
	s_addc_u32 s101, s29, 0
	s_mov_b32 m0, s46
	ds_read_b128 v[214:217], v177 offset:21504
	global_load_lds_dwordx4 v130, s[28:29]
	s_mov_b32 m0, s47
	ds_read_b128 v[210:213], v177 offset:20480
	global_load_lds_dwordx4 v134, s[28:29]
	s_waitcnt vmcnt(8) lgkmcnt(0)
	s_barrier
	s_setprio 1
	v_mfma_i32_16x16x64_i8 v[62:65], v[150:153], v[194:197], 0
	v_mfma_i32_16x16x64_i8 v[58:61], v[158:161], v[194:197], 0
	v_mfma_i32_16x16x64_i8 v[54:57], v[150:153], v[202:205], 0
	v_mfma_i32_16x16x64_i8 v[50:53], v[158:161], v[202:205], 0
	v_mfma_i32_16x16x64_i8 v[42:45], v[150:153], v[210:213], 0
	v_mfma_i32_16x16x64_i8 v[34:37], v[158:161], v[210:213], 0
	v_mfma_i32_16x16x64_i8 v[26:29], v[150:153], v[218:221], 0
	v_mfma_i32_16x16x64_i8 v[18:21], v[158:161], v[218:221], 0
	v_mfma_i32_16x16x64_i8 v[62:65], v[154:157], v[198:201], v[62:65]
	v_mfma_i32_16x16x64_i8 v[58:61], v[162:165], v[198:201], v[58:61]
	v_mfma_i32_16x16x64_i8 v[54:57], v[154:157], v[206:209], v[54:57]
	v_mfma_i32_16x16x64_i8 v[50:53], v[162:165], v[206:209], v[50:53]
	v_mfma_i32_16x16x64_i8 v[42:45], v[154:157], v[214:217], v[42:45]
	v_mfma_i32_16x16x64_i8 v[34:37], v[162:165], v[214:217], v[34:37]
	v_mfma_i32_16x16x64_i8 v[26:29], v[154:157], v[222:225], v[26:29]
	v_mfma_i32_16x16x64_i8 v[18:21], v[162:165], v[222:225], v[18:21]
	s_setprio 0
	s_setprio 1
	v_mfma_i32_16x16x64_i8 v[46:49], v[178:181], v[194:197], 0
	v_mfma_i32_16x16x64_i8 v[38:41], v[186:189], v[194:197], 0
	v_mfma_i32_16x16x64_i8 v[30:33], v[178:181], v[202:205], 0
	v_mfma_i32_16x16x64_i8 v[22:25], v[186:189], v[202:205], 0
	v_mfma_i32_16x16x64_i8 v[14:17], v[178:181], v[210:213], 0
	v_mfma_i32_16x16x64_i8 v[10:13], v[186:189], v[210:213], 0
	v_mfma_i32_16x16x64_i8 v[6:9], v[178:181], v[218:221], 0
	v_mfma_i32_16x16x64_i8 v[2:5], v[186:189], v[218:221], 0
	v_mfma_i32_16x16x64_i8 v[46:49], v[182:185], v[198:201], v[46:49]
	v_mfma_i32_16x16x64_i8 v[38:41], v[190:193], v[198:201], v[38:41]
	v_mfma_i32_16x16x64_i8 v[30:33], v[182:185], v[206:209], v[30:33]
	v_mfma_i32_16x16x64_i8 v[22:25], v[190:193], v[206:209], v[22:25]
	v_mfma_i32_16x16x64_i8 v[14:17], v[182:185], v[214:217], v[14:17]
	v_mfma_i32_16x16x64_i8 v[10:13], v[190:193], v[214:217], v[10:13]
	v_mfma_i32_16x16x64_i8 v[6:9], v[182:185], v[222:225], v[6:9]
	v_mfma_i32_16x16x64_i8 v[2:5], v[190:193], v[222:225], v[2:5]
	s_setprio 0
	s_barrier
; #define PG8_STAGE(bufoff, gbase, voff) do { _Pragma("unroll") for (int _i = 0; _i < 2; ++_i) \
;         __builtin_amdgcn_global_load_lds((const unsigned*)((const char*)(gbase) + (voff)[_i]), (PG8_LAS unsigned*)(lds + (bufoff) + ldsw + _i * 8192), 16, 0, 0); } while (0)
; #define PG8_LDA(dst, b, h) do { if constexpr (DT != 1) { _Pragma("unroll") for (int m = 0; m < 4; ++m) _Pragma("unroll") for (int k = 0; k < 2; ++k) dst[m][k] = *(const PG8_LAS bf16x8*)(lds + PG8_SA(b, h) + aoff + m * 2048 + k * 1024); } \
;         else { _Pragma("unroll") for (int m = 0; m < 4; ++m) dst##8[m] = ld32(lds + PG8_SA(b, h) + aoff + m * 2048); } } while (0)
; #define PG8_LDB(dst, b, h) do { if constexpr (DT != 1) { _Pragma("unroll") for (int n = 0; n < 2; ++n) _Pragma("unroll") for (int k = 0; k < 2; ++k) dst[n][k] = *(const PG8_LAS bf16x8*)(lds + PG8_SB(b, h) + boff + n * 2048 + k * 1024); } \
;         else { _Pragma("unroll") for (int n = 0; n < 2; ++n) dst##8[n] = ld32(lds + PG8_SB(b, h) + boff + n * 2048); } } while (0)
; #define PG8_WAIT_V(n) asm volatile("s_waitcnt vmcnt(" #n ")" ::: "memory")
; #define PG8_WAIT_L(n) asm volatile("s_waitcnt lgkmcnt(" #n ")" ::: "memory")
; #define PG8_BAR __builtin_amdgcn_s_barrier()
; #define PG8_SCHED __builtin_amdgcn_sched_barrier(0)
;     ...
;             PG8_LDB(B0, 0, 0); PG8_LDB(B1, 0, 1); PG8_SCHED; PG8_LDA(At, 0, 0); PG8_STAGE(PG8_SA(1, 1), a1 + hstepA, voffA);
;             PG8_WAIT_V(8); PG8_WAIT_L(0); PG8_BAR; PG8_MMA(0, 0, At, B0); PG8_MMA(0, 1, At, B1); PG8_BAR; PG8_SCHED;
;             PG8_LDA(At, 0, 1); PG8_STAGE(PG8_SB(0, 0), b2, voffB); PG8_STAGE(PG8_SB(0, 1), b2 + hstepB, voffB); PG8_STAGE(PG8_SA(0, 0), a2, voffA);
;             PG8_WAIT_V(8); PG8_WAIT_L(0); PG8_BAR; PG8_MMA(1, 0, At, B0); PG8_MMA(1, 1, At, B1); PG8_BAR; PG8_SCHED;
;             PG8_LDB(B0, 1, 0); PG8_LDB(B1, 1, 1); PG8_SCHED; PG8_LDA(At, 1, 0); PG8_STAGE(PG8_SA(0, 1), a2 + hstepA, voffA);
;             PG8_WAIT_V(8); PG8_WAIT_L(0); PG8_BAR; PG8_MMA(0, 0, At, B0); PG8_MMA(0, 1, At, B1); PG8_BAR; PG8_SCHED;
;             PG8_LDA(At, 1, 1); PG8_STAGE(PG8_SB(1, 0), b3, voffB); PG8_STAGE(PG8_SB(1, 1), b3 + hstepB, voffB); PG8_STAGE(PG8_SA(1, 0), a3, voffA);
;             PG8_WAIT_V(8); PG8_WAIT_L(0); PG8_BAR; PG8_MMA(1, 0, At, B0); PG8_MMA(1, 1, At, B1); PG8_BAR; PG8_SCHED;
	v_add_u32_e32 v162, s51, v168
	v_add_u32_e32 v190, s52, v168
	ds_read_b128 v[150:153], v162
	ds_read_b128 v[154:157], v162 offset:1024
	ds_read_b128 v[158:161], v162 offset:2048
	ds_read_b128 v[162:165], v162 offset:3072
	ds_read_b128 v[178:181], v190
	ds_read_b128 v[182:185], v190 offset:1024
	ds_read_b128 v[186:189], v190 offset:2048
	ds_read_b128 v[190:193], v190 offset:3072
	s_add_u32 s28, s28, 0x40000
	s_addc_u32 s29, s29, 0
	s_mov_b32 m0, s48
	ds_read_b128 v[194:197], v177 offset:32768
	ds_read_b128 v[198:201], v177 offset:33792
	ds_read_b128 v[202:205], v177 offset:34816
	ds_read_b128 v[206:209], v177 offset:35840
	ds_read_b128 v[210:213], v177 offset:36864
	ds_read_b128 v[214:217], v177 offset:37888
	ds_read_b128 v[218:221], v177 offset:38912
	global_load_lds_dwordx4 v130, s[28:29]
	s_mov_b32 m0, s49
	ds_read_b128 v[222:225], v177 offset:39936
	global_load_lds_dwordx4 v134, s[28:29]
	s_waitcnt vmcnt(8) lgkmcnt(0)
	s_barrier
	s_setprio 1
	v_mfma_i32_16x16x64_i8 v[126:129], v[150:153], v[194:197], v[126:129]
	v_mfma_i32_16x16x64_i8 v[122:125], v[158:161], v[194:197], v[122:125]
	v_mfma_i32_16x16x64_i8 v[118:121], v[150:153], v[202:205], v[118:121]
	v_mfma_i32_16x16x64_i8 v[114:117], v[158:161], v[202:205], v[114:117]
	v_mfma_i32_16x16x64_i8 v[106:109], v[150:153], v[210:213], v[106:109]
	v_mfma_i32_16x16x64_i8 v[98:101], v[158:161], v[210:213], v[98:101]
	v_mfma_i32_16x16x64_i8 v[90:93], v[150:153], v[218:221], v[90:93]
	v_mfma_i32_16x16x64_i8 v[82:85], v[158:161], v[218:221], v[82:85]
	v_mfma_i32_16x16x64_i8 v[126:129], v[154:157], v[198:201], v[126:129]
	v_mfma_i32_16x16x64_i8 v[122:125], v[162:165], v[198:201], v[122:125]
	v_mfma_i32_16x16x64_i8 v[118:121], v[154:157], v[206:209], v[118:121]
	v_mfma_i32_16x16x64_i8 v[114:117], v[162:165], v[206:209], v[114:117]
	v_mfma_i32_16x16x64_i8 v[106:109], v[154:157], v[214:217], v[106:109]
	v_mfma_i32_16x16x64_i8 v[98:101], v[162:165], v[214:217], v[98:101]
	v_mfma_i32_16x16x64_i8 v[90:93], v[154:157], v[222:225], v[90:93]
	v_mfma_i32_16x16x64_i8 v[82:85], v[162:165], v[222:225], v[82:85]
	s_setprio 0
	s_setprio 1
	v_mfma_i32_16x16x64_i8 v[110:113], v[178:181], v[194:197], v[110:113]
	v_mfma_i32_16x16x64_i8 v[102:105], v[186:189], v[194:197], v[102:105]
	v_mfma_i32_16x16x64_i8 v[94:97], v[178:181], v[202:205], v[94:97]
	v_mfma_i32_16x16x64_i8 v[86:89], v[186:189], v[202:205], v[86:89]
	v_mfma_i32_16x16x64_i8 v[78:81], v[178:181], v[210:213], v[78:81]
	v_mfma_i32_16x16x64_i8 v[74:77], v[186:189], v[210:213], v[74:77]
	v_mfma_i32_16x16x64_i8 v[70:73], v[178:181], v[218:221], v[70:73]
	v_mfma_i32_16x16x64_i8 v[66:69], v[186:189], v[218:221], v[66:69]
	v_mfma_i32_16x16x64_i8 v[110:113], v[182:185], v[198:201], v[110:113]
	v_mfma_i32_16x16x64_i8 v[102:105], v[190:193], v[198:201], v[102:105]
	v_mfma_i32_16x16x64_i8 v[94:97], v[182:185], v[206:209], v[94:97]
	v_mfma_i32_16x16x64_i8 v[86:89], v[190:193], v[206:209], v[86:89]
	v_mfma_i32_16x16x64_i8 v[78:81], v[182:185], v[214:217], v[78:81]
	v_mfma_i32_16x16x64_i8 v[74:77], v[190:193], v[214:217], v[74:77]
	v_mfma_i32_16x16x64_i8 v[70:73], v[182:185], v[222:225], v[70:73]
	v_mfma_i32_16x16x64_i8 v[66:69], v[190:193], v[222:225], v[66:69]
	s_setprio 0
	s_barrier
	s_mov_b32 m0, s55
	s_add_u32 s26, s26, 0x40080
	ds_read_b128 v[194:197], v177 offset:49152
	ds_read_b128 v[198:201], v177 offset:50176
	ds_read_b128 v[202:205], v177 offset:51200
	ds_read_b128 v[206:209], v177 offset:52224
	global_load_lds_dwordx4 v132, s[98:99]
	s_mov_b32 m0, s56
	s_addc_u32 s27, s27, 0
	global_load_lds_dwordx4 v136, s[98:99]
	s_mov_b32 m0, s59
	ds_read_b128 v[222:225], v177 offset:56320
	global_load_lds_dwordx4 v132, s[26:27]
	s_mov_b32 m0, s60
	ds_read_b128 v[218:221], v177 offset:55296
	global_load_lds_dwordx4 v136, s[26:27]
	s_mov_b32 m0, s57
	ds_read_b128 v[214:217], v177 offset:54272
	global_load_lds_dwordx4 v130, s[100:101]
	s_mov_b32 m0, s58
	ds_read_b128 v[210:213], v177 offset:53248
	global_load_lds_dwordx4 v134, s[100:101]
	s_waitcnt vmcnt(8) lgkmcnt(0)
	s_barrier
	s_setprio 1
	v_mfma_i32_16x16x64_i8 v[62:65], v[150:153], v[194:197], v[62:65]
	v_mfma_i32_16x16x64_i8 v[58:61], v[158:161], v[194:197], v[58:61]
	v_mfma_i32_16x16x64_i8 v[54:57], v[150:153], v[202:205], v[54:57]
	v_mfma_i32_16x16x64_i8 v[50:53], v[158:161], v[202:205], v[50:53]
	v_mfma_i32_16x16x64_i8 v[42:45], v[150:153], v[210:213], v[42:45]
	v_mfma_i32_16x16x64_i8 v[34:37], v[158:161], v[210:213], v[34:37]
	v_mfma_i32_16x16x64_i8 v[26:29], v[150:153], v[218:221], v[26:29]
	v_mfma_i32_16x16x64_i8 v[18:21], v[158:161], v[218:221], v[18:21]
	v_mfma_i32_16x16x64_i8 v[62:65], v[154:157], v[198:201], v[62:65]
	v_mfma_i32_16x16x64_i8 v[58:61], v[162:165], v[198:201], v[58:61]
	v_mfma_i32_16x16x64_i8 v[54:57], v[154:157], v[206:209], v[54:57]
	v_mfma_i32_16x16x64_i8 v[50:53], v[162:165], v[206:209], v[50:53]
	v_mfma_i32_16x16x64_i8 v[42:45], v[154:157], v[214:217], v[42:45]
	v_mfma_i32_16x16x64_i8 v[34:37], v[162:165], v[214:217], v[34:37]
	v_mfma_i32_16x16x64_i8 v[26:29], v[154:157], v[222:225], v[26:29]
	v_mfma_i32_16x16x64_i8 v[18:21], v[162:165], v[222:225], v[18:21]
	s_setprio 0
	s_setprio 1
	v_mfma_i32_16x16x64_i8 v[46:49], v[178:181], v[194:197], v[46:49]
	v_mfma_i32_16x16x64_i8 v[38:41], v[186:189], v[194:197], v[38:41]
	v_mfma_i32_16x16x64_i8 v[30:33], v[178:181], v[202:205], v[30:33]
	v_mfma_i32_16x16x64_i8 v[22:25], v[186:189], v[202:205], v[22:25]
	v_mfma_i32_16x16x64_i8 v[14:17], v[178:181], v[210:213], v[14:17]
	v_mfma_i32_16x16x64_i8 v[10:13], v[186:189], v[210:213], v[10:13]
	v_mfma_i32_16x16x64_i8 v[6:9], v[178:181], v[218:221], v[6:9]
	v_mfma_i32_16x16x64_i8 v[2:5], v[186:189], v[218:221], v[2:5]
	v_mfma_i32_16x16x64_i8 v[46:49], v[182:185], v[198:201], v[46:49]
	v_mfma_i32_16x16x64_i8 v[38:41], v[190:193], v[198:201], v[38:41]
	v_mfma_i32_16x16x64_i8 v[30:33], v[182:185], v[206:209], v[30:33]
	v_mfma_i32_16x16x64_i8 v[22:25], v[190:193], v[206:209], v[22:25]
	v_mfma_i32_16x16x64_i8 v[14:17], v[182:185], v[214:217], v[14:17]
	v_mfma_i32_16x16x64_i8 v[10:13], v[190:193], v[214:217], v[10:13]
	v_mfma_i32_16x16x64_i8 v[6:9], v[182:185], v[222:225], v[6:9]
	v_mfma_i32_16x16x64_i8 v[2:5], v[190:193], v[222:225], v[2:5]
	s_setprio 0
	s_barrier
	s_add_u32 s66, s66, 0x100
	s_addc_u32 s67, s67, 0
	s_add_u32 s24, s24, 0x100
	s_addc_u32 s25, s25, 0
	s_cmp_ge_i32 s68, s54
	s_mov_b32 s26, s68
	s_cbranch_scc0 .LBB0_1412
	s_branch .Lpx_8
; #define PG8_STAGE(bufoff, gbase, voff) do { _Pragma("unroll") for (int _i = 0; _i < 2; ++_i) \
;         __builtin_amdgcn_global_load_lds((const unsigned*)((const char*)(gbase) + (voff)[_i]), (PG8_LAS unsigned*)(lds + (bufoff) + ldsw + _i * 8192), 16, 0, 0); } while (0)
; #define PG8_LDA(dst, b, h) do { if constexpr (DT != 1) { _Pragma("unroll") for (int m = 0; m < 4; ++m) _Pragma("unroll") for (int k = 0; k < 2; ++k) dst[m][k] = *(const PG8_LAS bf16x8*)(lds + PG8_SA(b, h) + aoff + m * 2048 + k * 1024); } \
;         else { _Pragma("unroll") for (int m = 0; m < 4; ++m) dst##8[m] = ld32(lds + PG8_SA(b, h) + aoff + m * 2048); } } while (0)
; #define PG8_WAIT_V(n) asm volatile("s_waitcnt vmcnt(" #n ")" ::: "memory")
;     ...
;         const char* nA = has_next ? (const char*)g.A + (size_t)nxt.pm * tstepA : cA; const char* nB = has_next ? (const char*)g.Bt + (size_t)nxt.pn * tstepB : cB;
;         for (int t = 0; t < nt; t += 2) {
;             const bool last = (t == nt - 2);
;             const char* a1 = cA + (size_t)(t + 1) * kstep;
;             const char* a2 = last ? nA : cA + (size_t)(t + 2) * kstep; const char* b2 = last ? nB : cB + (size_t)(t + 2) * kstep;
;             const char* a3 = a2 + kstep; const char* b3 = b2 + kstep;
;             if (last && has_next) S.a_ready(nxt);
;             if constexpr (SP2) {
;             PG8_LDB(B0, 0, 0); PG8_LDB(B1, 0, 1); PG8_SCHED; PG8_LDA(At, 0, 0); PG8_STAGE(PG8_SA(1, 1), a1 + hstepA, voffA);
;             PG8_WAIT_V(8); PG8_WAIT_L(0); PG8_BAR; PG8_MMA(0, 0, At, B0); PG8_MMA(0, 1, At, B1); PG8_BAR; PG8_SCHED;
;             PG8_LDA(At, 0, 1); PG8_STAGE(PG8_SB(0, 0), b2, voffB); PG8_STAGE(PG8_SB(0, 1), b2 + hstepB, voffB); PG8_STAGE(PG8_SA(0, 0), a2, voffA);
;             PG8_WAIT_V(8); PG8_WAIT_L(0); PG8_BAR; PG8_MMA(1, 0, At, B0); PG8_MMA(1, 1, At, B1); PG8_BAR; PG8_SCHED;
;             PG8_LDB(B0, 1, 0); PG8_LDB(B1, 1, 1); PG8_SCHED; PG8_LDA(At, 1, 0); PG8_STAGE(PG8_SA(0, 1), a2 + hstepA, voffA);
;             PG8_WAIT_V(8); PG8_WAIT_L(0); PG8_BAR; PG8_MMA(0, 0, At, B0); PG8_MMA(0, 1, At, B1); PG8_BAR; PG8_SCHED;
;             PG8_LDA(At, 1, 1); PG8_STAGE(PG8_SB(1, 0), b3, voffB); PG8_STAGE(PG8_SB(1, 1), b3 + hstepB, voffB); PG8_STAGE(PG8_SA(1, 0), a3, voffA);
;             PG8_WAIT_V(8); PG8_WAIT_L(0); PG8_BAR; PG8_MMA(1, 0, At, B0); PG8_MMA(1, 1, At, B1); PG8_BAR; PG8_SCHED;
.LBB0_1412:
	v_add_u32_e32 v162, s35, v168
	v_add_u32_e32 v166, s36, v168
	ds_read_b128 v[150:153], v162
	ds_read_b128 v[154:157], v162 offset:1024
	ds_read_b128 v[158:161], v162 offset:2048
	ds_read_b128 v[162:165], v162 offset:3072
	ds_read_b128 v[178:181], v166
	ds_read_b128 v[182:185], v166 offset:1024
	ds_read_b128 v[186:189], v166 offset:2048
	ds_read_b128 v[190:193], v166 offset:3072
	s_add_i32 s68, s26, 2
	s_add_u32 s27, s24, 0xfffc0080
	s_addc_u32 s28, s25, -1
	s_cmp_eq_u32 s61, s26
	s_cselect_b32 s26, s65, s66
	s_cselect_b32 s29, s15, s28
	s_cselect_b32 s28, s17, s27
	s_cselect_b32 s27, s64, s67
	s_add_i32 m0, s46, 0xc000
	ds_read_b128 v[194:197], v177
	ds_read_b128 v[198:201], v177 offset:1024
	ds_read_b128 v[202:205], v177 offset:2048
	ds_read_b128 v[206:209], v177 offset:3072
	ds_read_b128 v[210:213], v177 offset:4096
	ds_read_b128 v[214:217], v177 offset:5120
	ds_read_b128 v[218:221], v177 offset:6144
	ds_read_b128 v[222:225], v177 offset:7168
	global_load_lds_dwordx4 v144, s[24:25]
	s_add_i32 m0, s46, 0xe000
	s_nop 0
	global_load_lds_dwordx4 v142, s[24:25]
	s_waitcnt vmcnt(8) lgkmcnt(0)
	s_barrier
	s_setprio 1
	v_mfma_i32_16x16x64_i8 v[126:129], v[150:153], v[194:197], v[126:129]
	v_mfma_i32_16x16x64_i8 v[122:125], v[158:161], v[194:197], v[122:125]
	v_mfma_i32_16x16x64_i8 v[118:121], v[150:153], v[202:205], v[118:121]
	v_mfma_i32_16x16x64_i8 v[114:117], v[158:161], v[202:205], v[114:117]
	v_mfma_i32_16x16x64_i8 v[106:109], v[150:153], v[210:213], v[106:109]
	v_mfma_i32_16x16x64_i8 v[98:101], v[158:161], v[210:213], v[98:101]
	v_mfma_i32_16x16x64_i8 v[90:93], v[150:153], v[218:221], v[90:93]
	v_mfma_i32_16x16x64_i8 v[82:85], v[158:161], v[218:221], v[82:85]
	v_mfma_i32_16x16x64_i8 v[126:129], v[154:157], v[198:201], v[126:129]
	v_mfma_i32_16x16x64_i8 v[122:125], v[162:165], v[198:201], v[122:125]
	v_mfma_i32_16x16x64_i8 v[118:121], v[154:157], v[206:209], v[118:121]
	v_mfma_i32_16x16x64_i8 v[114:117], v[162:165], v[206:209], v[114:117]
	v_mfma_i32_16x16x64_i8 v[106:109], v[154:157], v[214:217], v[106:109]
	v_mfma_i32_16x16x64_i8 v[98:101], v[162:165], v[214:217], v[98:101]
	v_mfma_i32_16x16x64_i8 v[90:93], v[154:157], v[222:225], v[90:93]
	v_mfma_i32_16x16x64_i8 v[82:85], v[162:165], v[222:225], v[82:85]
	s_setprio 0
	s_setprio 1
	v_mfma_i32_16x16x64_i8 v[110:113], v[178:181], v[194:197], v[110:113]
	v_mfma_i32_16x16x64_i8 v[102:105], v[186:189], v[194:197], v[102:105]
	v_mfma_i32_16x16x64_i8 v[94:97], v[178:181], v[202:205], v[94:97]
	v_mfma_i32_16x16x64_i8 v[86:89], v[186:189], v[202:205], v[86:89]
	v_mfma_i32_16x16x64_i8 v[78:81], v[178:181], v[210:213], v[78:81]
	v_mfma_i32_16x16x64_i8 v[74:77], v[186:189], v[210:213], v[74:77]
	v_mfma_i32_16x16x64_i8 v[70:73], v[178:181], v[218:221], v[70:73]
	v_mfma_i32_16x16x64_i8 v[66:69], v[186:189], v[218:221], v[66:69]
	v_mfma_i32_16x16x64_i8 v[110:113], v[182:185], v[198:201], v[110:113]
	v_mfma_i32_16x16x64_i8 v[102:105], v[190:193], v[198:201], v[102:105]
	v_mfma_i32_16x16x64_i8 v[94:97], v[182:185], v[206:209], v[94:97]
	v_mfma_i32_16x16x64_i8 v[86:89], v[190:193], v[206:209], v[86:89]
	v_mfma_i32_16x16x64_i8 v[78:81], v[182:185], v[214:217], v[78:81]
	v_mfma_i32_16x16x64_i8 v[74:77], v[190:193], v[214:217], v[74:77]
	v_mfma_i32_16x16x64_i8 v[70:73], v[182:185], v[222:225], v[70:73]
	v_mfma_i32_16x16x64_i8 v[66:69], v[190:193], v[222:225], v[66:69]
	s_setprio 0
	s_barrier
	s_mov_b32 m0, s23
	s_add_u32 s98, s26, 0x80
	s_addc_u32 s99, s27, 0
	s_add_u32 s70, s26, 0x40000
	ds_read_b128 v[194:197], v177 offset:16384
	ds_read_b128 v[198:201], v177 offset:17408
	ds_read_b128 v[202:205], v177 offset:18432
	ds_read_b128 v[206:209], v177 offset:19456
	global_load_lds_dwordx4 v132, s[26:27]
	s_mov_b32 m0, s43
	s_addc_u32 s71, s27, 0
	global_load_lds_dwordx4 v136, s[26:27]
	s_mov_b32 m0, s44
	ds_read_b128 v[222:225], v177 offset:23552
	global_load_lds_dwordx4 v132, s[70:71]
	s_mov_b32 m0, s45
	ds_read_b128 v[218:221], v177 offset:22528
	global_load_lds_dwordx4 v136, s[70:71]
	s_add_u32 s100, s28, 0x80
	s_addc_u32 s101, s29, 0
	s_mov_b32 m0, s46
	ds_read_b128 v[214:217], v177 offset:21504
	global_load_lds_dwordx4 v130, s[28:29]
	s_mov_b32 m0, s47
	ds_read_b128 v[210:213], v177 offset:20480
	global_load_lds_dwordx4 v134, s[28:29]
	s_waitcnt vmcnt(8) lgkmcnt(0)
	s_barrier
	s_setprio 1
	v_mfma_i32_16x16x64_i8 v[62:65], v[150:153], v[194:197], v[62:65]
	v_mfma_i32_16x16x64_i8 v[58:61], v[158:161], v[194:197], v[58:61]
	v_mfma_i32_16x16x64_i8 v[54:57], v[150:153], v[202:205], v[54:57]
	v_mfma_i32_16x16x64_i8 v[50:53], v[158:161], v[202:205], v[50:53]
	v_mfma_i32_16x16x64_i8 v[42:45], v[150:153], v[210:213], v[42:45]
	v_mfma_i32_16x16x64_i8 v[34:37], v[158:161], v[210:213], v[34:37]
	v_mfma_i32_16x16x64_i8 v[26:29], v[150:153], v[218:221], v[26:29]
	v_mfma_i32_16x16x64_i8 v[18:21], v[158:161], v[218:221], v[18:21]
	v_mfma_i32_16x16x64_i8 v[62:65], v[154:157], v[198:201], v[62:65]
	v_mfma_i32_16x16x64_i8 v[58:61], v[162:165], v[198:201], v[58:61]
	v_mfma_i32_16x16x64_i8 v[54:57], v[154:157], v[206:209], v[54:57]
	v_mfma_i32_16x16x64_i8 v[50:53], v[162:165], v[206:209], v[50:53]
	v_mfma_i32_16x16x64_i8 v[42:45], v[154:157], v[214:217], v[42:45]
	v_mfma_i32_16x16x64_i8 v[34:37], v[162:165], v[214:217], v[34:37]
	v_mfma_i32_16x16x64_i8 v[26:29], v[154:157], v[222:225], v[26:29]
	v_mfma_i32_16x16x64_i8 v[18:21], v[162:165], v[222:225], v[18:21]
	s_setprio 0
	s_setprio 1
	v_mfma_i32_16x16x64_i8 v[46:49], v[178:181], v[194:197], v[46:49]
	v_mfma_i32_16x16x64_i8 v[38:41], v[186:189], v[194:197], v[38:41]
	v_mfma_i32_16x16x64_i8 v[30:33], v[178:181], v[202:205], v[30:33]
	v_mfma_i32_16x16x64_i8 v[22:25], v[186:189], v[202:205], v[22:25]
	v_mfma_i32_16x16x64_i8 v[14:17], v[178:181], v[210:213], v[14:17]
	v_mfma_i32_16x16x64_i8 v[10:13], v[186:189], v[210:213], v[10:13]
	v_mfma_i32_16x16x64_i8 v[6:9], v[178:181], v[218:221], v[6:9]
	v_mfma_i32_16x16x64_i8 v[2:5], v[186:189], v[218:221], v[2:5]
	v_mfma_i32_16x16x64_i8 v[46:49], v[182:185], v[198:201], v[46:49]
	v_mfma_i32_16x16x64_i8 v[38:41], v[190:193], v[198:201], v[38:41]
	v_mfma_i32_16x16x64_i8 v[30:33], v[182:185], v[206:209], v[30:33]
	v_mfma_i32_16x16x64_i8 v[22:25], v[190:193], v[206:209], v[22:25]
	v_mfma_i32_16x16x64_i8 v[14:17], v[182:185], v[214:217], v[14:17]
	v_mfma_i32_16x16x64_i8 v[10:13], v[190:193], v[214:217], v[10:13]
	v_mfma_i32_16x16x64_i8 v[6:9], v[182:185], v[222:225], v[6:9]
	v_mfma_i32_16x16x64_i8 v[2:5], v[190:193], v[222:225], v[2:5]
	s_setprio 0
	s_barrier
; #define PG8_STAGE(bufoff, gbase, voff) do { _Pragma("unroll") for (int _i = 0; _i < 2; ++_i) \
;         __builtin_amdgcn_global_load_lds((const unsigned*)((const char*)(gbase) + (voff)[_i]), (PG8_LAS unsigned*)(lds + (bufoff) + ldsw + _i * 8192), 16, 0, 0); } while (0)
; #define PG8_LDA(dst, b, h) do { if constexpr (DT != 1) { _Pragma("unroll") for (int m = 0; m < 4; ++m) _Pragma("unroll") for (int k = 0; k < 2; ++k) dst[m][k] = *(const PG8_LAS bf16x8*)(lds + PG8_SA(b, h) + aoff + m * 2048 + k * 1024); } \
;         else { _Pragma("unroll") for (int m = 0; m < 4; ++m) dst##8[m] = ld32(lds + PG8_SA(b, h) + aoff + m * 2048); } } while (0)
; #define PG8_LDB(dst, b, h) do { if constexpr (DT != 1) { _Pragma("unroll") for (int n = 0; n < 2; ++n) _Pragma("unroll") for (int k = 0; k < 2; ++k) dst[n][k] = *(const PG8_LAS bf16x8*)(lds + PG8_SB(b, h) + boff + n * 2048 + k * 1024); } \
;         else { _Pragma("unroll") for (int n = 0; n < 2; ++n) dst##8[n] = ld32(lds + PG8_SB(b, h) + boff + n * 2048); } } while (0)
; #define PG8_WAIT_V(n) asm volatile("s_waitcnt vmcnt(" #n ")" ::: "memory")
; #define PG8_WAIT_L(n) asm volatile("s_waitcnt lgkmcnt(" #n ")" ::: "memory")
; #define PG8_BAR __builtin_amdgcn_s_barrier()
; #define PG8_SCHED __builtin_amdgcn_sched_barrier(0)
;     ...
;             PG8_LDB(B0, 0, 0); PG8_LDB(B1, 0, 1); PG8_SCHED; PG8_LDA(At, 0, 0); PG8_STAGE(PG8_SA(1, 1), a1 + hstepA, voffA);
;             PG8_WAIT_V(8); PG8_WAIT_L(0); PG8_BAR; PG8_MMA(0, 0, At, B0); PG8_MMA(0, 1, At, B1); PG8_BAR; PG8_SCHED;
;             PG8_LDA(At, 0, 1); PG8_STAGE(PG8_SB(0, 0), b2, voffB); PG8_STAGE(PG8_SB(0, 1), b2 + hstepB, voffB); PG8_STAGE(PG8_SA(0, 0), a2, voffA);
;             PG8_WAIT_V(8); PG8_WAIT_L(0); PG8_BAR; PG8_MMA(1, 0, At, B0); PG8_MMA(1, 1, At, B1); PG8_BAR; PG8_SCHED;
;             PG8_LDB(B0, 1, 0); PG8_LDB(B1, 1, 1); PG8_SCHED; PG8_LDA(At, 1, 0); PG8_STAGE(PG8_SA(0, 1), a2 + hstepA, voffA);
;             PG8_WAIT_V(8); PG8_WAIT_L(0); PG8_BAR; PG8_MMA(0, 0, At, B0); PG8_MMA(0, 1, At, B1); PG8_BAR; PG8_SCHED;
;             PG8_LDA(At, 1, 1); PG8_STAGE(PG8_SB(1, 0), b3, voffB); PG8_STAGE(PG8_SB(1, 1), b3 + hstepB, voffB); PG8_STAGE(PG8_SA(1, 0), a3, voffA);
;             PG8_WAIT_V(8); PG8_WAIT_L(0); PG8_BAR; PG8_MMA(1, 0, At, B0); PG8_MMA(1, 1, At, B1); PG8_BAR; PG8_SCHED;
	v_add_u32_e32 v162, s51, v168
	v_add_u32_e32 v190, s52, v168
	ds_read_b128 v[150:153], v162
	ds_read_b128 v[154:157], v162 offset:1024
	ds_read_b128 v[158:161], v162 offset:2048
	ds_read_b128 v[162:165], v162 offset:3072
	ds_read_b128 v[178:181], v190
	ds_read_b128 v[182:185], v190 offset:1024
	ds_read_b128 v[186:189], v190 offset:2048
	ds_read_b128 v[190:193], v190 offset:3072
	s_add_u32 s28, s28, 0x40000
	s_addc_u32 s29, s29, 0
	s_mov_b32 m0, s48
	ds_read_b128 v[194:197], v177 offset:32768
	ds_read_b128 v[198:201], v177 offset:33792
	ds_read_b128 v[202:205], v177 offset:34816
	ds_read_b128 v[206:209], v177 offset:35840
	ds_read_b128 v[210:213], v177 offset:36864
	ds_read_b128 v[214:217], v177 offset:37888
	ds_read_b128 v[218:221], v177 offset:38912
	global_load_lds_dwordx4 v130, s[28:29]
	s_mov_b32 m0, s49
	ds_read_b128 v[222:225], v177 offset:39936
	global_load_lds_dwordx4 v134, s[28:29]
	s_waitcnt vmcnt(8) lgkmcnt(0)
	s_barrier
	s_setprio 1
	v_mfma_i32_16x16x64_i8 v[126:129], v[150:153], v[194:197], v[126:129]
	v_mfma_i32_16x16x64_i8 v[122:125], v[158:161], v[194:197], v[122:125]
	v_mfma_i32_16x16x64_i8 v[118:121], v[150:153], v[202:205], v[118:121]
	v_mfma_i32_16x16x64_i8 v[114:117], v[158:161], v[202:205], v[114:117]
	v_mfma_i32_16x16x64_i8 v[106:109], v[150:153], v[210:213], v[106:109]
	v_mfma_i32_16x16x64_i8 v[98:101], v[158:161], v[210:213], v[98:101]
	v_mfma_i32_16x16x64_i8 v[90:93], v[150:153], v[218:221], v[90:93]
	v_mfma_i32_16x16x64_i8 v[82:85], v[158:161], v[218:221], v[82:85]
	v_mfma_i32_16x16x64_i8 v[126:129], v[154:157], v[198:201], v[126:129]
	v_mfma_i32_16x16x64_i8 v[122:125], v[162:165], v[198:201], v[122:125]
	v_mfma_i32_16x16x64_i8 v[118:121], v[154:157], v[206:209], v[118:121]
	v_mfma_i32_16x16x64_i8 v[114:117], v[162:165], v[206:209], v[114:117]
	v_mfma_i32_16x16x64_i8 v[106:109], v[154:157], v[214:217], v[106:109]
	v_mfma_i32_16x16x64_i8 v[98:101], v[162:165], v[214:217], v[98:101]
	v_mfma_i32_16x16x64_i8 v[90:93], v[154:157], v[222:225], v[90:93]
	v_mfma_i32_16x16x64_i8 v[82:85], v[162:165], v[222:225], v[82:85]
	s_setprio 0
	s_setprio 1
	v_mfma_i32_16x16x64_i8 v[110:113], v[178:181], v[194:197], v[110:113]
	v_mfma_i32_16x16x64_i8 v[102:105], v[186:189], v[194:197], v[102:105]
	v_mfma_i32_16x16x64_i8 v[94:97], v[178:181], v[202:205], v[94:97]
	v_mfma_i32_16x16x64_i8 v[86:89], v[186:189], v[202:205], v[86:89]
	v_mfma_i32_16x16x64_i8 v[78:81], v[178:181], v[210:213], v[78:81]
	v_mfma_i32_16x16x64_i8 v[74:77], v[186:189], v[210:213], v[74:77]
	v_mfma_i32_16x16x64_i8 v[70:73], v[178:181], v[218:221], v[70:73]
	v_mfma_i32_16x16x64_i8 v[66:69], v[186:189], v[218:221], v[66:69]
	v_mfma_i32_16x16x64_i8 v[110:113], v[182:185], v[198:201], v[110:113]
	v_mfma_i32_16x16x64_i8 v[102:105], v[190:193], v[198:201], v[102:105]
	v_mfma_i32_16x16x64_i8 v[94:97], v[182:185], v[206:209], v[94:97]
	v_mfma_i32_16x16x64_i8 v[86:89], v[190:193], v[206:209], v[86:89]
	v_mfma_i32_16x16x64_i8 v[78:81], v[182:185], v[214:217], v[78:81]
	v_mfma_i32_16x16x64_i8 v[74:77], v[190:193], v[214:217], v[74:77]
	v_mfma_i32_16x16x64_i8 v[70:73], v[182:185], v[222:225], v[70:73]
	v_mfma_i32_16x16x64_i8 v[66:69], v[190:193], v[222:225], v[66:69]
	s_setprio 0
	s_barrier
	s_mov_b32 m0, s55
	s_add_u32 s26, s26, 0x40080
	ds_read_b128 v[194:197], v177 offset:49152
	ds_read_b128 v[198:201], v177 offset:50176
	ds_read_b128 v[202:205], v177 offset:51200
	ds_read_b128 v[206:209], v177 offset:52224
	global_load_lds_dwordx4 v132, s[98:99]
	s_mov_b32 m0, s56
	s_addc_u32 s27, s27, 0
	global_load_lds_dwordx4 v136, s[98:99]
	s_mov_b32 m0, s59
	ds_read_b128 v[222:225], v177 offset:56320
	global_load_lds_dwordx4 v132, s[26:27]
	s_mov_b32 m0, s60
	ds_read_b128 v[218:221], v177 offset:55296
	global_load_lds_dwordx4 v136, s[26:27]
	s_mov_b32 m0, s57
	ds_read_b128 v[214:217], v177 offset:54272
	global_load_lds_dwordx4 v130, s[100:101]
	s_mov_b32 m0, s58
	ds_read_b128 v[210:213], v177 offset:53248
	global_load_lds_dwordx4 v134, s[100:101]
	s_waitcnt vmcnt(8) lgkmcnt(0)
	s_barrier
	s_setprio 1
	v_mfma_i32_16x16x64_i8 v[62:65], v[150:153], v[194:197], v[62:65]
	v_mfma_i32_16x16x64_i8 v[58:61], v[158:161], v[194:197], v[58:61]
	v_mfma_i32_16x16x64_i8 v[54:57], v[150:153], v[202:205], v[54:57]
	v_mfma_i32_16x16x64_i8 v[50:53], v[158:161], v[202:205], v[50:53]
	v_mfma_i32_16x16x64_i8 v[42:45], v[150:153], v[210:213], v[42:45]
	v_mfma_i32_16x16x64_i8 v[34:37], v[158:161], v[210:213], v[34:37]
	v_mfma_i32_16x16x64_i8 v[26:29], v[150:153], v[218:221], v[26:29]
	v_mfma_i32_16x16x64_i8 v[18:21], v[158:161], v[218:221], v[18:21]
	v_mfma_i32_16x16x64_i8 v[62:65], v[154:157], v[198:201], v[62:65]
	v_mfma_i32_16x16x64_i8 v[58:61], v[162:165], v[198:201], v[58:61]
	v_mfma_i32_16x16x64_i8 v[54:57], v[154:157], v[206:209], v[54:57]
	v_mfma_i32_16x16x64_i8 v[50:53], v[162:165], v[206:209], v[50:53]
	v_mfma_i32_16x16x64_i8 v[42:45], v[154:157], v[214:217], v[42:45]
	v_mfma_i32_16x16x64_i8 v[34:37], v[162:165], v[214:217], v[34:37]
	v_mfma_i32_16x16x64_i8 v[26:29], v[154:157], v[222:225], v[26:29]
	v_mfma_i32_16x16x64_i8 v[18:21], v[162:165], v[222:225], v[18:21]
	s_setprio 0
	s_setprio 1
	v_mfma_i32_16x16x64_i8 v[46:49], v[178:181], v[194:197], v[46:49]
	v_mfma_i32_16x16x64_i8 v[38:41], v[186:189], v[194:197], v[38:41]
	v_mfma_i32_16x16x64_i8 v[30:33], v[178:181], v[202:205], v[30:33]
	v_mfma_i32_16x16x64_i8 v[22:25], v[186:189], v[202:205], v[22:25]
	v_mfma_i32_16x16x64_i8 v[14:17], v[178:181], v[210:213], v[14:17]
	v_mfma_i32_16x16x64_i8 v[10:13], v[186:189], v[210:213], v[10:13]
	v_mfma_i32_16x16x64_i8 v[6:9], v[178:181], v[218:221], v[6:9]
	v_mfma_i32_16x16x64_i8 v[2:5], v[186:189], v[218:221], v[2:5]
	v_mfma_i32_16x16x64_i8 v[46:49], v[182:185], v[198:201], v[46:49]
	v_mfma_i32_16x16x64_i8 v[38:41], v[190:193], v[198:201], v[38:41]
	v_mfma_i32_16x16x64_i8 v[30:33], v[182:185], v[206:209], v[30:33]
	v_mfma_i32_16x16x64_i8 v[22:25], v[190:193], v[206:209], v[22:25]
	v_mfma_i32_16x16x64_i8 v[14:17], v[182:185], v[214:217], v[14:17]
	v_mfma_i32_16x16x64_i8 v[10:13], v[190:193], v[214:217], v[10:13]
	v_mfma_i32_16x16x64_i8 v[6:9], v[182:185], v[222:225], v[6:9]
	v_mfma_i32_16x16x64_i8 v[2:5], v[190:193], v[222:225], v[2:5]
	s_setprio 0
	s_barrier
	s_add_u32 s66, s66, 0x100
	s_addc_u32 s67, s67, 0
	s_add_u32 s24, s24, 0x100
	s_addc_u32 s25, s25, 0
	s_cmp_ge_i32 s68, s54
	s_mov_b32 s26, s68
	s_cbranch_scc0 .LBB0_1412

; #define PG8_STAGE(bufoff, gbase, voff) do { _Pragma("unroll") for (int _i = 0; _i < 2; ++_i) \
;         __builtin_amdgcn_global_load_lds((const unsigned*)((const char*)(gbase) + (voff)[_i]), (PG8_LAS unsigned*)(lds + (bufoff) + ldsw + _i * 8192), 16, 0, 0); } while (0)
; #define PG8_LDA(dst, b, h) do { if constexpr (DT != 1) { _Pragma("unroll") for (int m = 0; m < 4; ++m) _Pragma("unroll") for (int k = 0; k < 2; ++k) dst[m][k] = *(const PG8_LAS bf16x8*)(lds + PG8_SA(b, h) + aoff + m * 2048 + k * 1024); } \
;         else { _Pragma("unroll") for (int m = 0; m < 4; ++m) dst##8[m] = ld32(lds + PG8_SA(b, h) + aoff + m * 2048); } } while (0)
; #define PG8_WAIT_V(n) asm volatile("s_waitcnt vmcnt(" #n ")" ::: "memory")
;     ...
;         const char* nA = has_next ? (const char*)g.A + (size_t)nxt.pm * tstepA : cA; const char* nB = has_next ? (const char*)g.Bt + (size_t)nxt.pn * tstepB : cB;
;         for (int t = 0; t < nt; t += 2) {
;             const bool last = (t == nt - 2);
;             const char* a1 = cA + (size_t)(t + 1) * kstep;
;             const char* a2 = last ? nA : cA + (size_t)(t + 2) * kstep; const char* b2 = last ? nB : cB + (size_t)(t + 2) * kstep;
;             const char* a3 = a2 + kstep; const char* b3 = b2 + kstep;
;             if (last && has_next) S.a_ready(nxt);
;             if constexpr (SP2) {
;             PG8_LDB(B0, 0, 0); PG8_LDB(B1, 0, 1); PG8_SCHED; PG8_LDA(At, 0, 0); PG8_STAGE(PG8_SA(1, 1), a1 + hstepA, voffA);
;             PG8_WAIT_V(8); PG8_WAIT_L(0); PG8_BAR; PG8_MMA(0, 0, At, B0); PG8_MMA(0, 1, At, B1); PG8_BAR; PG8_SCHED;
;             PG8_LDA(At, 0, 1); PG8_STAGE(PG8_SB(0, 0), b2, voffB); PG8_STAGE(PG8_SB(0, 1), b2 + hstepB, voffB); PG8_STAGE(PG8_SA(0, 0), a2, voffA);
;             PG8_WAIT_V(8); PG8_WAIT_L(0); PG8_BAR; PG8_MMA(1, 0, At, B0); PG8_MMA(1, 1, At, B1); PG8_BAR; PG8_SCHED;
;             PG8_LDB(B0, 1, 0); PG8_LDB(B1, 1, 1); PG8_SCHED; PG8_LDA(At, 1, 0); PG8_STAGE(PG8_SA(0, 1), a2 + hstepA, voffA);
;             PG8_WAIT_V(8); PG8_WAIT_L(0); PG8_BAR; PG8_MMA(0, 0, At, B0); PG8_MMA(0, 1, At, B1); PG8_BAR; PG8_SCHED;
;             PG8_LDA(At, 1, 1); PG8_STAGE(PG8_SB(1, 0), b3, voffB); PG8_STAGE(PG8_SB(1, 1), b3 + hstepB, voffB); PG8_STAGE(PG8_SA(1, 0), a3, voffA);
;             PG8_WAIT_V(8); PG8_WAIT_L(0); PG8_BAR; PG8_MMA(1, 0, At, B0); PG8_MMA(1, 1, At, B1); PG8_BAR; PG8_SCHED;
.Lzs_9:
	s_cbranch_vccnz .LBB0_2263
	s_and_b64 s[30:31], s[4:5], exec
	s_cselect_b32 s2, s19, s29
	s_cselect_b32 s15, s18, s28
	s_cselect_b32 s17, s21, s27
	s_cselect_b32 s23, s20, s26
	s_add_u32 s25, s26, 0x100
	s_addc_u32 s64, s27, 0
	s_add_u32 s26, s28, 0x80080
	s_addc_u32 s27, s29, 0
	s_mov_b32 s28, 0
	ds_read_b128 v[154:157], v148
	ds_read_b128 v[158:161], v148 offset:1024
	ds_read_b128 v[162:165], v148 offset:2048
	ds_read_b128 v[166:169], v148 offset:3072
	ds_read_b128 v[170:173], v149
	ds_read_b128 v[174:177], v149 offset:1024
	ds_read_b128 v[178:181], v149 offset:2048
	ds_read_b128 v[182:185], v149 offset:3072
	s_add_i32 s65, s28, 2
	s_add_u32 s29, s26, 0xfff80080
	s_addc_u32 s30, s27, -1
	s_cmp_eq_u32 s61, s28
	s_cselect_b32 s28, s23, s25
	s_cselect_b32 s31, s2, s30
	s_cselect_b32 s30, s15, s29
	s_cselect_b32 s29, s17, s64
	s_add_i32 m0, s44, 0xc000
	ds_read_b128 v[186:189], v150
	ds_read_b128 v[190:193], v150 offset:1024
	ds_read_b128 v[194:197], v150 offset:2048
	ds_read_b128 v[198:201], v150 offset:3072
	ds_read_b128 v[202:205], v150 offset:4096
	ds_read_b128 v[206:209], v150 offset:5120
	ds_read_b128 v[210:213], v150 offset:6144
	ds_read_b128 v[214:217], v150 offset:7168
	global_load_lds_dwordx4 v142, s[26:27]
	s_add_i32 m0, s44, 0xe000
	s_nop 0
	global_load_lds_dwordx4 v140, s[26:27]
	s_waitcnt vmcnt(8) lgkmcnt(0)
	s_barrier
	s_setprio 1
	v_mfma_f32_16x16x32_bf16 v[126:129], v[154:157], v[186:189], 0
	v_mfma_f32_16x16x32_bf16 v[122:125], v[162:165], v[186:189], 0
	v_mfma_f32_16x16x32_bf16 v[110:113], v[154:157], v[194:197], 0
	v_mfma_f32_16x16x32_bf16 v[106:109], v[162:165], v[194:197], 0
	v_mfma_f32_16x16x32_bf16 v[94:97], v[154:157], v[202:205], 0
	v_mfma_f32_16x16x32_bf16 v[90:93], v[162:165], v[202:205], 0
	v_mfma_f32_16x16x32_bf16 v[78:81], v[154:157], v[210:213], 0
	v_mfma_f32_16x16x32_bf16 v[74:77], v[162:165], v[210:213], 0
	v_mfma_f32_16x16x32_bf16 v[126:129], v[158:161], v[190:193], v[126:129]
	v_mfma_f32_16x16x32_bf16 v[122:125], v[166:169], v[190:193], v[122:125]
	v_mfma_f32_16x16x32_bf16 v[110:113], v[158:161], v[198:201], v[110:113]
	v_mfma_f32_16x16x32_bf16 v[106:109], v[166:169], v[198:201], v[106:109]
	v_mfma_f32_16x16x32_bf16 v[94:97], v[158:161], v[206:209], v[94:97]
	v_mfma_f32_16x16x32_bf16 v[90:93], v[166:169], v[206:209], v[90:93]
	v_mfma_f32_16x16x32_bf16 v[78:81], v[158:161], v[214:217], v[78:81]
	v_mfma_f32_16x16x32_bf16 v[74:77], v[166:169], v[214:217], v[74:77]
	s_setprio 0
	s_setprio 1
	v_mfma_f32_16x16x32_bf16 v[118:121], v[170:173], v[186:189], 0
	v_mfma_f32_16x16x32_bf16 v[114:117], v[178:181], v[186:189], 0
	v_mfma_f32_16x16x32_bf16 v[102:105], v[170:173], v[194:197], 0
	v_mfma_f32_16x16x32_bf16 v[98:101], v[178:181], v[194:197], 0
	v_mfma_f32_16x16x32_bf16 v[86:89], v[170:173], v[202:205], 0
	v_mfma_f32_16x16x32_bf16 v[82:85], v[178:181], v[202:205], 0
	v_mfma_f32_16x16x32_bf16 v[70:73], v[170:173], v[210:213], 0
	v_mfma_f32_16x16x32_bf16 v[66:69], v[178:181], v[210:213], 0
	v_mfma_f32_16x16x32_bf16 v[118:121], v[174:177], v[190:193], v[118:121]
	v_mfma_f32_16x16x32_bf16 v[114:117], v[182:185], v[190:193], v[114:117]
	v_mfma_f32_16x16x32_bf16 v[102:105], v[174:177], v[198:201], v[102:105]
	v_mfma_f32_16x16x32_bf16 v[98:101], v[182:185], v[198:201], v[98:101]
	v_mfma_f32_16x16x32_bf16 v[86:89], v[174:177], v[206:209], v[86:89]
	v_mfma_f32_16x16x32_bf16 v[82:85], v[182:185], v[206:209], v[82:85]
	v_mfma_f32_16x16x32_bf16 v[70:73], v[174:177], v[214:217], v[70:73]
	v_mfma_f32_16x16x32_bf16 v[66:69], v[182:185], v[214:217], v[66:69]
	s_setprio 0
	s_barrier
	s_mov_b32 m0, s40
	s_add_u32 s98, s28, 0x80
	s_addc_u32 s99, s29, 0
	s_add_u32 s66, s28, 0x80000
	ds_read_b128 v[186:189], v150 offset:16384
	ds_read_b128 v[190:193], v150 offset:17408
	ds_read_b128 v[194:197], v150 offset:18432
	ds_read_b128 v[198:201], v150 offset:19456
	global_load_lds_dwordx4 v132, s[28:29]
	s_mov_b32 m0, s41
	s_addc_u32 s67, s29, 0
	global_load_lds_dwordx4 v136, s[28:29]
	s_mov_b32 m0, s42
	ds_read_b128 v[214:217], v150 offset:23552
	global_load_lds_dwordx4 v132, s[66:67]
	s_mov_b32 m0, s43
	ds_read_b128 v[210:213], v150 offset:22528
	global_load_lds_dwordx4 v136, s[66:67]
	s_add_u32 s100, s30, 0x80
	s_addc_u32 s101, s31, 0
	s_mov_b32 m0, s44
	ds_read_b128 v[206:209], v150 offset:21504
	global_load_lds_dwordx4 v130, s[30:31]
	s_mov_b32 m0, s45
	ds_read_b128 v[202:205], v150 offset:20480
	global_load_lds_dwordx4 v134, s[30:31]
	s_waitcnt vmcnt(8) lgkmcnt(0)
	s_barrier
	s_setprio 1
	v_mfma_f32_16x16x32_bf16 v[62:65], v[154:157], v[186:189], 0
	v_mfma_f32_16x16x32_bf16 v[58:61], v[162:165], v[186:189], 0
	v_mfma_f32_16x16x32_bf16 v[46:49], v[154:157], v[194:197], 0
	v_mfma_f32_16x16x32_bf16 v[42:45], v[162:165], v[194:197], 0
	v_mfma_f32_16x16x32_bf16 v[30:33], v[154:157], v[202:205], 0
	v_mfma_f32_16x16x32_bf16 v[26:29], v[162:165], v[202:205], 0
	v_mfma_f32_16x16x32_bf16 v[14:17], v[154:157], v[210:213], 0
	v_mfma_f32_16x16x32_bf16 v[10:13], v[162:165], v[210:213], 0
	v_mfma_f32_16x16x32_bf16 v[62:65], v[158:161], v[190:193], v[62:65]
	v_mfma_f32_16x16x32_bf16 v[58:61], v[166:169], v[190:193], v[58:61]
	v_mfma_f32_16x16x32_bf16 v[46:49], v[158:161], v[198:201], v[46:49]
	v_mfma_f32_16x16x32_bf16 v[42:45], v[166:169], v[198:201], v[42:45]
	v_mfma_f32_16x16x32_bf16 v[30:33], v[158:161], v[206:209], v[30:33]
	v_mfma_f32_16x16x32_bf16 v[26:29], v[166:169], v[206:209], v[26:29]
	v_mfma_f32_16x16x32_bf16 v[14:17], v[158:161], v[214:217], v[14:17]
	v_mfma_f32_16x16x32_bf16 v[10:13], v[166:169], v[214:217], v[10:13]
	s_setprio 0
	s_setprio 1
	v_mfma_f32_16x16x32_bf16 v[54:57], v[170:173], v[186:189], 0
	v_mfma_f32_16x16x32_bf16 v[50:53], v[178:181], v[186:189], 0
	v_mfma_f32_16x16x32_bf16 v[38:41], v[170:173], v[194:197], 0
	v_mfma_f32_16x16x32_bf16 v[34:37], v[178:181], v[194:197], 0
	v_mfma_f32_16x16x32_bf16 v[22:25], v[170:173], v[202:205], 0
	v_mfma_f32_16x16x32_bf16 v[18:21], v[178:181], v[202:205], 0
	v_mfma_f32_16x16x32_bf16 v[6:9], v[170:173], v[210:213], 0
	v_mfma_f32_16x16x32_bf16 v[2:5], v[178:181], v[210:213], 0
	v_mfma_f32_16x16x32_bf16 v[54:57], v[174:177], v[190:193], v[54:57]
	v_mfma_f32_16x16x32_bf16 v[50:53], v[182:185], v[190:193], v[50:53]
	v_mfma_f32_16x16x32_bf16 v[38:41], v[174:177], v[198:201], v[38:41]
	v_mfma_f32_16x16x32_bf16 v[34:37], v[182:185], v[198:201], v[34:37]
	v_mfma_f32_16x16x32_bf16 v[22:25], v[174:177], v[206:209], v[22:25]
	v_mfma_f32_16x16x32_bf16 v[18:21], v[182:185], v[206:209], v[18:21]
	v_mfma_f32_16x16x32_bf16 v[6:9], v[174:177], v[214:217], v[6:9]
	v_mfma_f32_16x16x32_bf16 v[2:5], v[182:185], v[214:217], v[2:5]
	s_setprio 0
	s_barrier
; #define PG8_STAGE(bufoff, gbase, voff) do { _Pragma("unroll") for (int _i = 0; _i < 2; ++_i) \
;         __builtin_amdgcn_global_load_lds((const unsigned*)((const char*)(gbase) + (voff)[_i]), (PG8_LAS unsigned*)(lds + (bufoff) + ldsw + _i * 8192), 16, 0, 0); } while (0)
; #define PG8_LDA(dst, b, h) do { if constexpr (DT != 1) { _Pragma("unroll") for (int m = 0; m < 4; ++m) _Pragma("unroll") for (int k = 0; k < 2; ++k) dst[m][k] = *(const PG8_LAS bf16x8*)(lds + PG8_SA(b, h) + aoff + m * 2048 + k * 1024); } \
;         else { _Pragma("unroll") for (int m = 0; m < 4; ++m) dst##8[m] = ld32(lds + PG8_SA(b, h) + aoff + m * 2048); } } while (0)
; #define PG8_LDB(dst, b, h) do { if constexpr (DT != 1) { _Pragma("unroll") for (int n = 0; n < 2; ++n) _Pragma("unroll") for (int k = 0; k < 2; ++k) dst[n][k] = *(const PG8_LAS bf16x8*)(lds + PG8_SB(b, h) + boff + n * 2048 + k * 1024); } \
;         else { _Pragma("unroll") for (int n = 0; n < 2; ++n) dst##8[n] = ld32(lds + PG8_SB(b, h) + boff + n * 2048); } } while (0)
; #define PG8_WAIT_V(n) asm volatile("s_waitcnt vmcnt(" #n ")" ::: "memory")
; #define PG8_WAIT_L(n) asm volatile("s_waitcnt lgkmcnt(" #n ")" ::: "memory")
; #define PG8_BAR __builtin_amdgcn_s_barrier()
; #define PG8_SCHED __builtin_amdgcn_sched_barrier(0)
;     ...
;             PG8_LDB(B0, 0, 0); PG8_LDB(B1, 0, 1); PG8_SCHED; PG8_LDA(At, 0, 0); PG8_STAGE(PG8_SA(1, 1), a1 + hstepA, voffA);
;             PG8_WAIT_V(8); PG8_WAIT_L(0); PG8_BAR; PG8_MMA(0, 0, At, B0); PG8_MMA(0, 1, At, B1); PG8_BAR; PG8_SCHED;
;             PG8_LDA(At, 0, 1); PG8_STAGE(PG8_SB(0, 0), b2, voffB); PG8_STAGE(PG8_SB(0, 1), b2 + hstepB, voffB); PG8_STAGE(PG8_SA(0, 0), a2, voffA);
;             PG8_WAIT_V(8); PG8_WAIT_L(0); PG8_BAR; PG8_MMA(1, 0, At, B0); PG8_MMA(1, 1, At, B1); PG8_BAR; PG8_SCHED;
;             PG8_LDB(B0, 1, 0); PG8_LDB(B1, 1, 1); PG8_SCHED; PG8_LDA(At, 1, 0); PG8_STAGE(PG8_SA(0, 1), a2 + hstepA, voffA);
;             PG8_WAIT_V(8); PG8_WAIT_L(0); PG8_BAR; PG8_MMA(0, 0, At, B0); PG8_MMA(0, 1, At, B1); PG8_BAR; PG8_SCHED;
;             PG8_LDA(At, 1, 1); PG8_STAGE(PG8_SB(1, 0), b3, voffB); PG8_STAGE(PG8_SB(1, 1), b3 + hstepB, voffB); PG8_STAGE(PG8_SA(1, 0), a3, voffA);
;             PG8_WAIT_V(8); PG8_WAIT_L(0); PG8_BAR; PG8_MMA(1, 0, At, B0); PG8_MMA(1, 1, At, B1); PG8_BAR; PG8_SCHED;
	ds_read_b128 v[154:157], v151
	ds_read_b128 v[158:161], v151 offset:1024
	ds_read_b128 v[162:165], v151 offset:2048
	ds_read_b128 v[166:169], v151 offset:3072
	ds_read_b128 v[170:173], v152
	ds_read_b128 v[174:177], v152 offset:1024
	ds_read_b128 v[178:181], v152 offset:2048
	ds_read_b128 v[182:185], v152 offset:3072
	s_add_u32 s30, s30, 0x80000
	s_addc_u32 s31, s31, 0
	s_mov_b32 m0, s46
	ds_read_b128 v[186:189], v150 offset:32768
	ds_read_b128 v[190:193], v150 offset:33792
	ds_read_b128 v[194:197], v150 offset:34816
	ds_read_b128 v[198:201], v150 offset:35840
	ds_read_b128 v[202:205], v150 offset:36864
	ds_read_b128 v[206:209], v150 offset:37888
	ds_read_b128 v[210:213], v150 offset:38912
	global_load_lds_dwordx4 v130, s[30:31]
	s_mov_b32 m0, s47
	ds_read_b128 v[214:217], v150 offset:39936
	global_load_lds_dwordx4 v134, s[30:31]
	s_waitcnt vmcnt(8) lgkmcnt(0)
	s_barrier
	s_setprio 1
	v_mfma_f32_16x16x32_bf16 v[126:129], v[154:157], v[186:189], v[126:129]
	v_mfma_f32_16x16x32_bf16 v[122:125], v[162:165], v[186:189], v[122:125]
	v_mfma_f32_16x16x32_bf16 v[110:113], v[154:157], v[194:197], v[110:113]
	v_mfma_f32_16x16x32_bf16 v[106:109], v[162:165], v[194:197], v[106:109]
	v_mfma_f32_16x16x32_bf16 v[94:97], v[154:157], v[202:205], v[94:97]
	v_mfma_f32_16x16x32_bf16 v[90:93], v[162:165], v[202:205], v[90:93]
	v_mfma_f32_16x16x32_bf16 v[78:81], v[154:157], v[210:213], v[78:81]
	v_mfma_f32_16x16x32_bf16 v[74:77], v[162:165], v[210:213], v[74:77]
	v_mfma_f32_16x16x32_bf16 v[126:129], v[158:161], v[190:193], v[126:129]
	v_mfma_f32_16x16x32_bf16 v[122:125], v[166:169], v[190:193], v[122:125]
	v_mfma_f32_16x16x32_bf16 v[110:113], v[158:161], v[198:201], v[110:113]
	v_mfma_f32_16x16x32_bf16 v[106:109], v[166:169], v[198:201], v[106:109]
	v_mfma_f32_16x16x32_bf16 v[94:97], v[158:161], v[206:209], v[94:97]
	v_mfma_f32_16x16x32_bf16 v[90:93], v[166:169], v[206:209], v[90:93]
	v_mfma_f32_16x16x32_bf16 v[78:81], v[158:161], v[214:217], v[78:81]
	v_mfma_f32_16x16x32_bf16 v[74:77], v[166:169], v[214:217], v[74:77]
	s_setprio 0
	s_setprio 1
	v_mfma_f32_16x16x32_bf16 v[118:121], v[170:173], v[186:189], v[118:121]
	v_mfma_f32_16x16x32_bf16 v[114:117], v[178:181], v[186:189], v[114:117]
	v_mfma_f32_16x16x32_bf16 v[102:105], v[170:173], v[194:197], v[102:105]
	v_mfma_f32_16x16x32_bf16 v[98:101], v[178:181], v[194:197], v[98:101]
	v_mfma_f32_16x16x32_bf16 v[86:89], v[170:173], v[202:205], v[86:89]
	v_mfma_f32_16x16x32_bf16 v[82:85], v[178:181], v[202:205], v[82:85]
	v_mfma_f32_16x16x32_bf16 v[70:73], v[170:173], v[210:213], v[70:73]
	v_mfma_f32_16x16x32_bf16 v[66:69], v[178:181], v[210:213], v[66:69]
	v_mfma_f32_16x16x32_bf16 v[118:121], v[174:177], v[190:193], v[118:121]
	v_mfma_f32_16x16x32_bf16 v[114:117], v[182:185], v[190:193], v[114:117]
	v_mfma_f32_16x16x32_bf16 v[102:105], v[174:177], v[198:201], v[102:105]
	v_mfma_f32_16x16x32_bf16 v[98:101], v[182:185], v[198:201], v[98:101]
	v_mfma_f32_16x16x32_bf16 v[86:89], v[174:177], v[206:209], v[86:89]
	v_mfma_f32_16x16x32_bf16 v[82:85], v[182:185], v[206:209], v[82:85]
	v_mfma_f32_16x16x32_bf16 v[70:73], v[174:177], v[214:217], v[70:73]
	v_mfma_f32_16x16x32_bf16 v[66:69], v[182:185], v[214:217], v[66:69]
	s_setprio 0
	s_barrier
	s_mov_b32 m0, s53
	s_add_u32 s28, s28, 0x80080
	ds_read_b128 v[186:189], v150 offset:49152
	ds_read_b128 v[190:193], v150 offset:50176
	ds_read_b128 v[194:197], v150 offset:51200
	ds_read_b128 v[198:201], v150 offset:52224
	global_load_lds_dwordx4 v132, s[98:99]
	s_mov_b32 m0, s54
	s_addc_u32 s29, s29, 0
	global_load_lds_dwordx4 v136, s[98:99]
	s_mov_b32 m0, s57
	ds_read_b128 v[214:217], v150 offset:56320
	global_load_lds_dwordx4 v132, s[28:29]
	s_mov_b32 m0, s58
	ds_read_b128 v[210:213], v150 offset:55296
	global_load_lds_dwordx4 v136, s[28:29]
	s_mov_b32 m0, s55
	ds_read_b128 v[206:209], v150 offset:54272
	global_load_lds_dwordx4 v130, s[100:101]
	s_mov_b32 m0, s56
	ds_read_b128 v[202:205], v150 offset:53248
	global_load_lds_dwordx4 v134, s[100:101]
	s_waitcnt vmcnt(8) lgkmcnt(0)
	s_barrier
	s_setprio 1
	v_mfma_f32_16x16x32_bf16 v[62:65], v[154:157], v[186:189], v[62:65]
	v_mfma_f32_16x16x32_bf16 v[58:61], v[162:165], v[186:189], v[58:61]
	v_mfma_f32_16x16x32_bf16 v[46:49], v[154:157], v[194:197], v[46:49]
	v_mfma_f32_16x16x32_bf16 v[42:45], v[162:165], v[194:197], v[42:45]
	v_mfma_f32_16x16x32_bf16 v[30:33], v[154:157], v[202:205], v[30:33]
	v_mfma_f32_16x16x32_bf16 v[26:29], v[162:165], v[202:205], v[26:29]
	v_mfma_f32_16x16x32_bf16 v[14:17], v[154:157], v[210:213], v[14:17]
	v_mfma_f32_16x16x32_bf16 v[10:13], v[162:165], v[210:213], v[10:13]
	v_mfma_f32_16x16x32_bf16 v[62:65], v[158:161], v[190:193], v[62:65]
	v_mfma_f32_16x16x32_bf16 v[58:61], v[166:169], v[190:193], v[58:61]
	v_mfma_f32_16x16x32_bf16 v[46:49], v[158:161], v[198:201], v[46:49]
	v_mfma_f32_16x16x32_bf16 v[42:45], v[166:169], v[198:201], v[42:45]
	v_mfma_f32_16x16x32_bf16 v[30:33], v[158:161], v[206:209], v[30:33]
	v_mfma_f32_16x16x32_bf16 v[26:29], v[166:169], v[206:209], v[26:29]
	v_mfma_f32_16x16x32_bf16 v[14:17], v[158:161], v[214:217], v[14:17]
	v_mfma_f32_16x16x32_bf16 v[10:13], v[166:169], v[214:217], v[10:13]
	s_setprio 0
	s_setprio 1
	v_mfma_f32_16x16x32_bf16 v[54:57], v[170:173], v[186:189], v[54:57]
	v_mfma_f32_16x16x32_bf16 v[50:53], v[178:181], v[186:189], v[50:53]
	v_mfma_f32_16x16x32_bf16 v[38:41], v[170:173], v[194:197], v[38:41]
	v_mfma_f32_16x16x32_bf16 v[34:37], v[178:181], v[194:197], v[34:37]
	v_mfma_f32_16x16x32_bf16 v[22:25], v[170:173], v[202:205], v[22:25]
	v_mfma_f32_16x16x32_bf16 v[18:21], v[178:181], v[202:205], v[18:21]
	v_mfma_f32_16x16x32_bf16 v[6:9], v[170:173], v[210:213], v[6:9]
	v_mfma_f32_16x16x32_bf16 v[2:5], v[178:181], v[210:213], v[2:5]
	v_mfma_f32_16x16x32_bf16 v[54:57], v[174:177], v[190:193], v[54:57]
	v_mfma_f32_16x16x32_bf16 v[50:53], v[182:185], v[190:193], v[50:53]
	v_mfma_f32_16x16x32_bf16 v[38:41], v[174:177], v[198:201], v[38:41]
	v_mfma_f32_16x16x32_bf16 v[34:37], v[182:185], v[198:201], v[34:37]
	v_mfma_f32_16x16x32_bf16 v[22:25], v[174:177], v[206:209], v[22:25]
	v_mfma_f32_16x16x32_bf16 v[18:21], v[182:185], v[206:209], v[18:21]
	v_mfma_f32_16x16x32_bf16 v[6:9], v[174:177], v[214:217], v[6:9]
	v_mfma_f32_16x16x32_bf16 v[2:5], v[182:185], v[214:217], v[2:5]
	s_setprio 0
	s_barrier
	s_add_u32 s25, s25, 0x100
	s_addc_u32 s64, s64, 0
	s_add_u32 s26, s26, 0x100
	s_addc_u32 s27, s27, 0
	s_cmp_ge_i32 s65, s52
	s_mov_b32 s28, s65
	s_cbranch_scc0 .LBB0_2262
	s_branch .LBB0_2263
; #define PG8_STAGE(bufoff, gbase, voff) do { _Pragma("unroll") for (int _i = 0; _i < 2; ++_i) \
;         __builtin_amdgcn_global_load_lds((const unsigned*)((const char*)(gbase) + (voff)[_i]), (PG8_LAS unsigned*)(lds + (bufoff) + ldsw + _i * 8192), 16, 0, 0); } while (0)
; #define PG8_LDA(dst, b, h) do { if constexpr (DT != 1) { _Pragma("unroll") for (int m = 0; m < 4; ++m) _Pragma("unroll") for (int k = 0; k < 2; ++k) dst[m][k] = *(const PG8_LAS bf16x8*)(lds + PG8_SA(b, h) + aoff + m * 2048 + k * 1024); } \
;         else { _Pragma("unroll") for (int m = 0; m < 4; ++m) dst##8[m] = ld32(lds + PG8_SA(b, h) + aoff + m * 2048); } } while (0)
; #define PG8_WAIT_V(n) asm volatile("s_waitcnt vmcnt(" #n ")" ::: "memory")
;     ...
;         const char* nA = has_next ? (const char*)g.A + (size_t)nxt.pm * tstepA : cA; const char* nB = has_next ? (const char*)g.Bt + (size_t)nxt.pn * tstepB : cB;
;         for (int t = 0; t < nt; t += 2) {
;             const bool last = (t == nt - 2);
;             const char* a1 = cA + (size_t)(t + 1) * kstep;
;             const char* a2 = last ? nA : cA + (size_t)(t + 2) * kstep; const char* b2 = last ? nB : cB + (size_t)(t + 2) * kstep;
;             const char* a3 = a2 + kstep; const char* b3 = b2 + kstep;
;             if (last && has_next) S.a_ready(nxt);
;             if constexpr (SP2) {
;             PG8_LDB(B0, 0, 0); PG8_LDB(B1, 0, 1); PG8_SCHED; PG8_LDA(At, 0, 0); PG8_STAGE(PG8_SA(1, 1), a1 + hstepA, voffA);
;             PG8_WAIT_V(8); PG8_WAIT_L(0); PG8_BAR; PG8_MMA(0, 0, At, B0); PG8_MMA(0, 1, At, B1); PG8_BAR; PG8_SCHED;
;             PG8_LDA(At, 0, 1); PG8_STAGE(PG8_SB(0, 0), b2, voffB); PG8_STAGE(PG8_SB(0, 1), b2 + hstepB, voffB); PG8_STAGE(PG8_SA(0, 0), a2, voffA);
;             PG8_WAIT_V(8); PG8_WAIT_L(0); PG8_BAR; PG8_MMA(1, 0, At, B0); PG8_MMA(1, 1, At, B1); PG8_BAR; PG8_SCHED;
;             PG8_LDB(B0, 1, 0); PG8_LDB(B1, 1, 1); PG8_SCHED; PG8_LDA(At, 1, 0); PG8_STAGE(PG8_SA(0, 1), a2 + hstepA, voffA);
;             PG8_WAIT_V(8); PG8_WAIT_L(0); PG8_BAR; PG8_MMA(0, 0, At, B0); PG8_MMA(0, 1, At, B1); PG8_BAR; PG8_SCHED;
;             PG8_LDA(At, 1, 1); PG8_STAGE(PG8_SB(1, 0), b3, voffB); PG8_STAGE(PG8_SB(1, 1), b3 + hstepB, voffB); PG8_STAGE(PG8_SA(1, 0), a3, voffA);
;             PG8_WAIT_V(8); PG8_WAIT_L(0); PG8_BAR; PG8_MMA(1, 0, At, B0); PG8_MMA(1, 1, At, B1); PG8_BAR; PG8_SCHED;
.LBB0_2262:
	ds_read_b128 v[154:157], v148
	ds_read_b128 v[158:161], v148 offset:1024
	ds_read_b128 v[162:165], v148 offset:2048
	ds_read_b128 v[166:169], v148 offset:3072
	ds_read_b128 v[170:173], v149
	ds_read_b128 v[174:177], v149 offset:1024
	ds_read_b128 v[178:181], v149 offset:2048
	ds_read_b128 v[182:185], v149 offset:3072
	s_add_i32 s65, s28, 2
	s_add_u32 s29, s26, 0xfff80080
	s_addc_u32 s30, s27, -1
	s_cmp_eq_u32 s61, s28
	s_cselect_b32 s28, s23, s25
	s_cselect_b32 s31, s2, s30
	s_cselect_b32 s30, s15, s29
	s_cselect_b32 s29, s17, s64
	s_add_i32 m0, s44, 0xc000
	ds_read_b128 v[186:189], v150
	ds_read_b128 v[190:193], v150 offset:1024
	ds_read_b128 v[194:197], v150 offset:2048
	ds_read_b128 v[198:201], v150 offset:3072
	ds_read_b128 v[202:205], v150 offset:4096
	ds_read_b128 v[206:209], v150 offset:5120
	ds_read_b128 v[210:213], v150 offset:6144
	ds_read_b128 v[214:217], v150 offset:7168
	global_load_lds_dwordx4 v142, s[26:27]
	s_add_i32 m0, s44, 0xe000
	s_nop 0
	global_load_lds_dwordx4 v140, s[26:27]
	s_waitcnt vmcnt(8) lgkmcnt(0)
	s_barrier
	s_setprio 1
	v_mfma_f32_16x16x32_bf16 v[126:129], v[154:157], v[186:189], v[126:129]
	v_mfma_f32_16x16x32_bf16 v[122:125], v[162:165], v[186:189], v[122:125]
	v_mfma_f32_16x16x32_bf16 v[110:113], v[154:157], v[194:197], v[110:113]
	v_mfma_f32_16x16x32_bf16 v[106:109], v[162:165], v[194:197], v[106:109]
	v_mfma_f32_16x16x32_bf16 v[94:97], v[154:157], v[202:205], v[94:97]
	v_mfma_f32_16x16x32_bf16 v[90:93], v[162:165], v[202:205], v[90:93]
	v_mfma_f32_16x16x32_bf16 v[78:81], v[154:157], v[210:213], v[78:81]
	v_mfma_f32_16x16x32_bf16 v[74:77], v[162:165], v[210:213], v[74:77]
	v_mfma_f32_16x16x32_bf16 v[126:129], v[158:161], v[190:193], v[126:129]
	v_mfma_f32_16x16x32_bf16 v[122:125], v[166:169], v[190:193], v[122:125]
	v_mfma_f32_16x16x32_bf16 v[110:113], v[158:161], v[198:201], v[110:113]
	v_mfma_f32_16x16x32_bf16 v[106:109], v[166:169], v[198:201], v[106:109]
	v_mfma_f32_16x16x32_bf16 v[94:97], v[158:161], v[206:209], v[94:97]
	v_mfma_f32_16x16x32_bf16 v[90:93], v[166:169], v[206:209], v[90:93]
	v_mfma_f32_16x16x32_bf16 v[78:81], v[158:161], v[214:217], v[78:81]
	v_mfma_f32_16x16x32_bf16 v[74:77], v[166:169], v[214:217], v[74:77]
	s_setprio 0
	s_setprio 1
	v_mfma_f32_16x16x32_bf16 v[118:121], v[170:173], v[186:189], v[118:121]
	v_mfma_f32_16x16x32_bf16 v[114:117], v[178:181], v[186:189], v[114:117]
	v_mfma_f32_16x16x32_bf16 v[102:105], v[170:173], v[194:197], v[102:105]
	v_mfma_f32_16x16x32_bf16 v[98:101], v[178:181], v[194:197], v[98:101]
	v_mfma_f32_16x16x32_bf16 v[86:89], v[170:173], v[202:205], v[86:89]
	v_mfma_f32_16x16x32_bf16 v[82:85], v[178:181], v[202:205], v[82:85]
	v_mfma_f32_16x16x32_bf16 v[70:73], v[170:173], v[210:213], v[70:73]
	v_mfma_f32_16x16x32_bf16 v[66:69], v[178:181], v[210:213], v[66:69]
	v_mfma_f32_16x16x32_bf16 v[118:121], v[174:177], v[190:193], v[118:121]
	v_mfma_f32_16x16x32_bf16 v[114:117], v[182:185], v[190:193], v[114:117]
	v_mfma_f32_16x16x32_bf16 v[102:105], v[174:177], v[198:201], v[102:105]
	v_mfma_f32_16x16x32_bf16 v[98:101], v[182:185], v[198:201], v[98:101]
	v_mfma_f32_16x16x32_bf16 v[86:89], v[174:177], v[206:209], v[86:89]
	v_mfma_f32_16x16x32_bf16 v[82:85], v[182:185], v[206:209], v[82:85]
	v_mfma_f32_16x16x32_bf16 v[70:73], v[174:177], v[214:217], v[70:73]
	v_mfma_f32_16x16x32_bf16 v[66:69], v[182:185], v[214:217], v[66:69]
	s_setprio 0
	s_barrier
	s_mov_b32 m0, s40
	s_add_u32 s98, s28, 0x80
	s_addc_u32 s99, s29, 0
	s_add_u32 s66, s28, 0x80000
	ds_read_b128 v[186:189], v150 offset:16384
	ds_read_b128 v[190:193], v150 offset:17408
	ds_read_b128 v[194:197], v150 offset:18432
	ds_read_b128 v[198:201], v150 offset:19456
	global_load_lds_dwordx4 v132, s[28:29]
	s_mov_b32 m0, s41
	s_addc_u32 s67, s29, 0
	global_load_lds_dwordx4 v136, s[28:29]
	s_mov_b32 m0, s42
	ds_read_b128 v[214:217], v150 offset:23552
	global_load_lds_dwordx4 v132, s[66:67]
	s_mov_b32 m0, s43
	ds_read_b128 v[210:213], v150 offset:22528
	global_load_lds_dwordx4 v136, s[66:67]
	s_add_u32 s100, s30, 0x80
	s_addc_u32 s101, s31, 0
	s_mov_b32 m0, s44
	ds_read_b128 v[206:209], v150 offset:21504
	global_load_lds_dwordx4 v130, s[30:31]
	s_mov_b32 m0, s45
	ds_read_b128 v[202:205], v150 offset:20480
	global_load_lds_dwordx4 v134, s[30:31]
	s_waitcnt vmcnt(8) lgkmcnt(0)
	s_barrier
	s_setprio 1
	v_mfma_f32_16x16x32_bf16 v[62:65], v[154:157], v[186:189], v[62:65]
	v_mfma_f32_16x16x32_bf16 v[58:61], v[162:165], v[186:189], v[58:61]
	v_mfma_f32_16x16x32_bf16 v[46:49], v[154:157], v[194:197], v[46:49]
	v_mfma_f32_16x16x32_bf16 v[42:45], v[162:165], v[194:197], v[42:45]
	v_mfma_f32_16x16x32_bf16 v[30:33], v[154:157], v[202:205], v[30:33]
	v_mfma_f32_16x16x32_bf16 v[26:29], v[162:165], v[202:205], v[26:29]
	v_mfma_f32_16x16x32_bf16 v[14:17], v[154:157], v[210:213], v[14:17]
	v_mfma_f32_16x16x32_bf16 v[10:13], v[162:165], v[210:213], v[10:13]
	v_mfma_f32_16x16x32_bf16 v[62:65], v[158:161], v[190:193], v[62:65]
	v_mfma_f32_16x16x32_bf16 v[58:61], v[166:169], v[190:193], v[58:61]
	v_mfma_f32_16x16x32_bf16 v[46:49], v[158:161], v[198:201], v[46:49]
	v_mfma_f32_16x16x32_bf16 v[42:45], v[166:169], v[198:201], v[42:45]
	v_mfma_f32_16x16x32_bf16 v[30:33], v[158:161], v[206:209], v[30:33]
	v_mfma_f32_16x16x32_bf16 v[26:29], v[166:169], v[206:209], v[26:29]
	v_mfma_f32_16x16x32_bf16 v[14:17], v[158:161], v[214:217], v[14:17]
	v_mfma_f32_16x16x32_bf16 v[10:13], v[166:169], v[214:217], v[10:13]
	s_setprio 0
	s_setprio 1
	v_mfma_f32_16x16x32_bf16 v[54:57], v[170:173], v[186:189], v[54:57]
	v_mfma_f32_16x16x32_bf16 v[50:53], v[178:181], v[186:189], v[50:53]
	v_mfma_f32_16x16x32_bf16 v[38:41], v[170:173], v[194:197], v[38:41]
	v_mfma_f32_16x16x32_bf16 v[34:37], v[178:181], v[194:197], v[34:37]
	v_mfma_f32_16x16x32_bf16 v[22:25], v[170:173], v[202:205], v[22:25]
	v_mfma_f32_16x16x32_bf16 v[18:21], v[178:181], v[202:205], v[18:21]
	v_mfma_f32_16x16x32_bf16 v[6:9], v[170:173], v[210:213], v[6:9]
	v_mfma_f32_16x16x32_bf16 v[2:5], v[178:181], v[210:213], v[2:5]
	v_mfma_f32_16x16x32_bf16 v[54:57], v[174:177], v[190:193], v[54:57]
	v_mfma_f32_16x16x32_bf16 v[50:53], v[182:185], v[190:193], v[50:53]
	v_mfma_f32_16x16x32_bf16 v[38:41], v[174:177], v[198:201], v[38:41]
	v_mfma_f32_16x16x32_bf16 v[34:37], v[182:185], v[198:201], v[34:37]
	v_mfma_f32_16x16x32_bf16 v[22:25], v[174:177], v[206:209], v[22:25]
	v_mfma_f32_16x16x32_bf16 v[18:21], v[182:185], v[206:209], v[18:21]
	v_mfma_f32_16x16x32_bf16 v[6:9], v[174:177], v[214:217], v[6:9]
	v_mfma_f32_16x16x32_bf16 v[2:5], v[182:185], v[214:217], v[2:5]
	s_setprio 0
	s_barrier
; #define PG8_STAGE(bufoff, gbase, voff) do { _Pragma("unroll") for (int _i = 0; _i < 2; ++_i) \
;         __builtin_amdgcn_global_load_lds((const unsigned*)((const char*)(gbase) + (voff)[_i]), (PG8_LAS unsigned*)(lds + (bufoff) + ldsw + _i * 8192), 16, 0, 0); } while (0)
; #define PG8_LDA(dst, b, h) do { if constexpr (DT != 1) { _Pragma("unroll") for (int m = 0; m < 4; ++m) _Pragma("unroll") for (int k = 0; k < 2; ++k) dst[m][k] = *(const PG8_LAS bf16x8*)(lds + PG8_SA(b, h) + aoff + m * 2048 + k * 1024); } \
;         else { _Pragma("unroll") for (int m = 0; m < 4; ++m) dst##8[m] = ld32(lds + PG8_SA(b, h) + aoff + m * 2048); } } while (0)
; #define PG8_LDB(dst, b, h) do { if constexpr (DT != 1) { _Pragma("unroll") for (int n = 0; n < 2; ++n) _Pragma("unroll") for (int k = 0; k < 2; ++k) dst[n][k] = *(const PG8_LAS bf16x8*)(lds + PG8_SB(b, h) + boff + n * 2048 + k * 1024); } \
;         else { _Pragma("unroll") for (int n = 0; n < 2; ++n) dst##8[n] = ld32(lds + PG8_SB(b, h) + boff + n * 2048); } } while (0)
; #define PG8_WAIT_V(n) asm volatile("s_waitcnt vmcnt(" #n ")" ::: "memory")
; #define PG8_WAIT_L(n) asm volatile("s_waitcnt lgkmcnt(" #n ")" ::: "memory")
; #define PG8_BAR __builtin_amdgcn_s_barrier()
; #define PG8_SCHED __builtin_amdgcn_sched_barrier(0)
;     ...
;             PG8_LDB(B0, 0, 0); PG8_LDB(B1, 0, 1); PG8_SCHED; PG8_LDA(At, 0, 0); PG8_STAGE(PG8_SA(1, 1), a1 + hstepA, voffA);
;             PG8_WAIT_V(8); PG8_WAIT_L(0); PG8_BAR; PG8_MMA(0, 0, At, B0); PG8_MMA(0, 1, At, B1); PG8_BAR; PG8_SCHED;
;             PG8_LDA(At, 0, 1); PG8_STAGE(PG8_SB(0, 0), b2, voffB); PG8_STAGE(PG8_SB(0, 1), b2 + hstepB, voffB); PG8_STAGE(PG8_SA(0, 0), a2, voffA);
;             PG8_WAIT_V(8); PG8_WAIT_L(0); PG8_BAR; PG8_MMA(1, 0, At, B0); PG8_MMA(1, 1, At, B1); PG8_BAR; PG8_SCHED;
;             PG8_LDB(B0, 1, 0); PG8_LDB(B1, 1, 1); PG8_SCHED; PG8_LDA(At, 1, 0); PG8_STAGE(PG8_SA(0, 1), a2 + hstepA, voffA);
;             PG8_WAIT_V(8); PG8_WAIT_L(0); PG8_BAR; PG8_MMA(0, 0, At, B0); PG8_MMA(0, 1, At, B1); PG8_BAR; PG8_SCHED;
;             PG8_LDA(At, 1, 1); PG8_STAGE(PG8_SB(1, 0), b3, voffB); PG8_STAGE(PG8_SB(1, 1), b3 + hstepB, voffB); PG8_STAGE(PG8_SA(1, 0), a3, voffA);
;             PG8_WAIT_V(8); PG8_WAIT_L(0); PG8_BAR; PG8_MMA(1, 0, At, B0); PG8_MMA(1, 1, At, B1); PG8_BAR; PG8_SCHED;
	ds_read_b128 v[154:157], v151
	ds_read_b128 v[158:161], v151 offset:1024
	ds_read_b128 v[162:165], v151 offset:2048
	ds_read_b128 v[166:169], v151 offset:3072
	ds_read_b128 v[170:173], v152
	ds_read_b128 v[174:177], v152 offset:1024
	ds_read_b128 v[178:181], v152 offset:2048
	ds_read_b128 v[182:185], v152 offset:3072
	s_add_u32 s30, s30, 0x80000
	s_addc_u32 s31, s31, 0
	s_mov_b32 m0, s46
	ds_read_b128 v[186:189], v150 offset:32768
	ds_read_b128 v[190:193], v150 offset:33792
	ds_read_b128 v[194:197], v150 offset:34816
	ds_read_b128 v[198:201], v150 offset:35840
	ds_read_b128 v[202:205], v150 offset:36864
	ds_read_b128 v[206:209], v150 offset:37888
	ds_read_b128 v[210:213], v150 offset:38912
	global_load_lds_dwordx4 v130, s[30:31]
	s_mov_b32 m0, s47
	ds_read_b128 v[214:217], v150 offset:39936
	global_load_lds_dwordx4 v134, s[30:31]
	s_waitcnt vmcnt(8) lgkmcnt(0)
	s_barrier
	s_setprio 1
	v_mfma_f32_16x16x32_bf16 v[126:129], v[154:157], v[186:189], v[126:129]
	v_mfma_f32_16x16x32_bf16 v[122:125], v[162:165], v[186:189], v[122:125]
	v_mfma_f32_16x16x32_bf16 v[110:113], v[154:157], v[194:197], v[110:113]
	v_mfma_f32_16x16x32_bf16 v[106:109], v[162:165], v[194:197], v[106:109]
	v_mfma_f32_16x16x32_bf16 v[94:97], v[154:157], v[202:205], v[94:97]
	v_mfma_f32_16x16x32_bf16 v[90:93], v[162:165], v[202:205], v[90:93]
	v_mfma_f32_16x16x32_bf16 v[78:81], v[154:157], v[210:213], v[78:81]
	v_mfma_f32_16x16x32_bf16 v[74:77], v[162:165], v[210:213], v[74:77]
	v_mfma_f32_16x16x32_bf16 v[126:129], v[158:161], v[190:193], v[126:129]
	v_mfma_f32_16x16x32_bf16 v[122:125], v[166:169], v[190:193], v[122:125]
	v_mfma_f32_16x16x32_bf16 v[110:113], v[158:161], v[198:201], v[110:113]
	v_mfma_f32_16x16x32_bf16 v[106:109], v[166:169], v[198:201], v[106:109]
	v_mfma_f32_16x16x32_bf16 v[94:97], v[158:161], v[206:209], v[94:97]
	v_mfma_f32_16x16x32_bf16 v[90:93], v[166:169], v[206:209], v[90:93]
	v_mfma_f32_16x16x32_bf16 v[78:81], v[158:161], v[214:217], v[78:81]
	v_mfma_f32_16x16x32_bf16 v[74:77], v[166:169], v[214:217], v[74:77]
	s_setprio 0
	s_setprio 1
	v_mfma_f32_16x16x32_bf16 v[118:121], v[170:173], v[186:189], v[118:121]
	v_mfma_f32_16x16x32_bf16 v[114:117], v[178:181], v[186:189], v[114:117]
	v_mfma_f32_16x16x32_bf16 v[102:105], v[170:173], v[194:197], v[102:105]
	v_mfma_f32_16x16x32_bf16 v[98:101], v[178:181], v[194:197], v[98:101]
	v_mfma_f32_16x16x32_bf16 v[86:89], v[170:173], v[202:205], v[86:89]
	v_mfma_f32_16x16x32_bf16 v[82:85], v[178:181], v[202:205], v[82:85]
	v_mfma_f32_16x16x32_bf16 v[70:73], v[170:173], v[210:213], v[70:73]
	v_mfma_f32_16x16x32_bf16 v[66:69], v[178:181], v[210:213], v[66:69]
	v_mfma_f32_16x16x32_bf16 v[118:121], v[174:177], v[190:193], v[118:121]
	v_mfma_f32_16x16x32_bf16 v[114:117], v[182:185], v[190:193], v[114:117]
	v_mfma_f32_16x16x32_bf16 v[102:105], v[174:177], v[198:201], v[102:105]
	v_mfma_f32_16x16x32_bf16 v[98:101], v[182:185], v[198:201], v[98:101]
	v_mfma_f32_16x16x32_bf16 v[86:89], v[174:177], v[206:209], v[86:89]
	v_mfma_f32_16x16x32_bf16 v[82:85], v[182:185], v[206:209], v[82:85]
	v_mfma_f32_16x16x32_bf16 v[70:73], v[174:177], v[214:217], v[70:73]
	v_mfma_f32_16x16x32_bf16 v[66:69], v[182:185], v[214:217], v[66:69]
	s_setprio 0
	s_barrier
	s_mov_b32 m0, s53
	s_add_u32 s28, s28, 0x80080
	ds_read_b128 v[186:189], v150 offset:49152
	ds_read_b128 v[190:193], v150 offset:50176
	ds_read_b128 v[194:197], v150 offset:51200
	ds_read_b128 v[198:201], v150 offset:52224
	global_load_lds_dwordx4 v132, s[98:99]
	s_mov_b32 m0, s54
	s_addc_u32 s29, s29, 0
	global_load_lds_dwordx4 v136, s[98:99]
	s_mov_b32 m0, s57
	ds_read_b128 v[214:217], v150 offset:56320
	global_load_lds_dwordx4 v132, s[28:29]
	s_mov_b32 m0, s58
	ds_read_b128 v[210:213], v150 offset:55296
	global_load_lds_dwordx4 v136, s[28:29]
	s_mov_b32 m0, s55
	ds_read_b128 v[206:209], v150 offset:54272
	global_load_lds_dwordx4 v130, s[100:101]
	s_mov_b32 m0, s56
	ds_read_b128 v[202:205], v150 offset:53248
	global_load_lds_dwordx4 v134, s[100:101]
	s_waitcnt vmcnt(8) lgkmcnt(0)
	s_barrier
	s_setprio 1
	v_mfma_f32_16x16x32_bf16 v[62:65], v[154:157], v[186:189], v[62:65]
	v_mfma_f32_16x16x32_bf16 v[58:61], v[162:165], v[186:189], v[58:61]
	v_mfma_f32_16x16x32_bf16 v[46:49], v[154:157], v[194:197], v[46:49]
	v_mfma_f32_16x16x32_bf16 v[42:45], v[162:165], v[194:197], v[42:45]
	v_mfma_f32_16x16x32_bf16 v[30:33], v[154:157], v[202:205], v[30:33]
	v_mfma_f32_16x16x32_bf16 v[26:29], v[162:165], v[202:205], v[26:29]
	v_mfma_f32_16x16x32_bf16 v[14:17], v[154:157], v[210:213], v[14:17]
	v_mfma_f32_16x16x32_bf16 v[10:13], v[162:165], v[210:213], v[10:13]
	v_mfma_f32_16x16x32_bf16 v[62:65], v[158:161], v[190:193], v[62:65]
	v_mfma_f32_16x16x32_bf16 v[58:61], v[166:169], v[190:193], v[58:61]
	v_mfma_f32_16x16x32_bf16 v[46:49], v[158:161], v[198:201], v[46:49]
	v_mfma_f32_16x16x32_bf16 v[42:45], v[166:169], v[198:201], v[42:45]
	v_mfma_f32_16x16x32_bf16 v[30:33], v[158:161], v[206:209], v[30:33]
	v_mfma_f32_16x16x32_bf16 v[26:29], v[166:169], v[206:209], v[26:29]
	v_mfma_f32_16x16x32_bf16 v[14:17], v[158:161], v[214:217], v[14:17]
	v_mfma_f32_16x16x32_bf16 v[10:13], v[166:169], v[214:217], v[10:13]
	s_setprio 0
	s_setprio 1
	v_mfma_f32_16x16x32_bf16 v[54:57], v[170:173], v[186:189], v[54:57]
	v_mfma_f32_16x16x32_bf16 v[50:53], v[178:181], v[186:189], v[50:53]
	v_mfma_f32_16x16x32_bf16 v[38:41], v[170:173], v[194:197], v[38:41]
	v_mfma_f32_16x16x32_bf16 v[34:37], v[178:181], v[194:197], v[34:37]
	v_mfma_f32_16x16x32_bf16 v[22:25], v[170:173], v[202:205], v[22:25]
	v_mfma_f32_16x16x32_bf16 v[18:21], v[178:181], v[202:205], v[18:21]
	v_mfma_f32_16x16x32_bf16 v[6:9], v[170:173], v[210:213], v[6:9]
	v_mfma_f32_16x16x32_bf16 v[2:5], v[178:181], v[210:213], v[2:5]
	v_mfma_f32_16x16x32_bf16 v[54:57], v[174:177], v[190:193], v[54:57]
	v_mfma_f32_16x16x32_bf16 v[50:53], v[182:185], v[190:193], v[50:53]
	v_mfma_f32_16x16x32_bf16 v[38:41], v[174:177], v[198:201], v[38:41]
	v_mfma_f32_16x16x32_bf16 v[34:37], v[182:185], v[198:201], v[34:37]
	v_mfma_f32_16x16x32_bf16 v[22:25], v[174:177], v[206:209], v[22:25]
	v_mfma_f32_16x16x32_bf16 v[18:21], v[182:185], v[206:209], v[18:21]
	v_mfma_f32_16x16x32_bf16 v[6:9], v[174:177], v[214:217], v[6:9]
	v_mfma_f32_16x16x32_bf16 v[2:5], v[182:185], v[214:217], v[2:5]
	s_setprio 0
	s_barrier
	s_add_u32 s25, s25, 0x100
	s_addc_u32 s64, s64, 0
	s_add_u32 s26, s26, 0x100
	s_addc_u32 s27, s27, 0
	s_cmp_ge_i32 s65, s52
	s_mov_b32 s28, s65
	s_cbranch_scc0 .LBB0_2262

; #define PG8_STAGE(bufoff, gbase, voff) do { _Pragma("unroll") for (int _i = 0; _i < 2; ++_i) \
;         __builtin_amdgcn_global_load_lds((const unsigned*)((const char*)(gbase) + (voff)[_i]), (PG8_LAS unsigned*)(lds + (bufoff) + ldsw + _i * 8192), 16, 0, 0); } while (0)
; #define PG8_LDA(dst, b, h) do { if constexpr (DT != 1) { _Pragma("unroll") for (int m = 0; m < 4; ++m) _Pragma("unroll") for (int k = 0; k < 2; ++k) dst[m][k] = *(const PG8_LAS bf16x8*)(lds + PG8_SA(b, h) + aoff + m * 2048 + k * 1024); } \
;         else { _Pragma("unroll") for (int m = 0; m < 4; ++m) dst##8[m] = ld32(lds + PG8_SA(b, h) + aoff + m * 2048); } } while (0)
; #define PG8_WAIT_V(n) asm volatile("s_waitcnt vmcnt(" #n ")" ::: "memory")
;     ...
;         const char* nA = has_next ? (const char*)g.A + (size_t)nxt.pm * tstepA : cA; const char* nB = has_next ? (const char*)g.Bt + (size_t)nxt.pn * tstepB : cB;
;         for (int t = 0; t < nt; t += 2) {
;             const bool last = (t == nt - 2);
;             const char* a1 = cA + (size_t)(t + 1) * kstep;
;             const char* a2 = last ? nA : cA + (size_t)(t + 2) * kstep; const char* b2 = last ? nB : cB + (size_t)(t + 2) * kstep;
;             const char* a3 = a2 + kstep; const char* b3 = b2 + kstep;
;             if (last && has_next) S.a_ready(nxt);
;             if constexpr (SP2) {
;             PG8_LDB(B0, 0, 0); PG8_LDB(B1, 0, 1); PG8_SCHED; PG8_LDA(At, 0, 0); PG8_STAGE(PG8_SA(1, 1), a1 + hstepA, voffA);
;             PG8_WAIT_V(8); PG8_WAIT_L(0); PG8_BAR; PG8_MMA(0, 0, At, B0); PG8_MMA(0, 1, At, B1); PG8_BAR; PG8_SCHED;
;             PG8_LDA(At, 0, 1); PG8_STAGE(PG8_SB(0, 0), b2, voffB); PG8_STAGE(PG8_SB(0, 1), b2 + hstepB, voffB); PG8_STAGE(PG8_SA(0, 0), a2, voffA);
;             PG8_WAIT_V(8); PG8_WAIT_L(0); PG8_BAR; PG8_MMA(1, 0, At, B0); PG8_MMA(1, 1, At, B1); PG8_BAR; PG8_SCHED;
;             PG8_LDB(B0, 1, 0); PG8_LDB(B1, 1, 1); PG8_SCHED; PG8_LDA(At, 1, 0); PG8_STAGE(PG8_SA(0, 1), a2 + hstepA, voffA);
;             PG8_WAIT_V(8); PG8_WAIT_L(0); PG8_BAR; PG8_MMA(0, 0, At, B0); PG8_MMA(0, 1, At, B1); PG8_BAR; PG8_SCHED;
;             PG8_LDA(At, 1, 1); PG8_STAGE(PG8_SB(1, 0), b3, voffB); PG8_STAGE(PG8_SB(1, 1), b3 + hstepB, voffB); PG8_STAGE(PG8_SA(1, 0), a3, voffA);
;             PG8_WAIT_V(8); PG8_WAIT_L(0); PG8_BAR; PG8_MMA(1, 0, At, B0); PG8_MMA(1, 1, At, B1); PG8_BAR; PG8_SCHED;
.Lzs_10:
	s_cbranch_vccnz .LBB0_3358
	s_and_b64 s[44:45], s[0:1], exec
	s_cselect_b32 s3, s35, s43
	s_cselect_b32 s29, s34, s42
	s_cselect_b32 s31, s37, s41
	s_cselect_b32 s39, s36, s40
	s_add_u32 s76, s40, 0x100
	s_addc_u32 s77, s41, 0
	s_add_u32 s40, s42, 0x10080
	s_addc_u32 s41, s43, 0
	s_mov_b32 s42, 0
	ds_read_b128 v[130:133], v173
	ds_read_b128 v[134:137], v173 offset:1024
	ds_read_b128 v[138:141], v173 offset:2048
	ds_read_b128 v[142:145], v173 offset:3072
	ds_read_b128 v[164:167], v174
	ds_read_b128 v[168:171], v174 offset:1024
	ds_read_b128 v[178:181], v174 offset:2048
	ds_read_b128 v[182:185], v174 offset:3072
	s_add_i32 s78, s42, 2
	s_add_u32 s43, s40, 0xffff0080
	s_addc_u32 s44, s41, -1
	s_cmp_eq_u32 s74, s42
	s_cselect_b32 s42, s39, s76
	s_cselect_b32 s45, s3, s44
	s_cselect_b32 s44, s29, s43
	s_cselect_b32 s43, s31, s77
	s_add_i32 m0, s56, 0xc000
	ds_read_b128 v[186:189], v175
	ds_read_b128 v[190:193], v175 offset:1024
	ds_read_b128 v[194:197], v175 offset:2048
	ds_read_b128 v[198:201], v175 offset:3072
	ds_read_b128 v[202:205], v175 offset:4096
	ds_read_b128 v[206:209], v175 offset:5120
	ds_read_b128 v[210:213], v175 offset:6144
	ds_read_b128 v[214:217], v175 offset:7168
	global_load_lds_dwordx4 v158, s[40:41]
	s_add_i32 m0, s56, 0xe000
	s_nop 0
	global_load_lds_dwordx4 v156, s[40:41]
	s_waitcnt vmcnt(8) lgkmcnt(0)
	s_barrier
	s_setprio 1
	v_mfma_f32_16x16x32_bf16 v[126:129], v[130:133], v[186:189], 0
	v_mfma_f32_16x16x32_bf16 v[122:125], v[138:141], v[186:189], 0
	v_mfma_f32_16x16x32_bf16 v[110:113], v[130:133], v[194:197], 0
	v_mfma_f32_16x16x32_bf16 v[106:109], v[138:141], v[194:197], 0
	v_mfma_f32_16x16x32_bf16 v[94:97], v[130:133], v[202:205], 0
	v_mfma_f32_16x16x32_bf16 v[90:93], v[138:141], v[202:205], 0
	v_mfma_f32_16x16x32_bf16 v[78:81], v[130:133], v[210:213], 0
	v_mfma_f32_16x16x32_bf16 v[74:77], v[138:141], v[210:213], 0
	v_mfma_f32_16x16x32_bf16 v[126:129], v[134:137], v[190:193], v[126:129]
	v_mfma_f32_16x16x32_bf16 v[122:125], v[142:145], v[190:193], v[122:125]
	v_mfma_f32_16x16x32_bf16 v[110:113], v[134:137], v[198:201], v[110:113]
	v_mfma_f32_16x16x32_bf16 v[106:109], v[142:145], v[198:201], v[106:109]
	v_mfma_f32_16x16x32_bf16 v[94:97], v[134:137], v[206:209], v[94:97]
	v_mfma_f32_16x16x32_bf16 v[90:93], v[142:145], v[206:209], v[90:93]
	v_mfma_f32_16x16x32_bf16 v[78:81], v[134:137], v[214:217], v[78:81]
	v_mfma_f32_16x16x32_bf16 v[74:77], v[142:145], v[214:217], v[74:77]
	s_setprio 0
	s_setprio 1
	v_mfma_f32_16x16x32_bf16 v[118:121], v[164:167], v[186:189], 0
	v_mfma_f32_16x16x32_bf16 v[114:117], v[178:181], v[186:189], 0
	v_mfma_f32_16x16x32_bf16 v[102:105], v[164:167], v[194:197], 0
	v_mfma_f32_16x16x32_bf16 v[98:101], v[178:181], v[194:197], 0
	v_mfma_f32_16x16x32_bf16 v[86:89], v[164:167], v[202:205], 0
	v_mfma_f32_16x16x32_bf16 v[82:85], v[178:181], v[202:205], 0
	v_mfma_f32_16x16x32_bf16 v[70:73], v[164:167], v[210:213], 0
	v_mfma_f32_16x16x32_bf16 v[66:69], v[178:181], v[210:213], 0
	v_mfma_f32_16x16x32_bf16 v[118:121], v[168:171], v[190:193], v[118:121]
	v_mfma_f32_16x16x32_bf16 v[114:117], v[182:185], v[190:193], v[114:117]
	v_mfma_f32_16x16x32_bf16 v[102:105], v[168:171], v[198:201], v[102:105]
	v_mfma_f32_16x16x32_bf16 v[98:101], v[182:185], v[198:201], v[98:101]
	v_mfma_f32_16x16x32_bf16 v[86:89], v[168:171], v[206:209], v[86:89]
	v_mfma_f32_16x16x32_bf16 v[82:85], v[182:185], v[206:209], v[82:85]
	v_mfma_f32_16x16x32_bf16 v[70:73], v[168:171], v[214:217], v[70:73]
	v_mfma_f32_16x16x32_bf16 v[66:69], v[182:185], v[214:217], v[66:69]
	s_setprio 0
	s_barrier
	s_mov_b32 m0, s52
	s_add_u32 s98, s42, 0x80
	s_addc_u32 s99, s43, 0
	s_add_u32 s80, s42, 0x10000
	ds_read_b128 v[186:189], v175 offset:16384
	ds_read_b128 v[190:193], v175 offset:17408
	ds_read_b128 v[194:197], v175 offset:18432
	ds_read_b128 v[198:201], v175 offset:19456
	global_load_lds_dwordx4 v148, s[42:43]
	s_mov_b32 m0, s53
	s_addc_u32 s81, s43, 0
	global_load_lds_dwordx4 v152, s[42:43]
	s_mov_b32 m0, s54
	ds_read_b128 v[214:217], v175 offset:23552
	global_load_lds_dwordx4 v148, s[80:81]
	s_mov_b32 m0, s55
	ds_read_b128 v[210:213], v175 offset:22528
	global_load_lds_dwordx4 v152, s[80:81]
	s_add_u32 s100, s44, 0x80
	s_addc_u32 s101, s45, 0
	s_mov_b32 m0, s56
	ds_read_b128 v[206:209], v175 offset:21504
	global_load_lds_dwordx4 v146, s[44:45]
	s_mov_b32 m0, s57
	ds_read_b128 v[202:205], v175 offset:20480
	global_load_lds_dwordx4 v150, s[44:45]
	s_waitcnt vmcnt(8) lgkmcnt(0)
	s_barrier
	s_setprio 1
	v_mfma_f32_16x16x32_bf16 v[62:65], v[130:133], v[186:189], 0
	v_mfma_f32_16x16x32_bf16 v[58:61], v[138:141], v[186:189], 0
	v_mfma_f32_16x16x32_bf16 v[46:49], v[130:133], v[194:197], 0
	v_mfma_f32_16x16x32_bf16 v[42:45], v[138:141], v[194:197], 0
	v_mfma_f32_16x16x32_bf16 v[30:33], v[130:133], v[202:205], 0
	v_mfma_f32_16x16x32_bf16 v[26:29], v[138:141], v[202:205], 0
	v_mfma_f32_16x16x32_bf16 v[14:17], v[130:133], v[210:213], 0
	v_mfma_f32_16x16x32_bf16 v[10:13], v[138:141], v[210:213], 0
	v_mfma_f32_16x16x32_bf16 v[62:65], v[134:137], v[190:193], v[62:65]
	v_mfma_f32_16x16x32_bf16 v[58:61], v[142:145], v[190:193], v[58:61]
	v_mfma_f32_16x16x32_bf16 v[46:49], v[134:137], v[198:201], v[46:49]
	v_mfma_f32_16x16x32_bf16 v[42:45], v[142:145], v[198:201], v[42:45]
	v_mfma_f32_16x16x32_bf16 v[30:33], v[134:137], v[206:209], v[30:33]
	v_mfma_f32_16x16x32_bf16 v[26:29], v[142:145], v[206:209], v[26:29]
	v_mfma_f32_16x16x32_bf16 v[14:17], v[134:137], v[214:217], v[14:17]
	v_mfma_f32_16x16x32_bf16 v[10:13], v[142:145], v[214:217], v[10:13]
	s_setprio 0
	s_setprio 1
	v_mfma_f32_16x16x32_bf16 v[54:57], v[164:167], v[186:189], 0
	v_mfma_f32_16x16x32_bf16 v[50:53], v[178:181], v[186:189], 0
	v_mfma_f32_16x16x32_bf16 v[38:41], v[164:167], v[194:197], 0
	v_mfma_f32_16x16x32_bf16 v[34:37], v[178:181], v[194:197], 0
	v_mfma_f32_16x16x32_bf16 v[22:25], v[164:167], v[202:205], 0
	v_mfma_f32_16x16x32_bf16 v[18:21], v[178:181], v[202:205], 0
	v_mfma_f32_16x16x32_bf16 v[6:9], v[164:167], v[210:213], 0
	v_mfma_f32_16x16x32_bf16 v[2:5], v[178:181], v[210:213], 0
	v_mfma_f32_16x16x32_bf16 v[54:57], v[168:171], v[190:193], v[54:57]
	v_mfma_f32_16x16x32_bf16 v[50:53], v[182:185], v[190:193], v[50:53]
	v_mfma_f32_16x16x32_bf16 v[38:41], v[168:171], v[198:201], v[38:41]
	v_mfma_f32_16x16x32_bf16 v[34:37], v[182:185], v[198:201], v[34:37]
	v_mfma_f32_16x16x32_bf16 v[22:25], v[168:171], v[206:209], v[22:25]
	v_mfma_f32_16x16x32_bf16 v[18:21], v[182:185], v[206:209], v[18:21]
	v_mfma_f32_16x16x32_bf16 v[6:9], v[168:171], v[214:217], v[6:9]
	v_mfma_f32_16x16x32_bf16 v[2:5], v[182:185], v[214:217], v[2:5]
	s_setprio 0
	s_barrier
; #define PG8_STAGE(bufoff, gbase, voff) do { _Pragma("unroll") for (int _i = 0; _i < 2; ++_i) \
;         __builtin_amdgcn_global_load_lds((const unsigned*)((const char*)(gbase) + (voff)[_i]), (PG8_LAS unsigned*)(lds + (bufoff) + ldsw + _i * 8192), 16, 0, 0); } while (0)
; #define PG8_LDA(dst, b, h) do { if constexpr (DT != 1) { _Pragma("unroll") for (int m = 0; m < 4; ++m) _Pragma("unroll") for (int k = 0; k < 2; ++k) dst[m][k] = *(const PG8_LAS bf16x8*)(lds + PG8_SA(b, h) + aoff + m * 2048 + k * 1024); } \
;         else { _Pragma("unroll") for (int m = 0; m < 4; ++m) dst##8[m] = ld32(lds + PG8_SA(b, h) + aoff + m * 2048); } } while (0)
; #define PG8_LDB(dst, b, h) do { if constexpr (DT != 1) { _Pragma("unroll") for (int n = 0; n < 2; ++n) _Pragma("unroll") for (int k = 0; k < 2; ++k) dst[n][k] = *(const PG8_LAS bf16x8*)(lds + PG8_SB(b, h) + boff + n * 2048 + k * 1024); } \
;         else { _Pragma("unroll") for (int n = 0; n < 2; ++n) dst##8[n] = ld32(lds + PG8_SB(b, h) + boff + n * 2048); } } while (0)
; #define PG8_WAIT_V(n) asm volatile("s_waitcnt vmcnt(" #n ")" ::: "memory")
; #define PG8_WAIT_L(n) asm volatile("s_waitcnt lgkmcnt(" #n ")" ::: "memory")
; #define PG8_BAR __builtin_amdgcn_s_barrier()
; #define PG8_SCHED __builtin_amdgcn_sched_barrier(0)
;     ...
;             PG8_LDB(B0, 0, 0); PG8_LDB(B1, 0, 1); PG8_SCHED; PG8_LDA(At, 0, 0); PG8_STAGE(PG8_SA(1, 1), a1 + hstepA, voffA);
;             PG8_WAIT_V(8); PG8_WAIT_L(0); PG8_BAR; PG8_MMA(0, 0, At, B0); PG8_MMA(0, 1, At, B1); PG8_BAR; PG8_SCHED;
;             PG8_LDA(At, 0, 1); PG8_STAGE(PG8_SB(0, 0), b2, voffB); PG8_STAGE(PG8_SB(0, 1), b2 + hstepB, voffB); PG8_STAGE(PG8_SA(0, 0), a2, voffA);
;             PG8_WAIT_V(8); PG8_WAIT_L(0); PG8_BAR; PG8_MMA(1, 0, At, B0); PG8_MMA(1, 1, At, B1); PG8_BAR; PG8_SCHED;
;             PG8_LDB(B0, 1, 0); PG8_LDB(B1, 1, 1); PG8_SCHED; PG8_LDA(At, 1, 0); PG8_STAGE(PG8_SA(0, 1), a2 + hstepA, voffA);
;             PG8_WAIT_V(8); PG8_WAIT_L(0); PG8_BAR; PG8_MMA(0, 0, At, B0); PG8_MMA(0, 1, At, B1); PG8_BAR; PG8_SCHED;
;             PG8_LDA(At, 1, 1); PG8_STAGE(PG8_SB(1, 0), b3, voffB); PG8_STAGE(PG8_SB(1, 1), b3 + hstepB, voffB); PG8_STAGE(PG8_SA(1, 0), a3, voffA);
;             PG8_WAIT_V(8); PG8_WAIT_L(0); PG8_BAR; PG8_MMA(1, 0, At, B0); PG8_MMA(1, 1, At, B1); PG8_BAR; PG8_SCHED;
	ds_read_b128 v[130:133], v176
	ds_read_b128 v[134:137], v176 offset:1024
	ds_read_b128 v[138:141], v176 offset:2048
	ds_read_b128 v[142:145], v176 offset:3072
	ds_read_b128 v[164:167], v177
	ds_read_b128 v[168:171], v177 offset:1024
	ds_read_b128 v[178:181], v177 offset:2048
	ds_read_b128 v[182:185], v177 offset:3072
	s_add_u32 s44, s44, 0x10000
	s_addc_u32 s45, s45, 0
	s_mov_b32 m0, s58
	ds_read_b128 v[186:189], v175 offset:32768
	ds_read_b128 v[190:193], v175 offset:33792
	ds_read_b128 v[194:197], v175 offset:34816
	ds_read_b128 v[198:201], v175 offset:35840
	ds_read_b128 v[202:205], v175 offset:36864
	ds_read_b128 v[206:209], v175 offset:37888
	ds_read_b128 v[210:213], v175 offset:38912
	global_load_lds_dwordx4 v146, s[44:45]
	s_mov_b32 m0, s59
	ds_read_b128 v[214:217], v175 offset:39936
	global_load_lds_dwordx4 v150, s[44:45]
	s_waitcnt vmcnt(8) lgkmcnt(0)
	s_barrier
	s_setprio 1
	v_mfma_f32_16x16x32_bf16 v[126:129], v[130:133], v[186:189], v[126:129]
	v_mfma_f32_16x16x32_bf16 v[122:125], v[138:141], v[186:189], v[122:125]
	v_mfma_f32_16x16x32_bf16 v[110:113], v[130:133], v[194:197], v[110:113]
	v_mfma_f32_16x16x32_bf16 v[106:109], v[138:141], v[194:197], v[106:109]
	v_mfma_f32_16x16x32_bf16 v[94:97], v[130:133], v[202:205], v[94:97]
	v_mfma_f32_16x16x32_bf16 v[90:93], v[138:141], v[202:205], v[90:93]
	v_mfma_f32_16x16x32_bf16 v[78:81], v[130:133], v[210:213], v[78:81]
	v_mfma_f32_16x16x32_bf16 v[74:77], v[138:141], v[210:213], v[74:77]
	v_mfma_f32_16x16x32_bf16 v[126:129], v[134:137], v[190:193], v[126:129]
	v_mfma_f32_16x16x32_bf16 v[122:125], v[142:145], v[190:193], v[122:125]
	v_mfma_f32_16x16x32_bf16 v[110:113], v[134:137], v[198:201], v[110:113]
	v_mfma_f32_16x16x32_bf16 v[106:109], v[142:145], v[198:201], v[106:109]
	v_mfma_f32_16x16x32_bf16 v[94:97], v[134:137], v[206:209], v[94:97]
	v_mfma_f32_16x16x32_bf16 v[90:93], v[142:145], v[206:209], v[90:93]
	v_mfma_f32_16x16x32_bf16 v[78:81], v[134:137], v[214:217], v[78:81]
	v_mfma_f32_16x16x32_bf16 v[74:77], v[142:145], v[214:217], v[74:77]
	s_setprio 0
	s_setprio 1
	v_mfma_f32_16x16x32_bf16 v[118:121], v[164:167], v[186:189], v[118:121]
	v_mfma_f32_16x16x32_bf16 v[114:117], v[178:181], v[186:189], v[114:117]
	v_mfma_f32_16x16x32_bf16 v[102:105], v[164:167], v[194:197], v[102:105]
	v_mfma_f32_16x16x32_bf16 v[98:101], v[178:181], v[194:197], v[98:101]
	v_mfma_f32_16x16x32_bf16 v[86:89], v[164:167], v[202:205], v[86:89]
	v_mfma_f32_16x16x32_bf16 v[82:85], v[178:181], v[202:205], v[82:85]
	v_mfma_f32_16x16x32_bf16 v[70:73], v[164:167], v[210:213], v[70:73]
	v_mfma_f32_16x16x32_bf16 v[66:69], v[178:181], v[210:213], v[66:69]
	v_mfma_f32_16x16x32_bf16 v[118:121], v[168:171], v[190:193], v[118:121]
	v_mfma_f32_16x16x32_bf16 v[114:117], v[182:185], v[190:193], v[114:117]
	v_mfma_f32_16x16x32_bf16 v[102:105], v[168:171], v[198:201], v[102:105]
	v_mfma_f32_16x16x32_bf16 v[98:101], v[182:185], v[198:201], v[98:101]
	v_mfma_f32_16x16x32_bf16 v[86:89], v[168:171], v[206:209], v[86:89]
	v_mfma_f32_16x16x32_bf16 v[82:85], v[182:185], v[206:209], v[82:85]
	v_mfma_f32_16x16x32_bf16 v[70:73], v[168:171], v[214:217], v[70:73]
	v_mfma_f32_16x16x32_bf16 v[66:69], v[182:185], v[214:217], v[66:69]
	s_setprio 0
	s_barrier
	s_mov_b32 m0, s66
	s_add_u32 s42, s42, 0x10080
	ds_read_b128 v[186:189], v175 offset:49152
	ds_read_b128 v[190:193], v175 offset:50176
	ds_read_b128 v[194:197], v175 offset:51200
	ds_read_b128 v[198:201], v175 offset:52224
	global_load_lds_dwordx4 v148, s[98:99]
	s_mov_b32 m0, s67
	s_addc_u32 s43, s43, 0
	global_load_lds_dwordx4 v152, s[98:99]
	s_mov_b32 m0, s70
	ds_read_b128 v[214:217], v175 offset:56320
	global_load_lds_dwordx4 v148, s[42:43]
	s_mov_b32 m0, s71
	ds_read_b128 v[210:213], v175 offset:55296
	global_load_lds_dwordx4 v152, s[42:43]
	s_mov_b32 m0, s68
	ds_read_b128 v[206:209], v175 offset:54272
	global_load_lds_dwordx4 v146, s[100:101]
	s_mov_b32 m0, s69
	ds_read_b128 v[202:205], v175 offset:53248
	global_load_lds_dwordx4 v150, s[100:101]
	s_waitcnt vmcnt(8) lgkmcnt(0)
	s_barrier
	s_setprio 1
	v_mfma_f32_16x16x32_bf16 v[62:65], v[130:133], v[186:189], v[62:65]
	v_mfma_f32_16x16x32_bf16 v[58:61], v[138:141], v[186:189], v[58:61]
	v_mfma_f32_16x16x32_bf16 v[46:49], v[130:133], v[194:197], v[46:49]
	v_mfma_f32_16x16x32_bf16 v[42:45], v[138:141], v[194:197], v[42:45]
	v_mfma_f32_16x16x32_bf16 v[30:33], v[130:133], v[202:205], v[30:33]
	v_mfma_f32_16x16x32_bf16 v[26:29], v[138:141], v[202:205], v[26:29]
	v_mfma_f32_16x16x32_bf16 v[14:17], v[130:133], v[210:213], v[14:17]
	v_mfma_f32_16x16x32_bf16 v[10:13], v[138:141], v[210:213], v[10:13]
	v_mfma_f32_16x16x32_bf16 v[62:65], v[134:137], v[190:193], v[62:65]
	v_mfma_f32_16x16x32_bf16 v[58:61], v[142:145], v[190:193], v[58:61]
	v_mfma_f32_16x16x32_bf16 v[46:49], v[134:137], v[198:201], v[46:49]
	v_mfma_f32_16x16x32_bf16 v[42:45], v[142:145], v[198:201], v[42:45]
	v_mfma_f32_16x16x32_bf16 v[30:33], v[134:137], v[206:209], v[30:33]
	v_mfma_f32_16x16x32_bf16 v[26:29], v[142:145], v[206:209], v[26:29]
	v_mfma_f32_16x16x32_bf16 v[14:17], v[134:137], v[214:217], v[14:17]
	v_mfma_f32_16x16x32_bf16 v[10:13], v[142:145], v[214:217], v[10:13]
	s_setprio 0
	s_setprio 1
	v_mfma_f32_16x16x32_bf16 v[54:57], v[164:167], v[186:189], v[54:57]
	v_mfma_f32_16x16x32_bf16 v[50:53], v[178:181], v[186:189], v[50:53]
	v_mfma_f32_16x16x32_bf16 v[38:41], v[164:167], v[194:197], v[38:41]
	v_mfma_f32_16x16x32_bf16 v[34:37], v[178:181], v[194:197], v[34:37]
	v_mfma_f32_16x16x32_bf16 v[22:25], v[164:167], v[202:205], v[22:25]
	v_mfma_f32_16x16x32_bf16 v[18:21], v[178:181], v[202:205], v[18:21]
	v_mfma_f32_16x16x32_bf16 v[6:9], v[164:167], v[210:213], v[6:9]
	v_mfma_f32_16x16x32_bf16 v[2:5], v[178:181], v[210:213], v[2:5]
	v_mfma_f32_16x16x32_bf16 v[54:57], v[168:171], v[190:193], v[54:57]
	v_mfma_f32_16x16x32_bf16 v[50:53], v[182:185], v[190:193], v[50:53]
	v_mfma_f32_16x16x32_bf16 v[38:41], v[168:171], v[198:201], v[38:41]
	v_mfma_f32_16x16x32_bf16 v[34:37], v[182:185], v[198:201], v[34:37]
	v_mfma_f32_16x16x32_bf16 v[22:25], v[168:171], v[206:209], v[22:25]
	v_mfma_f32_16x16x32_bf16 v[18:21], v[182:185], v[206:209], v[18:21]
	v_mfma_f32_16x16x32_bf16 v[6:9], v[168:171], v[214:217], v[6:9]
	v_mfma_f32_16x16x32_bf16 v[2:5], v[182:185], v[214:217], v[2:5]
	s_setprio 0
	s_barrier
	s_add_u32 s76, s76, 0x100
	s_addc_u32 s77, s77, 0
	s_add_u32 s40, s40, 0x100
	s_addc_u32 s41, s41, 0
	s_cmp_ge_i32 s78, s65
	s_mov_b32 s42, s78
	s_cbranch_scc0 .LBB0_3356
	s_branch .Lpx_15
; #define PG8_STAGE(bufoff, gbase, voff) do { _Pragma("unroll") for (int _i = 0; _i < 2; ++_i) \
;         __builtin_amdgcn_global_load_lds((const unsigned*)((const char*)(gbase) + (voff)[_i]), (PG8_LAS unsigned*)(lds + (bufoff) + ldsw + _i * 8192), 16, 0, 0); } while (0)
; #define PG8_LDA(dst, b, h) do { if constexpr (DT != 1) { _Pragma("unroll") for (int m = 0; m < 4; ++m) _Pragma("unroll") for (int k = 0; k < 2; ++k) dst[m][k] = *(const PG8_LAS bf16x8*)(lds + PG8_SA(b, h) + aoff + m * 2048 + k * 1024); } \
;         else { _Pragma("unroll") for (int m = 0; m < 4; ++m) dst##8[m] = ld32(lds + PG8_SA(b, h) + aoff + m * 2048); } } while (0)
; #define PG8_WAIT_V(n) asm volatile("s_waitcnt vmcnt(" #n ")" ::: "memory")
;     ...
;         const char* nA = has_next ? (const char*)g.A + (size_t)nxt.pm * tstepA : cA; const char* nB = has_next ? (const char*)g.Bt + (size_t)nxt.pn * tstepB : cB;
;         for (int t = 0; t < nt; t += 2) {
;             const bool last = (t == nt - 2);
;             const char* a1 = cA + (size_t)(t + 1) * kstep;
;             const char* a2 = last ? nA : cA + (size_t)(t + 2) * kstep; const char* b2 = last ? nB : cB + (size_t)(t + 2) * kstep;
;             const char* a3 = a2 + kstep; const char* b3 = b2 + kstep;
;             if (last && has_next) S.a_ready(nxt);
;             if constexpr (SP2) {
;             PG8_LDB(B0, 0, 0); PG8_LDB(B1, 0, 1); PG8_SCHED; PG8_LDA(At, 0, 0); PG8_STAGE(PG8_SA(1, 1), a1 + hstepA, voffA);
;             PG8_WAIT_V(8); PG8_WAIT_L(0); PG8_BAR; PG8_MMA(0, 0, At, B0); PG8_MMA(0, 1, At, B1); PG8_BAR; PG8_SCHED;
;             PG8_LDA(At, 0, 1); PG8_STAGE(PG8_SB(0, 0), b2, voffB); PG8_STAGE(PG8_SB(0, 1), b2 + hstepB, voffB); PG8_STAGE(PG8_SA(0, 0), a2, voffA);
;             PG8_WAIT_V(8); PG8_WAIT_L(0); PG8_BAR; PG8_MMA(1, 0, At, B0); PG8_MMA(1, 1, At, B1); PG8_BAR; PG8_SCHED;
;             PG8_LDB(B0, 1, 0); PG8_LDB(B1, 1, 1); PG8_SCHED; PG8_LDA(At, 1, 0); PG8_STAGE(PG8_SA(0, 1), a2 + hstepA, voffA);
;             PG8_WAIT_V(8); PG8_WAIT_L(0); PG8_BAR; PG8_MMA(0, 0, At, B0); PG8_MMA(0, 1, At, B1); PG8_BAR; PG8_SCHED;
;             PG8_LDA(At, 1, 1); PG8_STAGE(PG8_SB(1, 0), b3, voffB); PG8_STAGE(PG8_SB(1, 1), b3 + hstepB, voffB); PG8_STAGE(PG8_SA(1, 0), a3, voffA);
;             PG8_WAIT_V(8); PG8_WAIT_L(0); PG8_BAR; PG8_MMA(1, 0, At, B0); PG8_MMA(1, 1, At, B1); PG8_BAR; PG8_SCHED;
.LBB0_3356:
	ds_read_b128 v[130:133], v173
	ds_read_b128 v[134:137], v173 offset:1024
	ds_read_b128 v[138:141], v173 offset:2048
	ds_read_b128 v[142:145], v173 offset:3072
	ds_read_b128 v[164:167], v174
	ds_read_b128 v[168:171], v174 offset:1024
	ds_read_b128 v[178:181], v174 offset:2048
	ds_read_b128 v[182:185], v174 offset:3072
	s_add_i32 s78, s42, 2
	s_add_u32 s43, s40, 0xffff0080
	s_addc_u32 s44, s41, -1
	s_cmp_eq_u32 s74, s42
	s_cselect_b32 s42, s39, s76
	s_cselect_b32 s45, s3, s44
	s_cselect_b32 s44, s29, s43
	s_cselect_b32 s43, s31, s77
	s_add_i32 m0, s56, 0xc000
	ds_read_b128 v[186:189], v175
	ds_read_b128 v[190:193], v175 offset:1024
	ds_read_b128 v[194:197], v175 offset:2048
	ds_read_b128 v[198:201], v175 offset:3072
	ds_read_b128 v[202:205], v175 offset:4096
	ds_read_b128 v[206:209], v175 offset:5120
	ds_read_b128 v[210:213], v175 offset:6144
	ds_read_b128 v[214:217], v175 offset:7168
	global_load_lds_dwordx4 v158, s[40:41]
	s_add_i32 m0, s56, 0xe000
	s_nop 0
	global_load_lds_dwordx4 v156, s[40:41]
	s_waitcnt vmcnt(8) lgkmcnt(0)
	s_barrier
	s_setprio 1
	v_mfma_f32_16x16x32_bf16 v[126:129], v[130:133], v[186:189], v[126:129]
	v_mfma_f32_16x16x32_bf16 v[122:125], v[138:141], v[186:189], v[122:125]
	v_mfma_f32_16x16x32_bf16 v[110:113], v[130:133], v[194:197], v[110:113]
	v_mfma_f32_16x16x32_bf16 v[106:109], v[138:141], v[194:197], v[106:109]
	v_mfma_f32_16x16x32_bf16 v[94:97], v[130:133], v[202:205], v[94:97]
	v_mfma_f32_16x16x32_bf16 v[90:93], v[138:141], v[202:205], v[90:93]
	v_mfma_f32_16x16x32_bf16 v[78:81], v[130:133], v[210:213], v[78:81]
	v_mfma_f32_16x16x32_bf16 v[74:77], v[138:141], v[210:213], v[74:77]
	v_mfma_f32_16x16x32_bf16 v[126:129], v[134:137], v[190:193], v[126:129]
	v_mfma_f32_16x16x32_bf16 v[122:125], v[142:145], v[190:193], v[122:125]
	v_mfma_f32_16x16x32_bf16 v[110:113], v[134:137], v[198:201], v[110:113]
	v_mfma_f32_16x16x32_bf16 v[106:109], v[142:145], v[198:201], v[106:109]
	v_mfma_f32_16x16x32_bf16 v[94:97], v[134:137], v[206:209], v[94:97]
	v_mfma_f32_16x16x32_bf16 v[90:93], v[142:145], v[206:209], v[90:93]
	v_mfma_f32_16x16x32_bf16 v[78:81], v[134:137], v[214:217], v[78:81]
	v_mfma_f32_16x16x32_bf16 v[74:77], v[142:145], v[214:217], v[74:77]
	s_setprio 0
	s_setprio 1
	v_mfma_f32_16x16x32_bf16 v[118:121], v[164:167], v[186:189], v[118:121]
	v_mfma_f32_16x16x32_bf16 v[114:117], v[178:181], v[186:189], v[114:117]
	v_mfma_f32_16x16x32_bf16 v[102:105], v[164:167], v[194:197], v[102:105]
	v_mfma_f32_16x16x32_bf16 v[98:101], v[178:181], v[194:197], v[98:101]
	v_mfma_f32_16x16x32_bf16 v[86:89], v[164:167], v[202:205], v[86:89]
	v_mfma_f32_16x16x32_bf16 v[82:85], v[178:181], v[202:205], v[82:85]
	v_mfma_f32_16x16x32_bf16 v[70:73], v[164:167], v[210:213], v[70:73]
	v_mfma_f32_16x16x32_bf16 v[66:69], v[178:181], v[210:213], v[66:69]
	v_mfma_f32_16x16x32_bf16 v[118:121], v[168:171], v[190:193], v[118:121]
	v_mfma_f32_16x16x32_bf16 v[114:117], v[182:185], v[190:193], v[114:117]
	v_mfma_f32_16x16x32_bf16 v[102:105], v[168:171], v[198:201], v[102:105]
	v_mfma_f32_16x16x32_bf16 v[98:101], v[182:185], v[198:201], v[98:101]
	v_mfma_f32_16x16x32_bf16 v[86:89], v[168:171], v[206:209], v[86:89]
	v_mfma_f32_16x16x32_bf16 v[82:85], v[182:185], v[206:209], v[82:85]
	v_mfma_f32_16x16x32_bf16 v[70:73], v[168:171], v[214:217], v[70:73]
	v_mfma_f32_16x16x32_bf16 v[66:69], v[182:185], v[214:217], v[66:69]
	s_setprio 0
	s_barrier
	s_mov_b32 m0, s52
	s_add_u32 s98, s42, 0x80
	s_addc_u32 s99, s43, 0
	s_add_u32 s80, s42, 0x10000
	ds_read_b128 v[186:189], v175 offset:16384
	ds_read_b128 v[190:193], v175 offset:17408
	ds_read_b128 v[194:197], v175 offset:18432
	ds_read_b128 v[198:201], v175 offset:19456
	global_load_lds_dwordx4 v148, s[42:43]
	s_mov_b32 m0, s53
	s_addc_u32 s81, s43, 0
	global_load_lds_dwordx4 v152, s[42:43]
	s_mov_b32 m0, s54
	ds_read_b128 v[214:217], v175 offset:23552
	global_load_lds_dwordx4 v148, s[80:81]
	s_mov_b32 m0, s55
	ds_read_b128 v[210:213], v175 offset:22528
	global_load_lds_dwordx4 v152, s[80:81]
	s_add_u32 s100, s44, 0x80
	s_addc_u32 s101, s45, 0
	s_mov_b32 m0, s56
	ds_read_b128 v[206:209], v175 offset:21504
	global_load_lds_dwordx4 v146, s[44:45]
	s_mov_b32 m0, s57
	ds_read_b128 v[202:205], v175 offset:20480
	global_load_lds_dwordx4 v150, s[44:45]
	s_waitcnt vmcnt(8) lgkmcnt(0)
	s_barrier
	s_setprio 1
	v_mfma_f32_16x16x32_bf16 v[62:65], v[130:133], v[186:189], v[62:65]
	v_mfma_f32_16x16x32_bf16 v[58:61], v[138:141], v[186:189], v[58:61]
	v_mfma_f32_16x16x32_bf16 v[46:49], v[130:133], v[194:197], v[46:49]
	v_mfma_f32_16x16x32_bf16 v[42:45], v[138:141], v[194:197], v[42:45]
	v_mfma_f32_16x16x32_bf16 v[30:33], v[130:133], v[202:205], v[30:33]
	v_mfma_f32_16x16x32_bf16 v[26:29], v[138:141], v[202:205], v[26:29]
	v_mfma_f32_16x16x32_bf16 v[14:17], v[130:133], v[210:213], v[14:17]
	v_mfma_f32_16x16x32_bf16 v[10:13], v[138:141], v[210:213], v[10:13]
	v_mfma_f32_16x16x32_bf16 v[62:65], v[134:137], v[190:193], v[62:65]
	v_mfma_f32_16x16x32_bf16 v[58:61], v[142:145], v[190:193], v[58:61]
	v_mfma_f32_16x16x32_bf16 v[46:49], v[134:137], v[198:201], v[46:49]
	v_mfma_f32_16x16x32_bf16 v[42:45], v[142:145], v[198:201], v[42:45]
	v_mfma_f32_16x16x32_bf16 v[30:33], v[134:137], v[206:209], v[30:33]
	v_mfma_f32_16x16x32_bf16 v[26:29], v[142:145], v[206:209], v[26:29]
	v_mfma_f32_16x16x32_bf16 v[14:17], v[134:137], v[214:217], v[14:17]
	v_mfma_f32_16x16x32_bf16 v[10:13], v[142:145], v[214:217], v[10:13]
	s_setprio 0
	s_setprio 1
	v_mfma_f32_16x16x32_bf16 v[54:57], v[164:167], v[186:189], v[54:57]
	v_mfma_f32_16x16x32_bf16 v[50:53], v[178:181], v[186:189], v[50:53]
	v_mfma_f32_16x16x32_bf16 v[38:41], v[164:167], v[194:197], v[38:41]
	v_mfma_f32_16x16x32_bf16 v[34:37], v[178:181], v[194:197], v[34:37]
	v_mfma_f32_16x16x32_bf16 v[22:25], v[164:167], v[202:205], v[22:25]
	v_mfma_f32_16x16x32_bf16 v[18:21], v[178:181], v[202:205], v[18:21]
	v_mfma_f32_16x16x32_bf16 v[6:9], v[164:167], v[210:213], v[6:9]
	v_mfma_f32_16x16x32_bf16 v[2:5], v[178:181], v[210:213], v[2:5]
	v_mfma_f32_16x16x32_bf16 v[54:57], v[168:171], v[190:193], v[54:57]
	v_mfma_f32_16x16x32_bf16 v[50:53], v[182:185], v[190:193], v[50:53]
	v_mfma_f32_16x16x32_bf16 v[38:41], v[168:171], v[198:201], v[38:41]
	v_mfma_f32_16x16x32_bf16 v[34:37], v[182:185], v[198:201], v[34:37]
	v_mfma_f32_16x16x32_bf16 v[22:25], v[168:171], v[206:209], v[22:25]
	v_mfma_f32_16x16x32_bf16 v[18:21], v[182:185], v[206:209], v[18:21]
	v_mfma_f32_16x16x32_bf16 v[6:9], v[168:171], v[214:217], v[6:9]
	v_mfma_f32_16x16x32_bf16 v[2:5], v[182:185], v[214:217], v[2:5]
	s_setprio 0
	s_barrier
; #define PG8_STAGE(bufoff, gbase, voff) do { _Pragma("unroll") for (int _i = 0; _i < 2; ++_i) \
;         __builtin_amdgcn_global_load_lds((const unsigned*)((const char*)(gbase) + (voff)[_i]), (PG8_LAS unsigned*)(lds + (bufoff) + ldsw + _i * 8192), 16, 0, 0); } while (0)
; #define PG8_LDA(dst, b, h) do { if constexpr (DT != 1) { _Pragma("unroll") for (int m = 0; m < 4; ++m) _Pragma("unroll") for (int k = 0; k < 2; ++k) dst[m][k] = *(const PG8_LAS bf16x8*)(lds + PG8_SA(b, h) + aoff + m * 2048 + k * 1024); } \
;         else { _Pragma("unroll") for (int m = 0; m < 4; ++m) dst##8[m] = ld32(lds + PG8_SA(b, h) + aoff + m * 2048); } } while (0)
; #define PG8_LDB(dst, b, h) do { if constexpr (DT != 1) { _Pragma("unroll") for (int n = 0; n < 2; ++n) _Pragma("unroll") for (int k = 0; k < 2; ++k) dst[n][k] = *(const PG8_LAS bf16x8*)(lds + PG8_SB(b, h) + boff + n * 2048 + k * 1024); } \
;         else { _Pragma("unroll") for (int n = 0; n < 2; ++n) dst##8[n] = ld32(lds + PG8_SB(b, h) + boff + n * 2048); } } while (0)
; #define PG8_WAIT_V(n) asm volatile("s_waitcnt vmcnt(" #n ")" ::: "memory")
; #define PG8_WAIT_L(n) asm volatile("s_waitcnt lgkmcnt(" #n ")" ::: "memory")
; #define PG8_BAR __builtin_amdgcn_s_barrier()
; #define PG8_SCHED __builtin_amdgcn_sched_barrier(0)
;     ...
;             PG8_LDB(B0, 0, 0); PG8_LDB(B1, 0, 1); PG8_SCHED; PG8_LDA(At, 0, 0); PG8_STAGE(PG8_SA(1, 1), a1 + hstepA, voffA);
;             PG8_WAIT_V(8); PG8_WAIT_L(0); PG8_BAR; PG8_MMA(0, 0, At, B0); PG8_MMA(0, 1, At, B1); PG8_BAR; PG8_SCHED;
;             PG8_LDA(At, 0, 1); PG8_STAGE(PG8_SB(0, 0), b2, voffB); PG8_STAGE(PG8_SB(0, 1), b2 + hstepB, voffB); PG8_STAGE(PG8_SA(0, 0), a2, voffA);
;             PG8_WAIT_V(8); PG8_WAIT_L(0); PG8_BAR; PG8_MMA(1, 0, At, B0); PG8_MMA(1, 1, At, B1); PG8_BAR; PG8_SCHED;
;             PG8_LDB(B0, 1, 0); PG8_LDB(B1, 1, 1); PG8_SCHED; PG8_LDA(At, 1, 0); PG8_STAGE(PG8_SA(0, 1), a2 + hstepA, voffA);
;             PG8_WAIT_V(8); PG8_WAIT_L(0); PG8_BAR; PG8_MMA(0, 0, At, B0); PG8_MMA(0, 1, At, B1); PG8_BAR; PG8_SCHED;
;             PG8_LDA(At, 1, 1); PG8_STAGE(PG8_SB(1, 0), b3, voffB); PG8_STAGE(PG8_SB(1, 1), b3 + hstepB, voffB); PG8_STAGE(PG8_SA(1, 0), a3, voffA);
;             PG8_WAIT_V(8); PG8_WAIT_L(0); PG8_BAR; PG8_MMA(1, 0, At, B0); PG8_MMA(1, 1, At, B1); PG8_BAR; PG8_SCHED;
	ds_read_b128 v[130:133], v176
	ds_read_b128 v[134:137], v176 offset:1024
	ds_read_b128 v[138:141], v176 offset:2048
	ds_read_b128 v[142:145], v176 offset:3072
	ds_read_b128 v[164:167], v177
	ds_read_b128 v[168:171], v177 offset:1024
	ds_read_b128 v[178:181], v177 offset:2048
	ds_read_b128 v[182:185], v177 offset:3072
	s_add_u32 s44, s44, 0x10000
	s_addc_u32 s45, s45, 0
	s_mov_b32 m0, s58
	ds_read_b128 v[186:189], v175 offset:32768
	ds_read_b128 v[190:193], v175 offset:33792
	ds_read_b128 v[194:197], v175 offset:34816
	ds_read_b128 v[198:201], v175 offset:35840
	ds_read_b128 v[202:205], v175 offset:36864
	ds_read_b128 v[206:209], v175 offset:37888
	ds_read_b128 v[210:213], v175 offset:38912
	global_load_lds_dwordx4 v146, s[44:45]
	s_mov_b32 m0, s59
	ds_read_b128 v[214:217], v175 offset:39936
	global_load_lds_dwordx4 v150, s[44:45]
	s_waitcnt vmcnt(8) lgkmcnt(0)
	s_barrier
	s_setprio 1
	v_mfma_f32_16x16x32_bf16 v[126:129], v[130:133], v[186:189], v[126:129]
	v_mfma_f32_16x16x32_bf16 v[122:125], v[138:141], v[186:189], v[122:125]
	v_mfma_f32_16x16x32_bf16 v[110:113], v[130:133], v[194:197], v[110:113]
	v_mfma_f32_16x16x32_bf16 v[106:109], v[138:141], v[194:197], v[106:109]
	v_mfma_f32_16x16x32_bf16 v[94:97], v[130:133], v[202:205], v[94:97]
	v_mfma_f32_16x16x32_bf16 v[90:93], v[138:141], v[202:205], v[90:93]
	v_mfma_f32_16x16x32_bf16 v[78:81], v[130:133], v[210:213], v[78:81]
	v_mfma_f32_16x16x32_bf16 v[74:77], v[138:141], v[210:213], v[74:77]
	v_mfma_f32_16x16x32_bf16 v[126:129], v[134:137], v[190:193], v[126:129]
	v_mfma_f32_16x16x32_bf16 v[122:125], v[142:145], v[190:193], v[122:125]
	v_mfma_f32_16x16x32_bf16 v[110:113], v[134:137], v[198:201], v[110:113]
	v_mfma_f32_16x16x32_bf16 v[106:109], v[142:145], v[198:201], v[106:109]
	v_mfma_f32_16x16x32_bf16 v[94:97], v[134:137], v[206:209], v[94:97]
	v_mfma_f32_16x16x32_bf16 v[90:93], v[142:145], v[206:209], v[90:93]
	v_mfma_f32_16x16x32_bf16 v[78:81], v[134:137], v[214:217], v[78:81]
	v_mfma_f32_16x16x32_bf16 v[74:77], v[142:145], v[214:217], v[74:77]
	s_setprio 0
	s_setprio 1
	v_mfma_f32_16x16x32_bf16 v[118:121], v[164:167], v[186:189], v[118:121]
	v_mfma_f32_16x16x32_bf16 v[114:117], v[178:181], v[186:189], v[114:117]
	v_mfma_f32_16x16x32_bf16 v[102:105], v[164:167], v[194:197], v[102:105]
	v_mfma_f32_16x16x32_bf16 v[98:101], v[178:181], v[194:197], v[98:101]
	v_mfma_f32_16x16x32_bf16 v[86:89], v[164:167], v[202:205], v[86:89]
	v_mfma_f32_16x16x32_bf16 v[82:85], v[178:181], v[202:205], v[82:85]
	v_mfma_f32_16x16x32_bf16 v[70:73], v[164:167], v[210:213], v[70:73]
	v_mfma_f32_16x16x32_bf16 v[66:69], v[178:181], v[210:213], v[66:69]
	v_mfma_f32_16x16x32_bf16 v[118:121], v[168:171], v[190:193], v[118:121]
	v_mfma_f32_16x16x32_bf16 v[114:117], v[182:185], v[190:193], v[114:117]
	v_mfma_f32_16x16x32_bf16 v[102:105], v[168:171], v[198:201], v[102:105]
	v_mfma_f32_16x16x32_bf16 v[98:101], v[182:185], v[198:201], v[98:101]
	v_mfma_f32_16x16x32_bf16 v[86:89], v[168:171], v[206:209], v[86:89]
	v_mfma_f32_16x16x32_bf16 v[82:85], v[182:185], v[206:209], v[82:85]
	v_mfma_f32_16x16x32_bf16 v[70:73], v[168:171], v[214:217], v[70:73]
	v_mfma_f32_16x16x32_bf16 v[66:69], v[182:185], v[214:217], v[66:69]
	s_setprio 0
	s_barrier
	s_mov_b32 m0, s66
	s_add_u32 s42, s42, 0x10080
	ds_read_b128 v[186:189], v175 offset:49152
	ds_read_b128 v[190:193], v175 offset:50176
	ds_read_b128 v[194:197], v175 offset:51200
	ds_read_b128 v[198:201], v175 offset:52224
	global_load_lds_dwordx4 v148, s[98:99]
	s_mov_b32 m0, s67
	s_addc_u32 s43, s43, 0
	global_load_lds_dwordx4 v152, s[98:99]
	s_mov_b32 m0, s70
	ds_read_b128 v[214:217], v175 offset:56320
	global_load_lds_dwordx4 v148, s[42:43]
	s_mov_b32 m0, s71
	ds_read_b128 v[210:213], v175 offset:55296
	global_load_lds_dwordx4 v152, s[42:43]
	s_mov_b32 m0, s68
	ds_read_b128 v[206:209], v175 offset:54272
	global_load_lds_dwordx4 v146, s[100:101]
	s_mov_b32 m0, s69
	ds_read_b128 v[202:205], v175 offset:53248
	global_load_lds_dwordx4 v150, s[100:101]
	s_waitcnt vmcnt(8) lgkmcnt(0)
	s_barrier
	s_setprio 1
	v_mfma_f32_16x16x32_bf16 v[62:65], v[130:133], v[186:189], v[62:65]
	v_mfma_f32_16x16x32_bf16 v[58:61], v[138:141], v[186:189], v[58:61]
	v_mfma_f32_16x16x32_bf16 v[46:49], v[130:133], v[194:197], v[46:49]
	v_mfma_f32_16x16x32_bf16 v[42:45], v[138:141], v[194:197], v[42:45]
	v_mfma_f32_16x16x32_bf16 v[30:33], v[130:133], v[202:205], v[30:33]
	v_mfma_f32_16x16x32_bf16 v[26:29], v[138:141], v[202:205], v[26:29]
	v_mfma_f32_16x16x32_bf16 v[14:17], v[130:133], v[210:213], v[14:17]
	v_mfma_f32_16x16x32_bf16 v[10:13], v[138:141], v[210:213], v[10:13]
	v_mfma_f32_16x16x32_bf16 v[62:65], v[134:137], v[190:193], v[62:65]
	v_mfma_f32_16x16x32_bf16 v[58:61], v[142:145], v[190:193], v[58:61]
	v_mfma_f32_16x16x32_bf16 v[46:49], v[134:137], v[198:201], v[46:49]
	v_mfma_f32_16x16x32_bf16 v[42:45], v[142:145], v[198:201], v[42:45]
	v_mfma_f32_16x16x32_bf16 v[30:33], v[134:137], v[206:209], v[30:33]
	v_mfma_f32_16x16x32_bf16 v[26:29], v[142:145], v[206:209], v[26:29]
	v_mfma_f32_16x16x32_bf16 v[14:17], v[134:137], v[214:217], v[14:17]
	v_mfma_f32_16x16x32_bf16 v[10:13], v[142:145], v[214:217], v[10:13]
	s_setprio 0
	s_setprio 1
	v_mfma_f32_16x16x32_bf16 v[54:57], v[164:167], v[186:189], v[54:57]
	v_mfma_f32_16x16x32_bf16 v[50:53], v[178:181], v[186:189], v[50:53]
	v_mfma_f32_16x16x32_bf16 v[38:41], v[164:167], v[194:197], v[38:41]
	v_mfma_f32_16x16x32_bf16 v[34:37], v[178:181], v[194:197], v[34:37]
	v_mfma_f32_16x16x32_bf16 v[22:25], v[164:167], v[202:205], v[22:25]
	v_mfma_f32_16x16x32_bf16 v[18:21], v[178:181], v[202:205], v[18:21]
	v_mfma_f32_16x16x32_bf16 v[6:9], v[164:167], v[210:213], v[6:9]
	v_mfma_f32_16x16x32_bf16 v[2:5], v[178:181], v[210:213], v[2:5]
	v_mfma_f32_16x16x32_bf16 v[54:57], v[168:171], v[190:193], v[54:57]
	v_mfma_f32_16x16x32_bf16 v[50:53], v[182:185], v[190:193], v[50:53]
	v_mfma_f32_16x16x32_bf16 v[38:41], v[168:171], v[198:201], v[38:41]
	v_mfma_f32_16x16x32_bf16 v[34:37], v[182:185], v[198:201], v[34:37]
	v_mfma_f32_16x16x32_bf16 v[22:25], v[168:171], v[206:209], v[22:25]
	v_mfma_f32_16x16x32_bf16 v[18:21], v[182:185], v[206:209], v[18:21]
	v_mfma_f32_16x16x32_bf16 v[6:9], v[168:171], v[214:217], v[6:9]
	v_mfma_f32_16x16x32_bf16 v[2:5], v[182:185], v[214:217], v[2:5]
	s_setprio 0
	s_barrier
	s_add_u32 s76, s76, 0x100
	s_addc_u32 s77, s77, 0
	s_add_u32 s40, s40, 0x100
	s_addc_u32 s41, s41, 0
	s_cmp_ge_i32 s78, s65
	s_mov_b32 s42, s78
	s_cbranch_scc0 .LBB0_3356

; #define PG8_STAGE(bufoff, gbase, voff) do { _Pragma("unroll") for (int _i = 0; _i < 2; ++_i) \
;         __builtin_amdgcn_global_load_lds((const unsigned*)((const char*)(gbase) + (voff)[_i]), (PG8_LAS unsigned*)(lds + (bufoff) + ldsw + _i * 8192), 16, 0, 0); } while (0)
; #define PG8_LDA(dst, b, h) do { if constexpr (DT != 1) { _Pragma("unroll") for (int m = 0; m < 4; ++m) _Pragma("unroll") for (int k = 0; k < 2; ++k) dst[m][k] = *(const PG8_LAS bf16x8*)(lds + PG8_SA(b, h) + aoff + m * 2048 + k * 1024); } \
;         else { _Pragma("unroll") for (int m = 0; m < 4; ++m) dst##8[m] = ld32(lds + PG8_SA(b, h) + aoff + m * 2048); } } while (0)
; #define PG8_WAIT_V(n) asm volatile("s_waitcnt vmcnt(" #n ")" ::: "memory")
;     ...
;         const char* nA = has_next ? (const char*)g.A + (size_t)nxt.pm * tstepA : cA; const char* nB = has_next ? (const char*)g.Bt + (size_t)nxt.pn * tstepB : cB;
;         for (int t = 0; t < nt; t += 2) {
;             const bool last = (t == nt - 2);
;             const char* a1 = cA + (size_t)(t + 1) * kstep;
;             const char* a2 = last ? nA : cA + (size_t)(t + 2) * kstep; const char* b2 = last ? nB : cB + (size_t)(t + 2) * kstep;
;             const char* a3 = a2 + kstep; const char* b3 = b2 + kstep;
;             if (last && has_next) S.a_ready(nxt);
;             if constexpr (SP2) {
;             PG8_LDB(B0, 0, 0); PG8_LDB(B1, 0, 1); PG8_SCHED; PG8_LDA(At, 0, 0); PG8_STAGE(PG8_SA(1, 1), a1 + hstepA, voffA);
;             PG8_WAIT_V(8); PG8_WAIT_L(0); PG8_BAR; PG8_MMA(0, 0, At, B0); PG8_MMA(0, 1, At, B1); PG8_BAR; PG8_SCHED;
;             PG8_LDA(At, 0, 1); PG8_STAGE(PG8_SB(0, 0), b2, voffB); PG8_STAGE(PG8_SB(0, 1), b2 + hstepB, voffB); PG8_STAGE(PG8_SA(0, 0), a2, voffA);
;             PG8_WAIT_V(8); PG8_WAIT_L(0); PG8_BAR; PG8_MMA(1, 0, At, B0); PG8_MMA(1, 1, At, B1); PG8_BAR; PG8_SCHED;
;             PG8_LDB(B0, 1, 0); PG8_LDB(B1, 1, 1); PG8_SCHED; PG8_LDA(At, 1, 0); PG8_STAGE(PG8_SA(0, 1), a2 + hstepA, voffA);
;             PG8_WAIT_V(8); PG8_WAIT_L(0); PG8_BAR; PG8_MMA(0, 0, At, B0); PG8_MMA(0, 1, At, B1); PG8_BAR; PG8_SCHED;
;             PG8_LDA(At, 1, 1); PG8_STAGE(PG8_SB(1, 0), b3, voffB); PG8_STAGE(PG8_SB(1, 1), b3 + hstepB, voffB); PG8_STAGE(PG8_SA(1, 0), a3, voffA);
;             PG8_WAIT_V(8); PG8_WAIT_L(0); PG8_BAR; PG8_MMA(1, 0, At, B0); PG8_MMA(1, 1, At, B1); PG8_BAR; PG8_SCHED;
.Lzs_13:
	s_cbranch_vccnz .LBB0_4142
	s_and_b64 s[28:29], s[0:1], exec
	s_cselect_b32 s15, s19, s27
	s_cselect_b32 s17, s18, s26
	s_cselect_b32 s65, s21, s25
	s_cselect_b32 s66, s20, s24
	s_add_u32 s67, s24, 0x100
	s_addc_u32 s68, s25, 0
	s_add_u32 s24, s26, 0x40080
	s_addc_u32 s25, s27, 0
	s_mov_b32 s26, 0
	v_add_u32_e32 v160, s35, v164
	ds_read_b128 v[122:125], v160
	ds_read_b128 v[126:129], v160 offset:1024
	ds_read_b128 v[130:133], v160 offset:2048
	ds_read_b128 v[170:173], v160 offset:3072
	v_add_u32_e32 v160, s36, v164
	ds_read_b128 v[174:177], v160
	ds_read_b128 v[178:181], v160 offset:1024
	ds_read_b128 v[182:185], v160 offset:2048
	ds_read_b128 v[186:189], v160 offset:3072
	s_add_i32 s69, s26, 2
	s_add_u32 s27, s24, 0xfffc0080
	s_addc_u32 s28, s25, -1
	s_cmp_eq_u32 s61, s26
	s_cselect_b32 s26, s66, s67
	s_cselect_b32 s29, s15, s28
	s_cselect_b32 s28, s17, s27
	s_cselect_b32 s27, s65, s68
	s_add_i32 m0, s46, 0xc000
	ds_read_b128 v[190:193], v167
	ds_read_b128 v[194:197], v167 offset:1024
	ds_read_b128 v[198:201], v167 offset:2048
	ds_read_b128 v[202:205], v167 offset:3072
	ds_read_b128 v[206:209], v167 offset:4096
	ds_read_b128 v[210:213], v167 offset:5120
	ds_read_b128 v[214:217], v167 offset:6144
	ds_read_b128 v[218:221], v167 offset:7168
	global_load_lds_dwordx4 v154, s[24:25]
	s_add_i32 m0, s46, 0xe000
	s_nop 0
	global_load_lds_dwordx4 v152, s[24:25]
	s_waitcnt vmcnt(8) lgkmcnt(0)
	s_barrier
	s_setprio 1
	v_mfma_i32_16x16x64_i8 v[134:137], v[122:125], v[190:193], 0
	v_mfma_i32_16x16x64_i8 v[114:117], v[130:133], v[190:193], 0
	v_mfma_i32_16x16x64_i8 v[106:109], v[122:125], v[198:201], 0
	v_mfma_i32_16x16x64_i8 v[98:101], v[130:133], v[198:201], 0
	v_mfma_i32_16x16x64_i8 v[90:93], v[122:125], v[206:209], 0
	v_mfma_i32_16x16x64_i8 v[82:85], v[130:133], v[206:209], 0
	v_mfma_i32_16x16x64_i8 v[74:77], v[122:125], v[214:217], 0
	v_mfma_i32_16x16x64_i8 v[66:69], v[130:133], v[214:217], 0
	v_mfma_i32_16x16x64_i8 v[134:137], v[126:129], v[194:197], v[134:137]
	v_mfma_i32_16x16x64_i8 v[114:117], v[170:173], v[194:197], v[114:117]
	v_mfma_i32_16x16x64_i8 v[106:109], v[126:129], v[202:205], v[106:109]
	v_mfma_i32_16x16x64_i8 v[98:101], v[170:173], v[202:205], v[98:101]
	v_mfma_i32_16x16x64_i8 v[90:93], v[126:129], v[210:213], v[90:93]
	v_mfma_i32_16x16x64_i8 v[82:85], v[170:173], v[210:213], v[82:85]
	v_mfma_i32_16x16x64_i8 v[74:77], v[126:129], v[218:221], v[74:77]
	v_mfma_i32_16x16x64_i8 v[66:69], v[170:173], v[218:221], v[66:69]
	s_setprio 0
	s_setprio 1
	v_mfma_i32_16x16x64_i8 v[138:141], v[174:177], v[190:193], 0
	v_mfma_i32_16x16x64_i8 v[118:121], v[182:185], v[190:193], 0
	v_mfma_i32_16x16x64_i8 v[110:113], v[174:177], v[198:201], 0
	v_mfma_i32_16x16x64_i8 v[102:105], v[182:185], v[198:201], 0
	v_mfma_i32_16x16x64_i8 v[94:97], v[174:177], v[206:209], 0
	v_mfma_i32_16x16x64_i8 v[86:89], v[182:185], v[206:209], 0
	v_mfma_i32_16x16x64_i8 v[78:81], v[174:177], v[214:217], 0
	v_mfma_i32_16x16x64_i8 v[70:73], v[182:185], v[214:217], 0
	v_mfma_i32_16x16x64_i8 v[138:141], v[178:181], v[194:197], v[138:141]
	v_mfma_i32_16x16x64_i8 v[118:121], v[186:189], v[194:197], v[118:121]
	v_mfma_i32_16x16x64_i8 v[110:113], v[178:181], v[202:205], v[110:113]
	v_mfma_i32_16x16x64_i8 v[102:105], v[186:189], v[202:205], v[102:105]
	v_mfma_i32_16x16x64_i8 v[94:97], v[178:181], v[210:213], v[94:97]
	v_mfma_i32_16x16x64_i8 v[86:89], v[186:189], v[210:213], v[86:89]
	v_mfma_i32_16x16x64_i8 v[78:81], v[178:181], v[218:221], v[78:81]
	v_mfma_i32_16x16x64_i8 v[70:73], v[186:189], v[218:221], v[70:73]
	s_setprio 0
	s_barrier
	s_mov_b32 m0, s23
	s_add_u32 s98, s26, 0x80
	s_addc_u32 s99, s27, 0
	s_add_u32 s70, s26, 0x40000
	ds_read_b128 v[190:193], v167 offset:16384
	ds_read_b128 v[194:197], v167 offset:17408
	ds_read_b128 v[198:201], v167 offset:18432
	ds_read_b128 v[202:205], v167 offset:19456
	global_load_lds_dwordx4 v144, s[26:27]
	s_mov_b32 m0, s43
	s_addc_u32 s71, s27, 0
	global_load_lds_dwordx4 v148, s[26:27]
	s_mov_b32 m0, s44
	ds_read_b128 v[218:221], v167 offset:23552
	global_load_lds_dwordx4 v144, s[70:71]
	s_mov_b32 m0, s45
	ds_read_b128 v[214:217], v167 offset:22528
	global_load_lds_dwordx4 v148, s[70:71]
	s_add_u32 s100, s28, 0x80
	s_addc_u32 s101, s29, 0
	s_mov_b32 m0, s46
	ds_read_b128 v[210:213], v167 offset:21504
	global_load_lds_dwordx4 v142, s[28:29]
	s_mov_b32 m0, s47
	ds_read_b128 v[206:209], v167 offset:20480
	global_load_lds_dwordx4 v146, s[28:29]
	s_waitcnt vmcnt(8) lgkmcnt(0)
	s_barrier
	s_setprio 1
	v_mfma_i32_16x16x64_i8 v[58:61], v[122:125], v[190:193], 0
	v_mfma_i32_16x16x64_i8 v[50:53], v[130:133], v[190:193], 0
	v_mfma_i32_16x16x64_i8 v[42:45], v[122:125], v[198:201], 0
	v_mfma_i32_16x16x64_i8 v[34:37], v[130:133], v[198:201], 0
	v_mfma_i32_16x16x64_i8 v[26:29], v[122:125], v[206:209], 0
	v_mfma_i32_16x16x64_i8 v[18:21], v[130:133], v[206:209], 0
	v_mfma_i32_16x16x64_i8 v[10:13], v[122:125], v[214:217], 0
	v_mfma_i32_16x16x64_i8 v[2:5], v[130:133], v[214:217], 0
	v_mfma_i32_16x16x64_i8 v[58:61], v[126:129], v[194:197], v[58:61]
	v_mfma_i32_16x16x64_i8 v[50:53], v[170:173], v[194:197], v[50:53]
	v_mfma_i32_16x16x64_i8 v[42:45], v[126:129], v[202:205], v[42:45]
	v_mfma_i32_16x16x64_i8 v[34:37], v[170:173], v[202:205], v[34:37]
	v_mfma_i32_16x16x64_i8 v[26:29], v[126:129], v[210:213], v[26:29]
	v_mfma_i32_16x16x64_i8 v[18:21], v[170:173], v[210:213], v[18:21]
	v_mfma_i32_16x16x64_i8 v[10:13], v[126:129], v[218:221], v[10:13]
	v_mfma_i32_16x16x64_i8 v[2:5], v[170:173], v[218:221], v[2:5]
	s_setprio 0
	s_setprio 1
	v_mfma_i32_16x16x64_i8 v[62:65], v[174:177], v[190:193], 0
	v_mfma_i32_16x16x64_i8 v[54:57], v[182:185], v[190:193], 0
	v_mfma_i32_16x16x64_i8 v[46:49], v[174:177], v[198:201], 0
	v_mfma_i32_16x16x64_i8 v[38:41], v[182:185], v[198:201], 0
	v_mfma_i32_16x16x64_i8 v[30:33], v[174:177], v[206:209], 0
	v_mfma_i32_16x16x64_i8 v[22:25], v[182:185], v[206:209], 0
	v_mfma_i32_16x16x64_i8 v[14:17], v[174:177], v[214:217], 0
	v_mfma_i32_16x16x64_i8 v[6:9], v[182:185], v[214:217], 0
	v_mfma_i32_16x16x64_i8 v[62:65], v[178:181], v[194:197], v[62:65]
	v_mfma_i32_16x16x64_i8 v[54:57], v[186:189], v[194:197], v[54:57]
	v_mfma_i32_16x16x64_i8 v[46:49], v[178:181], v[202:205], v[46:49]
	v_mfma_i32_16x16x64_i8 v[38:41], v[186:189], v[202:205], v[38:41]
	v_mfma_i32_16x16x64_i8 v[30:33], v[178:181], v[210:213], v[30:33]
	v_mfma_i32_16x16x64_i8 v[22:25], v[186:189], v[210:213], v[22:25]
	v_mfma_i32_16x16x64_i8 v[14:17], v[178:181], v[218:221], v[14:17]
	v_mfma_i32_16x16x64_i8 v[6:9], v[186:189], v[218:221], v[6:9]
	s_setprio 0
	s_barrier
; #define PG8_STAGE(bufoff, gbase, voff) do { _Pragma("unroll") for (int _i = 0; _i < 2; ++_i) \
;         __builtin_amdgcn_global_load_lds((const unsigned*)((const char*)(gbase) + (voff)[_i]), (PG8_LAS unsigned*)(lds + (bufoff) + ldsw + _i * 8192), 16, 0, 0); } while (0)
; #define PG8_LDA(dst, b, h) do { if constexpr (DT != 1) { _Pragma("unroll") for (int m = 0; m < 4; ++m) _Pragma("unroll") for (int k = 0; k < 2; ++k) dst[m][k] = *(const PG8_LAS bf16x8*)(lds + PG8_SA(b, h) + aoff + m * 2048 + k * 1024); } \
;         else { _Pragma("unroll") for (int m = 0; m < 4; ++m) dst##8[m] = ld32(lds + PG8_SA(b, h) + aoff + m * 2048); } } while (0)
; #define PG8_LDB(dst, b, h) do { if constexpr (DT != 1) { _Pragma("unroll") for (int n = 0; n < 2; ++n) _Pragma("unroll") for (int k = 0; k < 2; ++k) dst[n][k] = *(const PG8_LAS bf16x8*)(lds + PG8_SB(b, h) + boff + n * 2048 + k * 1024); } \
;         else { _Pragma("unroll") for (int n = 0; n < 2; ++n) dst##8[n] = ld32(lds + PG8_SB(b, h) + boff + n * 2048); } } while (0)
; #define PG8_WAIT_V(n) asm volatile("s_waitcnt vmcnt(" #n ")" ::: "memory")
; #define PG8_WAIT_L(n) asm volatile("s_waitcnt lgkmcnt(" #n ")" ::: "memory")
; #define PG8_BAR __builtin_amdgcn_s_barrier()
; #define PG8_SCHED __builtin_amdgcn_sched_barrier(0)
;     ...
;             PG8_LDB(B0, 0, 0); PG8_LDB(B1, 0, 1); PG8_SCHED; PG8_LDA(At, 0, 0); PG8_STAGE(PG8_SA(1, 1), a1 + hstepA, voffA);
;             PG8_WAIT_V(8); PG8_WAIT_L(0); PG8_BAR; PG8_MMA(0, 0, At, B0); PG8_MMA(0, 1, At, B1); PG8_BAR; PG8_SCHED;
;             PG8_LDA(At, 0, 1); PG8_STAGE(PG8_SB(0, 0), b2, voffB); PG8_STAGE(PG8_SB(0, 1), b2 + hstepB, voffB); PG8_STAGE(PG8_SA(0, 0), a2, voffA);
;             PG8_WAIT_V(8); PG8_WAIT_L(0); PG8_BAR; PG8_MMA(1, 0, At, B0); PG8_MMA(1, 1, At, B1); PG8_BAR; PG8_SCHED;
;             PG8_LDB(B0, 1, 0); PG8_LDB(B1, 1, 1); PG8_SCHED; PG8_LDA(At, 1, 0); PG8_STAGE(PG8_SA(0, 1), a2 + hstepA, voffA);
;             PG8_WAIT_V(8); PG8_WAIT_L(0); PG8_BAR; PG8_MMA(0, 0, At, B0); PG8_MMA(0, 1, At, B1); PG8_BAR; PG8_SCHED;
;             PG8_LDA(At, 1, 1); PG8_STAGE(PG8_SB(1, 0), b3, voffB); PG8_STAGE(PG8_SB(1, 1), b3 + hstepB, voffB); PG8_STAGE(PG8_SA(1, 0), a3, voffA);
;             PG8_WAIT_V(8); PG8_WAIT_L(0); PG8_BAR; PG8_MMA(1, 0, At, B0); PG8_MMA(1, 1, At, B1); PG8_BAR; PG8_SCHED;
	v_add_u32_e32 v160, s51, v164
	ds_read_b128 v[122:125], v160
	ds_read_b128 v[126:129], v160 offset:1024
	ds_read_b128 v[130:133], v160 offset:2048
	ds_read_b128 v[170:173], v160 offset:3072
	v_add_u32_e32 v160, s52, v164
	ds_read_b128 v[174:177], v160
	ds_read_b128 v[178:181], v160 offset:1024
	ds_read_b128 v[182:185], v160 offset:2048
	ds_read_b128 v[186:189], v160 offset:3072
	s_add_u32 s28, s28, 0x40000
	s_addc_u32 s29, s29, 0
	s_mov_b32 m0, s48
	ds_read_b128 v[190:193], v167 offset:32768
	ds_read_b128 v[194:197], v167 offset:33792
	ds_read_b128 v[198:201], v167 offset:34816
	ds_read_b128 v[202:205], v167 offset:35840
	ds_read_b128 v[206:209], v167 offset:36864
	ds_read_b128 v[210:213], v167 offset:37888
	ds_read_b128 v[214:217], v167 offset:38912
	global_load_lds_dwordx4 v142, s[28:29]
	s_mov_b32 m0, s49
	ds_read_b128 v[218:221], v167 offset:39936
	global_load_lds_dwordx4 v146, s[28:29]
	s_waitcnt vmcnt(8) lgkmcnt(0)
	s_barrier
	s_setprio 1
	v_mfma_i32_16x16x64_i8 v[134:137], v[122:125], v[190:193], v[134:137]
	v_mfma_i32_16x16x64_i8 v[114:117], v[130:133], v[190:193], v[114:117]
	v_mfma_i32_16x16x64_i8 v[106:109], v[122:125], v[198:201], v[106:109]
	v_mfma_i32_16x16x64_i8 v[98:101], v[130:133], v[198:201], v[98:101]
	v_mfma_i32_16x16x64_i8 v[90:93], v[122:125], v[206:209], v[90:93]
	v_mfma_i32_16x16x64_i8 v[82:85], v[130:133], v[206:209], v[82:85]
	v_mfma_i32_16x16x64_i8 v[74:77], v[122:125], v[214:217], v[74:77]
	v_mfma_i32_16x16x64_i8 v[66:69], v[130:133], v[214:217], v[66:69]
	v_mfma_i32_16x16x64_i8 v[134:137], v[126:129], v[194:197], v[134:137]
	v_mfma_i32_16x16x64_i8 v[114:117], v[170:173], v[194:197], v[114:117]
	v_mfma_i32_16x16x64_i8 v[106:109], v[126:129], v[202:205], v[106:109]
	v_mfma_i32_16x16x64_i8 v[98:101], v[170:173], v[202:205], v[98:101]
	v_mfma_i32_16x16x64_i8 v[90:93], v[126:129], v[210:213], v[90:93]
	v_mfma_i32_16x16x64_i8 v[82:85], v[170:173], v[210:213], v[82:85]
	v_mfma_i32_16x16x64_i8 v[74:77], v[126:129], v[218:221], v[74:77]
	v_mfma_i32_16x16x64_i8 v[66:69], v[170:173], v[218:221], v[66:69]
	s_setprio 0
	s_setprio 1
	v_mfma_i32_16x16x64_i8 v[138:141], v[174:177], v[190:193], v[138:141]
	v_mfma_i32_16x16x64_i8 v[118:121], v[182:185], v[190:193], v[118:121]
	v_mfma_i32_16x16x64_i8 v[110:113], v[174:177], v[198:201], v[110:113]
	v_mfma_i32_16x16x64_i8 v[102:105], v[182:185], v[198:201], v[102:105]
	v_mfma_i32_16x16x64_i8 v[94:97], v[174:177], v[206:209], v[94:97]
	v_mfma_i32_16x16x64_i8 v[86:89], v[182:185], v[206:209], v[86:89]
	v_mfma_i32_16x16x64_i8 v[78:81], v[174:177], v[214:217], v[78:81]
	v_mfma_i32_16x16x64_i8 v[70:73], v[182:185], v[214:217], v[70:73]
	v_mfma_i32_16x16x64_i8 v[138:141], v[178:181], v[194:197], v[138:141]
	v_mfma_i32_16x16x64_i8 v[118:121], v[186:189], v[194:197], v[118:121]
	v_mfma_i32_16x16x64_i8 v[110:113], v[178:181], v[202:205], v[110:113]
	v_mfma_i32_16x16x64_i8 v[102:105], v[186:189], v[202:205], v[102:105]
	v_mfma_i32_16x16x64_i8 v[94:97], v[178:181], v[210:213], v[94:97]
	v_mfma_i32_16x16x64_i8 v[86:89], v[186:189], v[210:213], v[86:89]
	v_mfma_i32_16x16x64_i8 v[78:81], v[178:181], v[218:221], v[78:81]
	v_mfma_i32_16x16x64_i8 v[70:73], v[186:189], v[218:221], v[70:73]
	s_setprio 0
	s_barrier
	s_mov_b32 m0, s55
	s_add_u32 s26, s26, 0x40080
	ds_read_b128 v[190:193], v167 offset:49152
	ds_read_b128 v[194:197], v167 offset:50176
	ds_read_b128 v[198:201], v167 offset:51200
	ds_read_b128 v[202:205], v167 offset:52224
	global_load_lds_dwordx4 v144, s[98:99]
	s_mov_b32 m0, s56
	s_addc_u32 s27, s27, 0
	global_load_lds_dwordx4 v148, s[98:99]
	s_mov_b32 m0, s59
	ds_read_b128 v[218:221], v167 offset:56320
	global_load_lds_dwordx4 v144, s[26:27]
	s_mov_b32 m0, s60
	ds_read_b128 v[214:217], v167 offset:55296
	global_load_lds_dwordx4 v148, s[26:27]
	s_mov_b32 m0, s57
	ds_read_b128 v[210:213], v167 offset:54272
	global_load_lds_dwordx4 v142, s[100:101]
	s_mov_b32 m0, s58
	ds_read_b128 v[206:209], v167 offset:53248
	global_load_lds_dwordx4 v146, s[100:101]
	s_waitcnt vmcnt(8) lgkmcnt(0)
	s_barrier
	s_setprio 1
	v_mfma_i32_16x16x64_i8 v[58:61], v[122:125], v[190:193], v[58:61]
	v_mfma_i32_16x16x64_i8 v[50:53], v[130:133], v[190:193], v[50:53]
	v_mfma_i32_16x16x64_i8 v[42:45], v[122:125], v[198:201], v[42:45]
	v_mfma_i32_16x16x64_i8 v[34:37], v[130:133], v[198:201], v[34:37]
	v_mfma_i32_16x16x64_i8 v[26:29], v[122:125], v[206:209], v[26:29]
	v_mfma_i32_16x16x64_i8 v[18:21], v[130:133], v[206:209], v[18:21]
	v_mfma_i32_16x16x64_i8 v[10:13], v[122:125], v[214:217], v[10:13]
	v_mfma_i32_16x16x64_i8 v[2:5], v[130:133], v[214:217], v[2:5]
	v_mfma_i32_16x16x64_i8 v[58:61], v[126:129], v[194:197], v[58:61]
	v_mfma_i32_16x16x64_i8 v[50:53], v[170:173], v[194:197], v[50:53]
	v_mfma_i32_16x16x64_i8 v[42:45], v[126:129], v[202:205], v[42:45]
	v_mfma_i32_16x16x64_i8 v[34:37], v[170:173], v[202:205], v[34:37]
	v_mfma_i32_16x16x64_i8 v[26:29], v[126:129], v[210:213], v[26:29]
	v_mfma_i32_16x16x64_i8 v[18:21], v[170:173], v[210:213], v[18:21]
	v_mfma_i32_16x16x64_i8 v[10:13], v[126:129], v[218:221], v[10:13]
	v_mfma_i32_16x16x64_i8 v[2:5], v[170:173], v[218:221], v[2:5]
	s_setprio 0
	s_setprio 1
	v_mfma_i32_16x16x64_i8 v[62:65], v[174:177], v[190:193], v[62:65]
	v_mfma_i32_16x16x64_i8 v[54:57], v[182:185], v[190:193], v[54:57]
	v_mfma_i32_16x16x64_i8 v[46:49], v[174:177], v[198:201], v[46:49]
	v_mfma_i32_16x16x64_i8 v[38:41], v[182:185], v[198:201], v[38:41]
	v_mfma_i32_16x16x64_i8 v[30:33], v[174:177], v[206:209], v[30:33]
	v_mfma_i32_16x16x64_i8 v[22:25], v[182:185], v[206:209], v[22:25]
	v_mfma_i32_16x16x64_i8 v[14:17], v[174:177], v[214:217], v[14:17]
	v_mfma_i32_16x16x64_i8 v[6:9], v[182:185], v[214:217], v[6:9]
	v_mfma_i32_16x16x64_i8 v[62:65], v[178:181], v[194:197], v[62:65]
	v_mfma_i32_16x16x64_i8 v[54:57], v[186:189], v[194:197], v[54:57]
	v_mfma_i32_16x16x64_i8 v[46:49], v[178:181], v[202:205], v[46:49]
	v_mfma_i32_16x16x64_i8 v[38:41], v[186:189], v[202:205], v[38:41]
	v_mfma_i32_16x16x64_i8 v[30:33], v[178:181], v[210:213], v[30:33]
	v_mfma_i32_16x16x64_i8 v[22:25], v[186:189], v[210:213], v[22:25]
	v_mfma_i32_16x16x64_i8 v[14:17], v[178:181], v[218:221], v[14:17]
	v_mfma_i32_16x16x64_i8 v[6:9], v[186:189], v[218:221], v[6:9]
	s_setprio 0
	s_barrier
	s_add_u32 s67, s67, 0x100
	s_addc_u32 s68, s68, 0
	s_add_u32 s24, s24, 0x100
	s_addc_u32 s25, s25, 0
	s_cmp_ge_i32 s69, s54
	s_mov_b32 s26, s69
	s_cbranch_scc0 .LBB0_4141
	s_branch .LBB0_4142
; #define PG8_STAGE(bufoff, gbase, voff) do { _Pragma("unroll") for (int _i = 0; _i < 2; ++_i) \
;         __builtin_amdgcn_global_load_lds((const unsigned*)((const char*)(gbase) + (voff)[_i]), (PG8_LAS unsigned*)(lds + (bufoff) + ldsw + _i * 8192), 16, 0, 0); } while (0)
; #define PG8_LDA(dst, b, h) do { if constexpr (DT != 1) { _Pragma("unroll") for (int m = 0; m < 4; ++m) _Pragma("unroll") for (int k = 0; k < 2; ++k) dst[m][k] = *(const PG8_LAS bf16x8*)(lds + PG8_SA(b, h) + aoff + m * 2048 + k * 1024); } \
;         else { _Pragma("unroll") for (int m = 0; m < 4; ++m) dst##8[m] = ld32(lds + PG8_SA(b, h) + aoff + m * 2048); } } while (0)
; #define PG8_WAIT_V(n) asm volatile("s_waitcnt vmcnt(" #n ")" ::: "memory")
;     ...
;         const char* nA = has_next ? (const char*)g.A + (size_t)nxt.pm * tstepA : cA; const char* nB = has_next ? (const char*)g.Bt + (size_t)nxt.pn * tstepB : cB;
;         for (int t = 0; t < nt; t += 2) {
;             const bool last = (t == nt - 2);
;             const char* a1 = cA + (size_t)(t + 1) * kstep;
;             const char* a2 = last ? nA : cA + (size_t)(t + 2) * kstep; const char* b2 = last ? nB : cB + (size_t)(t + 2) * kstep;
;             const char* a3 = a2 + kstep; const char* b3 = b2 + kstep;
;             if (last && has_next) S.a_ready(nxt);
;             if constexpr (SP2) {
;             PG8_LDB(B0, 0, 0); PG8_LDB(B1, 0, 1); PG8_SCHED; PG8_LDA(At, 0, 0); PG8_STAGE(PG8_SA(1, 1), a1 + hstepA, voffA);
;             PG8_WAIT_V(8); PG8_WAIT_L(0); PG8_BAR; PG8_MMA(0, 0, At, B0); PG8_MMA(0, 1, At, B1); PG8_BAR; PG8_SCHED;
;             PG8_LDA(At, 0, 1); PG8_STAGE(PG8_SB(0, 0), b2, voffB); PG8_STAGE(PG8_SB(0, 1), b2 + hstepB, voffB); PG8_STAGE(PG8_SA(0, 0), a2, voffA);
;             PG8_WAIT_V(8); PG8_WAIT_L(0); PG8_BAR; PG8_MMA(1, 0, At, B0); PG8_MMA(1, 1, At, B1); PG8_BAR; PG8_SCHED;
;             PG8_LDB(B0, 1, 0); PG8_LDB(B1, 1, 1); PG8_SCHED; PG8_LDA(At, 1, 0); PG8_STAGE(PG8_SA(0, 1), a2 + hstepA, voffA);
;             PG8_WAIT_V(8); PG8_WAIT_L(0); PG8_BAR; PG8_MMA(0, 0, At, B0); PG8_MMA(0, 1, At, B1); PG8_BAR; PG8_SCHED;
;             PG8_LDA(At, 1, 1); PG8_STAGE(PG8_SB(1, 0), b3, voffB); PG8_STAGE(PG8_SB(1, 1), b3 + hstepB, voffB); PG8_STAGE(PG8_SA(1, 0), a3, voffA);
;             PG8_WAIT_V(8); PG8_WAIT_L(0); PG8_BAR; PG8_MMA(1, 0, At, B0); PG8_MMA(1, 1, At, B1); PG8_BAR; PG8_SCHED;
.LBB0_4141:
	v_add_u32_e32 v160, s35, v164
	ds_read_b128 v[122:125], v160
	ds_read_b128 v[126:129], v160 offset:1024
	ds_read_b128 v[130:133], v160 offset:2048
	ds_read_b128 v[170:173], v160 offset:3072
	v_add_u32_e32 v160, s36, v164
	ds_read_b128 v[174:177], v160
	ds_read_b128 v[178:181], v160 offset:1024
	ds_read_b128 v[182:185], v160 offset:2048
	ds_read_b128 v[186:189], v160 offset:3072
	s_add_i32 s69, s26, 2
	s_add_u32 s27, s24, 0xfffc0080
	s_addc_u32 s28, s25, -1
	s_cmp_eq_u32 s61, s26
	s_cselect_b32 s26, s66, s67
	s_cselect_b32 s29, s15, s28
	s_cselect_b32 s28, s17, s27
	s_cselect_b32 s27, s65, s68
	s_add_i32 m0, s46, 0xc000
	ds_read_b128 v[190:193], v167
	ds_read_b128 v[194:197], v167 offset:1024
	ds_read_b128 v[198:201], v167 offset:2048
	ds_read_b128 v[202:205], v167 offset:3072
	ds_read_b128 v[206:209], v167 offset:4096
	ds_read_b128 v[210:213], v167 offset:5120
	ds_read_b128 v[214:217], v167 offset:6144
	ds_read_b128 v[218:221], v167 offset:7168
	global_load_lds_dwordx4 v154, s[24:25]
	s_add_i32 m0, s46, 0xe000
	s_nop 0
	global_load_lds_dwordx4 v152, s[24:25]
	s_waitcnt vmcnt(8) lgkmcnt(0)
	s_barrier
	s_setprio 1
	v_mfma_i32_16x16x64_i8 v[134:137], v[122:125], v[190:193], v[134:137]
	v_mfma_i32_16x16x64_i8 v[114:117], v[130:133], v[190:193], v[114:117]
	v_mfma_i32_16x16x64_i8 v[106:109], v[122:125], v[198:201], v[106:109]
	v_mfma_i32_16x16x64_i8 v[98:101], v[130:133], v[198:201], v[98:101]
	v_mfma_i32_16x16x64_i8 v[90:93], v[122:125], v[206:209], v[90:93]
	v_mfma_i32_16x16x64_i8 v[82:85], v[130:133], v[206:209], v[82:85]
	v_mfma_i32_16x16x64_i8 v[74:77], v[122:125], v[214:217], v[74:77]
	v_mfma_i32_16x16x64_i8 v[66:69], v[130:133], v[214:217], v[66:69]
	v_mfma_i32_16x16x64_i8 v[134:137], v[126:129], v[194:197], v[134:137]
	v_mfma_i32_16x16x64_i8 v[114:117], v[170:173], v[194:197], v[114:117]
	v_mfma_i32_16x16x64_i8 v[106:109], v[126:129], v[202:205], v[106:109]
	v_mfma_i32_16x16x64_i8 v[98:101], v[170:173], v[202:205], v[98:101]
	v_mfma_i32_16x16x64_i8 v[90:93], v[126:129], v[210:213], v[90:93]
	v_mfma_i32_16x16x64_i8 v[82:85], v[170:173], v[210:213], v[82:85]
	v_mfma_i32_16x16x64_i8 v[74:77], v[126:129], v[218:221], v[74:77]
	v_mfma_i32_16x16x64_i8 v[66:69], v[170:173], v[218:221], v[66:69]
	s_setprio 0
	s_setprio 1
	v_mfma_i32_16x16x64_i8 v[138:141], v[174:177], v[190:193], v[138:141]
	v_mfma_i32_16x16x64_i8 v[118:121], v[182:185], v[190:193], v[118:121]
	v_mfma_i32_16x16x64_i8 v[110:113], v[174:177], v[198:201], v[110:113]
	v_mfma_i32_16x16x64_i8 v[102:105], v[182:185], v[198:201], v[102:105]
	v_mfma_i32_16x16x64_i8 v[94:97], v[174:177], v[206:209], v[94:97]
	v_mfma_i32_16x16x64_i8 v[86:89], v[182:185], v[206:209], v[86:89]
	v_mfma_i32_16x16x64_i8 v[78:81], v[174:177], v[214:217], v[78:81]
	v_mfma_i32_16x16x64_i8 v[70:73], v[182:185], v[214:217], v[70:73]
	v_mfma_i32_16x16x64_i8 v[138:141], v[178:181], v[194:197], v[138:141]
	v_mfma_i32_16x16x64_i8 v[118:121], v[186:189], v[194:197], v[118:121]
	v_mfma_i32_16x16x64_i8 v[110:113], v[178:181], v[202:205], v[110:113]
	v_mfma_i32_16x16x64_i8 v[102:105], v[186:189], v[202:205], v[102:105]
	v_mfma_i32_16x16x64_i8 v[94:97], v[178:181], v[210:213], v[94:97]
	v_mfma_i32_16x16x64_i8 v[86:89], v[186:189], v[210:213], v[86:89]
	v_mfma_i32_16x16x64_i8 v[78:81], v[178:181], v[218:221], v[78:81]
	v_mfma_i32_16x16x64_i8 v[70:73], v[186:189], v[218:221], v[70:73]
	s_setprio 0
	s_barrier
	s_mov_b32 m0, s23
	s_add_u32 s98, s26, 0x80
	s_addc_u32 s99, s27, 0
	s_add_u32 s70, s26, 0x40000
	ds_read_b128 v[190:193], v167 offset:16384
	ds_read_b128 v[194:197], v167 offset:17408
	ds_read_b128 v[198:201], v167 offset:18432
	ds_read_b128 v[202:205], v167 offset:19456
	global_load_lds_dwordx4 v144, s[26:27]
	s_mov_b32 m0, s43
	s_addc_u32 s71, s27, 0
	global_load_lds_dwordx4 v148, s[26:27]
	s_mov_b32 m0, s44
	ds_read_b128 v[218:221], v167 offset:23552
	global_load_lds_dwordx4 v144, s[70:71]
	s_mov_b32 m0, s45
	ds_read_b128 v[214:217], v167 offset:22528
	global_load_lds_dwordx4 v148, s[70:71]
	s_add_u32 s100, s28, 0x80
	s_addc_u32 s101, s29, 0
	s_mov_b32 m0, s46
	ds_read_b128 v[210:213], v167 offset:21504
	global_load_lds_dwordx4 v142, s[28:29]
	s_mov_b32 m0, s47
	ds_read_b128 v[206:209], v167 offset:20480
	global_load_lds_dwordx4 v146, s[28:29]
	s_waitcnt vmcnt(8) lgkmcnt(0)
	s_barrier
	s_setprio 1
	v_mfma_i32_16x16x64_i8 v[58:61], v[122:125], v[190:193], v[58:61]
	v_mfma_i32_16x16x64_i8 v[50:53], v[130:133], v[190:193], v[50:53]
	v_mfma_i32_16x16x64_i8 v[42:45], v[122:125], v[198:201], v[42:45]
	v_mfma_i32_16x16x64_i8 v[34:37], v[130:133], v[198:201], v[34:37]
	v_mfma_i32_16x16x64_i8 v[26:29], v[122:125], v[206:209], v[26:29]
	v_mfma_i32_16x16x64_i8 v[18:21], v[130:133], v[206:209], v[18:21]
	v_mfma_i32_16x16x64_i8 v[10:13], v[122:125], v[214:217], v[10:13]
	v_mfma_i32_16x16x64_i8 v[2:5], v[130:133], v[214:217], v[2:5]
	v_mfma_i32_16x16x64_i8 v[58:61], v[126:129], v[194:197], v[58:61]
	v_mfma_i32_16x16x64_i8 v[50:53], v[170:173], v[194:197], v[50:53]
	v_mfma_i32_16x16x64_i8 v[42:45], v[126:129], v[202:205], v[42:45]
	v_mfma_i32_16x16x64_i8 v[34:37], v[170:173], v[202:205], v[34:37]
	v_mfma_i32_16x16x64_i8 v[26:29], v[126:129], v[210:213], v[26:29]
	v_mfma_i32_16x16x64_i8 v[18:21], v[170:173], v[210:213], v[18:21]
	v_mfma_i32_16x16x64_i8 v[10:13], v[126:129], v[218:221], v[10:13]
	v_mfma_i32_16x16x64_i8 v[2:5], v[170:173], v[218:221], v[2:5]
	s_setprio 0
	s_setprio 1
	v_mfma_i32_16x16x64_i8 v[62:65], v[174:177], v[190:193], v[62:65]
	v_mfma_i32_16x16x64_i8 v[54:57], v[182:185], v[190:193], v[54:57]
	v_mfma_i32_16x16x64_i8 v[46:49], v[174:177], v[198:201], v[46:49]
	v_mfma_i32_16x16x64_i8 v[38:41], v[182:185], v[198:201], v[38:41]
	v_mfma_i32_16x16x64_i8 v[30:33], v[174:177], v[206:209], v[30:33]
	v_mfma_i32_16x16x64_i8 v[22:25], v[182:185], v[206:209], v[22:25]
	v_mfma_i32_16x16x64_i8 v[14:17], v[174:177], v[214:217], v[14:17]
	v_mfma_i32_16x16x64_i8 v[6:9], v[182:185], v[214:217], v[6:9]
	v_mfma_i32_16x16x64_i8 v[62:65], v[178:181], v[194:197], v[62:65]
	v_mfma_i32_16x16x64_i8 v[54:57], v[186:189], v[194:197], v[54:57]
	v_mfma_i32_16x16x64_i8 v[46:49], v[178:181], v[202:205], v[46:49]
	v_mfma_i32_16x16x64_i8 v[38:41], v[186:189], v[202:205], v[38:41]
	v_mfma_i32_16x16x64_i8 v[30:33], v[178:181], v[210:213], v[30:33]
	v_mfma_i32_16x16x64_i8 v[22:25], v[186:189], v[210:213], v[22:25]
	v_mfma_i32_16x16x64_i8 v[14:17], v[178:181], v[218:221], v[14:17]
	v_mfma_i32_16x16x64_i8 v[6:9], v[186:189], v[218:221], v[6:9]
	s_setprio 0
	s_barrier
; #define PG8_STAGE(bufoff, gbase, voff) do { _Pragma("unroll") for (int _i = 0; _i < 2; ++_i) \
;         __builtin_amdgcn_global_load_lds((const unsigned*)((const char*)(gbase) + (voff)[_i]), (PG8_LAS unsigned*)(lds + (bufoff) + ldsw + _i * 8192), 16, 0, 0); } while (0)
; #define PG8_LDA(dst, b, h) do { if constexpr (DT != 1) { _Pragma("unroll") for (int m = 0; m < 4; ++m) _Pragma("unroll") for (int k = 0; k < 2; ++k) dst[m][k] = *(const PG8_LAS bf16x8*)(lds + PG8_SA(b, h) + aoff + m * 2048 + k * 1024); } \
;         else { _Pragma("unroll") for (int m = 0; m < 4; ++m) dst##8[m] = ld32(lds + PG8_SA(b, h) + aoff + m * 2048); } } while (0)
; #define PG8_LDB(dst, b, h) do { if constexpr (DT != 1) { _Pragma("unroll") for (int n = 0; n < 2; ++n) _Pragma("unroll") for (int k = 0; k < 2; ++k) dst[n][k] = *(const PG8_LAS bf16x8*)(lds + PG8_SB(b, h) + boff + n * 2048 + k * 1024); } \
;         else { _Pragma("unroll") for (int n = 0; n < 2; ++n) dst##8[n] = ld32(lds + PG8_SB(b, h) + boff + n * 2048); } } while (0)
; #define PG8_WAIT_V(n) asm volatile("s_waitcnt vmcnt(" #n ")" ::: "memory")
; #define PG8_WAIT_L(n) asm volatile("s_waitcnt lgkmcnt(" #n ")" ::: "memory")
; #define PG8_BAR __builtin_amdgcn_s_barrier()
; #define PG8_SCHED __builtin_amdgcn_sched_barrier(0)
;     ...
;             PG8_LDB(B0, 0, 0); PG8_LDB(B1, 0, 1); PG8_SCHED; PG8_LDA(At, 0, 0); PG8_STAGE(PG8_SA(1, 1), a1 + hstepA, voffA);
;             PG8_WAIT_V(8); PG8_WAIT_L(0); PG8_BAR; PG8_MMA(0, 0, At, B0); PG8_MMA(0, 1, At, B1); PG8_BAR; PG8_SCHED;
;             PG8_LDA(At, 0, 1); PG8_STAGE(PG8_SB(0, 0), b2, voffB); PG8_STAGE(PG8_SB(0, 1), b2 + hstepB, voffB); PG8_STAGE(PG8_SA(0, 0), a2, voffA);
;             PG8_WAIT_V(8); PG8_WAIT_L(0); PG8_BAR; PG8_MMA(1, 0, At, B0); PG8_MMA(1, 1, At, B1); PG8_BAR; PG8_SCHED;
;             PG8_LDB(B0, 1, 0); PG8_LDB(B1, 1, 1); PG8_SCHED; PG8_LDA(At, 1, 0); PG8_STAGE(PG8_SA(0, 1), a2 + hstepA, voffA);
;             PG8_WAIT_V(8); PG8_WAIT_L(0); PG8_BAR; PG8_MMA(0, 0, At, B0); PG8_MMA(0, 1, At, B1); PG8_BAR; PG8_SCHED;
;             PG8_LDA(At, 1, 1); PG8_STAGE(PG8_SB(1, 0), b3, voffB); PG8_STAGE(PG8_SB(1, 1), b3 + hstepB, voffB); PG8_STAGE(PG8_SA(1, 0), a3, voffA);
;             PG8_WAIT_V(8); PG8_WAIT_L(0); PG8_BAR; PG8_MMA(1, 0, At, B0); PG8_MMA(1, 1, At, B1); PG8_BAR; PG8_SCHED;
	v_add_u32_e32 v160, s51, v164
	ds_read_b128 v[122:125], v160
	ds_read_b128 v[126:129], v160 offset:1024
	ds_read_b128 v[130:133], v160 offset:2048
	ds_read_b128 v[170:173], v160 offset:3072
	v_add_u32_e32 v160, s52, v164
	ds_read_b128 v[174:177], v160
	ds_read_b128 v[178:181], v160 offset:1024
	ds_read_b128 v[182:185], v160 offset:2048
	ds_read_b128 v[186:189], v160 offset:3072
	s_add_u32 s28, s28, 0x40000
	s_addc_u32 s29, s29, 0
	s_mov_b32 m0, s48
	ds_read_b128 v[190:193], v167 offset:32768
	ds_read_b128 v[194:197], v167 offset:33792
	ds_read_b128 v[198:201], v167 offset:34816
	ds_read_b128 v[202:205], v167 offset:35840
	ds_read_b128 v[206:209], v167 offset:36864
	ds_read_b128 v[210:213], v167 offset:37888
	ds_read_b128 v[214:217], v167 offset:38912
	global_load_lds_dwordx4 v142, s[28:29]
	s_mov_b32 m0, s49
	ds_read_b128 v[218:221], v167 offset:39936
	global_load_lds_dwordx4 v146, s[28:29]
	s_waitcnt vmcnt(8) lgkmcnt(0)
	s_barrier
	s_setprio 1
	v_mfma_i32_16x16x64_i8 v[134:137], v[122:125], v[190:193], v[134:137]
	v_mfma_i32_16x16x64_i8 v[114:117], v[130:133], v[190:193], v[114:117]
	v_mfma_i32_16x16x64_i8 v[106:109], v[122:125], v[198:201], v[106:109]
	v_mfma_i32_16x16x64_i8 v[98:101], v[130:133], v[198:201], v[98:101]
	v_mfma_i32_16x16x64_i8 v[90:93], v[122:125], v[206:209], v[90:93]
	v_mfma_i32_16x16x64_i8 v[82:85], v[130:133], v[206:209], v[82:85]
	v_mfma_i32_16x16x64_i8 v[74:77], v[122:125], v[214:217], v[74:77]
	v_mfma_i32_16x16x64_i8 v[66:69], v[130:133], v[214:217], v[66:69]
	v_mfma_i32_16x16x64_i8 v[134:137], v[126:129], v[194:197], v[134:137]
	v_mfma_i32_16x16x64_i8 v[114:117], v[170:173], v[194:197], v[114:117]
	v_mfma_i32_16x16x64_i8 v[106:109], v[126:129], v[202:205], v[106:109]
	v_mfma_i32_16x16x64_i8 v[98:101], v[170:173], v[202:205], v[98:101]
	v_mfma_i32_16x16x64_i8 v[90:93], v[126:129], v[210:213], v[90:93]
	v_mfma_i32_16x16x64_i8 v[82:85], v[170:173], v[210:213], v[82:85]
	v_mfma_i32_16x16x64_i8 v[74:77], v[126:129], v[218:221], v[74:77]
	v_mfma_i32_16x16x64_i8 v[66:69], v[170:173], v[218:221], v[66:69]
	s_setprio 0
	s_setprio 1
	v_mfma_i32_16x16x64_i8 v[138:141], v[174:177], v[190:193], v[138:141]
	v_mfma_i32_16x16x64_i8 v[118:121], v[182:185], v[190:193], v[118:121]
	v_mfma_i32_16x16x64_i8 v[110:113], v[174:177], v[198:201], v[110:113]
	v_mfma_i32_16x16x64_i8 v[102:105], v[182:185], v[198:201], v[102:105]
	v_mfma_i32_16x16x64_i8 v[94:97], v[174:177], v[206:209], v[94:97]
	v_mfma_i32_16x16x64_i8 v[86:89], v[182:185], v[206:209], v[86:89]
	v_mfma_i32_16x16x64_i8 v[78:81], v[174:177], v[214:217], v[78:81]
	v_mfma_i32_16x16x64_i8 v[70:73], v[182:185], v[214:217], v[70:73]
	v_mfma_i32_16x16x64_i8 v[138:141], v[178:181], v[194:197], v[138:141]
	v_mfma_i32_16x16x64_i8 v[118:121], v[186:189], v[194:197], v[118:121]
	v_mfma_i32_16x16x64_i8 v[110:113], v[178:181], v[202:205], v[110:113]
	v_mfma_i32_16x16x64_i8 v[102:105], v[186:189], v[202:205], v[102:105]
	v_mfma_i32_16x16x64_i8 v[94:97], v[178:181], v[210:213], v[94:97]
	v_mfma_i32_16x16x64_i8 v[86:89], v[186:189], v[210:213], v[86:89]
	v_mfma_i32_16x16x64_i8 v[78:81], v[178:181], v[218:221], v[78:81]
	v_mfma_i32_16x16x64_i8 v[70:73], v[186:189], v[218:221], v[70:73]
	s_setprio 0
	s_barrier
	s_mov_b32 m0, s55
	s_add_u32 s26, s26, 0x40080
	ds_read_b128 v[190:193], v167 offset:49152
	ds_read_b128 v[194:197], v167 offset:50176
	ds_read_b128 v[198:201], v167 offset:51200
	ds_read_b128 v[202:205], v167 offset:52224
	global_load_lds_dwordx4 v144, s[98:99]
	s_mov_b32 m0, s56
	s_addc_u32 s27, s27, 0
	global_load_lds_dwordx4 v148, s[98:99]
	s_mov_b32 m0, s59
	ds_read_b128 v[218:221], v167 offset:56320
	global_load_lds_dwordx4 v144, s[26:27]
	s_mov_b32 m0, s60
	ds_read_b128 v[214:217], v167 offset:55296
	global_load_lds_dwordx4 v148, s[26:27]
	s_mov_b32 m0, s57
	ds_read_b128 v[210:213], v167 offset:54272
	global_load_lds_dwordx4 v142, s[100:101]
	s_mov_b32 m0, s58
	ds_read_b128 v[206:209], v167 offset:53248
	global_load_lds_dwordx4 v146, s[100:101]
	s_waitcnt vmcnt(8) lgkmcnt(0)
	s_barrier
	s_setprio 1
	v_mfma_i32_16x16x64_i8 v[58:61], v[122:125], v[190:193], v[58:61]
	v_mfma_i32_16x16x64_i8 v[50:53], v[130:133], v[190:193], v[50:53]
	v_mfma_i32_16x16x64_i8 v[42:45], v[122:125], v[198:201], v[42:45]
	v_mfma_i32_16x16x64_i8 v[34:37], v[130:133], v[198:201], v[34:37]
	v_mfma_i32_16x16x64_i8 v[26:29], v[122:125], v[206:209], v[26:29]
	v_mfma_i32_16x16x64_i8 v[18:21], v[130:133], v[206:209], v[18:21]
	v_mfma_i32_16x16x64_i8 v[10:13], v[122:125], v[214:217], v[10:13]
	v_mfma_i32_16x16x64_i8 v[2:5], v[130:133], v[214:217], v[2:5]
	v_mfma_i32_16x16x64_i8 v[58:61], v[126:129], v[194:197], v[58:61]
	v_mfma_i32_16x16x64_i8 v[50:53], v[170:173], v[194:197], v[50:53]
	v_mfma_i32_16x16x64_i8 v[42:45], v[126:129], v[202:205], v[42:45]
	v_mfma_i32_16x16x64_i8 v[34:37], v[170:173], v[202:205], v[34:37]
	v_mfma_i32_16x16x64_i8 v[26:29], v[126:129], v[210:213], v[26:29]
	v_mfma_i32_16x16x64_i8 v[18:21], v[170:173], v[210:213], v[18:21]
	v_mfma_i32_16x16x64_i8 v[10:13], v[126:129], v[218:221], v[10:13]
	v_mfma_i32_16x16x64_i8 v[2:5], v[170:173], v[218:221], v[2:5]
	s_setprio 0
	s_setprio 1
	v_mfma_i32_16x16x64_i8 v[62:65], v[174:177], v[190:193], v[62:65]
	v_mfma_i32_16x16x64_i8 v[54:57], v[182:185], v[190:193], v[54:57]
	v_mfma_i32_16x16x64_i8 v[46:49], v[174:177], v[198:201], v[46:49]
	v_mfma_i32_16x16x64_i8 v[38:41], v[182:185], v[198:201], v[38:41]
	v_mfma_i32_16x16x64_i8 v[30:33], v[174:177], v[206:209], v[30:33]
	v_mfma_i32_16x16x64_i8 v[22:25], v[182:185], v[206:209], v[22:25]
	v_mfma_i32_16x16x64_i8 v[14:17], v[174:177], v[214:217], v[14:17]
	v_mfma_i32_16x16x64_i8 v[6:9], v[182:185], v[214:217], v[6:9]
	v_mfma_i32_16x16x64_i8 v[62:65], v[178:181], v[194:197], v[62:65]
	v_mfma_i32_16x16x64_i8 v[54:57], v[186:189], v[194:197], v[54:57]
	v_mfma_i32_16x16x64_i8 v[46:49], v[178:181], v[202:205], v[46:49]
	v_mfma_i32_16x16x64_i8 v[38:41], v[186:189], v[202:205], v[38:41]
	v_mfma_i32_16x16x64_i8 v[30:33], v[178:181], v[210:213], v[30:33]
	v_mfma_i32_16x16x64_i8 v[22:25], v[186:189], v[210:213], v[22:25]
	v_mfma_i32_16x16x64_i8 v[14:17], v[178:181], v[218:221], v[14:17]
	v_mfma_i32_16x16x64_i8 v[6:9], v[186:189], v[218:221], v[6:9]
	s_setprio 0
	s_barrier
	s_add_u32 s67, s67, 0x100
	s_addc_u32 s68, s68, 0
	s_add_u32 s24, s24, 0x100
	s_addc_u32 s25, s25, 0
	s_cmp_ge_i32 s69, s54
	s_mov_b32 s26, s69
	s_cbranch_scc0 .LBB0_4141

; #define PG8_STAGE(bufoff, gbase, voff) do { _Pragma("unroll") for (int _i = 0; _i < 2; ++_i) \
;         __builtin_amdgcn_global_load_lds((const unsigned*)((const char*)(gbase) + (voff)[_i]), (PG8_LAS unsigned*)(lds + (bufoff) + ldsw + _i * 8192), 16, 0, 0); } while (0)
; #define PG8_LDA(dst, b, h) do { if constexpr (DT != 1) { _Pragma("unroll") for (int m = 0; m < 4; ++m) _Pragma("unroll") for (int k = 0; k < 2; ++k) dst[m][k] = *(const PG8_LAS bf16x8*)(lds + PG8_SA(b, h) + aoff + m * 2048 + k * 1024); } \
;         else { _Pragma("unroll") for (int m = 0; m < 4; ++m) dst##8[m] = ld32(lds + PG8_SA(b, h) + aoff + m * 2048); } } while (0)
; #define PG8_LDB(dst, b, h) do { if constexpr (DT != 1) { _Pragma("unroll") for (int n = 0; n < 2; ++n) _Pragma("unroll") for (int k = 0; k < 2; ++k) dst[n][k] = *(const PG8_LAS bf16x8*)(lds + PG8_SB(b, h) + boff + n * 2048 + k * 1024); } \
;         else { _Pragma("unroll") for (int n = 0; n < 2; ++n) dst##8[n] = ld32(lds + PG8_SB(b, h) + boff + n * 2048); } } while (0)
; #define PG8_WAIT_V(n) asm volatile("s_waitcnt vmcnt(" #n ")" ::: "memory")
; #define PG8_WAIT_L(n) asm volatile("s_waitcnt lgkmcnt(" #n ")" ::: "memory")
; #define PG8_BAR __builtin_amdgcn_s_barrier()
; #define PG8_SCHED __builtin_amdgcn_sched_barrier(0)
;     ...
;             PG8_LDB(B0, 0, 0); PG8_LDB(B1, 0, 1); PG8_SCHED; PG8_LDA(At, 0, 0); PG8_STAGE(PG8_SA(1, 1), a1 + hstepA, voffA);
;             PG8_WAIT_V(8); PG8_WAIT_L(0); PG8_BAR; PG8_MMA(0, 0, At, B0); PG8_MMA(0, 1, At, B1); PG8_BAR; PG8_SCHED;
;             PG8_LDA(At, 0, 1); PG8_STAGE(PG8_SB(0, 0), b2, voffB); PG8_STAGE(PG8_SB(0, 1), b2 + hstepB, voffB); PG8_STAGE(PG8_SA(0, 0), a2, voffA);
;             PG8_WAIT_V(8); PG8_WAIT_L(0); PG8_BAR; PG8_MMA(1, 0, At, B0); PG8_MMA(1, 1, At, B1); PG8_BAR; PG8_SCHED;
.Lzs_14:
	s_cbranch_vccnz .LBB0_4218
	s_add_u32 s66, s30, 0x100
	s_addc_u32 s67, s31, 0
	s_mov_b32 s34, 0
	ds_read_b128 v[18:21], v187
	ds_read_b128 v[22:25], v187 offset:16
	ds_read_b128 v[26:29], v187 offset:2048
	ds_read_b128 v[30:33], v187 offset:2064
	ds_read_b128 v[2:5], v188
	ds_read_b128 v[6:9], v188 offset:16
	ds_read_b128 v[10:13], v188 offset:2048
	ds_read_b128 v[14:17], v188 offset:2064
	s_add_i32 s68, s34, 2
	s_add_u32 s30, s28, 0x100
	s_addc_u32 s31, s29, 0
	s_cmp_eq_u32 s59, s34
	s_cselect_b32 s34, s26, s66
	s_cselect_b32 s37, s3, s31
	s_cselect_b32 s36, s2, s30
	s_cselect_b32 s35, s27, s67
	v_lshl_add_u64 v[218:219], s[28:29], 0, v[172:173]
	s_add_i32 m0, s47, 0xc000
	ds_read_b128 v[178:181], v189
	ds_read_b128 v[182:185], v189 offset:16
	ds_read_b128 v[194:197], v189 offset:2048
	ds_read_b128 v[198:201], v189 offset:2064
	ds_read_b128 v[202:205], v189 offset:4096
	ds_read_b128 v[206:209], v189 offset:4112
	ds_read_b128 v[210:213], v189 offset:6144
	ds_read_b128 v[214:217], v189 offset:6160
	global_load_lds_dwordx4 v[218:219], off
	v_lshl_add_u64 v[218:219], s[28:29], 0, v[170:171]
	s_add_i32 m0, s47, 0xe000
	s_nop 0
	global_load_lds_dwordx4 v[218:219], off
	s_waitcnt vmcnt(8) lgkmcnt(0)
	s_barrier
	s_setprio 1
	v_mfma_scale_f32_16x16x128_f8f6f4 v[158:161], v[18:25], v[178:185], 0, v190, v190 op_sel_hi:[0,0,0]
	v_mfma_scale_f32_16x16x128_f8f6f4 v[154:157], v[26:33], v[178:185], 0, v190, v190 op_sel_hi:[0,0,0]
	v_mfma_scale_f32_16x16x128_f8f6f4 v[150:153], v[18:25], v[194:201], 0, v190, v190 op_sel_hi:[0,0,0]
	v_mfma_scale_f32_16x16x128_f8f6f4 v[146:149], v[26:33], v[194:201], 0, v190, v190 op_sel_hi:[0,0,0]
	v_mfma_scale_f32_16x16x128_f8f6f4 v[126:129], v[18:25], v[202:209], 0, v190, v190 op_sel_hi:[0,0,0]
	v_mfma_scale_f32_16x16x128_f8f6f4 v[122:125], v[26:33], v[202:209], 0, v190, v190 op_sel_hi:[0,0,0]
	v_mfma_scale_f32_16x16x128_f8f6f4 v[118:121], v[18:25], v[210:217], 0, v190, v190 op_sel_hi:[0,0,0]
	v_mfma_scale_f32_16x16x128_f8f6f4 v[110:113], v[26:33], v[210:217], 0, v190, v190 op_sel_hi:[0,0,0]
	s_setprio 0
	s_setprio 1
	v_mfma_scale_f32_16x16x128_f8f6f4 v[142:145], v[2:9], v[178:185], 0, v190, v190 op_sel_hi:[0,0,0]
	v_mfma_scale_f32_16x16x128_f8f6f4 v[138:141], v[10:17], v[178:185], 0, v190, v190 op_sel_hi:[0,0,0]
	v_mfma_scale_f32_16x16x128_f8f6f4 v[134:137], v[2:9], v[194:201], 0, v190, v190 op_sel_hi:[0,0,0]
	v_mfma_scale_f32_16x16x128_f8f6f4 v[130:133], v[10:17], v[194:201], 0, v190, v190 op_sel_hi:[0,0,0]
	v_mfma_scale_f32_16x16x128_f8f6f4 v[114:117], v[2:9], v[202:209], 0, v190, v190 op_sel_hi:[0,0,0]
	v_mfma_scale_f32_16x16x128_f8f6f4 v[106:109], v[10:17], v[202:209], 0, v190, v190 op_sel_hi:[0,0,0]
	v_mfma_scale_f32_16x16x128_f8f6f4 v[102:105], v[2:9], v[210:217], 0, v190, v190 op_sel_hi:[0,0,0]
	v_mfma_scale_f32_16x16x128_f8f6f4 v[98:101], v[10:17], v[210:217], 0, v190, v190 op_sel_hi:[0,0,0]
	s_setprio 0
	s_barrier
	s_mov_b32 m0, s43
	s_add_u32 s98, s34, 0x80
	s_addc_u32 s99, s35, 0
	s_add_u32 s28, s34, 0xb0000
	ds_read_b128 v[194:197], v189 offset:16384
	ds_read_b128 v[198:201], v189 offset:16400
	ds_read_b128 v[202:205], v189 offset:18432
	ds_read_b128 v[206:209], v189 offset:18448
	global_load_lds_dwordx4 v164, s[34:35]
	s_mov_b32 m0, s44
	s_addc_u32 s29, s35, 0
	global_load_lds_dwordx4 v168, s[34:35]
	s_mov_b32 m0, s45
	ds_read_b128 v[222:225], v189 offset:22544
	global_load_lds_dwordx4 v164, s[28:29]
	s_mov_b32 m0, s46
	ds_read_b128 v[218:221], v189 offset:22528
	global_load_lds_dwordx4 v168, s[28:29]
	s_add_u32 s100, s36, 0x80
	s_addc_u32 s101, s37, 0
	s_mov_b32 m0, s47
	ds_read_b128 v[214:217], v189 offset:20496
	global_load_lds_dwordx4 v162, s[36:37]
	s_mov_b32 m0, s48
	ds_read_b128 v[210:213], v189 offset:20480
	global_load_lds_dwordx4 v166, s[36:37]
	s_waitcnt vmcnt(8) lgkmcnt(0)
	s_barrier
	s_setprio 1
	v_mfma_scale_f32_16x16x128_f8f6f4 v[94:97], v[18:25], v[194:201], 0, v190, v190 op_sel_hi:[0,0,0]
	v_mfma_scale_f32_16x16x128_f8f6f4 v[90:93], v[26:33], v[194:201], 0, v190, v190 op_sel_hi:[0,0,0]
	v_mfma_scale_f32_16x16x128_f8f6f4 v[78:81], v[18:25], v[202:209], 0, v190, v190 op_sel_hi:[0,0,0]
	v_mfma_scale_f32_16x16x128_f8f6f4 v[74:77], v[26:33], v[202:209], 0, v190, v190 op_sel_hi:[0,0,0]
	v_mfma_scale_f32_16x16x128_f8f6f4 v[226:229], v[18:25], v[210:217], 0, v190, v190 op_sel_hi:[0,0,0]
	v_mfma_scale_f32_16x16x128_f8f6f4 v[230:233], v[26:33], v[210:217], 0, v190, v190 op_sel_hi:[0,0,0]
	v_mfma_scale_f32_16x16x128_f8f6f4 v[234:237], v[18:25], v[218:225], 0, v190, v190 op_sel_hi:[0,0,0]
	v_mfma_scale_f32_16x16x128_f8f6f4 v[238:241], v[26:33], v[218:225], 0, v190, v190 op_sel_hi:[0,0,0]
	s_setprio 0
	s_setprio 1
	v_mfma_scale_f32_16x16x128_f8f6f4 v[86:89], v[2:9], v[194:201], 0, v190, v190 op_sel_hi:[0,0,0]
	v_mfma_scale_f32_16x16x128_f8f6f4 v[82:85], v[10:17], v[194:201], 0, v190, v190 op_sel_hi:[0,0,0]
	v_mfma_scale_f32_16x16x128_f8f6f4 v[70:73], v[2:9], v[202:209], 0, v190, v190 op_sel_hi:[0,0,0]
	v_mfma_scale_f32_16x16x128_f8f6f4 v[66:69], v[10:17], v[202:209], 0, v190, v190 op_sel_hi:[0,0,0]
	v_mfma_scale_f32_16x16x128_f8f6f4 v[242:245], v[2:9], v[210:217], 0, v190, v190 op_sel_hi:[0,0,0]
	v_mfma_scale_f32_16x16x128_f8f6f4 v[210:213], v[10:17], v[210:217], 0, v190, v190 op_sel_hi:[0,0,0]
	v_mfma_scale_f32_16x16x128_f8f6f4 v[214:217], v[2:9], v[218:225], 0, v190, v190 op_sel_hi:[0,0,0]
	v_mfma_scale_f32_16x16x128_f8f6f4 v[218:221], v[10:17], v[218:225], 0, v190, v190 op_sel_hi:[0,0,0]
	s_setprio 0
	s_barrier
; #define PG8_STAGE(bufoff, gbase, voff) do { _Pragma("unroll") for (int _i = 0; _i < 2; ++_i) \
;         __builtin_amdgcn_global_load_lds((const unsigned*)((const char*)(gbase) + (voff)[_i]), (PG8_LAS unsigned*)(lds + (bufoff) + ldsw + _i * 8192), 16, 0, 0); } while (0)
; #define PG8_LDA(dst, b, h) do { if constexpr (DT != 1) { _Pragma("unroll") for (int m = 0; m < 4; ++m) _Pragma("unroll") for (int k = 0; k < 2; ++k) dst[m][k] = *(const PG8_LAS bf16x8*)(lds + PG8_SA(b, h) + aoff + m * 2048 + k * 1024); } \
;         else { _Pragma("unroll") for (int m = 0; m < 4; ++m) dst##8[m] = ld32(lds + PG8_SA(b, h) + aoff + m * 2048); } } while (0)
; #define PG8_LDB(dst, b, h) do { if constexpr (DT != 1) { _Pragma("unroll") for (int n = 0; n < 2; ++n) _Pragma("unroll") for (int k = 0; k < 2; ++k) dst[n][k] = *(const PG8_LAS bf16x8*)(lds + PG8_SB(b, h) + boff + n * 2048 + k * 1024); } \
;         else { _Pragma("unroll") for (int n = 0; n < 2; ++n) dst##8[n] = ld32(lds + PG8_SB(b, h) + boff + n * 2048); } } while (0)
; #define PG8_WAIT_V(n) asm volatile("s_waitcnt vmcnt(" #n ")" ::: "memory")
; #define PG8_WAIT_L(n) asm volatile("s_waitcnt lgkmcnt(" #n ")" ::: "memory")
; #define PG8_BAR __builtin_amdgcn_s_barrier()
; #define PG8_SCHED __builtin_amdgcn_sched_barrier(0)
;     ...
;             PG8_LDB(B0, 1, 0); PG8_LDB(B1, 1, 1); PG8_SCHED; PG8_LDA(At, 1, 0); PG8_STAGE(PG8_SA(0, 1), a2 + hstepA, voffA);
;             PG8_WAIT_V(8); PG8_WAIT_L(0); PG8_BAR; PG8_MMA(0, 0, At, B0); PG8_MMA(0, 1, At, B1); PG8_BAR; PG8_SCHED;
;             PG8_LDA(At, 1, 1); PG8_STAGE(PG8_SB(1, 0), b3, voffB); PG8_STAGE(PG8_SB(1, 1), b3 + hstepB, voffB); PG8_STAGE(PG8_SA(1, 0), a3, voffA);
;             PG8_WAIT_V(8); PG8_WAIT_L(0); PG8_BAR; PG8_MMA(1, 0, At, B0); PG8_MMA(1, 1, At, B1); PG8_BAR; PG8_SCHED;
	ds_read_b128 v[2:5], v191
	ds_read_b128 v[6:9], v191 offset:16
	ds_read_b128 v[10:13], v191 offset:2048
	ds_read_b128 v[14:17], v191 offset:2064
	ds_read_b128 v[18:21], v192
	ds_read_b128 v[22:25], v192 offset:16
	ds_read_b128 v[26:29], v192 offset:2048
	ds_read_b128 v[30:33], v192 offset:2064
	s_add_u32 s28, s36, 0xb0000
	s_addc_u32 s29, s37, 0
	s_mov_b32 m0, s49
	ds_read_b128 v[34:37], v189 offset:32768
	ds_read_b128 v[38:41], v189 offset:32784
	ds_read_b128 v[42:45], v189 offset:34816
	ds_read_b128 v[46:49], v189 offset:34832
	ds_read_b128 v[50:53], v189 offset:36864
	ds_read_b128 v[54:57], v189 offset:36880
	ds_read_b128 v[58:61], v189 offset:38912
	global_load_lds_dwordx4 v162, s[28:29]
	s_mov_b32 m0, s50
	ds_read_b128 v[62:65], v189 offset:38928
	global_load_lds_dwordx4 v166, s[28:29]
	s_waitcnt vmcnt(8) lgkmcnt(0)
	s_barrier
	s_setprio 1
	v_mfma_scale_f32_16x16x128_f8f6f4 v[158:161], v[2:9], v[34:41], v[158:161], v190, v190 op_sel_hi:[0,0,0]
	v_mfma_scale_f32_16x16x128_f8f6f4 v[154:157], v[10:17], v[34:41], v[154:157], v190, v190 op_sel_hi:[0,0,0]
	v_mfma_scale_f32_16x16x128_f8f6f4 v[150:153], v[2:9], v[42:49], v[150:153], v190, v190 op_sel_hi:[0,0,0]
	v_mfma_scale_f32_16x16x128_f8f6f4 v[146:149], v[10:17], v[42:49], v[146:149], v190, v190 op_sel_hi:[0,0,0]
	v_mfma_scale_f32_16x16x128_f8f6f4 v[126:129], v[2:9], v[50:57], v[126:129], v190, v190 op_sel_hi:[0,0,0]
	v_mfma_scale_f32_16x16x128_f8f6f4 v[122:125], v[10:17], v[50:57], v[122:125], v190, v190 op_sel_hi:[0,0,0]
	v_mfma_scale_f32_16x16x128_f8f6f4 v[118:121], v[2:9], v[58:65], v[118:121], v190, v190 op_sel_hi:[0,0,0]
	v_mfma_scale_f32_16x16x128_f8f6f4 v[110:113], v[10:17], v[58:65], v[110:113], v190, v190 op_sel_hi:[0,0,0]
	s_setprio 0
	s_setprio 1
	v_mfma_scale_f32_16x16x128_f8f6f4 v[142:145], v[18:25], v[34:41], v[142:145], v190, v190 op_sel_hi:[0,0,0]
	v_mfma_scale_f32_16x16x128_f8f6f4 v[138:141], v[26:33], v[34:41], v[138:141], v190, v190 op_sel_hi:[0,0,0]
	v_mfma_scale_f32_16x16x128_f8f6f4 v[134:137], v[18:25], v[42:49], v[134:137], v190, v190 op_sel_hi:[0,0,0]
	v_mfma_scale_f32_16x16x128_f8f6f4 v[130:133], v[26:33], v[42:49], v[130:133], v190, v190 op_sel_hi:[0,0,0]
	v_mfma_scale_f32_16x16x128_f8f6f4 v[114:117], v[18:25], v[50:57], v[114:117], v190, v190 op_sel_hi:[0,0,0]
	v_mfma_scale_f32_16x16x128_f8f6f4 v[106:109], v[26:33], v[50:57], v[106:109], v190, v190 op_sel_hi:[0,0,0]
	v_mfma_scale_f32_16x16x128_f8f6f4 v[102:105], v[18:25], v[58:65], v[102:105], v190, v190 op_sel_hi:[0,0,0]
	v_mfma_scale_f32_16x16x128_f8f6f4 v[98:101], v[26:33], v[58:65], v[98:101], v190, v190 op_sel_hi:[0,0,0]
	s_setprio 0
	s_barrier
	s_mov_b32 m0, s53
	s_add_u32 s28, s34, 0xb0080
	ds_read_b128 v[34:37], v189 offset:49152
	ds_read_b128 v[38:41], v189 offset:49168
	ds_read_b128 v[50:53], v189 offset:51200
	ds_read_b128 v[54:57], v189 offset:51216
	global_load_lds_dwordx4 v164, s[98:99]
	s_mov_b32 m0, s54
	s_addc_u32 s29, s35, 0
	global_load_lds_dwordx4 v168, s[98:99]
	s_mov_b32 m0, s57
	ds_read_b128 v[206:209], v189 offset:55312
	global_load_lds_dwordx4 v164, s[28:29]
	s_mov_b32 m0, s58
	ds_read_b128 v[202:205], v189 offset:55296
	global_load_lds_dwordx4 v168, s[28:29]
	s_mov_b32 m0, s55
	ds_read_b128 v[198:201], v189 offset:53264
	global_load_lds_dwordx4 v162, s[100:101]
	s_mov_b32 m0, s56
	ds_read_b128 v[194:197], v189 offset:53248
	global_load_lds_dwordx4 v166, s[100:101]
	s_waitcnt vmcnt(8) lgkmcnt(0)
	s_barrier
	s_setprio 1
	v_mfma_scale_f32_16x16x128_f8f6f4 v[94:97], v[2:9], v[34:41], v[94:97], v190, v190 op_sel_hi:[0,0,0]
	v_mfma_scale_f32_16x16x128_f8f6f4 v[90:93], v[10:17], v[34:41], v[90:93], v190, v190 op_sel_hi:[0,0,0]
	v_mfma_scale_f32_16x16x128_f8f6f4 v[78:81], v[2:9], v[50:57], v[78:81], v190, v190 op_sel_hi:[0,0,0]
	v_mfma_scale_f32_16x16x128_f8f6f4 v[74:77], v[10:17], v[50:57], v[74:77], v190, v190 op_sel_hi:[0,0,0]
	v_mfma_scale_f32_16x16x128_f8f6f4 v[62:65], v[2:9], v[194:201], v[226:229], v190, v190 op_sel_hi:[0,0,0]
	v_mfma_scale_f32_16x16x128_f8f6f4 v[58:61], v[10:17], v[194:201], v[230:233], v190, v190 op_sel_hi:[0,0,0]
	v_mfma_scale_f32_16x16x128_f8f6f4 v[46:49], v[2:9], v[202:209], v[234:237], v190, v190 op_sel_hi:[0,0,0]
	v_mfma_scale_f32_16x16x128_f8f6f4 v[42:45], v[10:17], v[202:209], v[238:241], v190, v190 op_sel_hi:[0,0,0]
	s_setprio 0
	s_setprio 1
	v_mfma_scale_f32_16x16x128_f8f6f4 v[86:89], v[18:25], v[34:41], v[86:89], v190, v190 op_sel_hi:[0,0,0]
	v_mfma_scale_f32_16x16x128_f8f6f4 v[82:85], v[26:33], v[34:41], v[82:85], v190, v190 op_sel_hi:[0,0,0]
	v_mfma_scale_f32_16x16x128_f8f6f4 v[70:73], v[18:25], v[50:57], v[70:73], v190, v190 op_sel_hi:[0,0,0]
	v_mfma_scale_f32_16x16x128_f8f6f4 v[66:69], v[26:33], v[50:57], v[66:69], v190, v190 op_sel_hi:[0,0,0]
	v_mfma_scale_f32_16x16x128_f8f6f4 v[54:57], v[18:25], v[194:201], v[242:245], v190, v190 op_sel_hi:[0,0,0]
	v_mfma_scale_f32_16x16x128_f8f6f4 v[50:53], v[26:33], v[194:201], v[210:213], v190, v190 op_sel_hi:[0,0,0]
	v_mfma_scale_f32_16x16x128_f8f6f4 v[38:41], v[18:25], v[202:209], v[214:217], v190, v190 op_sel_hi:[0,0,0]
	v_mfma_scale_f32_16x16x128_f8f6f4 v[34:37], v[26:33], v[202:209], v[218:221], v190, v190 op_sel_hi:[0,0,0]
	s_setprio 0
	s_barrier
	s_add_u32 s66, s66, 0x100
	s_addc_u32 s67, s67, 0
	s_cmp_ge_i32 s68, s52
	s_mov_b64 s[28:29], s[30:31]
	s_mov_b32 s34, s68
	s_cbranch_scc0 .LBB0_4217
	s_branch .LBB0_4218
; #define PG8_STAGE(bufoff, gbase, voff) do { _Pragma("unroll") for (int _i = 0; _i < 2; ++_i) \
;         __builtin_amdgcn_global_load_lds((const unsigned*)((const char*)(gbase) + (voff)[_i]), (PG8_LAS unsigned*)(lds + (bufoff) + ldsw + _i * 8192), 16, 0, 0); } while (0)
; #define PG8_LDA(dst, b, h) do { if constexpr (DT != 1) { _Pragma("unroll") for (int m = 0; m < 4; ++m) _Pragma("unroll") for (int k = 0; k < 2; ++k) dst[m][k] = *(const PG8_LAS bf16x8*)(lds + PG8_SA(b, h) + aoff + m * 2048 + k * 1024); } \
;         else { _Pragma("unroll") for (int m = 0; m < 4; ++m) dst##8[m] = ld32(lds + PG8_SA(b, h) + aoff + m * 2048); } } while (0)
; #define PG8_LDB(dst, b, h) do { if constexpr (DT != 1) { _Pragma("unroll") for (int n = 0; n < 2; ++n) _Pragma("unroll") for (int k = 0; k < 2; ++k) dst[n][k] = *(const PG8_LAS bf16x8*)(lds + PG8_SB(b, h) + boff + n * 2048 + k * 1024); } \
;         else { _Pragma("unroll") for (int n = 0; n < 2; ++n) dst##8[n] = ld32(lds + PG8_SB(b, h) + boff + n * 2048); } } while (0)
; #define PG8_WAIT_V(n) asm volatile("s_waitcnt vmcnt(" #n ")" ::: "memory")
; #define PG8_WAIT_L(n) asm volatile("s_waitcnt lgkmcnt(" #n ")" ::: "memory")
; #define PG8_BAR __builtin_amdgcn_s_barrier()
; #define PG8_SCHED __builtin_amdgcn_sched_barrier(0)
;     ...
;             PG8_LDB(B0, 0, 0); PG8_LDB(B1, 0, 1); PG8_SCHED; PG8_LDA(At, 0, 0); PG8_STAGE(PG8_SA(1, 1), a1 + hstepA, voffA);
;             PG8_WAIT_V(8); PG8_WAIT_L(0); PG8_BAR; PG8_MMA(0, 0, At, B0); PG8_MMA(0, 1, At, B1); PG8_BAR; PG8_SCHED;
;             PG8_LDA(At, 0, 1); PG8_STAGE(PG8_SB(0, 0), b2, voffB); PG8_STAGE(PG8_SB(0, 1), b2 + hstepB, voffB); PG8_STAGE(PG8_SA(0, 0), a2, voffA);
;             PG8_WAIT_V(8); PG8_WAIT_L(0); PG8_BAR; PG8_MMA(1, 0, At, B0); PG8_MMA(1, 1, At, B1); PG8_BAR; PG8_SCHED;
.LBB0_4217:
	ds_read_b128 v[18:21], v187
	ds_read_b128 v[22:25], v187 offset:16
	ds_read_b128 v[26:29], v187 offset:2048
	ds_read_b128 v[30:33], v187 offset:2064
	ds_read_b128 v[2:5], v188
	ds_read_b128 v[6:9], v188 offset:16
	ds_read_b128 v[10:13], v188 offset:2048
	ds_read_b128 v[14:17], v188 offset:2064
	s_add_i32 s68, s34, 2
	s_add_u32 s30, s28, 0x100
	s_addc_u32 s31, s29, 0
	s_cmp_eq_u32 s59, s34
	s_cselect_b32 s34, s26, s66
	s_cselect_b32 s37, s3, s31
	s_cselect_b32 s36, s2, s30
	s_cselect_b32 s35, s27, s67
	v_lshl_add_u64 v[218:219], s[28:29], 0, v[172:173]
	s_add_i32 m0, s47, 0xc000
	ds_read_b128 v[178:181], v189
	ds_read_b128 v[182:185], v189 offset:16
	ds_read_b128 v[194:197], v189 offset:2048
	ds_read_b128 v[198:201], v189 offset:2064
	ds_read_b128 v[202:205], v189 offset:4096
	ds_read_b128 v[206:209], v189 offset:4112
	ds_read_b128 v[210:213], v189 offset:6144
	ds_read_b128 v[214:217], v189 offset:6160
	global_load_lds_dwordx4 v[218:219], off
	v_lshl_add_u64 v[218:219], s[28:29], 0, v[170:171]
	s_add_i32 m0, s47, 0xe000
	s_nop 0
	global_load_lds_dwordx4 v[218:219], off
	s_waitcnt vmcnt(8) lgkmcnt(0)
	s_barrier
	s_setprio 1
	v_mfma_scale_f32_16x16x128_f8f6f4 v[158:161], v[18:25], v[178:185], v[158:161], v190, v190 op_sel_hi:[0,0,0]
	v_mfma_scale_f32_16x16x128_f8f6f4 v[154:157], v[26:33], v[178:185], v[154:157], v190, v190 op_sel_hi:[0,0,0]
	v_mfma_scale_f32_16x16x128_f8f6f4 v[150:153], v[18:25], v[194:201], v[150:153], v190, v190 op_sel_hi:[0,0,0]
	v_mfma_scale_f32_16x16x128_f8f6f4 v[146:149], v[26:33], v[194:201], v[146:149], v190, v190 op_sel_hi:[0,0,0]
	v_mfma_scale_f32_16x16x128_f8f6f4 v[126:129], v[18:25], v[202:209], v[126:129], v190, v190 op_sel_hi:[0,0,0]
	v_mfma_scale_f32_16x16x128_f8f6f4 v[122:125], v[26:33], v[202:209], v[122:125], v190, v190 op_sel_hi:[0,0,0]
	v_mfma_scale_f32_16x16x128_f8f6f4 v[118:121], v[18:25], v[210:217], v[118:121], v190, v190 op_sel_hi:[0,0,0]
	v_mfma_scale_f32_16x16x128_f8f6f4 v[110:113], v[26:33], v[210:217], v[110:113], v190, v190 op_sel_hi:[0,0,0]
	s_setprio 0
	s_setprio 1
	v_mfma_scale_f32_16x16x128_f8f6f4 v[142:145], v[2:9], v[178:185], v[142:145], v190, v190 op_sel_hi:[0,0,0]
	v_mfma_scale_f32_16x16x128_f8f6f4 v[138:141], v[10:17], v[178:185], v[138:141], v190, v190 op_sel_hi:[0,0,0]
	v_mfma_scale_f32_16x16x128_f8f6f4 v[134:137], v[2:9], v[194:201], v[134:137], v190, v190 op_sel_hi:[0,0,0]
	v_mfma_scale_f32_16x16x128_f8f6f4 v[130:133], v[10:17], v[194:201], v[130:133], v190, v190 op_sel_hi:[0,0,0]
	v_mfma_scale_f32_16x16x128_f8f6f4 v[114:117], v[2:9], v[202:209], v[114:117], v190, v190 op_sel_hi:[0,0,0]
	v_mfma_scale_f32_16x16x128_f8f6f4 v[106:109], v[10:17], v[202:209], v[106:109], v190, v190 op_sel_hi:[0,0,0]
	v_mfma_scale_f32_16x16x128_f8f6f4 v[102:105], v[2:9], v[210:217], v[102:105], v190, v190 op_sel_hi:[0,0,0]
	v_mfma_scale_f32_16x16x128_f8f6f4 v[98:101], v[10:17], v[210:217], v[98:101], v190, v190 op_sel_hi:[0,0,0]
	s_setprio 0
	s_barrier
	s_mov_b32 m0, s43
	s_add_u32 s98, s34, 0x80
	s_addc_u32 s99, s35, 0
	s_add_u32 s28, s34, 0xb0000
	ds_read_b128 v[194:197], v189 offset:16384
	ds_read_b128 v[198:201], v189 offset:16400
	ds_read_b128 v[202:205], v189 offset:18432
	ds_read_b128 v[206:209], v189 offset:18448
	global_load_lds_dwordx4 v164, s[34:35]
	s_mov_b32 m0, s44
	s_addc_u32 s29, s35, 0
	global_load_lds_dwordx4 v168, s[34:35]
	s_mov_b32 m0, s45
	ds_read_b128 v[222:225], v189 offset:22544
	global_load_lds_dwordx4 v164, s[28:29]
	s_mov_b32 m0, s46
	ds_read_b128 v[218:221], v189 offset:22528
	global_load_lds_dwordx4 v168, s[28:29]
	s_add_u32 s100, s36, 0x80
	s_addc_u32 s101, s37, 0
	s_mov_b32 m0, s47
	ds_read_b128 v[214:217], v189 offset:20496
	global_load_lds_dwordx4 v162, s[36:37]
	s_mov_b32 m0, s48
	ds_read_b128 v[210:213], v189 offset:20480
	global_load_lds_dwordx4 v166, s[36:37]
	s_waitcnt vmcnt(8) lgkmcnt(0)
	s_barrier
	s_setprio 1
	v_mfma_scale_f32_16x16x128_f8f6f4 v[94:97], v[18:25], v[194:201], v[94:97], v190, v190 op_sel_hi:[0,0,0]
	v_mfma_scale_f32_16x16x128_f8f6f4 v[90:93], v[26:33], v[194:201], v[90:93], v190, v190 op_sel_hi:[0,0,0]
	v_mfma_scale_f32_16x16x128_f8f6f4 v[78:81], v[18:25], v[202:209], v[78:81], v190, v190 op_sel_hi:[0,0,0]
	v_mfma_scale_f32_16x16x128_f8f6f4 v[74:77], v[26:33], v[202:209], v[74:77], v190, v190 op_sel_hi:[0,0,0]
	v_mfma_scale_f32_16x16x128_f8f6f4 v[226:229], v[18:25], v[210:217], v[62:65], v190, v190 op_sel_hi:[0,0,0]
	v_mfma_scale_f32_16x16x128_f8f6f4 v[230:233], v[26:33], v[210:217], v[58:61], v190, v190 op_sel_hi:[0,0,0]
	v_mfma_scale_f32_16x16x128_f8f6f4 v[234:237], v[18:25], v[218:225], v[46:49], v190, v190 op_sel_hi:[0,0,0]
	v_mfma_scale_f32_16x16x128_f8f6f4 v[238:241], v[26:33], v[218:225], v[42:45], v190, v190 op_sel_hi:[0,0,0]
	s_setprio 0
	s_setprio 1
	v_mfma_scale_f32_16x16x128_f8f6f4 v[86:89], v[2:9], v[194:201], v[86:89], v190, v190 op_sel_hi:[0,0,0]
	v_mfma_scale_f32_16x16x128_f8f6f4 v[82:85], v[10:17], v[194:201], v[82:85], v190, v190 op_sel_hi:[0,0,0]
	v_mfma_scale_f32_16x16x128_f8f6f4 v[70:73], v[2:9], v[202:209], v[70:73], v190, v190 op_sel_hi:[0,0,0]
	v_mfma_scale_f32_16x16x128_f8f6f4 v[66:69], v[10:17], v[202:209], v[66:69], v190, v190 op_sel_hi:[0,0,0]
	v_mfma_scale_f32_16x16x128_f8f6f4 v[242:245], v[2:9], v[210:217], v[54:57], v190, v190 op_sel_hi:[0,0,0]
	v_mfma_scale_f32_16x16x128_f8f6f4 v[210:213], v[10:17], v[210:217], v[50:53], v190, v190 op_sel_hi:[0,0,0]
	v_mfma_scale_f32_16x16x128_f8f6f4 v[214:217], v[2:9], v[218:225], v[38:41], v190, v190 op_sel_hi:[0,0,0]
	v_mfma_scale_f32_16x16x128_f8f6f4 v[218:221], v[10:17], v[218:225], v[34:37], v190, v190 op_sel_hi:[0,0,0]
	s_setprio 0
	s_barrier
; #define PG8_STAGE(bufoff, gbase, voff) do { _Pragma("unroll") for (int _i = 0; _i < 2; ++_i) \
;         __builtin_amdgcn_global_load_lds((const unsigned*)((const char*)(gbase) + (voff)[_i]), (PG8_LAS unsigned*)(lds + (bufoff) + ldsw + _i * 8192), 16, 0, 0); } while (0)
; #define PG8_LDA(dst, b, h) do { if constexpr (DT != 1) { _Pragma("unroll") for (int m = 0; m < 4; ++m) _Pragma("unroll") for (int k = 0; k < 2; ++k) dst[m][k] = *(const PG8_LAS bf16x8*)(lds + PG8_SA(b, h) + aoff + m * 2048 + k * 1024); } \
;         else { _Pragma("unroll") for (int m = 0; m < 4; ++m) dst##8[m] = ld32(lds + PG8_SA(b, h) + aoff + m * 2048); } } while (0)
; #define PG8_LDB(dst, b, h) do { if constexpr (DT != 1) { _Pragma("unroll") for (int n = 0; n < 2; ++n) _Pragma("unroll") for (int k = 0; k < 2; ++k) dst[n][k] = *(const PG8_LAS bf16x8*)(lds + PG8_SB(b, h) + boff + n * 2048 + k * 1024); } \
;         else { _Pragma("unroll") for (int n = 0; n < 2; ++n) dst##8[n] = ld32(lds + PG8_SB(b, h) + boff + n * 2048); } } while (0)
; #define PG8_WAIT_V(n) asm volatile("s_waitcnt vmcnt(" #n ")" ::: "memory")
; #define PG8_WAIT_L(n) asm volatile("s_waitcnt lgkmcnt(" #n ")" ::: "memory")
; #define PG8_BAR __builtin_amdgcn_s_barrier()
; #define PG8_SCHED __builtin_amdgcn_sched_barrier(0)
;     ...
;             PG8_LDB(B0, 1, 0); PG8_LDB(B1, 1, 1); PG8_SCHED; PG8_LDA(At, 1, 0); PG8_STAGE(PG8_SA(0, 1), a2 + hstepA, voffA);
;             PG8_WAIT_V(8); PG8_WAIT_L(0); PG8_BAR; PG8_MMA(0, 0, At, B0); PG8_MMA(0, 1, At, B1); PG8_BAR; PG8_SCHED;
;             PG8_LDA(At, 1, 1); PG8_STAGE(PG8_SB(1, 0), b3, voffB); PG8_STAGE(PG8_SB(1, 1), b3 + hstepB, voffB); PG8_STAGE(PG8_SA(1, 0), a3, voffA);
;             PG8_WAIT_V(8); PG8_WAIT_L(0); PG8_BAR; PG8_MMA(1, 0, At, B0); PG8_MMA(1, 1, At, B1); PG8_BAR; PG8_SCHED;
	ds_read_b128 v[2:5], v191
	ds_read_b128 v[6:9], v191 offset:16
	ds_read_b128 v[10:13], v191 offset:2048
	ds_read_b128 v[14:17], v191 offset:2064
	ds_read_b128 v[18:21], v192
	ds_read_b128 v[22:25], v192 offset:16
	ds_read_b128 v[26:29], v192 offset:2048
	ds_read_b128 v[30:33], v192 offset:2064
	s_add_u32 s28, s36, 0xb0000
	s_addc_u32 s29, s37, 0
	s_mov_b32 m0, s49
	ds_read_b128 v[34:37], v189 offset:32768
	ds_read_b128 v[38:41], v189 offset:32784
	ds_read_b128 v[42:45], v189 offset:34816
	ds_read_b128 v[46:49], v189 offset:34832
	ds_read_b128 v[50:53], v189 offset:36864
	ds_read_b128 v[54:57], v189 offset:36880
	ds_read_b128 v[58:61], v189 offset:38912
	global_load_lds_dwordx4 v162, s[28:29]
	s_mov_b32 m0, s50
	ds_read_b128 v[62:65], v189 offset:38928
	global_load_lds_dwordx4 v166, s[28:29]
	s_waitcnt vmcnt(8) lgkmcnt(0)
	s_barrier
	s_setprio 1
	v_mfma_scale_f32_16x16x128_f8f6f4 v[158:161], v[2:9], v[34:41], v[158:161], v190, v190 op_sel_hi:[0,0,0]
	v_mfma_scale_f32_16x16x128_f8f6f4 v[154:157], v[10:17], v[34:41], v[154:157], v190, v190 op_sel_hi:[0,0,0]
	v_mfma_scale_f32_16x16x128_f8f6f4 v[150:153], v[2:9], v[42:49], v[150:153], v190, v190 op_sel_hi:[0,0,0]
	v_mfma_scale_f32_16x16x128_f8f6f4 v[146:149], v[10:17], v[42:49], v[146:149], v190, v190 op_sel_hi:[0,0,0]
	v_mfma_scale_f32_16x16x128_f8f6f4 v[126:129], v[2:9], v[50:57], v[126:129], v190, v190 op_sel_hi:[0,0,0]
	v_mfma_scale_f32_16x16x128_f8f6f4 v[122:125], v[10:17], v[50:57], v[122:125], v190, v190 op_sel_hi:[0,0,0]
	v_mfma_scale_f32_16x16x128_f8f6f4 v[118:121], v[2:9], v[58:65], v[118:121], v190, v190 op_sel_hi:[0,0,0]
	v_mfma_scale_f32_16x16x128_f8f6f4 v[110:113], v[10:17], v[58:65], v[110:113], v190, v190 op_sel_hi:[0,0,0]
	s_setprio 0
	s_setprio 1
	v_mfma_scale_f32_16x16x128_f8f6f4 v[142:145], v[18:25], v[34:41], v[142:145], v190, v190 op_sel_hi:[0,0,0]
	v_mfma_scale_f32_16x16x128_f8f6f4 v[138:141], v[26:33], v[34:41], v[138:141], v190, v190 op_sel_hi:[0,0,0]
	v_mfma_scale_f32_16x16x128_f8f6f4 v[134:137], v[18:25], v[42:49], v[134:137], v190, v190 op_sel_hi:[0,0,0]
	v_mfma_scale_f32_16x16x128_f8f6f4 v[130:133], v[26:33], v[42:49], v[130:133], v190, v190 op_sel_hi:[0,0,0]
	v_mfma_scale_f32_16x16x128_f8f6f4 v[114:117], v[18:25], v[50:57], v[114:117], v190, v190 op_sel_hi:[0,0,0]
	v_mfma_scale_f32_16x16x128_f8f6f4 v[106:109], v[26:33], v[50:57], v[106:109], v190, v190 op_sel_hi:[0,0,0]
	v_mfma_scale_f32_16x16x128_f8f6f4 v[102:105], v[18:25], v[58:65], v[102:105], v190, v190 op_sel_hi:[0,0,0]
	v_mfma_scale_f32_16x16x128_f8f6f4 v[98:101], v[26:33], v[58:65], v[98:101], v190, v190 op_sel_hi:[0,0,0]
	s_setprio 0
	s_barrier
	s_mov_b32 m0, s53
	s_add_u32 s28, s34, 0xb0080
	ds_read_b128 v[34:37], v189 offset:49152
	ds_read_b128 v[38:41], v189 offset:49168
	ds_read_b128 v[50:53], v189 offset:51200
	ds_read_b128 v[54:57], v189 offset:51216
	global_load_lds_dwordx4 v164, s[98:99]
	s_mov_b32 m0, s54
	s_addc_u32 s29, s35, 0
	global_load_lds_dwordx4 v168, s[98:99]
	s_mov_b32 m0, s57
	ds_read_b128 v[206:209], v189 offset:55312
	global_load_lds_dwordx4 v164, s[28:29]
	s_mov_b32 m0, s58
	ds_read_b128 v[202:205], v189 offset:55296
	global_load_lds_dwordx4 v168, s[28:29]
	s_mov_b32 m0, s55
	ds_read_b128 v[198:201], v189 offset:53264
	global_load_lds_dwordx4 v162, s[100:101]
	s_mov_b32 m0, s56
	ds_read_b128 v[194:197], v189 offset:53248
	global_load_lds_dwordx4 v166, s[100:101]
	s_waitcnt vmcnt(8) lgkmcnt(0)
	s_barrier
	s_setprio 1
	v_mfma_scale_f32_16x16x128_f8f6f4 v[94:97], v[2:9], v[34:41], v[94:97], v190, v190 op_sel_hi:[0,0,0]
	v_mfma_scale_f32_16x16x128_f8f6f4 v[90:93], v[10:17], v[34:41], v[90:93], v190, v190 op_sel_hi:[0,0,0]
	v_mfma_scale_f32_16x16x128_f8f6f4 v[78:81], v[2:9], v[50:57], v[78:81], v190, v190 op_sel_hi:[0,0,0]
	v_mfma_scale_f32_16x16x128_f8f6f4 v[74:77], v[10:17], v[50:57], v[74:77], v190, v190 op_sel_hi:[0,0,0]
	v_mfma_scale_f32_16x16x128_f8f6f4 v[62:65], v[2:9], v[194:201], v[226:229], v190, v190 op_sel_hi:[0,0,0]
	v_mfma_scale_f32_16x16x128_f8f6f4 v[58:61], v[10:17], v[194:201], v[230:233], v190, v190 op_sel_hi:[0,0,0]
	v_mfma_scale_f32_16x16x128_f8f6f4 v[46:49], v[2:9], v[202:209], v[234:237], v190, v190 op_sel_hi:[0,0,0]
	v_mfma_scale_f32_16x16x128_f8f6f4 v[42:45], v[10:17], v[202:209], v[238:241], v190, v190 op_sel_hi:[0,0,0]
	s_setprio 0
	s_setprio 1
	v_mfma_scale_f32_16x16x128_f8f6f4 v[86:89], v[18:25], v[34:41], v[86:89], v190, v190 op_sel_hi:[0,0,0]
	v_mfma_scale_f32_16x16x128_f8f6f4 v[82:85], v[26:33], v[34:41], v[82:85], v190, v190 op_sel_hi:[0,0,0]
	v_mfma_scale_f32_16x16x128_f8f6f4 v[70:73], v[18:25], v[50:57], v[70:73], v190, v190 op_sel_hi:[0,0,0]
	v_mfma_scale_f32_16x16x128_f8f6f4 v[66:69], v[26:33], v[50:57], v[66:69], v190, v190 op_sel_hi:[0,0,0]
	v_mfma_scale_f32_16x16x128_f8f6f4 v[54:57], v[18:25], v[194:201], v[242:245], v190, v190 op_sel_hi:[0,0,0]
	v_mfma_scale_f32_16x16x128_f8f6f4 v[50:53], v[26:33], v[194:201], v[210:213], v190, v190 op_sel_hi:[0,0,0]
	v_mfma_scale_f32_16x16x128_f8f6f4 v[38:41], v[18:25], v[202:209], v[214:217], v190, v190 op_sel_hi:[0,0,0]
	v_mfma_scale_f32_16x16x128_f8f6f4 v[34:37], v[26:33], v[202:209], v[218:221], v190, v190 op_sel_hi:[0,0,0]
	s_setprio 0
	s_barrier
	s_add_u32 s66, s66, 0x100
	s_addc_u32 s67, s67, 0
	s_cmp_ge_i32 s68, s52
	s_mov_b64 s[28:29], s[30:31]
	s_mov_b32 s34, s68
	s_cbranch_scc0 .LBB0_4217

;     __device__ bool next(int i, Unit& u) const { if (!b.next(i, u)) return false; const int seg = u.pn < 24 ? (u.pn >> 3) : u.pn - 21; u.pm += ((0x541320 >> (4 * seg)) & 7) * MROWS_TILES; return true; }
;     __device__ bool next(int i, Unit& u) const { if (!b.next(i, u)) return false; u.pm += (u.pn >> 3) * MROWS_TILES; return true; }
; #define PG8_STAGE(bufoff, gbase, voff) do { _Pragma("unroll") for (int _i = 0; _i < 2; ++_i) \
;         __builtin_amdgcn_global_load_lds((const unsigned*)((const char*)(gbase) + (voff)[_i]), (PG8_LAS unsigned*)(lds + (bufoff) + ldsw + _i * 8192), 16, 0, 0); } while (0)
; #define PG8_LDA(dst, b, h) do { if constexpr (DT != 1) { _Pragma("unroll") for (int m = 0; m < 4; ++m) _Pragma("unroll") for (int k = 0; k < 2; ++k) dst[m][k] = *(const PG8_LAS bf16x8*)(lds + PG8_SA(b, h) + aoff + m * 2048 + k * 1024); } \
;         else { _Pragma("unroll") for (int m = 0; m < 4; ++m) dst##8[m] = ld32(lds + PG8_SA(b, h) + aoff + m * 2048); } } while (0)
; #define PG8_WAIT_V(n) asm volatile("s_waitcnt vmcnt(" #n ")" ::: "memory")
; #define PG8_WAIT_L(n) asm volatile("s_waitcnt lgkmcnt(" #n ")" ::: "memory")
; #define PG8_BAR __builtin_amdgcn_s_barrier()
;     ...
;         const bool has_next = S.next(ui + 1, nxt);
;         const char* nA = has_next ? (const char*)g.A + (size_t)nxt.pm * tstepA : cA; const char* nB = has_next ? (const char*)g.Bt + (size_t)nxt.pn * tstepB : cB;
;         for (int t = 0; t < nt; t += 2) {
;             const bool last = (t == nt - 2);
;             const char* a1 = cA + (size_t)(t + 1) * kstep;
;             const char* a2 = last ? nA : cA + (size_t)(t + 2) * kstep; const char* b2 = last ? nB : cB + (size_t)(t + 2) * kstep;
;             const char* a3 = a2 + kstep; const char* b3 = b2 + kstep;
;             if (last && has_next) S.a_ready(nxt);
;             if constexpr (SP2) {
;             PG8_LDB(B0, 0, 0); PG8_LDB(B1, 0, 1); PG8_SCHED; PG8_LDA(At, 0, 0); PG8_STAGE(PG8_SA(1, 1), a1 + hstepA, voffA);
;             PG8_WAIT_V(8); PG8_WAIT_L(0); PG8_BAR; PG8_MMA(0, 0, At, B0); PG8_MMA(0, 1, At, B1); PG8_BAR; PG8_SCHED;
;     ...
; #pragma unroll
;         for (int a = 0; a < 2; ++a)
; #pragma unroll
;             for (int b = 0; b < 2; ++b)
; #pragma unroll
;                 for (int m = 0; m < 4; ++m)
; #pragma unroll
;                     for (int n = 0; n < 2; ++n) acc[a][b][m][n] = (f32x4){0.f, 0.f, 0.f, 0.f};
.LBB0_4348:
	s_ashr_i32 s19, s18, 31
	s_lshl_b64 s[20:21], s[18:19], 19
	s_add_u32 s20, s39, s20
	s_addc_u32 s21, s40, s21
	s_ashr_i32 s17, s16, 31
	s_lshl_b64 s[22:23], s[16:17], 19
	s_add_u32 s22, s41, s22
	v_mov_b32_e32 v161, 0
	s_addc_u32 s23, s42, s23
	s_andn2_b64 vcc, exec, s[10:11]
	v_mov_b32_e32 v160, 0
	v_mov_b32_e32 v167, 0
	v_mov_b32_e32 v166, v161
	v_mov_b32_e32 v165, 0
	v_mov_b32_e32 v164, 0
	v_mov_b32_e32 v163, 0
	v_mov_b32_e32 v162, v161
	v_mov_b32_e32 v155, 0
	v_mov_b32_e32 v154, 0
	v_mov_b32_e32 v153, 0
	v_mov_b32_e32 v152, v161
	v_mov_b32_e32 v159, 0
	v_mov_b32_e32 v158, 0
	v_mov_b32_e32 v157, 0
	v_mov_b32_e32 v156, v161
	v_mov_b32_e32 v113, 0
	v_mov_b32_e32 v112, 0
	v_mov_b32_e32 v111, 0
	v_mov_b32_e32 v110, v161
	v_mov_b32_e32 v109, 0
	v_mov_b32_e32 v108, 0
	v_mov_b32_e32 v107, 0
	v_mov_b32_e32 v106, v161
	v_mov_b32_e32 v105, 0
	v_mov_b32_e32 v104, 0
	v_mov_b32_e32 v103, 0
	v_mov_b32_e32 v102, v161
	v_mov_b32_e32 v101, 0
	v_mov_b32_e32 v100, 0
	v_mov_b32_e32 v99, 0
	v_mov_b32_e32 v98, v161
	v_mov_b32_e32 v117, 0
	v_mov_b32_e32 v116, 0
	v_mov_b32_e32 v115, 0
	v_mov_b32_e32 v114, 0
	v_mov_b32_e32 v121, 0
	v_mov_b32_e32 v120, 0
	v_mov_b32_e32 v119, 0
	v_mov_b32_e32 v118, 0
	v_mov_b32_e32 v125, 0
	v_mov_b32_e32 v124, 0
	v_mov_b32_e32 v123, 0
	v_mov_b32_e32 v122, 0
	v_mov_b32_e32 v129, 0
	v_mov_b32_e32 v128, 0
	v_mov_b32_e32 v127, 0
	v_mov_b32_e32 v126, 0
	v_mov_b32_e32 v97, 0
	v_mov_b32_e32 v96, 0
	v_mov_b32_e32 v89, 0
	v_mov_b32_e32 v88, 0
	v_mov_b32_e32 v95, 0
	v_mov_b32_e32 v94, 0
	v_mov_b32_e32 v87, 0
	v_mov_b32_e32 v86, 0
	v_mov_b32_e32 v81, 0
	v_mov_b32_e32 v80, 0
	v_mov_b32_e32 v73, 0
	v_mov_b32_e32 v72, 0
	v_mov_b32_e32 v79, 0
	v_mov_b32_e32 v78, 0
	v_mov_b32_e32 v71, 0
	v_mov_b32_e32 v70, 0
	v_mov_b32_e32 v93, 0
	v_mov_b32_e32 v92, 0
	v_mov_b32_e32 v91, 0
	v_mov_b32_e32 v90, v161
	v_mov_b32_e32 v85, 0
	v_mov_b32_e32 v84, 0
	v_mov_b32_e32 v83, 0
	v_mov_b32_e32 v82, v161
	v_mov_b32_e32 v77, 0
	v_mov_b32_e32 v76, 0
	v_mov_b32_e32 v75, 0
	v_mov_b32_e32 v74, v161
	v_mov_b32_e32 v69, 0
	v_mov_b32_e32 v68, 0
	v_mov_b32_e32 v67, 0
	v_mov_b32_e32 v66, v161
	v_mov_b32_e32 v61, 0
	v_mov_b32_e32 v60, 0
	v_mov_b32_e32 v59, 0
	v_mov_b32_e32 v58, v161
	v_mov_b32_e32 v53, 0
	v_mov_b32_e32 v52, 0
	v_mov_b32_e32 v51, 0
	v_mov_b32_e32 v50, v161
	v_mov_b32_e32 v45, 0
	v_mov_b32_e32 v44, 0
	v_mov_b32_e32 v43, 0
	v_mov_b32_e32 v42, v161
	v_mov_b32_e32 v37, 0
	v_mov_b32_e32 v36, 0
	v_mov_b32_e32 v35, 0
	v_mov_b32_e32 v34, v161
	v_mov_b32_e32 v65, 0
	v_mov_b32_e32 v64, 0
	v_mov_b32_e32 v57, 0
	v_mov_b32_e32 v56, 0
	v_mov_b32_e32 v63, 0
	v_mov_b32_e32 v62, 0
	v_mov_b32_e32 v55, 0
	v_mov_b32_e32 v54, 0
	v_mov_b32_e32 v49, 0
	v_mov_b32_e32 v48, 0
	v_mov_b32_e32 v41, 0
	v_mov_b32_e32 v40, 0
	v_mov_b32_e32 v47, 0
	v_mov_b32_e32 v46, 0
	v_mov_b32_e32 v39, 0
	v_mov_b32_e32 v38, 0
	v_mov_b32_e32 v33, 0
	v_mov_b32_e32 v32, 0
	v_mov_b32_e32 v29, 0
	v_mov_b32_e32 v28, 0
	v_mov_b32_e32 v31, 0
	v_mov_b32_e32 v30, 0
	v_mov_b32_e32 v27, 0
	v_mov_b32_e32 v26, 0
	v_mov_b32_e32 v25, 0
	v_mov_b32_e32 v24, 0
	v_mov_b32_e32 v21, 0
	v_mov_b32_e32 v20, 0
	v_mov_b32_e32 v23, 0
	v_mov_b32_e32 v22, 0
	v_mov_b32_e32 v19, 0
	v_mov_b32_e32 v18, 0
	s_cbranch_vccnz .LBB0_4352
	s_and_b64 s[30:31], s[0:1], exec
	s_cselect_b32 s17, s21, s29
	s_cselect_b32 s19, s20, s28
	s_cselect_b32 s66, s23, s27
	s_cselect_b32 s67, s22, s26
	s_add_u32 s68, s26, 0x100
	s_addc_u32 s69, s27, 0
	s_add_u32 s26, s28, 0x40080
	s_addc_u32 s27, s29, 0
	s_mov_b32 s28, 0
	s_waitcnt vmcnt(0)
	v_add_u32_e32 v164, s37, v170
	v_add_u32_e32 v168, s38, v170
	ds_read_b128 v[152:155], v164
	ds_read_b128 v[156:159], v164 offset:1024
	ds_read_b128 v[160:163], v164 offset:2048
	ds_read_b128 v[164:167], v164 offset:3072
	ds_read_b128 v[180:183], v168
	ds_read_b128 v[184:187], v168 offset:1024
	ds_read_b128 v[188:191], v168 offset:2048
	ds_read_b128 v[192:195], v168 offset:3072
	s_add_i32 s70, s28, 2
	s_add_u32 s29, s26, 0xfffc0080
	s_addc_u32 s30, s27, -1
	s_cmp_eq_u32 s64, s28
	s_cselect_b32 s28, s67, s68
	s_cselect_b32 s31, s17, s30
	s_cselect_b32 s30, s19, s29
	s_cselect_b32 s29, s66, s69
	s_add_i32 m0, s49, 0xc000
	ds_read_b128 v[196:199], v179
	ds_read_b128 v[200:203], v179 offset:1024
	ds_read_b128 v[204:207], v179 offset:2048
	ds_read_b128 v[208:211], v179 offset:3072
	ds_read_b128 v[212:215], v179 offset:4096
	ds_read_b128 v[216:219], v179 offset:5120
	ds_read_b128 v[220:223], v179 offset:6144
	ds_read_b128 v[224:227], v179 offset:7168
	global_load_lds_dwordx4 v146, s[26:27]
	s_add_i32 m0, s49, 0xe000
	s_nop 0
	global_load_lds_dwordx4 v144, s[26:27]
	s_waitcnt vmcnt(8) lgkmcnt(0)
	s_barrier
; #define PG8_STAGE(bufoff, gbase, voff) do { _Pragma("unroll") for (int _i = 0; _i < 2; ++_i) \
;         __builtin_amdgcn_global_load_lds((const unsigned*)((const char*)(gbase) + (voff)[_i]), (PG8_LAS unsigned*)(lds + (bufoff) + ldsw + _i * 8192), 16, 0, 0); } while (0)
; #define PG8_LDA(dst, b, h) do { if constexpr (DT != 1) { _Pragma("unroll") for (int m = 0; m < 4; ++m) _Pragma("unroll") for (int k = 0; k < 2; ++k) dst[m][k] = *(const PG8_LAS bf16x8*)(lds + PG8_SA(b, h) + aoff + m * 2048 + k * 1024); } \
;         else { _Pragma("unroll") for (int m = 0; m < 4; ++m) dst##8[m] = ld32(lds + PG8_SA(b, h) + aoff + m * 2048); } } while (0)
; #define PG8_LDB(dst, b, h) do { if constexpr (DT != 1) { _Pragma("unroll") for (int n = 0; n < 2; ++n) _Pragma("unroll") for (int k = 0; k < 2; ++k) dst[n][k] = *(const PG8_LAS bf16x8*)(lds + PG8_SB(b, h) + boff + n * 2048 + k * 1024); } \
;         else { _Pragma("unroll") for (int n = 0; n < 2; ++n) dst##8[n] = ld32(lds + PG8_SB(b, h) + boff + n * 2048); } } while (0)
; #define PG8_WAIT_V(n) asm volatile("s_waitcnt vmcnt(" #n ")" ::: "memory")
; #define PG8_WAIT_L(n) asm volatile("s_waitcnt lgkmcnt(" #n ")" ::: "memory")
; #define PG8_BAR __builtin_amdgcn_s_barrier()
; #define PG8_SCHED __builtin_amdgcn_sched_barrier(0)
;     ...
;             PG8_LDB(B0, 0, 0); PG8_LDB(B1, 0, 1); PG8_SCHED; PG8_LDA(At, 0, 0); PG8_STAGE(PG8_SA(1, 1), a1 + hstepA, voffA);
;             PG8_WAIT_V(8); PG8_WAIT_L(0); PG8_BAR; PG8_MMA(0, 0, At, B0); PG8_MMA(0, 1, At, B1); PG8_BAR; PG8_SCHED;
;             PG8_LDA(At, 0, 1); PG8_STAGE(PG8_SB(0, 0), b2, voffB); PG8_STAGE(PG8_SB(0, 1), b2 + hstepB, voffB); PG8_STAGE(PG8_SA(0, 0), a2, voffA);
;             PG8_WAIT_V(8); PG8_WAIT_L(0); PG8_BAR; PG8_MMA(1, 0, At, B0); PG8_MMA(1, 1, At, B1); PG8_BAR; PG8_SCHED;
;             PG8_LDB(B0, 1, 0); PG8_LDB(B1, 1, 1); PG8_SCHED; PG8_LDA(At, 1, 0); PG8_STAGE(PG8_SA(0, 1), a2 + hstepA, voffA);
;             PG8_WAIT_V(8); PG8_WAIT_L(0); PG8_BAR; PG8_MMA(0, 0, At, B0); PG8_MMA(0, 1, At, B1); PG8_BAR; PG8_SCHED;
	s_setprio 1
	v_mfma_i32_16x16x64_i8 v[126:129], v[152:155], v[196:199], 0
	v_mfma_i32_16x16x64_i8 v[122:125], v[160:163], v[196:199], 0
	v_mfma_i32_16x16x64_i8 v[118:121], v[152:155], v[204:207], 0
	v_mfma_i32_16x16x64_i8 v[114:117], v[160:163], v[204:207], 0
	v_mfma_i32_16x16x64_i8 v[110:113], v[152:155], v[212:215], 0
	v_mfma_i32_16x16x64_i8 v[106:109], v[160:163], v[212:215], 0
	v_mfma_i32_16x16x64_i8 v[102:105], v[152:155], v[220:223], 0
	v_mfma_i32_16x16x64_i8 v[98:101], v[160:163], v[220:223], 0
	v_mfma_i32_16x16x64_i8 v[126:129], v[156:159], v[200:203], v[126:129]
	v_mfma_i32_16x16x64_i8 v[122:125], v[164:167], v[200:203], v[122:125]
	v_mfma_i32_16x16x64_i8 v[118:121], v[156:159], v[208:211], v[118:121]
	v_mfma_i32_16x16x64_i8 v[114:117], v[164:167], v[208:211], v[114:117]
	v_mfma_i32_16x16x64_i8 v[110:113], v[156:159], v[216:219], v[110:113]
	v_mfma_i32_16x16x64_i8 v[106:109], v[164:167], v[216:219], v[106:109]
	v_mfma_i32_16x16x64_i8 v[102:105], v[156:159], v[224:227], v[102:105]
	v_mfma_i32_16x16x64_i8 v[98:101], v[164:167], v[224:227], v[98:101]
	s_setprio 0
	s_setprio 1
	v_mfma_i32_16x16x64_i8 v[94:97], v[180:183], v[196:199], 0
	v_mfma_i32_16x16x64_i8 v[86:89], v[188:191], v[196:199], 0
	v_mfma_i32_16x16x64_i8 v[78:81], v[180:183], v[204:207], 0
	v_mfma_i32_16x16x64_i8 v[70:73], v[188:191], v[204:207], 0
	v_mfma_i32_16x16x64_i8 v[62:65], v[180:183], v[212:215], 0
	v_mfma_i32_16x16x64_i8 v[54:57], v[188:191], v[212:215], 0
	v_mfma_i32_16x16x64_i8 v[46:49], v[180:183], v[220:223], 0
	v_mfma_i32_16x16x64_i8 v[38:41], v[188:191], v[220:223], 0
	v_mfma_i32_16x16x64_i8 v[94:97], v[184:187], v[200:203], v[94:97]
	v_mfma_i32_16x16x64_i8 v[86:89], v[192:195], v[200:203], v[86:89]
	v_mfma_i32_16x16x64_i8 v[78:81], v[184:187], v[208:211], v[78:81]
	v_mfma_i32_16x16x64_i8 v[70:73], v[192:195], v[208:211], v[70:73]
	v_mfma_i32_16x16x64_i8 v[62:65], v[184:187], v[216:219], v[62:65]
	v_mfma_i32_16x16x64_i8 v[54:57], v[192:195], v[216:219], v[54:57]
	v_mfma_i32_16x16x64_i8 v[46:49], v[184:187], v[224:227], v[46:49]
	v_mfma_i32_16x16x64_i8 v[38:41], v[192:195], v[224:227], v[38:41]
	s_setprio 0
	s_barrier
	s_mov_b32 m0, s45
	s_add_u32 s98, s28, 0x80
	s_addc_u32 s99, s29, 0
	s_add_u32 s72, s28, 0x40000
	ds_read_b128 v[196:199], v179 offset:16384
	ds_read_b128 v[200:203], v179 offset:17408
	ds_read_b128 v[204:207], v179 offset:18432
	ds_read_b128 v[208:211], v179 offset:19456
	global_load_lds_dwordx4 v132, s[28:29]
	s_mov_b32 m0, s46
	s_addc_u32 s73, s29, 0
	global_load_lds_dwordx4 v136, s[28:29]
	s_mov_b32 m0, s47
	ds_read_b128 v[224:227], v179 offset:23552
	global_load_lds_dwordx4 v132, s[72:73]
	s_mov_b32 m0, s48
	ds_read_b128 v[220:223], v179 offset:22528
	global_load_lds_dwordx4 v136, s[72:73]
	s_add_u32 s100, s30, 0x80
	s_addc_u32 s101, s31, 0
	s_mov_b32 m0, s49
	ds_read_b128 v[216:219], v179 offset:21504
	global_load_lds_dwordx4 v130, s[30:31]
	s_mov_b32 m0, s50
	ds_read_b128 v[212:215], v179 offset:20480
	global_load_lds_dwordx4 v134, s[30:31]
	s_waitcnt vmcnt(8) lgkmcnt(0)
	s_barrier
	s_setprio 1
	v_mfma_i32_16x16x64_i8 v[90:93], v[152:155], v[196:199], 0
	v_mfma_i32_16x16x64_i8 v[82:85], v[160:163], v[196:199], 0
	v_mfma_i32_16x16x64_i8 v[74:77], v[152:155], v[204:207], 0
	v_mfma_i32_16x16x64_i8 v[66:69], v[160:163], v[204:207], 0
	v_mfma_i32_16x16x64_i8 v[58:61], v[152:155], v[212:215], 0
	v_mfma_i32_16x16x64_i8 v[50:53], v[160:163], v[212:215], 0
	v_mfma_i32_16x16x64_i8 v[42:45], v[152:155], v[220:223], 0
	v_mfma_i32_16x16x64_i8 v[34:37], v[160:163], v[220:223], 0
	v_mfma_i32_16x16x64_i8 v[90:93], v[156:159], v[200:203], v[90:93]
	v_mfma_i32_16x16x64_i8 v[82:85], v[164:167], v[200:203], v[82:85]
	v_mfma_i32_16x16x64_i8 v[74:77], v[156:159], v[208:211], v[74:77]
	v_mfma_i32_16x16x64_i8 v[66:69], v[164:167], v[208:211], v[66:69]
	v_mfma_i32_16x16x64_i8 v[58:61], v[156:159], v[216:219], v[58:61]
	v_mfma_i32_16x16x64_i8 v[50:53], v[164:167], v[216:219], v[50:53]
	v_mfma_i32_16x16x64_i8 v[42:45], v[156:159], v[224:227], v[42:45]
	v_mfma_i32_16x16x64_i8 v[34:37], v[164:167], v[224:227], v[34:37]
	s_setprio 0
	s_setprio 1
	v_mfma_i32_16x16x64_i8 v[30:33], v[180:183], v[196:199], 0
	v_mfma_i32_16x16x64_i8 v[26:29], v[188:191], v[196:199], 0
	v_mfma_i32_16x16x64_i8 v[22:25], v[180:183], v[204:207], 0
	v_mfma_i32_16x16x64_i8 v[18:21], v[188:191], v[204:207], 0
	v_mfma_i32_16x16x64_i8 v[14:17], v[180:183], v[212:215], 0
	v_mfma_i32_16x16x64_i8 v[10:13], v[188:191], v[212:215], 0
	v_mfma_i32_16x16x64_i8 v[6:9], v[180:183], v[220:223], 0
	v_mfma_i32_16x16x64_i8 v[2:5], v[188:191], v[220:223], 0
	v_mfma_i32_16x16x64_i8 v[30:33], v[184:187], v[200:203], v[30:33]
	v_mfma_i32_16x16x64_i8 v[26:29], v[192:195], v[200:203], v[26:29]
	v_mfma_i32_16x16x64_i8 v[22:25], v[184:187], v[208:211], v[22:25]
	v_mfma_i32_16x16x64_i8 v[18:21], v[192:195], v[208:211], v[18:21]
	v_mfma_i32_16x16x64_i8 v[14:17], v[184:187], v[216:219], v[14:17]
	v_mfma_i32_16x16x64_i8 v[10:13], v[192:195], v[216:219], v[10:13]
	v_mfma_i32_16x16x64_i8 v[6:9], v[184:187], v[224:227], v[6:9]
	v_mfma_i32_16x16x64_i8 v[2:5], v[192:195], v[224:227], v[2:5]
	s_setprio 0
	s_barrier
	v_add_u32_e32 v164, s54, v170
	v_add_u32_e32 v192, s55, v170
	ds_read_b128 v[152:155], v164
	ds_read_b128 v[156:159], v164 offset:1024
	ds_read_b128 v[160:163], v164 offset:2048
	ds_read_b128 v[164:167], v164 offset:3072
	ds_read_b128 v[180:183], v192
	ds_read_b128 v[184:187], v192 offset:1024
	ds_read_b128 v[188:191], v192 offset:2048
	ds_read_b128 v[192:195], v192 offset:3072
	s_add_u32 s30, s30, 0x40000
	s_addc_u32 s31, s31, 0
	s_mov_b32 m0, s51
	ds_read_b128 v[196:199], v179 offset:32768
	ds_read_b128 v[200:203], v179 offset:33792
	ds_read_b128 v[204:207], v179 offset:34816
	ds_read_b128 v[208:211], v179 offset:35840
	ds_read_b128 v[212:215], v179 offset:36864
	ds_read_b128 v[216:219], v179 offset:37888
	ds_read_b128 v[220:223], v179 offset:38912
	global_load_lds_dwordx4 v130, s[30:31]
	s_mov_b32 m0, s52
	ds_read_b128 v[224:227], v179 offset:39936
	global_load_lds_dwordx4 v134, s[30:31]
	s_waitcnt vmcnt(8) lgkmcnt(0)
	s_barrier
; #define PG8_STAGE(bufoff, gbase, voff) do { _Pragma("unroll") for (int _i = 0; _i < 2; ++_i) \
;         __builtin_amdgcn_global_load_lds((const unsigned*)((const char*)(gbase) + (voff)[_i]), (PG8_LAS unsigned*)(lds + (bufoff) + ldsw + _i * 8192), 16, 0, 0); } while (0)
; #define PG8_LDA(dst, b, h) do { if constexpr (DT != 1) { _Pragma("unroll") for (int m = 0; m < 4; ++m) _Pragma("unroll") for (int k = 0; k < 2; ++k) dst[m][k] = *(const PG8_LAS bf16x8*)(lds + PG8_SA(b, h) + aoff + m * 2048 + k * 1024); } \
;         else { _Pragma("unroll") for (int m = 0; m < 4; ++m) dst##8[m] = ld32(lds + PG8_SA(b, h) + aoff + m * 2048); } } while (0)
; #define PG8_WAIT_V(n) asm volatile("s_waitcnt vmcnt(" #n ")" ::: "memory")
; #define PG8_WAIT_L(n) asm volatile("s_waitcnt lgkmcnt(" #n ")" ::: "memory")
; #define PG8_BAR __builtin_amdgcn_s_barrier()
; #define PG8_SCHED __builtin_amdgcn_sched_barrier(0)
;     ...
;         for (int t = 0; t < nt; t += 2) {
;     ...
;             PG8_WAIT_V(8); PG8_WAIT_L(0); PG8_BAR; PG8_MMA(0, 0, At, B0); PG8_MMA(0, 1, At, B1); PG8_BAR; PG8_SCHED;
;             PG8_LDA(At, 1, 1); PG8_STAGE(PG8_SB(1, 0), b3, voffB); PG8_STAGE(PG8_SB(1, 1), b3 + hstepB, voffB); PG8_STAGE(PG8_SA(1, 0), a3, voffA);
;             PG8_WAIT_V(8); PG8_WAIT_L(0); PG8_BAR; PG8_MMA(1, 0, At, B0); PG8_MMA(1, 1, At, B1); PG8_BAR; PG8_SCHED;
	s_setprio 1
	v_mfma_i32_16x16x64_i8 v[126:129], v[152:155], v[196:199], v[126:129]
	v_mfma_i32_16x16x64_i8 v[122:125], v[160:163], v[196:199], v[122:125]
	v_mfma_i32_16x16x64_i8 v[118:121], v[152:155], v[204:207], v[118:121]
	v_mfma_i32_16x16x64_i8 v[114:117], v[160:163], v[204:207], v[114:117]
	v_mfma_i32_16x16x64_i8 v[110:113], v[152:155], v[212:215], v[110:113]
	v_mfma_i32_16x16x64_i8 v[106:109], v[160:163], v[212:215], v[106:109]
	v_mfma_i32_16x16x64_i8 v[102:105], v[152:155], v[220:223], v[102:105]
	v_mfma_i32_16x16x64_i8 v[98:101], v[160:163], v[220:223], v[98:101]
	v_mfma_i32_16x16x64_i8 v[126:129], v[156:159], v[200:203], v[126:129]
	v_mfma_i32_16x16x64_i8 v[122:125], v[164:167], v[200:203], v[122:125]
	v_mfma_i32_16x16x64_i8 v[118:121], v[156:159], v[208:211], v[118:121]
	v_mfma_i32_16x16x64_i8 v[114:117], v[164:167], v[208:211], v[114:117]
	v_mfma_i32_16x16x64_i8 v[110:113], v[156:159], v[216:219], v[110:113]
	v_mfma_i32_16x16x64_i8 v[106:109], v[164:167], v[216:219], v[106:109]
	v_mfma_i32_16x16x64_i8 v[102:105], v[156:159], v[224:227], v[102:105]
	v_mfma_i32_16x16x64_i8 v[98:101], v[164:167], v[224:227], v[98:101]
	s_setprio 0
	s_setprio 1
	v_mfma_i32_16x16x64_i8 v[94:97], v[180:183], v[196:199], v[94:97]
	v_mfma_i32_16x16x64_i8 v[86:89], v[188:191], v[196:199], v[86:89]
	v_mfma_i32_16x16x64_i8 v[78:81], v[180:183], v[204:207], v[78:81]
	v_mfma_i32_16x16x64_i8 v[70:73], v[188:191], v[204:207], v[70:73]
	v_mfma_i32_16x16x64_i8 v[62:65], v[180:183], v[212:215], v[62:65]
	v_mfma_i32_16x16x64_i8 v[54:57], v[188:191], v[212:215], v[54:57]
	v_mfma_i32_16x16x64_i8 v[46:49], v[180:183], v[220:223], v[46:49]
	v_mfma_i32_16x16x64_i8 v[38:41], v[188:191], v[220:223], v[38:41]
	v_mfma_i32_16x16x64_i8 v[94:97], v[184:187], v[200:203], v[94:97]
	v_mfma_i32_16x16x64_i8 v[86:89], v[192:195], v[200:203], v[86:89]
	v_mfma_i32_16x16x64_i8 v[78:81], v[184:187], v[208:211], v[78:81]
	v_mfma_i32_16x16x64_i8 v[70:73], v[192:195], v[208:211], v[70:73]
	v_mfma_i32_16x16x64_i8 v[62:65], v[184:187], v[216:219], v[62:65]
	v_mfma_i32_16x16x64_i8 v[54:57], v[192:195], v[216:219], v[54:57]
	v_mfma_i32_16x16x64_i8 v[46:49], v[184:187], v[224:227], v[46:49]
	v_mfma_i32_16x16x64_i8 v[38:41], v[192:195], v[224:227], v[38:41]
	s_setprio 0
	s_barrier
	s_mov_b32 m0, s58
	s_add_u32 s28, s28, 0x40080
	ds_read_b128 v[196:199], v179 offset:49152
	ds_read_b128 v[200:203], v179 offset:50176
	ds_read_b128 v[204:207], v179 offset:51200
	ds_read_b128 v[208:211], v179 offset:52224
	global_load_lds_dwordx4 v132, s[98:99]
	s_mov_b32 m0, s59
	s_addc_u32 s29, s29, 0
	global_load_lds_dwordx4 v136, s[98:99]
	s_mov_b32 m0, s62
	ds_read_b128 v[224:227], v179 offset:56320
	global_load_lds_dwordx4 v132, s[28:29]
	s_mov_b32 m0, s63
	ds_read_b128 v[220:223], v179 offset:55296
	global_load_lds_dwordx4 v136, s[28:29]
	s_mov_b32 m0, s60
	ds_read_b128 v[216:219], v179 offset:54272
	global_load_lds_dwordx4 v130, s[100:101]
	s_mov_b32 m0, s61
	ds_read_b128 v[212:215], v179 offset:53248
	global_load_lds_dwordx4 v134, s[100:101]
	s_waitcnt vmcnt(8) lgkmcnt(0)
	s_barrier
	s_setprio 1
	v_mfma_i32_16x16x64_i8 v[90:93], v[152:155], v[196:199], v[90:93]
	v_mfma_i32_16x16x64_i8 v[82:85], v[160:163], v[196:199], v[82:85]
	v_mfma_i32_16x16x64_i8 v[74:77], v[152:155], v[204:207], v[74:77]
	v_mfma_i32_16x16x64_i8 v[66:69], v[160:163], v[204:207], v[66:69]
	v_mfma_i32_16x16x64_i8 v[58:61], v[152:155], v[212:215], v[58:61]
	v_mfma_i32_16x16x64_i8 v[50:53], v[160:163], v[212:215], v[50:53]
	v_mfma_i32_16x16x64_i8 v[42:45], v[152:155], v[220:223], v[42:45]
	v_mfma_i32_16x16x64_i8 v[34:37], v[160:163], v[220:223], v[34:37]
	v_mfma_i32_16x16x64_i8 v[90:93], v[156:159], v[200:203], v[90:93]
	v_mfma_i32_16x16x64_i8 v[82:85], v[164:167], v[200:203], v[82:85]
	v_mfma_i32_16x16x64_i8 v[74:77], v[156:159], v[208:211], v[74:77]
	v_mfma_i32_16x16x64_i8 v[66:69], v[164:167], v[208:211], v[66:69]
	v_mfma_i32_16x16x64_i8 v[58:61], v[156:159], v[216:219], v[58:61]
	v_mfma_i32_16x16x64_i8 v[50:53], v[164:167], v[216:219], v[50:53]
	v_mfma_i32_16x16x64_i8 v[42:45], v[156:159], v[224:227], v[42:45]
	v_mfma_i32_16x16x64_i8 v[34:37], v[164:167], v[224:227], v[34:37]
	s_setprio 0
	s_setprio 1
	v_mfma_i32_16x16x64_i8 v[30:33], v[180:183], v[196:199], v[30:33]
	v_mfma_i32_16x16x64_i8 v[26:29], v[188:191], v[196:199], v[26:29]
	v_mfma_i32_16x16x64_i8 v[22:25], v[180:183], v[204:207], v[22:25]
	v_mfma_i32_16x16x64_i8 v[18:21], v[188:191], v[204:207], v[18:21]
	v_mfma_i32_16x16x64_i8 v[14:17], v[180:183], v[212:215], v[14:17]
	v_mfma_i32_16x16x64_i8 v[10:13], v[188:191], v[212:215], v[10:13]
	v_mfma_i32_16x16x64_i8 v[6:9], v[180:183], v[220:223], v[6:9]
	v_mfma_i32_16x16x64_i8 v[2:5], v[188:191], v[220:223], v[2:5]
	v_mfma_i32_16x16x64_i8 v[30:33], v[184:187], v[200:203], v[30:33]
	v_mfma_i32_16x16x64_i8 v[26:29], v[192:195], v[200:203], v[26:29]
	v_mfma_i32_16x16x64_i8 v[22:25], v[184:187], v[208:211], v[22:25]
	v_mfma_i32_16x16x64_i8 v[18:21], v[192:195], v[208:211], v[18:21]
	v_mfma_i32_16x16x64_i8 v[14:17], v[184:187], v[216:219], v[14:17]
	v_mfma_i32_16x16x64_i8 v[10:13], v[192:195], v[216:219], v[10:13]
	v_mfma_i32_16x16x64_i8 v[6:9], v[184:187], v[224:227], v[6:9]
	v_mfma_i32_16x16x64_i8 v[2:5], v[192:195], v[224:227], v[2:5]
	s_setprio 0
	s_barrier
	s_add_u32 s68, s68, 0x100
	s_addc_u32 s69, s69, 0
	s_add_u32 s26, s26, 0x100
	s_addc_u32 s27, s27, 0
	s_cmp_ge_i32 s70, s57
	s_mov_b32 s28, s70
	s_cbranch_scc0 .LBB0_4350
	s_branch .Lpx_21
; #define PG8_STAGE(bufoff, gbase, voff) do { _Pragma("unroll") for (int _i = 0; _i < 2; ++_i) \
;         __builtin_amdgcn_global_load_lds((const unsigned*)((const char*)(gbase) + (voff)[_i]), (PG8_LAS unsigned*)(lds + (bufoff) + ldsw + _i * 8192), 16, 0, 0); } while (0)
; #define PG8_LDA(dst, b, h) do { if constexpr (DT != 1) { _Pragma("unroll") for (int m = 0; m < 4; ++m) _Pragma("unroll") for (int k = 0; k < 2; ++k) dst[m][k] = *(const PG8_LAS bf16x8*)(lds + PG8_SA(b, h) + aoff + m * 2048 + k * 1024); } \
;         else { _Pragma("unroll") for (int m = 0; m < 4; ++m) dst##8[m] = ld32(lds + PG8_SA(b, h) + aoff + m * 2048); } } while (0)
; #define PG8_LDB(dst, b, h) do { if constexpr (DT != 1) { _Pragma("unroll") for (int n = 0; n < 2; ++n) _Pragma("unroll") for (int k = 0; k < 2; ++k) dst[n][k] = *(const PG8_LAS bf16x8*)(lds + PG8_SB(b, h) + boff + n * 2048 + k * 1024); } \
;         else { _Pragma("unroll") for (int n = 0; n < 2; ++n) dst##8[n] = ld32(lds + PG8_SB(b, h) + boff + n * 2048); } } while (0)
; #define PG8_WAIT_V(n) asm volatile("s_waitcnt vmcnt(" #n ")" ::: "memory")
; #define PG8_WAIT_L(n) asm volatile("s_waitcnt lgkmcnt(" #n ")" ::: "memory")
; #define PG8_BAR __builtin_amdgcn_s_barrier()
; #define PG8_SCHED __builtin_amdgcn_sched_barrier(0)
;     ...
;             PG8_LDB(B0, 0, 0); PG8_LDB(B1, 0, 1); PG8_SCHED; PG8_LDA(At, 0, 0); PG8_STAGE(PG8_SA(1, 1), a1 + hstepA, voffA);
;             PG8_WAIT_V(8); PG8_WAIT_L(0); PG8_BAR; PG8_MMA(0, 0, At, B0); PG8_MMA(0, 1, At, B1); PG8_BAR; PG8_SCHED;
;             PG8_LDA(At, 0, 1); PG8_STAGE(PG8_SB(0, 0), b2, voffB); PG8_STAGE(PG8_SB(0, 1), b2 + hstepB, voffB); PG8_STAGE(PG8_SA(0, 0), a2, voffA);
;             PG8_WAIT_V(8); PG8_WAIT_L(0); PG8_BAR; PG8_MMA(1, 0, At, B0); PG8_MMA(1, 1, At, B1); PG8_BAR; PG8_SCHED;
;             PG8_LDB(B0, 1, 0); PG8_LDB(B1, 1, 1); PG8_SCHED; PG8_LDA(At, 1, 0); PG8_STAGE(PG8_SA(0, 1), a2 + hstepA, voffA);
;             PG8_WAIT_V(8); PG8_WAIT_L(0); PG8_BAR; PG8_MMA(0, 0, At, B0); PG8_MMA(0, 1, At, B1); PG8_BAR; PG8_SCHED;
.LBB0_4350:
	v_add_u32_e32 v164, s37, v170
	v_add_u32_e32 v168, s38, v170
	ds_read_b128 v[152:155], v164
	ds_read_b128 v[156:159], v164 offset:1024
	ds_read_b128 v[160:163], v164 offset:2048
	ds_read_b128 v[164:167], v164 offset:3072
	ds_read_b128 v[180:183], v168
	ds_read_b128 v[184:187], v168 offset:1024
	ds_read_b128 v[188:191], v168 offset:2048
	ds_read_b128 v[192:195], v168 offset:3072
	s_add_i32 s70, s28, 2
	s_add_u32 s29, s26, 0xfffc0080
	s_addc_u32 s30, s27, -1
	s_cmp_eq_u32 s64, s28
	s_cselect_b32 s28, s67, s68
	s_cselect_b32 s31, s17, s30
	s_cselect_b32 s30, s19, s29
	s_cselect_b32 s29, s66, s69
	s_add_i32 m0, s49, 0xc000
	ds_read_b128 v[196:199], v179
	ds_read_b128 v[200:203], v179 offset:1024
	ds_read_b128 v[204:207], v179 offset:2048
	ds_read_b128 v[208:211], v179 offset:3072
	ds_read_b128 v[212:215], v179 offset:4096
	ds_read_b128 v[216:219], v179 offset:5120
	ds_read_b128 v[220:223], v179 offset:6144
	ds_read_b128 v[224:227], v179 offset:7168
	global_load_lds_dwordx4 v146, s[26:27]
	s_add_i32 m0, s49, 0xe000
	s_nop 0
	global_load_lds_dwordx4 v144, s[26:27]
	s_waitcnt vmcnt(8) lgkmcnt(0)
	s_barrier
	s_setprio 1
	v_mfma_i32_16x16x64_i8 v[126:129], v[152:155], v[196:199], v[126:129]
	v_mfma_i32_16x16x64_i8 v[122:125], v[160:163], v[196:199], v[122:125]
	v_mfma_i32_16x16x64_i8 v[118:121], v[152:155], v[204:207], v[118:121]
	v_mfma_i32_16x16x64_i8 v[114:117], v[160:163], v[204:207], v[114:117]
	v_mfma_i32_16x16x64_i8 v[110:113], v[152:155], v[212:215], v[110:113]
	v_mfma_i32_16x16x64_i8 v[106:109], v[160:163], v[212:215], v[106:109]
	v_mfma_i32_16x16x64_i8 v[102:105], v[152:155], v[220:223], v[102:105]
	v_mfma_i32_16x16x64_i8 v[98:101], v[160:163], v[220:223], v[98:101]
	v_mfma_i32_16x16x64_i8 v[126:129], v[156:159], v[200:203], v[126:129]
	v_mfma_i32_16x16x64_i8 v[122:125], v[164:167], v[200:203], v[122:125]
	v_mfma_i32_16x16x64_i8 v[118:121], v[156:159], v[208:211], v[118:121]
	v_mfma_i32_16x16x64_i8 v[114:117], v[164:167], v[208:211], v[114:117]
	v_mfma_i32_16x16x64_i8 v[110:113], v[156:159], v[216:219], v[110:113]
	v_mfma_i32_16x16x64_i8 v[106:109], v[164:167], v[216:219], v[106:109]
	v_mfma_i32_16x16x64_i8 v[102:105], v[156:159], v[224:227], v[102:105]
	v_mfma_i32_16x16x64_i8 v[98:101], v[164:167], v[224:227], v[98:101]
	s_setprio 0
	s_setprio 1
	v_mfma_i32_16x16x64_i8 v[94:97], v[180:183], v[196:199], v[94:97]
	v_mfma_i32_16x16x64_i8 v[86:89], v[188:191], v[196:199], v[86:89]
	v_mfma_i32_16x16x64_i8 v[78:81], v[180:183], v[204:207], v[78:81]
	v_mfma_i32_16x16x64_i8 v[70:73], v[188:191], v[204:207], v[70:73]
	v_mfma_i32_16x16x64_i8 v[62:65], v[180:183], v[212:215], v[62:65]
	v_mfma_i32_16x16x64_i8 v[54:57], v[188:191], v[212:215], v[54:57]
	v_mfma_i32_16x16x64_i8 v[46:49], v[180:183], v[220:223], v[46:49]
	v_mfma_i32_16x16x64_i8 v[38:41], v[188:191], v[220:223], v[38:41]
	v_mfma_i32_16x16x64_i8 v[94:97], v[184:187], v[200:203], v[94:97]
	v_mfma_i32_16x16x64_i8 v[86:89], v[192:195], v[200:203], v[86:89]
	v_mfma_i32_16x16x64_i8 v[78:81], v[184:187], v[208:211], v[78:81]
	v_mfma_i32_16x16x64_i8 v[70:73], v[192:195], v[208:211], v[70:73]
	v_mfma_i32_16x16x64_i8 v[62:65], v[184:187], v[216:219], v[62:65]
	v_mfma_i32_16x16x64_i8 v[54:57], v[192:195], v[216:219], v[54:57]
	v_mfma_i32_16x16x64_i8 v[46:49], v[184:187], v[224:227], v[46:49]
	v_mfma_i32_16x16x64_i8 v[38:41], v[192:195], v[224:227], v[38:41]
	s_setprio 0
	s_barrier
	s_mov_b32 m0, s45
	s_add_u32 s98, s28, 0x80
	s_addc_u32 s99, s29, 0
	s_add_u32 s72, s28, 0x40000
	ds_read_b128 v[196:199], v179 offset:16384
	ds_read_b128 v[200:203], v179 offset:17408
	ds_read_b128 v[204:207], v179 offset:18432
	ds_read_b128 v[208:211], v179 offset:19456
	global_load_lds_dwordx4 v132, s[28:29]
	s_mov_b32 m0, s46
	s_addc_u32 s73, s29, 0
	global_load_lds_dwordx4 v136, s[28:29]
	s_mov_b32 m0, s47
	ds_read_b128 v[224:227], v179 offset:23552
	global_load_lds_dwordx4 v132, s[72:73]
	s_mov_b32 m0, s48
	ds_read_b128 v[220:223], v179 offset:22528
	global_load_lds_dwordx4 v136, s[72:73]
	s_add_u32 s100, s30, 0x80
	s_addc_u32 s101, s31, 0
	s_mov_b32 m0, s49
	ds_read_b128 v[216:219], v179 offset:21504
	global_load_lds_dwordx4 v130, s[30:31]
	s_mov_b32 m0, s50
	ds_read_b128 v[212:215], v179 offset:20480
	global_load_lds_dwordx4 v134, s[30:31]
	s_waitcnt vmcnt(8) lgkmcnt(0)
	s_barrier
	s_setprio 1
	v_mfma_i32_16x16x64_i8 v[90:93], v[152:155], v[196:199], v[90:93]
	v_mfma_i32_16x16x64_i8 v[82:85], v[160:163], v[196:199], v[82:85]
	v_mfma_i32_16x16x64_i8 v[74:77], v[152:155], v[204:207], v[74:77]
	v_mfma_i32_16x16x64_i8 v[66:69], v[160:163], v[204:207], v[66:69]
	v_mfma_i32_16x16x64_i8 v[58:61], v[152:155], v[212:215], v[58:61]
	v_mfma_i32_16x16x64_i8 v[50:53], v[160:163], v[212:215], v[50:53]
	v_mfma_i32_16x16x64_i8 v[42:45], v[152:155], v[220:223], v[42:45]
	v_mfma_i32_16x16x64_i8 v[34:37], v[160:163], v[220:223], v[34:37]
	v_mfma_i32_16x16x64_i8 v[90:93], v[156:159], v[200:203], v[90:93]
	v_mfma_i32_16x16x64_i8 v[82:85], v[164:167], v[200:203], v[82:85]
	v_mfma_i32_16x16x64_i8 v[74:77], v[156:159], v[208:211], v[74:77]
	v_mfma_i32_16x16x64_i8 v[66:69], v[164:167], v[208:211], v[66:69]
	v_mfma_i32_16x16x64_i8 v[58:61], v[156:159], v[216:219], v[58:61]
	v_mfma_i32_16x16x64_i8 v[50:53], v[164:167], v[216:219], v[50:53]
	v_mfma_i32_16x16x64_i8 v[42:45], v[156:159], v[224:227], v[42:45]
	v_mfma_i32_16x16x64_i8 v[34:37], v[164:167], v[224:227], v[34:37]
	s_setprio 0
	s_setprio 1
	v_mfma_i32_16x16x64_i8 v[30:33], v[180:183], v[196:199], v[30:33]
	v_mfma_i32_16x16x64_i8 v[26:29], v[188:191], v[196:199], v[26:29]
	v_mfma_i32_16x16x64_i8 v[22:25], v[180:183], v[204:207], v[22:25]
	v_mfma_i32_16x16x64_i8 v[18:21], v[188:191], v[204:207], v[18:21]
	v_mfma_i32_16x16x64_i8 v[14:17], v[180:183], v[212:215], v[14:17]
	v_mfma_i32_16x16x64_i8 v[10:13], v[188:191], v[212:215], v[10:13]
	v_mfma_i32_16x16x64_i8 v[6:9], v[180:183], v[220:223], v[6:9]
	v_mfma_i32_16x16x64_i8 v[2:5], v[188:191], v[220:223], v[2:5]
	v_mfma_i32_16x16x64_i8 v[30:33], v[184:187], v[200:203], v[30:33]
	v_mfma_i32_16x16x64_i8 v[26:29], v[192:195], v[200:203], v[26:29]
	v_mfma_i32_16x16x64_i8 v[22:25], v[184:187], v[208:211], v[22:25]
	v_mfma_i32_16x16x64_i8 v[18:21], v[192:195], v[208:211], v[18:21]
	v_mfma_i32_16x16x64_i8 v[14:17], v[184:187], v[216:219], v[14:17]
	v_mfma_i32_16x16x64_i8 v[10:13], v[192:195], v[216:219], v[10:13]
	v_mfma_i32_16x16x64_i8 v[6:9], v[184:187], v[224:227], v[6:9]
	v_mfma_i32_16x16x64_i8 v[2:5], v[192:195], v[224:227], v[2:5]
	s_setprio 0
	s_barrier
; #define PG8_STAGE(bufoff, gbase, voff) do { _Pragma("unroll") for (int _i = 0; _i < 2; ++_i) \
;         __builtin_amdgcn_global_load_lds((const unsigned*)((const char*)(gbase) + (voff)[_i]), (PG8_LAS unsigned*)(lds + (bufoff) + ldsw + _i * 8192), 16, 0, 0); } while (0)
; #define PG8_LDA(dst, b, h) do { if constexpr (DT != 1) { _Pragma("unroll") for (int m = 0; m < 4; ++m) _Pragma("unroll") for (int k = 0; k < 2; ++k) dst[m][k] = *(const PG8_LAS bf16x8*)(lds + PG8_SA(b, h) + aoff + m * 2048 + k * 1024); } \
;         else { _Pragma("unroll") for (int m = 0; m < 4; ++m) dst##8[m] = ld32(lds + PG8_SA(b, h) + aoff + m * 2048); } } while (0)
; #define PG8_LDB(dst, b, h) do { if constexpr (DT != 1) { _Pragma("unroll") for (int n = 0; n < 2; ++n) _Pragma("unroll") for (int k = 0; k < 2; ++k) dst[n][k] = *(const PG8_LAS bf16x8*)(lds + PG8_SB(b, h) + boff + n * 2048 + k * 1024); } \
;         else { _Pragma("unroll") for (int n = 0; n < 2; ++n) dst##8[n] = ld32(lds + PG8_SB(b, h) + boff + n * 2048); } } while (0)
; #define PG8_WAIT_V(n) asm volatile("s_waitcnt vmcnt(" #n ")" ::: "memory")
; #define PG8_WAIT_L(n) asm volatile("s_waitcnt lgkmcnt(" #n ")" ::: "memory")
; #define PG8_BAR __builtin_amdgcn_s_barrier()
; #define PG8_SCHED __builtin_amdgcn_sched_barrier(0)
;     ...
;             PG8_LDB(B0, 1, 0); PG8_LDB(B1, 1, 1); PG8_SCHED; PG8_LDA(At, 1, 0); PG8_STAGE(PG8_SA(0, 1), a2 + hstepA, voffA);
;             PG8_WAIT_V(8); PG8_WAIT_L(0); PG8_BAR; PG8_MMA(0, 0, At, B0); PG8_MMA(0, 1, At, B1); PG8_BAR; PG8_SCHED;
;             PG8_LDA(At, 1, 1); PG8_STAGE(PG8_SB(1, 0), b3, voffB); PG8_STAGE(PG8_SB(1, 1), b3 + hstepB, voffB); PG8_STAGE(PG8_SA(1, 0), a3, voffA);
;             PG8_WAIT_V(8); PG8_WAIT_L(0); PG8_BAR; PG8_MMA(1, 0, At, B0); PG8_MMA(1, 1, At, B1); PG8_BAR; PG8_SCHED;
	v_add_u32_e32 v164, s54, v170
	v_add_u32_e32 v192, s55, v170
	ds_read_b128 v[152:155], v164
	ds_read_b128 v[156:159], v164 offset:1024
	ds_read_b128 v[160:163], v164 offset:2048
	ds_read_b128 v[164:167], v164 offset:3072
	ds_read_b128 v[180:183], v192
	ds_read_b128 v[184:187], v192 offset:1024
	ds_read_b128 v[188:191], v192 offset:2048
	ds_read_b128 v[192:195], v192 offset:3072
	s_add_u32 s30, s30, 0x40000
	s_addc_u32 s31, s31, 0
	s_mov_b32 m0, s51
	ds_read_b128 v[196:199], v179 offset:32768
	ds_read_b128 v[200:203], v179 offset:33792
	ds_read_b128 v[204:207], v179 offset:34816
	ds_read_b128 v[208:211], v179 offset:35840
	ds_read_b128 v[212:215], v179 offset:36864
	ds_read_b128 v[216:219], v179 offset:37888
	ds_read_b128 v[220:223], v179 offset:38912
	global_load_lds_dwordx4 v130, s[30:31]
	s_mov_b32 m0, s52
	ds_read_b128 v[224:227], v179 offset:39936
	global_load_lds_dwordx4 v134, s[30:31]
	s_waitcnt vmcnt(8) lgkmcnt(0)
	s_barrier
	s_setprio 1
	v_mfma_i32_16x16x64_i8 v[126:129], v[152:155], v[196:199], v[126:129]
	v_mfma_i32_16x16x64_i8 v[122:125], v[160:163], v[196:199], v[122:125]
	v_mfma_i32_16x16x64_i8 v[118:121], v[152:155], v[204:207], v[118:121]
	v_mfma_i32_16x16x64_i8 v[114:117], v[160:163], v[204:207], v[114:117]
	v_mfma_i32_16x16x64_i8 v[110:113], v[152:155], v[212:215], v[110:113]
	v_mfma_i32_16x16x64_i8 v[106:109], v[160:163], v[212:215], v[106:109]
	v_mfma_i32_16x16x64_i8 v[102:105], v[152:155], v[220:223], v[102:105]
	v_mfma_i32_16x16x64_i8 v[98:101], v[160:163], v[220:223], v[98:101]
	v_mfma_i32_16x16x64_i8 v[126:129], v[156:159], v[200:203], v[126:129]
	v_mfma_i32_16x16x64_i8 v[122:125], v[164:167], v[200:203], v[122:125]
	v_mfma_i32_16x16x64_i8 v[118:121], v[156:159], v[208:211], v[118:121]
	v_mfma_i32_16x16x64_i8 v[114:117], v[164:167], v[208:211], v[114:117]
	v_mfma_i32_16x16x64_i8 v[110:113], v[156:159], v[216:219], v[110:113]
	v_mfma_i32_16x16x64_i8 v[106:109], v[164:167], v[216:219], v[106:109]
	v_mfma_i32_16x16x64_i8 v[102:105], v[156:159], v[224:227], v[102:105]
	v_mfma_i32_16x16x64_i8 v[98:101], v[164:167], v[224:227], v[98:101]
	s_setprio 0
	s_setprio 1
	v_mfma_i32_16x16x64_i8 v[94:97], v[180:183], v[196:199], v[94:97]
	v_mfma_i32_16x16x64_i8 v[86:89], v[188:191], v[196:199], v[86:89]
	v_mfma_i32_16x16x64_i8 v[78:81], v[180:183], v[204:207], v[78:81]
	v_mfma_i32_16x16x64_i8 v[70:73], v[188:191], v[204:207], v[70:73]
	v_mfma_i32_16x16x64_i8 v[62:65], v[180:183], v[212:215], v[62:65]
	v_mfma_i32_16x16x64_i8 v[54:57], v[188:191], v[212:215], v[54:57]
	v_mfma_i32_16x16x64_i8 v[46:49], v[180:183], v[220:223], v[46:49]
	v_mfma_i32_16x16x64_i8 v[38:41], v[188:191], v[220:223], v[38:41]
	v_mfma_i32_16x16x64_i8 v[94:97], v[184:187], v[200:203], v[94:97]
	v_mfma_i32_16x16x64_i8 v[86:89], v[192:195], v[200:203], v[86:89]
	v_mfma_i32_16x16x64_i8 v[78:81], v[184:187], v[208:211], v[78:81]
	v_mfma_i32_16x16x64_i8 v[70:73], v[192:195], v[208:211], v[70:73]
	v_mfma_i32_16x16x64_i8 v[62:65], v[184:187], v[216:219], v[62:65]
	v_mfma_i32_16x16x64_i8 v[54:57], v[192:195], v[216:219], v[54:57]
	v_mfma_i32_16x16x64_i8 v[46:49], v[184:187], v[224:227], v[46:49]
	v_mfma_i32_16x16x64_i8 v[38:41], v[192:195], v[224:227], v[38:41]
	s_setprio 0
	s_barrier
	s_mov_b32 m0, s58
	s_add_u32 s28, s28, 0x40080
	ds_read_b128 v[196:199], v179 offset:49152
	ds_read_b128 v[200:203], v179 offset:50176
	ds_read_b128 v[204:207], v179 offset:51200
	ds_read_b128 v[208:211], v179 offset:52224
	global_load_lds_dwordx4 v132, s[98:99]
	s_mov_b32 m0, s59
	s_addc_u32 s29, s29, 0
	global_load_lds_dwordx4 v136, s[98:99]
	s_mov_b32 m0, s62
	ds_read_b128 v[224:227], v179 offset:56320
	global_load_lds_dwordx4 v132, s[28:29]
	s_mov_b32 m0, s63
	ds_read_b128 v[220:223], v179 offset:55296
	global_load_lds_dwordx4 v136, s[28:29]
	s_mov_b32 m0, s60
	ds_read_b128 v[216:219], v179 offset:54272
	global_load_lds_dwordx4 v130, s[100:101]
	s_mov_b32 m0, s61
	ds_read_b128 v[212:215], v179 offset:53248
	global_load_lds_dwordx4 v134, s[100:101]
	s_waitcnt vmcnt(8) lgkmcnt(0)
	s_barrier
	s_setprio 1
	v_mfma_i32_16x16x64_i8 v[90:93], v[152:155], v[196:199], v[90:93]
	v_mfma_i32_16x16x64_i8 v[82:85], v[160:163], v[196:199], v[82:85]
	v_mfma_i32_16x16x64_i8 v[74:77], v[152:155], v[204:207], v[74:77]
	v_mfma_i32_16x16x64_i8 v[66:69], v[160:163], v[204:207], v[66:69]
	v_mfma_i32_16x16x64_i8 v[58:61], v[152:155], v[212:215], v[58:61]
	v_mfma_i32_16x16x64_i8 v[50:53], v[160:163], v[212:215], v[50:53]
	v_mfma_i32_16x16x64_i8 v[42:45], v[152:155], v[220:223], v[42:45]
	v_mfma_i32_16x16x64_i8 v[34:37], v[160:163], v[220:223], v[34:37]
	v_mfma_i32_16x16x64_i8 v[90:93], v[156:159], v[200:203], v[90:93]
	v_mfma_i32_16x16x64_i8 v[82:85], v[164:167], v[200:203], v[82:85]
	v_mfma_i32_16x16x64_i8 v[74:77], v[156:159], v[208:211], v[74:77]
	v_mfma_i32_16x16x64_i8 v[66:69], v[164:167], v[208:211], v[66:69]
	v_mfma_i32_16x16x64_i8 v[58:61], v[156:159], v[216:219], v[58:61]
	v_mfma_i32_16x16x64_i8 v[50:53], v[164:167], v[216:219], v[50:53]
	v_mfma_i32_16x16x64_i8 v[42:45], v[156:159], v[224:227], v[42:45]
	v_mfma_i32_16x16x64_i8 v[34:37], v[164:167], v[224:227], v[34:37]
	s_setprio 0
	s_setprio 1
	v_mfma_i32_16x16x64_i8 v[30:33], v[180:183], v[196:199], v[30:33]
	v_mfma_i32_16x16x64_i8 v[26:29], v[188:191], v[196:199], v[26:29]
	v_mfma_i32_16x16x64_i8 v[22:25], v[180:183], v[204:207], v[22:25]
	v_mfma_i32_16x16x64_i8 v[18:21], v[188:191], v[204:207], v[18:21]
	v_mfma_i32_16x16x64_i8 v[14:17], v[180:183], v[212:215], v[14:17]
	v_mfma_i32_16x16x64_i8 v[10:13], v[188:191], v[212:215], v[10:13]
	v_mfma_i32_16x16x64_i8 v[6:9], v[180:183], v[220:223], v[6:9]
	v_mfma_i32_16x16x64_i8 v[2:5], v[188:191], v[220:223], v[2:5]
	v_mfma_i32_16x16x64_i8 v[30:33], v[184:187], v[200:203], v[30:33]
	v_mfma_i32_16x16x64_i8 v[26:29], v[192:195], v[200:203], v[26:29]
	v_mfma_i32_16x16x64_i8 v[22:25], v[184:187], v[208:211], v[22:25]
	v_mfma_i32_16x16x64_i8 v[18:21], v[192:195], v[208:211], v[18:21]
	v_mfma_i32_16x16x64_i8 v[14:17], v[184:187], v[216:219], v[14:17]
	v_mfma_i32_16x16x64_i8 v[10:13], v[192:195], v[216:219], v[10:13]
	v_mfma_i32_16x16x64_i8 v[6:9], v[184:187], v[224:227], v[6:9]
	v_mfma_i32_16x16x64_i8 v[2:5], v[192:195], v[224:227], v[2:5]
	s_setprio 0
	s_barrier
	s_add_u32 s68, s68, 0x100
	s_addc_u32 s69, s69, 0
	s_add_u32 s26, s26, 0x100
	s_addc_u32 s27, s27, 0
	s_cmp_ge_i32 s70, s57
	s_mov_b32 s28, s70
	s_cbranch_scc0 .LBB0_4350

; #define PG8_STAGE(bufoff, gbase, voff) do { _Pragma("unroll") for (int _i = 0; _i < 2; ++_i) \
;         __builtin_amdgcn_global_load_lds((const unsigned*)((const char*)(gbase) + (voff)[_i]), (PG8_LAS unsigned*)(lds + (bufoff) + ldsw + _i * 8192), 16, 0, 0); } while (0)
; #define PG8_LDA(dst, b, h) do { if constexpr (DT != 1) { _Pragma("unroll") for (int m = 0; m < 4; ++m) _Pragma("unroll") for (int k = 0; k < 2; ++k) dst[m][k] = *(const PG8_LAS bf16x8*)(lds + PG8_SA(b, h) + aoff + m * 2048 + k * 1024); } \
;         else { _Pragma("unroll") for (int m = 0; m < 4; ++m) dst##8[m] = ld32(lds + PG8_SA(b, h) + aoff + m * 2048); } } while (0)
; #define PG8_LDB(dst, b, h) do { if constexpr (DT != 1) { _Pragma("unroll") for (int n = 0; n < 2; ++n) _Pragma("unroll") for (int k = 0; k < 2; ++k) dst[n][k] = *(const PG8_LAS bf16x8*)(lds + PG8_SB(b, h) + boff + n * 2048 + k * 1024); } \
;         else { _Pragma("unroll") for (int n = 0; n < 2; ++n) dst##8[n] = ld32(lds + PG8_SB(b, h) + boff + n * 2048); } } while (0)
; #define PG8_WAIT_V(n) asm volatile("s_waitcnt vmcnt(" #n ")" ::: "memory")
; #define PG8_WAIT_L(n) asm volatile("s_waitcnt lgkmcnt(" #n ")" ::: "memory")
; #define PG8_BAR __builtin_amdgcn_s_barrier()
; #define PG8_SCHED __builtin_amdgcn_sched_barrier(0)
;     ...
;             PG8_LDB(B0, 0, 0); PG8_LDB(B1, 0, 1); PG8_SCHED; PG8_LDA(At, 0, 0); PG8_STAGE(PG8_SA(1, 1), a1 + hstepA, voffA);
;             PG8_WAIT_V(8); PG8_WAIT_L(0); PG8_BAR; PG8_MMA(0, 0, At, B0); PG8_MMA(0, 1, At, B1); PG8_BAR; PG8_SCHED;
;             PG8_LDA(At, 0, 1); PG8_STAGE(PG8_SB(0, 0), b2, voffB); PG8_STAGE(PG8_SB(0, 1), b2 + hstepB, voffB); PG8_STAGE(PG8_SA(0, 0), a2, voffA);
;             PG8_WAIT_V(8); PG8_WAIT_L(0); PG8_BAR; PG8_MMA(1, 0, At, B0); PG8_MMA(1, 1, At, B1); PG8_BAR; PG8_SCHED;
.Lzs_15:
	s_cbranch_vccnz .LBB0_4647
	s_and_b64 s[40:41], s[0:1], exec
	s_cselect_b32 s25, s29, s39
	s_cselect_b32 s27, s28, s38
	s_cselect_b32 s67, s31, s37
	s_cselect_b32 s68, s30, s36
	s_add_u32 s69, s36, 0x100
	s_addc_u32 s70, s37, 0
	s_add_u32 s36, s38, 0x80080
	s_addc_u32 s37, s39, 0
	s_mov_b32 s38, 0
	ds_read_b128 v[146:149], v157
	ds_read_b128 v[150:153], v157 offset:1024
	ds_read_b128 v[162:165], v157 offset:2048
	ds_read_b128 v[166:169], v157 offset:3072
	ds_read_b128 v[170:173], v158
	ds_read_b128 v[174:177], v158 offset:1024
	ds_read_b128 v[178:181], v158 offset:2048
	ds_read_b128 v[182:185], v158 offset:3072
	s_add_i32 s71, s38, 2
	s_add_u32 s39, s36, 0xfff80080
	s_addc_u32 s40, s37, -1
	s_cmp_eq_u32 s63, s38
	s_cselect_b32 s38, s68, s69
	s_cselect_b32 s41, s25, s40
	s_cselect_b32 s40, s27, s39
	s_cselect_b32 s39, s67, s70
	s_add_i32 m0, s51, 0xc000
	ds_read_b128 v[186:189], v159
	ds_read_b128 v[190:193], v159 offset:1024
	ds_read_b128 v[194:197], v159 offset:2048
	ds_read_b128 v[198:201], v159 offset:3072
	ds_read_b128 v[202:205], v159 offset:4096
	ds_read_b128 v[206:209], v159 offset:5120
	ds_read_b128 v[210:213], v159 offset:6144
	ds_read_b128 v[214:217], v159 offset:7168
	global_load_lds_dwordx4 v140, s[36:37]
	s_add_i32 m0, s51, 0xe000
	s_nop 0
	global_load_lds_dwordx4 v138, s[36:37]
	s_waitcnt vmcnt(8) lgkmcnt(0)
	s_barrier
	s_setprio 1
	v_mfma_f32_16x16x32_bf16 v[122:125], v[146:149], v[186:189], 0
	v_mfma_f32_16x16x32_bf16 v[126:129], v[162:165], v[186:189], 0
	v_mfma_f32_16x16x32_bf16 v[110:113], v[146:149], v[194:197], 0
	v_mfma_f32_16x16x32_bf16 v[106:109], v[162:165], v[194:197], 0
	v_mfma_f32_16x16x32_bf16 v[94:97], v[146:149], v[202:205], 0
	v_mfma_f32_16x16x32_bf16 v[90:93], v[162:165], v[202:205], 0
	v_mfma_f32_16x16x32_bf16 v[78:81], v[146:149], v[210:213], 0
	v_mfma_f32_16x16x32_bf16 v[74:77], v[162:165], v[210:213], 0
	v_mfma_f32_16x16x32_bf16 v[122:125], v[150:153], v[190:193], v[122:125]
	v_mfma_f32_16x16x32_bf16 v[126:129], v[166:169], v[190:193], v[126:129]
	v_mfma_f32_16x16x32_bf16 v[110:113], v[150:153], v[198:201], v[110:113]
	v_mfma_f32_16x16x32_bf16 v[106:109], v[166:169], v[198:201], v[106:109]
	v_mfma_f32_16x16x32_bf16 v[94:97], v[150:153], v[206:209], v[94:97]
	v_mfma_f32_16x16x32_bf16 v[90:93], v[166:169], v[206:209], v[90:93]
	v_mfma_f32_16x16x32_bf16 v[78:81], v[150:153], v[214:217], v[78:81]
	v_mfma_f32_16x16x32_bf16 v[74:77], v[166:169], v[214:217], v[74:77]
	s_setprio 0
	s_setprio 1
	v_mfma_f32_16x16x32_bf16 v[118:121], v[170:173], v[186:189], 0
	v_mfma_f32_16x16x32_bf16 v[114:117], v[178:181], v[186:189], 0
	v_mfma_f32_16x16x32_bf16 v[102:105], v[170:173], v[194:197], 0
	v_mfma_f32_16x16x32_bf16 v[98:101], v[178:181], v[194:197], 0
	v_mfma_f32_16x16x32_bf16 v[86:89], v[170:173], v[202:205], 0
	v_mfma_f32_16x16x32_bf16 v[82:85], v[178:181], v[202:205], 0
	v_mfma_f32_16x16x32_bf16 v[70:73], v[170:173], v[210:213], 0
	v_mfma_f32_16x16x32_bf16 v[66:69], v[178:181], v[210:213], 0
	v_mfma_f32_16x16x32_bf16 v[118:121], v[174:177], v[190:193], v[118:121]
	v_mfma_f32_16x16x32_bf16 v[114:117], v[182:185], v[190:193], v[114:117]
	v_mfma_f32_16x16x32_bf16 v[102:105], v[174:177], v[198:201], v[102:105]
	v_mfma_f32_16x16x32_bf16 v[98:101], v[182:185], v[198:201], v[98:101]
	v_mfma_f32_16x16x32_bf16 v[86:89], v[174:177], v[206:209], v[86:89]
	v_mfma_f32_16x16x32_bf16 v[82:85], v[182:185], v[206:209], v[82:85]
	v_mfma_f32_16x16x32_bf16 v[70:73], v[174:177], v[214:217], v[70:73]
	v_mfma_f32_16x16x32_bf16 v[66:69], v[182:185], v[214:217], v[66:69]
	s_setprio 0
	s_barrier
	s_mov_b32 m0, s35
	s_add_u32 s98, s38, 0x80
	s_addc_u32 s99, s39, 0
	s_add_u32 s72, s38, 0x80000
	ds_read_b128 v[186:189], v159 offset:16384
	ds_read_b128 v[190:193], v159 offset:17408
	ds_read_b128 v[194:197], v159 offset:18432
	ds_read_b128 v[198:201], v159 offset:19456
	global_load_lds_dwordx4 v132, s[38:39]
	s_mov_b32 m0, s48
	s_addc_u32 s73, s39, 0
	global_load_lds_dwordx4 v136, s[38:39]
	s_mov_b32 m0, s49
	ds_read_b128 v[214:217], v159 offset:23552
	global_load_lds_dwordx4 v132, s[72:73]
	s_mov_b32 m0, s50
	ds_read_b128 v[210:213], v159 offset:22528
	global_load_lds_dwordx4 v136, s[72:73]
	s_add_u32 s100, s40, 0x80
	s_addc_u32 s101, s41, 0
	s_mov_b32 m0, s51
	ds_read_b128 v[206:209], v159 offset:21504
	global_load_lds_dwordx4 v130, s[40:41]
	s_mov_b32 m0, s52
	ds_read_b128 v[202:205], v159 offset:20480
	global_load_lds_dwordx4 v134, s[40:41]
	s_waitcnt vmcnt(8) lgkmcnt(0)
	s_barrier
	s_setprio 1
	v_mfma_f32_16x16x32_bf16 v[62:65], v[146:149], v[186:189], 0
	v_mfma_f32_16x16x32_bf16 v[58:61], v[162:165], v[186:189], 0
	v_mfma_f32_16x16x32_bf16 v[46:49], v[146:149], v[194:197], 0
	v_mfma_f32_16x16x32_bf16 v[42:45], v[162:165], v[194:197], 0
	v_mfma_f32_16x16x32_bf16 v[30:33], v[146:149], v[202:205], 0
	v_mfma_f32_16x16x32_bf16 v[26:29], v[162:165], v[202:205], 0
	v_mfma_f32_16x16x32_bf16 v[14:17], v[146:149], v[210:213], 0
	v_mfma_f32_16x16x32_bf16 v[10:13], v[162:165], v[210:213], 0
	v_mfma_f32_16x16x32_bf16 v[62:65], v[150:153], v[190:193], v[62:65]
	v_mfma_f32_16x16x32_bf16 v[58:61], v[166:169], v[190:193], v[58:61]
	v_mfma_f32_16x16x32_bf16 v[46:49], v[150:153], v[198:201], v[46:49]
	v_mfma_f32_16x16x32_bf16 v[42:45], v[166:169], v[198:201], v[42:45]
	v_mfma_f32_16x16x32_bf16 v[30:33], v[150:153], v[206:209], v[30:33]
	v_mfma_f32_16x16x32_bf16 v[26:29], v[166:169], v[206:209], v[26:29]
	v_mfma_f32_16x16x32_bf16 v[14:17], v[150:153], v[214:217], v[14:17]
	v_mfma_f32_16x16x32_bf16 v[10:13], v[166:169], v[214:217], v[10:13]
	s_setprio 0
	s_setprio 1
	v_mfma_f32_16x16x32_bf16 v[54:57], v[170:173], v[186:189], 0
	v_mfma_f32_16x16x32_bf16 v[50:53], v[178:181], v[186:189], 0
	v_mfma_f32_16x16x32_bf16 v[38:41], v[170:173], v[194:197], 0
	v_mfma_f32_16x16x32_bf16 v[34:37], v[178:181], v[194:197], 0
	v_mfma_f32_16x16x32_bf16 v[22:25], v[170:173], v[202:205], 0
	v_mfma_f32_16x16x32_bf16 v[18:21], v[178:181], v[202:205], 0
	v_mfma_f32_16x16x32_bf16 v[6:9], v[170:173], v[210:213], 0
	v_mfma_f32_16x16x32_bf16 v[2:5], v[178:181], v[210:213], 0
	v_mfma_f32_16x16x32_bf16 v[54:57], v[174:177], v[190:193], v[54:57]
	v_mfma_f32_16x16x32_bf16 v[50:53], v[182:185], v[190:193], v[50:53]
	v_mfma_f32_16x16x32_bf16 v[38:41], v[174:177], v[198:201], v[38:41]
	v_mfma_f32_16x16x32_bf16 v[34:37], v[182:185], v[198:201], v[34:37]
	v_mfma_f32_16x16x32_bf16 v[22:25], v[174:177], v[206:209], v[22:25]
	v_mfma_f32_16x16x32_bf16 v[18:21], v[182:185], v[206:209], v[18:21]
	v_mfma_f32_16x16x32_bf16 v[6:9], v[174:177], v[214:217], v[6:9]
	v_mfma_f32_16x16x32_bf16 v[2:5], v[182:185], v[214:217], v[2:5]
	s_setprio 0
	s_barrier
; #define PG8_STAGE(bufoff, gbase, voff) do { _Pragma("unroll") for (int _i = 0; _i < 2; ++_i) \
;         __builtin_amdgcn_global_load_lds((const unsigned*)((const char*)(gbase) + (voff)[_i]), (PG8_LAS unsigned*)(lds + (bufoff) + ldsw + _i * 8192), 16, 0, 0); } while (0)
; #define PG8_LDA(dst, b, h) do { if constexpr (DT != 1) { _Pragma("unroll") for (int m = 0; m < 4; ++m) _Pragma("unroll") for (int k = 0; k < 2; ++k) dst[m][k] = *(const PG8_LAS bf16x8*)(lds + PG8_SA(b, h) + aoff + m * 2048 + k * 1024); } \
;         else { _Pragma("unroll") for (int m = 0; m < 4; ++m) dst##8[m] = ld32(lds + PG8_SA(b, h) + aoff + m * 2048); } } while (0)
; #define PG8_LDB(dst, b, h) do { if constexpr (DT != 1) { _Pragma("unroll") for (int n = 0; n < 2; ++n) _Pragma("unroll") for (int k = 0; k < 2; ++k) dst[n][k] = *(const PG8_LAS bf16x8*)(lds + PG8_SB(b, h) + boff + n * 2048 + k * 1024); } \
;         else { _Pragma("unroll") for (int n = 0; n < 2; ++n) dst##8[n] = ld32(lds + PG8_SB(b, h) + boff + n * 2048); } } while (0)
; #define PG8_WAIT_V(n) asm volatile("s_waitcnt vmcnt(" #n ")" ::: "memory")
; #define PG8_WAIT_L(n) asm volatile("s_waitcnt lgkmcnt(" #n ")" ::: "memory")
; #define PG8_BAR __builtin_amdgcn_s_barrier()
; #define PG8_SCHED __builtin_amdgcn_sched_barrier(0)
;     ...
;         for (int t = 0; t < nt; t += 2) {
;     ...
;             PG8_LDB(B0, 1, 0); PG8_LDB(B1, 1, 1); PG8_SCHED; PG8_LDA(At, 1, 0); PG8_STAGE(PG8_SA(0, 1), a2 + hstepA, voffA);
;             PG8_WAIT_V(8); PG8_WAIT_L(0); PG8_BAR; PG8_MMA(0, 0, At, B0); PG8_MMA(0, 1, At, B1); PG8_BAR; PG8_SCHED;
;             PG8_LDA(At, 1, 1); PG8_STAGE(PG8_SB(1, 0), b3, voffB); PG8_STAGE(PG8_SB(1, 1), b3 + hstepB, voffB); PG8_STAGE(PG8_SA(1, 0), a3, voffA);
;             PG8_WAIT_V(8); PG8_WAIT_L(0); PG8_BAR; PG8_MMA(1, 0, At, B0); PG8_MMA(1, 1, At, B1); PG8_BAR; PG8_SCHED;
	ds_read_b128 v[146:149], v160
	ds_read_b128 v[150:153], v160 offset:1024
	ds_read_b128 v[162:165], v160 offset:2048
	ds_read_b128 v[166:169], v160 offset:3072
	ds_read_b128 v[170:173], v161
	ds_read_b128 v[174:177], v161 offset:1024
	ds_read_b128 v[178:181], v161 offset:2048
	ds_read_b128 v[182:185], v161 offset:3072
	s_add_u32 s40, s40, 0x80000
	s_addc_u32 s41, s41, 0
	s_mov_b32 m0, s53
	ds_read_b128 v[186:189], v159 offset:32768
	ds_read_b128 v[190:193], v159 offset:33792
	ds_read_b128 v[194:197], v159 offset:34816
	ds_read_b128 v[198:201], v159 offset:35840
	ds_read_b128 v[202:205], v159 offset:36864
	ds_read_b128 v[206:209], v159 offset:37888
	ds_read_b128 v[210:213], v159 offset:38912
	global_load_lds_dwordx4 v130, s[40:41]
	s_mov_b32 m0, s54
	ds_read_b128 v[214:217], v159 offset:39936
	global_load_lds_dwordx4 v134, s[40:41]
	s_waitcnt vmcnt(8) lgkmcnt(0)
	s_barrier
	s_setprio 1
	v_mfma_f32_16x16x32_bf16 v[122:125], v[146:149], v[186:189], v[122:125]
	v_mfma_f32_16x16x32_bf16 v[126:129], v[162:165], v[186:189], v[126:129]
	v_mfma_f32_16x16x32_bf16 v[110:113], v[146:149], v[194:197], v[110:113]
	v_mfma_f32_16x16x32_bf16 v[106:109], v[162:165], v[194:197], v[106:109]
	v_mfma_f32_16x16x32_bf16 v[94:97], v[146:149], v[202:205], v[94:97]
	v_mfma_f32_16x16x32_bf16 v[90:93], v[162:165], v[202:205], v[90:93]
	v_mfma_f32_16x16x32_bf16 v[78:81], v[146:149], v[210:213], v[78:81]
	v_mfma_f32_16x16x32_bf16 v[74:77], v[162:165], v[210:213], v[74:77]
	v_mfma_f32_16x16x32_bf16 v[122:125], v[150:153], v[190:193], v[122:125]
	v_mfma_f32_16x16x32_bf16 v[126:129], v[166:169], v[190:193], v[126:129]
	v_mfma_f32_16x16x32_bf16 v[110:113], v[150:153], v[198:201], v[110:113]
	v_mfma_f32_16x16x32_bf16 v[106:109], v[166:169], v[198:201], v[106:109]
	v_mfma_f32_16x16x32_bf16 v[94:97], v[150:153], v[206:209], v[94:97]
	v_mfma_f32_16x16x32_bf16 v[90:93], v[166:169], v[206:209], v[90:93]
	v_mfma_f32_16x16x32_bf16 v[78:81], v[150:153], v[214:217], v[78:81]
	v_mfma_f32_16x16x32_bf16 v[74:77], v[166:169], v[214:217], v[74:77]
	s_setprio 0
	s_setprio 1
	v_mfma_f32_16x16x32_bf16 v[118:121], v[170:173], v[186:189], v[118:121]
	v_mfma_f32_16x16x32_bf16 v[114:117], v[178:181], v[186:189], v[114:117]
	v_mfma_f32_16x16x32_bf16 v[102:105], v[170:173], v[194:197], v[102:105]
	v_mfma_f32_16x16x32_bf16 v[98:101], v[178:181], v[194:197], v[98:101]
	v_mfma_f32_16x16x32_bf16 v[86:89], v[170:173], v[202:205], v[86:89]
	v_mfma_f32_16x16x32_bf16 v[82:85], v[178:181], v[202:205], v[82:85]
	v_mfma_f32_16x16x32_bf16 v[70:73], v[170:173], v[210:213], v[70:73]
	v_mfma_f32_16x16x32_bf16 v[66:69], v[178:181], v[210:213], v[66:69]
	v_mfma_f32_16x16x32_bf16 v[118:121], v[174:177], v[190:193], v[118:121]
	v_mfma_f32_16x16x32_bf16 v[114:117], v[182:185], v[190:193], v[114:117]
	v_mfma_f32_16x16x32_bf16 v[102:105], v[174:177], v[198:201], v[102:105]
	v_mfma_f32_16x16x32_bf16 v[98:101], v[182:185], v[198:201], v[98:101]
	v_mfma_f32_16x16x32_bf16 v[86:89], v[174:177], v[206:209], v[86:89]
	v_mfma_f32_16x16x32_bf16 v[82:85], v[182:185], v[206:209], v[82:85]
	v_mfma_f32_16x16x32_bf16 v[70:73], v[174:177], v[214:217], v[70:73]
	v_mfma_f32_16x16x32_bf16 v[66:69], v[182:185], v[214:217], v[66:69]
	s_setprio 0
	s_barrier
	s_mov_b32 m0, s57
	s_add_u32 s38, s38, 0x80080
	ds_read_b128 v[186:189], v159 offset:49152
	ds_read_b128 v[190:193], v159 offset:50176
	ds_read_b128 v[194:197], v159 offset:51200
	ds_read_b128 v[198:201], v159 offset:52224
	global_load_lds_dwordx4 v132, s[98:99]
	s_mov_b32 m0, s58
	s_addc_u32 s39, s39, 0
	global_load_lds_dwordx4 v136, s[98:99]
	s_mov_b32 m0, s61
	ds_read_b128 v[214:217], v159 offset:56320
	global_load_lds_dwordx4 v132, s[38:39]
	s_mov_b32 m0, s62
	ds_read_b128 v[210:213], v159 offset:55296
	global_load_lds_dwordx4 v136, s[38:39]
	s_mov_b32 m0, s59
	ds_read_b128 v[206:209], v159 offset:54272
	global_load_lds_dwordx4 v130, s[100:101]
	s_mov_b32 m0, s60
	ds_read_b128 v[202:205], v159 offset:53248
	global_load_lds_dwordx4 v134, s[100:101]
	s_waitcnt vmcnt(8) lgkmcnt(0)
	s_barrier
	s_setprio 1
	v_mfma_f32_16x16x32_bf16 v[62:65], v[146:149], v[186:189], v[62:65]
	v_mfma_f32_16x16x32_bf16 v[58:61], v[162:165], v[186:189], v[58:61]
	v_mfma_f32_16x16x32_bf16 v[46:49], v[146:149], v[194:197], v[46:49]
	v_mfma_f32_16x16x32_bf16 v[42:45], v[162:165], v[194:197], v[42:45]
	v_mfma_f32_16x16x32_bf16 v[30:33], v[146:149], v[202:205], v[30:33]
	v_mfma_f32_16x16x32_bf16 v[26:29], v[162:165], v[202:205], v[26:29]
	v_mfma_f32_16x16x32_bf16 v[14:17], v[146:149], v[210:213], v[14:17]
	v_mfma_f32_16x16x32_bf16 v[10:13], v[162:165], v[210:213], v[10:13]
	v_mfma_f32_16x16x32_bf16 v[62:65], v[150:153], v[190:193], v[62:65]
	v_mfma_f32_16x16x32_bf16 v[58:61], v[166:169], v[190:193], v[58:61]
	v_mfma_f32_16x16x32_bf16 v[46:49], v[150:153], v[198:201], v[46:49]
	v_mfma_f32_16x16x32_bf16 v[42:45], v[166:169], v[198:201], v[42:45]
	v_mfma_f32_16x16x32_bf16 v[30:33], v[150:153], v[206:209], v[30:33]
	v_mfma_f32_16x16x32_bf16 v[26:29], v[166:169], v[206:209], v[26:29]
	v_mfma_f32_16x16x32_bf16 v[14:17], v[150:153], v[214:217], v[14:17]
	v_mfma_f32_16x16x32_bf16 v[10:13], v[166:169], v[214:217], v[10:13]
	s_setprio 0
	s_setprio 1
	v_mfma_f32_16x16x32_bf16 v[54:57], v[170:173], v[186:189], v[54:57]
	v_mfma_f32_16x16x32_bf16 v[50:53], v[178:181], v[186:189], v[50:53]
	v_mfma_f32_16x16x32_bf16 v[38:41], v[170:173], v[194:197], v[38:41]
	v_mfma_f32_16x16x32_bf16 v[34:37], v[178:181], v[194:197], v[34:37]
	v_mfma_f32_16x16x32_bf16 v[22:25], v[170:173], v[202:205], v[22:25]
	v_mfma_f32_16x16x32_bf16 v[18:21], v[178:181], v[202:205], v[18:21]
	v_mfma_f32_16x16x32_bf16 v[6:9], v[170:173], v[210:213], v[6:9]
	v_mfma_f32_16x16x32_bf16 v[2:5], v[178:181], v[210:213], v[2:5]
	v_mfma_f32_16x16x32_bf16 v[54:57], v[174:177], v[190:193], v[54:57]
	v_mfma_f32_16x16x32_bf16 v[50:53], v[182:185], v[190:193], v[50:53]
	v_mfma_f32_16x16x32_bf16 v[38:41], v[174:177], v[198:201], v[38:41]
	v_mfma_f32_16x16x32_bf16 v[34:37], v[182:185], v[198:201], v[34:37]
	v_mfma_f32_16x16x32_bf16 v[22:25], v[174:177], v[206:209], v[22:25]
	v_mfma_f32_16x16x32_bf16 v[18:21], v[182:185], v[206:209], v[18:21]
	v_mfma_f32_16x16x32_bf16 v[6:9], v[174:177], v[214:217], v[6:9]
	v_mfma_f32_16x16x32_bf16 v[2:5], v[182:185], v[214:217], v[2:5]
	s_setprio 0
	s_barrier
	s_add_u32 s69, s69, 0x100
	s_addc_u32 s70, s70, 0
	s_add_u32 s36, s36, 0x100
	s_addc_u32 s37, s37, 0
	s_cmp_ge_i32 s71, s56
	s_mov_b32 s38, s71
	s_cbranch_scc0 .LBB0_4646
	s_branch .LBB0_4647
; #define PG8_STAGE(bufoff, gbase, voff) do { _Pragma("unroll") for (int _i = 0; _i < 2; ++_i) \
;         __builtin_amdgcn_global_load_lds((const unsigned*)((const char*)(gbase) + (voff)[_i]), (PG8_LAS unsigned*)(lds + (bufoff) + ldsw + _i * 8192), 16, 0, 0); } while (0)
; #define PG8_LDA(dst, b, h) do { if constexpr (DT != 1) { _Pragma("unroll") for (int m = 0; m < 4; ++m) _Pragma("unroll") for (int k = 0; k < 2; ++k) dst[m][k] = *(const PG8_LAS bf16x8*)(lds + PG8_SA(b, h) + aoff + m * 2048 + k * 1024); } \
;         else { _Pragma("unroll") for (int m = 0; m < 4; ++m) dst##8[m] = ld32(lds + PG8_SA(b, h) + aoff + m * 2048); } } while (0)
; #define PG8_LDB(dst, b, h) do { if constexpr (DT != 1) { _Pragma("unroll") for (int n = 0; n < 2; ++n) _Pragma("unroll") for (int k = 0; k < 2; ++k) dst[n][k] = *(const PG8_LAS bf16x8*)(lds + PG8_SB(b, h) + boff + n * 2048 + k * 1024); } \
;         else { _Pragma("unroll") for (int n = 0; n < 2; ++n) dst##8[n] = ld32(lds + PG8_SB(b, h) + boff + n * 2048); } } while (0)
; #define PG8_WAIT_V(n) asm volatile("s_waitcnt vmcnt(" #n ")" ::: "memory")
; #define PG8_WAIT_L(n) asm volatile("s_waitcnt lgkmcnt(" #n ")" ::: "memory")
; #define PG8_BAR __builtin_amdgcn_s_barrier()
; #define PG8_SCHED __builtin_amdgcn_sched_barrier(0)
;     ...
;             PG8_LDB(B0, 0, 0); PG8_LDB(B1, 0, 1); PG8_SCHED; PG8_LDA(At, 0, 0); PG8_STAGE(PG8_SA(1, 1), a1 + hstepA, voffA);
;             PG8_WAIT_V(8); PG8_WAIT_L(0); PG8_BAR; PG8_MMA(0, 0, At, B0); PG8_MMA(0, 1, At, B1); PG8_BAR; PG8_SCHED;
;             PG8_LDA(At, 0, 1); PG8_STAGE(PG8_SB(0, 0), b2, voffB); PG8_STAGE(PG8_SB(0, 1), b2 + hstepB, voffB); PG8_STAGE(PG8_SA(0, 0), a2, voffA);
;             PG8_WAIT_V(8); PG8_WAIT_L(0); PG8_BAR; PG8_MMA(1, 0, At, B0); PG8_MMA(1, 1, At, B1); PG8_BAR; PG8_SCHED;
.LBB0_4646:
	ds_read_b128 v[146:149], v157
	ds_read_b128 v[150:153], v157 offset:1024
	ds_read_b128 v[162:165], v157 offset:2048
	ds_read_b128 v[166:169], v157 offset:3072
	ds_read_b128 v[170:173], v158
	ds_read_b128 v[174:177], v158 offset:1024
	ds_read_b128 v[178:181], v158 offset:2048
	ds_read_b128 v[182:185], v158 offset:3072
	s_add_i32 s71, s38, 2
	s_add_u32 s39, s36, 0xfff80080
	s_addc_u32 s40, s37, -1
	s_cmp_eq_u32 s63, s38
	s_cselect_b32 s38, s68, s69
	s_cselect_b32 s41, s25, s40
	s_cselect_b32 s40, s27, s39
	s_cselect_b32 s39, s67, s70
	s_add_i32 m0, s51, 0xc000
	ds_read_b128 v[186:189], v159
	ds_read_b128 v[190:193], v159 offset:1024
	ds_read_b128 v[194:197], v159 offset:2048
	ds_read_b128 v[198:201], v159 offset:3072
	ds_read_b128 v[202:205], v159 offset:4096
	ds_read_b128 v[206:209], v159 offset:5120
	ds_read_b128 v[210:213], v159 offset:6144
	ds_read_b128 v[214:217], v159 offset:7168
	global_load_lds_dwordx4 v140, s[36:37]
	s_add_i32 m0, s51, 0xe000
	s_nop 0
	global_load_lds_dwordx4 v138, s[36:37]
	s_waitcnt vmcnt(8) lgkmcnt(0)
	s_barrier
	s_setprio 1
	v_mfma_f32_16x16x32_bf16 v[122:125], v[146:149], v[186:189], v[122:125]
	v_mfma_f32_16x16x32_bf16 v[126:129], v[162:165], v[186:189], v[126:129]
	v_mfma_f32_16x16x32_bf16 v[110:113], v[146:149], v[194:197], v[110:113]
	v_mfma_f32_16x16x32_bf16 v[106:109], v[162:165], v[194:197], v[106:109]
	v_mfma_f32_16x16x32_bf16 v[94:97], v[146:149], v[202:205], v[94:97]
	v_mfma_f32_16x16x32_bf16 v[90:93], v[162:165], v[202:205], v[90:93]
	v_mfma_f32_16x16x32_bf16 v[78:81], v[146:149], v[210:213], v[78:81]
	v_mfma_f32_16x16x32_bf16 v[74:77], v[162:165], v[210:213], v[74:77]
	v_mfma_f32_16x16x32_bf16 v[122:125], v[150:153], v[190:193], v[122:125]
	v_mfma_f32_16x16x32_bf16 v[126:129], v[166:169], v[190:193], v[126:129]
	v_mfma_f32_16x16x32_bf16 v[110:113], v[150:153], v[198:201], v[110:113]
	v_mfma_f32_16x16x32_bf16 v[106:109], v[166:169], v[198:201], v[106:109]
	v_mfma_f32_16x16x32_bf16 v[94:97], v[150:153], v[206:209], v[94:97]
	v_mfma_f32_16x16x32_bf16 v[90:93], v[166:169], v[206:209], v[90:93]
	v_mfma_f32_16x16x32_bf16 v[78:81], v[150:153], v[214:217], v[78:81]
	v_mfma_f32_16x16x32_bf16 v[74:77], v[166:169], v[214:217], v[74:77]
	s_setprio 0
	s_setprio 1
	v_mfma_f32_16x16x32_bf16 v[118:121], v[170:173], v[186:189], v[118:121]
	v_mfma_f32_16x16x32_bf16 v[114:117], v[178:181], v[186:189], v[114:117]
	v_mfma_f32_16x16x32_bf16 v[102:105], v[170:173], v[194:197], v[102:105]
	v_mfma_f32_16x16x32_bf16 v[98:101], v[178:181], v[194:197], v[98:101]
	v_mfma_f32_16x16x32_bf16 v[86:89], v[170:173], v[202:205], v[86:89]
	v_mfma_f32_16x16x32_bf16 v[82:85], v[178:181], v[202:205], v[82:85]
	v_mfma_f32_16x16x32_bf16 v[70:73], v[170:173], v[210:213], v[70:73]
	v_mfma_f32_16x16x32_bf16 v[66:69], v[178:181], v[210:213], v[66:69]
	v_mfma_f32_16x16x32_bf16 v[118:121], v[174:177], v[190:193], v[118:121]
	v_mfma_f32_16x16x32_bf16 v[114:117], v[182:185], v[190:193], v[114:117]
	v_mfma_f32_16x16x32_bf16 v[102:105], v[174:177], v[198:201], v[102:105]
	v_mfma_f32_16x16x32_bf16 v[98:101], v[182:185], v[198:201], v[98:101]
	v_mfma_f32_16x16x32_bf16 v[86:89], v[174:177], v[206:209], v[86:89]
	v_mfma_f32_16x16x32_bf16 v[82:85], v[182:185], v[206:209], v[82:85]
	v_mfma_f32_16x16x32_bf16 v[70:73], v[174:177], v[214:217], v[70:73]
	v_mfma_f32_16x16x32_bf16 v[66:69], v[182:185], v[214:217], v[66:69]
	s_setprio 0
	s_barrier
	s_mov_b32 m0, s35
	s_add_u32 s98, s38, 0x80
	s_addc_u32 s99, s39, 0
	s_add_u32 s72, s38, 0x80000
	ds_read_b128 v[186:189], v159 offset:16384
	ds_read_b128 v[190:193], v159 offset:17408
	ds_read_b128 v[194:197], v159 offset:18432
	ds_read_b128 v[198:201], v159 offset:19456
	global_load_lds_dwordx4 v132, s[38:39]
	s_mov_b32 m0, s48
	s_addc_u32 s73, s39, 0
	global_load_lds_dwordx4 v136, s[38:39]
	s_mov_b32 m0, s49
	ds_read_b128 v[214:217], v159 offset:23552
	global_load_lds_dwordx4 v132, s[72:73]
	s_mov_b32 m0, s50
	ds_read_b128 v[210:213], v159 offset:22528
	global_load_lds_dwordx4 v136, s[72:73]
	s_add_u32 s100, s40, 0x80
	s_addc_u32 s101, s41, 0
	s_mov_b32 m0, s51
	ds_read_b128 v[206:209], v159 offset:21504
	global_load_lds_dwordx4 v130, s[40:41]
	s_mov_b32 m0, s52
	ds_read_b128 v[202:205], v159 offset:20480
	global_load_lds_dwordx4 v134, s[40:41]
	s_waitcnt vmcnt(8) lgkmcnt(0)
	s_barrier
	s_setprio 1
	v_mfma_f32_16x16x32_bf16 v[62:65], v[146:149], v[186:189], v[62:65]
	v_mfma_f32_16x16x32_bf16 v[58:61], v[162:165], v[186:189], v[58:61]
	v_mfma_f32_16x16x32_bf16 v[46:49], v[146:149], v[194:197], v[46:49]
	v_mfma_f32_16x16x32_bf16 v[42:45], v[162:165], v[194:197], v[42:45]
	v_mfma_f32_16x16x32_bf16 v[30:33], v[146:149], v[202:205], v[30:33]
	v_mfma_f32_16x16x32_bf16 v[26:29], v[162:165], v[202:205], v[26:29]
	v_mfma_f32_16x16x32_bf16 v[14:17], v[146:149], v[210:213], v[14:17]
	v_mfma_f32_16x16x32_bf16 v[10:13], v[162:165], v[210:213], v[10:13]
	v_mfma_f32_16x16x32_bf16 v[62:65], v[150:153], v[190:193], v[62:65]
	v_mfma_f32_16x16x32_bf16 v[58:61], v[166:169], v[190:193], v[58:61]
	v_mfma_f32_16x16x32_bf16 v[46:49], v[150:153], v[198:201], v[46:49]
	v_mfma_f32_16x16x32_bf16 v[42:45], v[166:169], v[198:201], v[42:45]
	v_mfma_f32_16x16x32_bf16 v[30:33], v[150:153], v[206:209], v[30:33]
	v_mfma_f32_16x16x32_bf16 v[26:29], v[166:169], v[206:209], v[26:29]
	v_mfma_f32_16x16x32_bf16 v[14:17], v[150:153], v[214:217], v[14:17]
	v_mfma_f32_16x16x32_bf16 v[10:13], v[166:169], v[214:217], v[10:13]
	s_setprio 0
	s_setprio 1
	v_mfma_f32_16x16x32_bf16 v[54:57], v[170:173], v[186:189], v[54:57]
	v_mfma_f32_16x16x32_bf16 v[50:53], v[178:181], v[186:189], v[50:53]
	v_mfma_f32_16x16x32_bf16 v[38:41], v[170:173], v[194:197], v[38:41]
	v_mfma_f32_16x16x32_bf16 v[34:37], v[178:181], v[194:197], v[34:37]
	v_mfma_f32_16x16x32_bf16 v[22:25], v[170:173], v[202:205], v[22:25]
	v_mfma_f32_16x16x32_bf16 v[18:21], v[178:181], v[202:205], v[18:21]
	v_mfma_f32_16x16x32_bf16 v[6:9], v[170:173], v[210:213], v[6:9]
	v_mfma_f32_16x16x32_bf16 v[2:5], v[178:181], v[210:213], v[2:5]
	v_mfma_f32_16x16x32_bf16 v[54:57], v[174:177], v[190:193], v[54:57]
	v_mfma_f32_16x16x32_bf16 v[50:53], v[182:185], v[190:193], v[50:53]
	v_mfma_f32_16x16x32_bf16 v[38:41], v[174:177], v[198:201], v[38:41]
	v_mfma_f32_16x16x32_bf16 v[34:37], v[182:185], v[198:201], v[34:37]
	v_mfma_f32_16x16x32_bf16 v[22:25], v[174:177], v[206:209], v[22:25]
	v_mfma_f32_16x16x32_bf16 v[18:21], v[182:185], v[206:209], v[18:21]
	v_mfma_f32_16x16x32_bf16 v[6:9], v[174:177], v[214:217], v[6:9]
	v_mfma_f32_16x16x32_bf16 v[2:5], v[182:185], v[214:217], v[2:5]
	s_setprio 0
	s_barrier
; #define PG8_STAGE(bufoff, gbase, voff) do { _Pragma("unroll") for (int _i = 0; _i < 2; ++_i) \
;         __builtin_amdgcn_global_load_lds((const unsigned*)((const char*)(gbase) + (voff)[_i]), (PG8_LAS unsigned*)(lds + (bufoff) + ldsw + _i * 8192), 16, 0, 0); } while (0)
; #define PG8_LDA(dst, b, h) do { if constexpr (DT != 1) { _Pragma("unroll") for (int m = 0; m < 4; ++m) _Pragma("unroll") for (int k = 0; k < 2; ++k) dst[m][k] = *(const PG8_LAS bf16x8*)(lds + PG8_SA(b, h) + aoff + m * 2048 + k * 1024); } \
;         else { _Pragma("unroll") for (int m = 0; m < 4; ++m) dst##8[m] = ld32(lds + PG8_SA(b, h) + aoff + m * 2048); } } while (0)
; #define PG8_LDB(dst, b, h) do { if constexpr (DT != 1) { _Pragma("unroll") for (int n = 0; n < 2; ++n) _Pragma("unroll") for (int k = 0; k < 2; ++k) dst[n][k] = *(const PG8_LAS bf16x8*)(lds + PG8_SB(b, h) + boff + n * 2048 + k * 1024); } \
;         else { _Pragma("unroll") for (int n = 0; n < 2; ++n) dst##8[n] = ld32(lds + PG8_SB(b, h) + boff + n * 2048); } } while (0)
; #define PG8_WAIT_V(n) asm volatile("s_waitcnt vmcnt(" #n ")" ::: "memory")
; #define PG8_WAIT_L(n) asm volatile("s_waitcnt lgkmcnt(" #n ")" ::: "memory")
; #define PG8_BAR __builtin_amdgcn_s_barrier()
; #define PG8_SCHED __builtin_amdgcn_sched_barrier(0)
;     ...
;             PG8_LDB(B0, 1, 0); PG8_LDB(B1, 1, 1); PG8_SCHED; PG8_LDA(At, 1, 0); PG8_STAGE(PG8_SA(0, 1), a2 + hstepA, voffA);
;             PG8_WAIT_V(8); PG8_WAIT_L(0); PG8_BAR; PG8_MMA(0, 0, At, B0); PG8_MMA(0, 1, At, B1); PG8_BAR; PG8_SCHED;
;             PG8_LDA(At, 1, 1); PG8_STAGE(PG8_SB(1, 0), b3, voffB); PG8_STAGE(PG8_SB(1, 1), b3 + hstepB, voffB); PG8_STAGE(PG8_SA(1, 0), a3, voffA);
;             PG8_WAIT_V(8); PG8_WAIT_L(0); PG8_BAR; PG8_MMA(1, 0, At, B0); PG8_MMA(1, 1, At, B1); PG8_BAR; PG8_SCHED;
	ds_read_b128 v[146:149], v160
	ds_read_b128 v[150:153], v160 offset:1024
	ds_read_b128 v[162:165], v160 offset:2048
	ds_read_b128 v[166:169], v160 offset:3072
	ds_read_b128 v[170:173], v161
	ds_read_b128 v[174:177], v161 offset:1024
	ds_read_b128 v[178:181], v161 offset:2048
	ds_read_b128 v[182:185], v161 offset:3072
	s_add_u32 s40, s40, 0x80000
	s_addc_u32 s41, s41, 0
	s_mov_b32 m0, s53
	ds_read_b128 v[186:189], v159 offset:32768
	ds_read_b128 v[190:193], v159 offset:33792
	ds_read_b128 v[194:197], v159 offset:34816
	ds_read_b128 v[198:201], v159 offset:35840
	ds_read_b128 v[202:205], v159 offset:36864
	ds_read_b128 v[206:209], v159 offset:37888
	ds_read_b128 v[210:213], v159 offset:38912
	global_load_lds_dwordx4 v130, s[40:41]
	s_mov_b32 m0, s54
	ds_read_b128 v[214:217], v159 offset:39936
	global_load_lds_dwordx4 v134, s[40:41]
	s_waitcnt vmcnt(8) lgkmcnt(0)
	s_barrier
	s_setprio 1
	v_mfma_f32_16x16x32_bf16 v[122:125], v[146:149], v[186:189], v[122:125]
	v_mfma_f32_16x16x32_bf16 v[126:129], v[162:165], v[186:189], v[126:129]
	v_mfma_f32_16x16x32_bf16 v[110:113], v[146:149], v[194:197], v[110:113]
	v_mfma_f32_16x16x32_bf16 v[106:109], v[162:165], v[194:197], v[106:109]
	v_mfma_f32_16x16x32_bf16 v[94:97], v[146:149], v[202:205], v[94:97]
	v_mfma_f32_16x16x32_bf16 v[90:93], v[162:165], v[202:205], v[90:93]
	v_mfma_f32_16x16x32_bf16 v[78:81], v[146:149], v[210:213], v[78:81]
	v_mfma_f32_16x16x32_bf16 v[74:77], v[162:165], v[210:213], v[74:77]
	v_mfma_f32_16x16x32_bf16 v[122:125], v[150:153], v[190:193], v[122:125]
	v_mfma_f32_16x16x32_bf16 v[126:129], v[166:169], v[190:193], v[126:129]
	v_mfma_f32_16x16x32_bf16 v[110:113], v[150:153], v[198:201], v[110:113]
	v_mfma_f32_16x16x32_bf16 v[106:109], v[166:169], v[198:201], v[106:109]
	v_mfma_f32_16x16x32_bf16 v[94:97], v[150:153], v[206:209], v[94:97]
	v_mfma_f32_16x16x32_bf16 v[90:93], v[166:169], v[206:209], v[90:93]
	v_mfma_f32_16x16x32_bf16 v[78:81], v[150:153], v[214:217], v[78:81]
	v_mfma_f32_16x16x32_bf16 v[74:77], v[166:169], v[214:217], v[74:77]
	s_setprio 0
	s_setprio 1
	v_mfma_f32_16x16x32_bf16 v[118:121], v[170:173], v[186:189], v[118:121]
	v_mfma_f32_16x16x32_bf16 v[114:117], v[178:181], v[186:189], v[114:117]
	v_mfma_f32_16x16x32_bf16 v[102:105], v[170:173], v[194:197], v[102:105]
	v_mfma_f32_16x16x32_bf16 v[98:101], v[178:181], v[194:197], v[98:101]
	v_mfma_f32_16x16x32_bf16 v[86:89], v[170:173], v[202:205], v[86:89]
	v_mfma_f32_16x16x32_bf16 v[82:85], v[178:181], v[202:205], v[82:85]
	v_mfma_f32_16x16x32_bf16 v[70:73], v[170:173], v[210:213], v[70:73]
	v_mfma_f32_16x16x32_bf16 v[66:69], v[178:181], v[210:213], v[66:69]
	v_mfma_f32_16x16x32_bf16 v[118:121], v[174:177], v[190:193], v[118:121]
	v_mfma_f32_16x16x32_bf16 v[114:117], v[182:185], v[190:193], v[114:117]
	v_mfma_f32_16x16x32_bf16 v[102:105], v[174:177], v[198:201], v[102:105]
	v_mfma_f32_16x16x32_bf16 v[98:101], v[182:185], v[198:201], v[98:101]
	v_mfma_f32_16x16x32_bf16 v[86:89], v[174:177], v[206:209], v[86:89]
	v_mfma_f32_16x16x32_bf16 v[82:85], v[182:185], v[206:209], v[82:85]
	v_mfma_f32_16x16x32_bf16 v[70:73], v[174:177], v[214:217], v[70:73]
	v_mfma_f32_16x16x32_bf16 v[66:69], v[182:185], v[214:217], v[66:69]
	s_setprio 0
	s_barrier
	s_mov_b32 m0, s57
	s_add_u32 s38, s38, 0x80080
	ds_read_b128 v[186:189], v159 offset:49152
	ds_read_b128 v[190:193], v159 offset:50176
	ds_read_b128 v[194:197], v159 offset:51200
	ds_read_b128 v[198:201], v159 offset:52224
	global_load_lds_dwordx4 v132, s[98:99]
	s_mov_b32 m0, s58
	s_addc_u32 s39, s39, 0
	global_load_lds_dwordx4 v136, s[98:99]
	s_mov_b32 m0, s61
	ds_read_b128 v[214:217], v159 offset:56320
	global_load_lds_dwordx4 v132, s[38:39]
	s_mov_b32 m0, s62
	ds_read_b128 v[210:213], v159 offset:55296
	global_load_lds_dwordx4 v136, s[38:39]
	s_mov_b32 m0, s59
	ds_read_b128 v[206:209], v159 offset:54272
	global_load_lds_dwordx4 v130, s[100:101]
	s_mov_b32 m0, s60
	ds_read_b128 v[202:205], v159 offset:53248
	global_load_lds_dwordx4 v134, s[100:101]
	s_waitcnt vmcnt(8) lgkmcnt(0)
	s_barrier
	s_setprio 1
	v_mfma_f32_16x16x32_bf16 v[62:65], v[146:149], v[186:189], v[62:65]
	v_mfma_f32_16x16x32_bf16 v[58:61], v[162:165], v[186:189], v[58:61]
	v_mfma_f32_16x16x32_bf16 v[46:49], v[146:149], v[194:197], v[46:49]
	v_mfma_f32_16x16x32_bf16 v[42:45], v[162:165], v[194:197], v[42:45]
	v_mfma_f32_16x16x32_bf16 v[30:33], v[146:149], v[202:205], v[30:33]
	v_mfma_f32_16x16x32_bf16 v[26:29], v[162:165], v[202:205], v[26:29]
	v_mfma_f32_16x16x32_bf16 v[14:17], v[146:149], v[210:213], v[14:17]
	v_mfma_f32_16x16x32_bf16 v[10:13], v[162:165], v[210:213], v[10:13]
	v_mfma_f32_16x16x32_bf16 v[62:65], v[150:153], v[190:193], v[62:65]
	v_mfma_f32_16x16x32_bf16 v[58:61], v[166:169], v[190:193], v[58:61]
	v_mfma_f32_16x16x32_bf16 v[46:49], v[150:153], v[198:201], v[46:49]
	v_mfma_f32_16x16x32_bf16 v[42:45], v[166:169], v[198:201], v[42:45]
	v_mfma_f32_16x16x32_bf16 v[30:33], v[150:153], v[206:209], v[30:33]
	v_mfma_f32_16x16x32_bf16 v[26:29], v[166:169], v[206:209], v[26:29]
	v_mfma_f32_16x16x32_bf16 v[14:17], v[150:153], v[214:217], v[14:17]
	v_mfma_f32_16x16x32_bf16 v[10:13], v[166:169], v[214:217], v[10:13]
	s_setprio 0
	s_setprio 1
	v_mfma_f32_16x16x32_bf16 v[54:57], v[170:173], v[186:189], v[54:57]
	v_mfma_f32_16x16x32_bf16 v[50:53], v[178:181], v[186:189], v[50:53]
	v_mfma_f32_16x16x32_bf16 v[38:41], v[170:173], v[194:197], v[38:41]
	v_mfma_f32_16x16x32_bf16 v[34:37], v[178:181], v[194:197], v[34:37]
	v_mfma_f32_16x16x32_bf16 v[22:25], v[170:173], v[202:205], v[22:25]
	v_mfma_f32_16x16x32_bf16 v[18:21], v[178:181], v[202:205], v[18:21]
	v_mfma_f32_16x16x32_bf16 v[6:9], v[170:173], v[210:213], v[6:9]
	v_mfma_f32_16x16x32_bf16 v[2:5], v[178:181], v[210:213], v[2:5]
	v_mfma_f32_16x16x32_bf16 v[54:57], v[174:177], v[190:193], v[54:57]
	v_mfma_f32_16x16x32_bf16 v[50:53], v[182:185], v[190:193], v[50:53]
	v_mfma_f32_16x16x32_bf16 v[38:41], v[174:177], v[198:201], v[38:41]
	v_mfma_f32_16x16x32_bf16 v[34:37], v[182:185], v[198:201], v[34:37]
	v_mfma_f32_16x16x32_bf16 v[22:25], v[174:177], v[206:209], v[22:25]
	v_mfma_f32_16x16x32_bf16 v[18:21], v[182:185], v[206:209], v[18:21]
	v_mfma_f32_16x16x32_bf16 v[6:9], v[174:177], v[214:217], v[6:9]
	v_mfma_f32_16x16x32_bf16 v[2:5], v[182:185], v[214:217], v[2:5]
	s_setprio 0
	s_barrier
	s_add_u32 s69, s69, 0x100
	s_addc_u32 s70, s70, 0
	s_add_u32 s36, s36, 0x100
	s_addc_u32 s37, s37, 0
	s_cmp_ge_i32 s71, s56
	s_mov_b32 s38, s71
	s_cbranch_scc0 .LBB0_4646

; #define PG8_STAGE(bufoff, gbase, voff) do { _Pragma("unroll") for (int _i = 0; _i < 2; ++_i) \
;         __builtin_amdgcn_global_load_lds((const unsigned*)((const char*)(gbase) + (voff)[_i]), (PG8_LAS unsigned*)(lds + (bufoff) + ldsw + _i * 8192), 16, 0, 0); } while (0)
; #define PG8_LDA(dst, b, h) do { if constexpr (DT != 1) { _Pragma("unroll") for (int m = 0; m < 4; ++m) _Pragma("unroll") for (int k = 0; k < 2; ++k) dst[m][k] = *(const PG8_LAS bf16x8*)(lds + PG8_SA(b, h) + aoff + m * 2048 + k * 1024); } \
;         else { _Pragma("unroll") for (int m = 0; m < 4; ++m) dst##8[m] = ld32(lds + PG8_SA(b, h) + aoff + m * 2048); } } while (0)
; #define PG8_LDB(dst, b, h) do { if constexpr (DT != 1) { _Pragma("unroll") for (int n = 0; n < 2; ++n) _Pragma("unroll") for (int k = 0; k < 2; ++k) dst[n][k] = *(const PG8_LAS bf16x8*)(lds + PG8_SB(b, h) + boff + n * 2048 + k * 1024); } \
;         else { _Pragma("unroll") for (int n = 0; n < 2; ++n) dst##8[n] = ld32(lds + PG8_SB(b, h) + boff + n * 2048); } } while (0)
; #define PG8_WAIT_V(n) asm volatile("s_waitcnt vmcnt(" #n ")" ::: "memory")
; #define PG8_WAIT_L(n) asm volatile("s_waitcnt lgkmcnt(" #n ")" ::: "memory")
; #define PG8_BAR __builtin_amdgcn_s_barrier()
; #define PG8_SCHED __builtin_amdgcn_sched_barrier(0)
;     ...
;             PG8_LDB(B0, 0, 0); PG8_LDB(B1, 0, 1); PG8_SCHED; PG8_LDA(At, 0, 0); PG8_STAGE(PG8_SA(1, 1), a1 + hstepA, voffA);
;             PG8_WAIT_V(8); PG8_WAIT_L(0); PG8_BAR; PG8_MMA(0, 0, At, B0); PG8_MMA(0, 1, At, B1); PG8_BAR; PG8_SCHED;
;             PG8_LDA(At, 0, 1); PG8_STAGE(PG8_SB(0, 0), b2, voffB); PG8_STAGE(PG8_SB(0, 1), b2 + hstepB, voffB); PG8_STAGE(PG8_SA(0, 0), a2, voffA);
;             PG8_WAIT_V(8); PG8_WAIT_L(0); PG8_BAR; PG8_MMA(1, 0, At, B0); PG8_MMA(1, 1, At, B1); PG8_BAR; PG8_SCHED;
.Lzs_17:
	s_cbranch_vccnz .LBB0_4856
	s_add_u32 s59, s24, 0x100
	s_addc_u32 s60, s25, 0
	s_mov_b32 s26, 0
	ds_read_b128 v[16:19], v186
	ds_read_b128 v[20:23], v186 offset:16
	ds_read_b128 v[24:27], v186 offset:2048
	ds_read_b128 v[28:31], v186 offset:2064
	ds_read_b128 v[0:3], v187
	ds_read_b128 v[4:7], v187 offset:16
	ds_read_b128 v[8:11], v187 offset:2048
	ds_read_b128 v[12:15], v187 offset:2064
	s_add_i32 s61, s26, 2
	s_add_u32 s24, s22, 0x100
	s_addc_u32 s25, s23, 0
	s_cmp_eq_u32 s52, s26
	s_cselect_b32 s26, s20, s59
	s_cselect_b32 s29, s3, s25
	s_cselect_b32 s28, s2, s24
	s_cselect_b32 s27, s21, s60
	v_lshl_add_u64 v[216:217], s[22:23], 0, v[170:171]
	s_add_i32 m0, s40, 0xc000
	ds_read_b128 v[176:179], v188
	ds_read_b128 v[180:183], v188 offset:16
	ds_read_b128 v[192:195], v188 offset:2048
	ds_read_b128 v[196:199], v188 offset:2064
	ds_read_b128 v[200:203], v188 offset:4096
	ds_read_b128 v[204:207], v188 offset:4112
	ds_read_b128 v[208:211], v188 offset:6144
	ds_read_b128 v[212:215], v188 offset:6160
	global_load_lds_dwordx4 v[216:217], off
	v_lshl_add_u64 v[216:217], s[22:23], 0, v[168:169]
	s_add_i32 m0, s40, 0xe000
	s_nop 0
	global_load_lds_dwordx4 v[216:217], off
	s_waitcnt vmcnt(8) lgkmcnt(0)
	s_barrier
	s_setprio 1
	v_mfma_scale_f32_16x16x128_f8f6f4 v[156:159], v[16:23], v[176:183], 0, v189, v189 op_sel_hi:[0,0,0]
	v_mfma_scale_f32_16x16x128_f8f6f4 v[152:155], v[24:31], v[176:183], 0, v189, v189 op_sel_hi:[0,0,0]
	v_mfma_scale_f32_16x16x128_f8f6f4 v[148:151], v[16:23], v[192:199], 0, v189, v189 op_sel_hi:[0,0,0]
	v_mfma_scale_f32_16x16x128_f8f6f4 v[144:147], v[24:31], v[192:199], 0, v189, v189 op_sel_hi:[0,0,0]
	v_mfma_scale_f32_16x16x128_f8f6f4 v[128:131], v[16:23], v[200:207], 0, v189, v189 op_sel_hi:[0,0,0]
	v_mfma_scale_f32_16x16x128_f8f6f4 v[120:123], v[24:31], v[200:207], 0, v189, v189 op_sel_hi:[0,0,0]
	v_mfma_scale_f32_16x16x128_f8f6f4 v[108:111], v[16:23], v[208:215], 0, v189, v189 op_sel_hi:[0,0,0]
	v_mfma_scale_f32_16x16x128_f8f6f4 v[104:107], v[24:31], v[208:215], 0, v189, v189 op_sel_hi:[0,0,0]
	s_setprio 0
	s_setprio 1
	v_mfma_scale_f32_16x16x128_f8f6f4 v[140:143], v[0:7], v[176:183], 0, v189, v189 op_sel_hi:[0,0,0]
	v_mfma_scale_f32_16x16x128_f8f6f4 v[136:139], v[8:15], v[176:183], 0, v189, v189 op_sel_hi:[0,0,0]
	v_mfma_scale_f32_16x16x128_f8f6f4 v[132:135], v[0:7], v[192:199], 0, v189, v189 op_sel_hi:[0,0,0]
	v_mfma_scale_f32_16x16x128_f8f6f4 v[124:127], v[8:15], v[192:199], 0, v189, v189 op_sel_hi:[0,0,0]
	v_mfma_scale_f32_16x16x128_f8f6f4 v[116:119], v[0:7], v[200:207], 0, v189, v189 op_sel_hi:[0,0,0]
	v_mfma_scale_f32_16x16x128_f8f6f4 v[112:115], v[8:15], v[200:207], 0, v189, v189 op_sel_hi:[0,0,0]
	v_mfma_scale_f32_16x16x128_f8f6f4 v[100:103], v[0:7], v[208:215], 0, v189, v189 op_sel_hi:[0,0,0]
	v_mfma_scale_f32_16x16x128_f8f6f4 v[96:99], v[8:15], v[208:215], 0, v189, v189 op_sel_hi:[0,0,0]
	s_setprio 0
	s_barrier
	s_mov_b32 m0, s36
	s_add_u32 s98, s26, 0x80
	s_addc_u32 s99, s27, 0
	s_add_u32 s22, s26, 0xb0000
	ds_read_b128 v[192:195], v188 offset:16384
	ds_read_b128 v[196:199], v188 offset:16400
	ds_read_b128 v[200:203], v188 offset:18432
	ds_read_b128 v[204:207], v188 offset:18448
	global_load_lds_dwordx4 v162, s[26:27]
	s_mov_b32 m0, s37
	s_addc_u32 s23, s27, 0
	global_load_lds_dwordx4 v166, s[26:27]
	s_mov_b32 m0, s38
	ds_read_b128 v[220:223], v188 offset:22544
	global_load_lds_dwordx4 v162, s[22:23]
	s_mov_b32 m0, s39
	ds_read_b128 v[216:219], v188 offset:22528
	global_load_lds_dwordx4 v166, s[22:23]
	s_add_u32 s100, s28, 0x80
	s_addc_u32 s101, s29, 0
	s_mov_b32 m0, s40
	ds_read_b128 v[212:215], v188 offset:20496
	global_load_lds_dwordx4 v160, s[28:29]
	s_mov_b32 m0, s41
	ds_read_b128 v[208:211], v188 offset:20480
	global_load_lds_dwordx4 v164, s[28:29]
	s_waitcnt vmcnt(8) lgkmcnt(0)
	s_barrier
	s_setprio 1
	v_mfma_scale_f32_16x16x128_f8f6f4 v[92:95], v[16:23], v[192:199], 0, v189, v189 op_sel_hi:[0,0,0]
	v_mfma_scale_f32_16x16x128_f8f6f4 v[88:91], v[24:31], v[192:199], 0, v189, v189 op_sel_hi:[0,0,0]
	v_mfma_scale_f32_16x16x128_f8f6f4 v[76:79], v[16:23], v[200:207], 0, v189, v189 op_sel_hi:[0,0,0]
	v_mfma_scale_f32_16x16x128_f8f6f4 v[72:75], v[24:31], v[200:207], 0, v189, v189 op_sel_hi:[0,0,0]
	v_mfma_scale_f32_16x16x128_f8f6f4 v[224:227], v[16:23], v[208:215], 0, v189, v189 op_sel_hi:[0,0,0]
	v_mfma_scale_f32_16x16x128_f8f6f4 v[228:231], v[24:31], v[208:215], 0, v189, v189 op_sel_hi:[0,0,0]
	v_mfma_scale_f32_16x16x128_f8f6f4 v[232:235], v[16:23], v[216:223], 0, v189, v189 op_sel_hi:[0,0,0]
	v_mfma_scale_f32_16x16x128_f8f6f4 v[236:239], v[24:31], v[216:223], 0, v189, v189 op_sel_hi:[0,0,0]
	s_setprio 0
	s_setprio 1
	v_mfma_scale_f32_16x16x128_f8f6f4 v[84:87], v[0:7], v[192:199], 0, v189, v189 op_sel_hi:[0,0,0]
	v_mfma_scale_f32_16x16x128_f8f6f4 v[80:83], v[8:15], v[192:199], 0, v189, v189 op_sel_hi:[0,0,0]
	v_mfma_scale_f32_16x16x128_f8f6f4 v[68:71], v[0:7], v[200:207], 0, v189, v189 op_sel_hi:[0,0,0]
	v_mfma_scale_f32_16x16x128_f8f6f4 v[64:67], v[8:15], v[200:207], 0, v189, v189 op_sel_hi:[0,0,0]
	v_mfma_scale_f32_16x16x128_f8f6f4 v[240:243], v[0:7], v[208:215], 0, v189, v189 op_sel_hi:[0,0,0]
	v_mfma_scale_f32_16x16x128_f8f6f4 v[208:211], v[8:15], v[208:215], 0, v189, v189 op_sel_hi:[0,0,0]
	v_mfma_scale_f32_16x16x128_f8f6f4 v[212:215], v[0:7], v[216:223], 0, v189, v189 op_sel_hi:[0,0,0]
	v_mfma_scale_f32_16x16x128_f8f6f4 v[216:219], v[8:15], v[216:223], 0, v189, v189 op_sel_hi:[0,0,0]
	s_setprio 0
	s_barrier
; #define PG8_STAGE(bufoff, gbase, voff) do { _Pragma("unroll") for (int _i = 0; _i < 2; ++_i) \
;         __builtin_amdgcn_global_load_lds((const unsigned*)((const char*)(gbase) + (voff)[_i]), (PG8_LAS unsigned*)(lds + (bufoff) + ldsw + _i * 8192), 16, 0, 0); } while (0)
; #define PG8_LDA(dst, b, h) do { if constexpr (DT != 1) { _Pragma("unroll") for (int m = 0; m < 4; ++m) _Pragma("unroll") for (int k = 0; k < 2; ++k) dst[m][k] = *(const PG8_LAS bf16x8*)(lds + PG8_SA(b, h) + aoff + m * 2048 + k * 1024); } \
;         else { _Pragma("unroll") for (int m = 0; m < 4; ++m) dst##8[m] = ld32(lds + PG8_SA(b, h) + aoff + m * 2048); } } while (0)
; #define PG8_LDB(dst, b, h) do { if constexpr (DT != 1) { _Pragma("unroll") for (int n = 0; n < 2; ++n) _Pragma("unroll") for (int k = 0; k < 2; ++k) dst[n][k] = *(const PG8_LAS bf16x8*)(lds + PG8_SB(b, h) + boff + n * 2048 + k * 1024); } \
;         else { _Pragma("unroll") for (int n = 0; n < 2; ++n) dst##8[n] = ld32(lds + PG8_SB(b, h) + boff + n * 2048); } } while (0)
; #define PG8_WAIT_V(n) asm volatile("s_waitcnt vmcnt(" #n ")" ::: "memory")
; #define PG8_WAIT_L(n) asm volatile("s_waitcnt lgkmcnt(" #n ")" ::: "memory")
; #define PG8_BAR __builtin_amdgcn_s_barrier()
; #define PG8_SCHED __builtin_amdgcn_sched_barrier(0)
;     ...
;         for (int t = 0; t < nt; t += 2) {
;     ...
;             PG8_LDB(B0, 1, 0); PG8_LDB(B1, 1, 1); PG8_SCHED; PG8_LDA(At, 1, 0); PG8_STAGE(PG8_SA(0, 1), a2 + hstepA, voffA);
;             PG8_WAIT_V(8); PG8_WAIT_L(0); PG8_BAR; PG8_MMA(0, 0, At, B0); PG8_MMA(0, 1, At, B1); PG8_BAR; PG8_SCHED;
;             PG8_LDA(At, 1, 1); PG8_STAGE(PG8_SB(1, 0), b3, voffB); PG8_STAGE(PG8_SB(1, 1), b3 + hstepB, voffB); PG8_STAGE(PG8_SA(1, 0), a3, voffA);
;             PG8_WAIT_V(8); PG8_WAIT_L(0); PG8_BAR; PG8_MMA(1, 0, At, B0); PG8_MMA(1, 1, At, B1); PG8_BAR; PG8_SCHED;
	ds_read_b128 v[0:3], v190
	ds_read_b128 v[4:7], v190 offset:16
	ds_read_b128 v[8:11], v190 offset:2048
	ds_read_b128 v[12:15], v190 offset:2064
	ds_read_b128 v[16:19], v191
	ds_read_b128 v[20:23], v191 offset:16
	ds_read_b128 v[24:27], v191 offset:2048
	ds_read_b128 v[28:31], v191 offset:2064
	s_add_u32 s22, s28, 0xb0000
	s_addc_u32 s23, s29, 0
	s_mov_b32 m0, s42
	ds_read_b128 v[32:35], v188 offset:32768
	ds_read_b128 v[36:39], v188 offset:32784
	ds_read_b128 v[40:43], v188 offset:34816
	ds_read_b128 v[44:47], v188 offset:34832
	ds_read_b128 v[48:51], v188 offset:36864
	ds_read_b128 v[52:55], v188 offset:36880
	ds_read_b128 v[56:59], v188 offset:38912
	global_load_lds_dwordx4 v160, s[22:23]
	s_mov_b32 m0, s43
	ds_read_b128 v[60:63], v188 offset:38928
	global_load_lds_dwordx4 v164, s[22:23]
	s_waitcnt vmcnt(8) lgkmcnt(0)
	s_barrier
	s_setprio 1
	v_mfma_scale_f32_16x16x128_f8f6f4 v[156:159], v[0:7], v[32:39], v[156:159], v189, v189 op_sel_hi:[0,0,0]
	v_mfma_scale_f32_16x16x128_f8f6f4 v[152:155], v[8:15], v[32:39], v[152:155], v189, v189 op_sel_hi:[0,0,0]
	v_mfma_scale_f32_16x16x128_f8f6f4 v[148:151], v[0:7], v[40:47], v[148:151], v189, v189 op_sel_hi:[0,0,0]
	v_mfma_scale_f32_16x16x128_f8f6f4 v[144:147], v[8:15], v[40:47], v[144:147], v189, v189 op_sel_hi:[0,0,0]
	v_mfma_scale_f32_16x16x128_f8f6f4 v[128:131], v[0:7], v[48:55], v[128:131], v189, v189 op_sel_hi:[0,0,0]
	v_mfma_scale_f32_16x16x128_f8f6f4 v[120:123], v[8:15], v[48:55], v[120:123], v189, v189 op_sel_hi:[0,0,0]
	v_mfma_scale_f32_16x16x128_f8f6f4 v[108:111], v[0:7], v[56:63], v[108:111], v189, v189 op_sel_hi:[0,0,0]
	v_mfma_scale_f32_16x16x128_f8f6f4 v[104:107], v[8:15], v[56:63], v[104:107], v189, v189 op_sel_hi:[0,0,0]
	s_setprio 0
	s_setprio 1
	v_mfma_scale_f32_16x16x128_f8f6f4 v[140:143], v[16:23], v[32:39], v[140:143], v189, v189 op_sel_hi:[0,0,0]
	v_mfma_scale_f32_16x16x128_f8f6f4 v[136:139], v[24:31], v[32:39], v[136:139], v189, v189 op_sel_hi:[0,0,0]
	v_mfma_scale_f32_16x16x128_f8f6f4 v[132:135], v[16:23], v[40:47], v[132:135], v189, v189 op_sel_hi:[0,0,0]
	v_mfma_scale_f32_16x16x128_f8f6f4 v[124:127], v[24:31], v[40:47], v[124:127], v189, v189 op_sel_hi:[0,0,0]
	v_mfma_scale_f32_16x16x128_f8f6f4 v[116:119], v[16:23], v[48:55], v[116:119], v189, v189 op_sel_hi:[0,0,0]
	v_mfma_scale_f32_16x16x128_f8f6f4 v[112:115], v[24:31], v[48:55], v[112:115], v189, v189 op_sel_hi:[0,0,0]
	v_mfma_scale_f32_16x16x128_f8f6f4 v[100:103], v[16:23], v[56:63], v[100:103], v189, v189 op_sel_hi:[0,0,0]
	v_mfma_scale_f32_16x16x128_f8f6f4 v[96:99], v[24:31], v[56:63], v[96:99], v189, v189 op_sel_hi:[0,0,0]
	s_setprio 0
	s_barrier
	s_mov_b32 m0, s46
	s_add_u32 s22, s26, 0xb0080
	ds_read_b128 v[32:35], v188 offset:49152
	ds_read_b128 v[36:39], v188 offset:49168
	ds_read_b128 v[48:51], v188 offset:51200
	ds_read_b128 v[52:55], v188 offset:51216
	global_load_lds_dwordx4 v162, s[98:99]
	s_mov_b32 m0, s47
	s_addc_u32 s23, s27, 0
	global_load_lds_dwordx4 v166, s[98:99]
	s_mov_b32 m0, s50
	ds_read_b128 v[204:207], v188 offset:55312
	global_load_lds_dwordx4 v162, s[22:23]
	s_mov_b32 m0, s51
	ds_read_b128 v[200:203], v188 offset:55296
	global_load_lds_dwordx4 v166, s[22:23]
	s_mov_b32 m0, s48
	ds_read_b128 v[196:199], v188 offset:53264
	global_load_lds_dwordx4 v160, s[100:101]
	s_mov_b32 m0, s49
	ds_read_b128 v[192:195], v188 offset:53248
	global_load_lds_dwordx4 v164, s[100:101]
	s_waitcnt vmcnt(8) lgkmcnt(0)
	s_barrier
	s_setprio 1
	v_mfma_scale_f32_16x16x128_f8f6f4 v[92:95], v[0:7], v[32:39], v[92:95], v189, v189 op_sel_hi:[0,0,0]
	v_mfma_scale_f32_16x16x128_f8f6f4 v[88:91], v[8:15], v[32:39], v[88:91], v189, v189 op_sel_hi:[0,0,0]
	v_mfma_scale_f32_16x16x128_f8f6f4 v[76:79], v[0:7], v[48:55], v[76:79], v189, v189 op_sel_hi:[0,0,0]
	v_mfma_scale_f32_16x16x128_f8f6f4 v[72:75], v[8:15], v[48:55], v[72:75], v189, v189 op_sel_hi:[0,0,0]
	v_mfma_scale_f32_16x16x128_f8f6f4 v[60:63], v[0:7], v[192:199], v[224:227], v189, v189 op_sel_hi:[0,0,0]
	v_mfma_scale_f32_16x16x128_f8f6f4 v[56:59], v[8:15], v[192:199], v[228:231], v189, v189 op_sel_hi:[0,0,0]
	v_mfma_scale_f32_16x16x128_f8f6f4 v[44:47], v[0:7], v[200:207], v[232:235], v189, v189 op_sel_hi:[0,0,0]
	v_mfma_scale_f32_16x16x128_f8f6f4 v[40:43], v[8:15], v[200:207], v[236:239], v189, v189 op_sel_hi:[0,0,0]
	s_setprio 0
	s_setprio 1
	v_mfma_scale_f32_16x16x128_f8f6f4 v[84:87], v[16:23], v[32:39], v[84:87], v189, v189 op_sel_hi:[0,0,0]
	v_mfma_scale_f32_16x16x128_f8f6f4 v[80:83], v[24:31], v[32:39], v[80:83], v189, v189 op_sel_hi:[0,0,0]
	v_mfma_scale_f32_16x16x128_f8f6f4 v[68:71], v[16:23], v[48:55], v[68:71], v189, v189 op_sel_hi:[0,0,0]
	v_mfma_scale_f32_16x16x128_f8f6f4 v[64:67], v[24:31], v[48:55], v[64:67], v189, v189 op_sel_hi:[0,0,0]
	v_mfma_scale_f32_16x16x128_f8f6f4 v[52:55], v[16:23], v[192:199], v[240:243], v189, v189 op_sel_hi:[0,0,0]
	v_mfma_scale_f32_16x16x128_f8f6f4 v[48:51], v[24:31], v[192:199], v[208:211], v189, v189 op_sel_hi:[0,0,0]
	v_mfma_scale_f32_16x16x128_f8f6f4 v[36:39], v[16:23], v[200:207], v[212:215], v189, v189 op_sel_hi:[0,0,0]
	v_mfma_scale_f32_16x16x128_f8f6f4 v[32:35], v[24:31], v[200:207], v[216:219], v189, v189 op_sel_hi:[0,0,0]
	s_setprio 0
	s_barrier
	s_add_u32 s59, s59, 0x100
	s_addc_u32 s60, s60, 0
	s_cmp_ge_i32 s61, s45
	s_mov_b64 s[22:23], s[24:25]
	s_mov_b32 s26, s61
	s_cbranch_scc0 .LBB0_4855
	s_branch .LBB0_4856
; #define PG8_STAGE(bufoff, gbase, voff) do { _Pragma("unroll") for (int _i = 0; _i < 2; ++_i) \
;         __builtin_amdgcn_global_load_lds((const unsigned*)((const char*)(gbase) + (voff)[_i]), (PG8_LAS unsigned*)(lds + (bufoff) + ldsw + _i * 8192), 16, 0, 0); } while (0)
; #define PG8_LDA(dst, b, h) do { if constexpr (DT != 1) { _Pragma("unroll") for (int m = 0; m < 4; ++m) _Pragma("unroll") for (int k = 0; k < 2; ++k) dst[m][k] = *(const PG8_LAS bf16x8*)(lds + PG8_SA(b, h) + aoff + m * 2048 + k * 1024); } \
;         else { _Pragma("unroll") for (int m = 0; m < 4; ++m) dst##8[m] = ld32(lds + PG8_SA(b, h) + aoff + m * 2048); } } while (0)
; #define PG8_LDB(dst, b, h) do { if constexpr (DT != 1) { _Pragma("unroll") for (int n = 0; n < 2; ++n) _Pragma("unroll") for (int k = 0; k < 2; ++k) dst[n][k] = *(const PG8_LAS bf16x8*)(lds + PG8_SB(b, h) + boff + n * 2048 + k * 1024); } \
;         else { _Pragma("unroll") for (int n = 0; n < 2; ++n) dst##8[n] = ld32(lds + PG8_SB(b, h) + boff + n * 2048); } } while (0)
; #define PG8_WAIT_V(n) asm volatile("s_waitcnt vmcnt(" #n ")" ::: "memory")
; #define PG8_WAIT_L(n) asm volatile("s_waitcnt lgkmcnt(" #n ")" ::: "memory")
; #define PG8_BAR __builtin_amdgcn_s_barrier()
; #define PG8_SCHED __builtin_amdgcn_sched_barrier(0)
;     ...
;             PG8_LDB(B0, 0, 0); PG8_LDB(B1, 0, 1); PG8_SCHED; PG8_LDA(At, 0, 0); PG8_STAGE(PG8_SA(1, 1), a1 + hstepA, voffA);
;             PG8_WAIT_V(8); PG8_WAIT_L(0); PG8_BAR; PG8_MMA(0, 0, At, B0); PG8_MMA(0, 1, At, B1); PG8_BAR; PG8_SCHED;
;             PG8_LDA(At, 0, 1); PG8_STAGE(PG8_SB(0, 0), b2, voffB); PG8_STAGE(PG8_SB(0, 1), b2 + hstepB, voffB); PG8_STAGE(PG8_SA(0, 0), a2, voffA);
;             PG8_WAIT_V(8); PG8_WAIT_L(0); PG8_BAR; PG8_MMA(1, 0, At, B0); PG8_MMA(1, 1, At, B1); PG8_BAR; PG8_SCHED;
.LBB0_4855:
	ds_read_b128 v[16:19], v186
	ds_read_b128 v[20:23], v186 offset:16
	ds_read_b128 v[24:27], v186 offset:2048
	ds_read_b128 v[28:31], v186 offset:2064
	ds_read_b128 v[0:3], v187
	ds_read_b128 v[4:7], v187 offset:16
	ds_read_b128 v[8:11], v187 offset:2048
	ds_read_b128 v[12:15], v187 offset:2064
	s_add_i32 s61, s26, 2
	s_add_u32 s24, s22, 0x100
	s_addc_u32 s25, s23, 0
	s_cmp_eq_u32 s52, s26
	s_cselect_b32 s26, s20, s59
	s_cselect_b32 s29, s3, s25
	s_cselect_b32 s28, s2, s24
	s_cselect_b32 s27, s21, s60
	v_lshl_add_u64 v[216:217], s[22:23], 0, v[170:171]
	s_add_i32 m0, s40, 0xc000
	ds_read_b128 v[176:179], v188
	ds_read_b128 v[180:183], v188 offset:16
	ds_read_b128 v[192:195], v188 offset:2048
	ds_read_b128 v[196:199], v188 offset:2064
	ds_read_b128 v[200:203], v188 offset:4096
	ds_read_b128 v[204:207], v188 offset:4112
	ds_read_b128 v[208:211], v188 offset:6144
	ds_read_b128 v[212:215], v188 offset:6160
	global_load_lds_dwordx4 v[216:217], off
	v_lshl_add_u64 v[216:217], s[22:23], 0, v[168:169]
	s_add_i32 m0, s40, 0xe000
	s_nop 0
	global_load_lds_dwordx4 v[216:217], off
	s_waitcnt vmcnt(8) lgkmcnt(0)
	s_barrier
	s_setprio 1
	v_mfma_scale_f32_16x16x128_f8f6f4 v[156:159], v[16:23], v[176:183], v[156:159], v189, v189 op_sel_hi:[0,0,0]
	v_mfma_scale_f32_16x16x128_f8f6f4 v[152:155], v[24:31], v[176:183], v[152:155], v189, v189 op_sel_hi:[0,0,0]
	v_mfma_scale_f32_16x16x128_f8f6f4 v[148:151], v[16:23], v[192:199], v[148:151], v189, v189 op_sel_hi:[0,0,0]
	v_mfma_scale_f32_16x16x128_f8f6f4 v[144:147], v[24:31], v[192:199], v[144:147], v189, v189 op_sel_hi:[0,0,0]
	v_mfma_scale_f32_16x16x128_f8f6f4 v[128:131], v[16:23], v[200:207], v[128:131], v189, v189 op_sel_hi:[0,0,0]
	v_mfma_scale_f32_16x16x128_f8f6f4 v[120:123], v[24:31], v[200:207], v[120:123], v189, v189 op_sel_hi:[0,0,0]
	v_mfma_scale_f32_16x16x128_f8f6f4 v[108:111], v[16:23], v[208:215], v[108:111], v189, v189 op_sel_hi:[0,0,0]
	v_mfma_scale_f32_16x16x128_f8f6f4 v[104:107], v[24:31], v[208:215], v[104:107], v189, v189 op_sel_hi:[0,0,0]
	s_setprio 0
	s_setprio 1
	v_mfma_scale_f32_16x16x128_f8f6f4 v[140:143], v[0:7], v[176:183], v[140:143], v189, v189 op_sel_hi:[0,0,0]
	v_mfma_scale_f32_16x16x128_f8f6f4 v[136:139], v[8:15], v[176:183], v[136:139], v189, v189 op_sel_hi:[0,0,0]
	v_mfma_scale_f32_16x16x128_f8f6f4 v[132:135], v[0:7], v[192:199], v[132:135], v189, v189 op_sel_hi:[0,0,0]
	v_mfma_scale_f32_16x16x128_f8f6f4 v[124:127], v[8:15], v[192:199], v[124:127], v189, v189 op_sel_hi:[0,0,0]
	v_mfma_scale_f32_16x16x128_f8f6f4 v[116:119], v[0:7], v[200:207], v[116:119], v189, v189 op_sel_hi:[0,0,0]
	v_mfma_scale_f32_16x16x128_f8f6f4 v[112:115], v[8:15], v[200:207], v[112:115], v189, v189 op_sel_hi:[0,0,0]
	v_mfma_scale_f32_16x16x128_f8f6f4 v[100:103], v[0:7], v[208:215], v[100:103], v189, v189 op_sel_hi:[0,0,0]
	v_mfma_scale_f32_16x16x128_f8f6f4 v[96:99], v[8:15], v[208:215], v[96:99], v189, v189 op_sel_hi:[0,0,0]
	s_setprio 0
	s_barrier
	s_mov_b32 m0, s36
	s_add_u32 s98, s26, 0x80
	s_addc_u32 s99, s27, 0
	s_add_u32 s22, s26, 0xb0000
	ds_read_b128 v[192:195], v188 offset:16384
	ds_read_b128 v[196:199], v188 offset:16400
	ds_read_b128 v[200:203], v188 offset:18432
	ds_read_b128 v[204:207], v188 offset:18448
	global_load_lds_dwordx4 v162, s[26:27]
	s_mov_b32 m0, s37
	s_addc_u32 s23, s27, 0
	global_load_lds_dwordx4 v166, s[26:27]
	s_mov_b32 m0, s38
	ds_read_b128 v[220:223], v188 offset:22544
	global_load_lds_dwordx4 v162, s[22:23]
	s_mov_b32 m0, s39
	ds_read_b128 v[216:219], v188 offset:22528
	global_load_lds_dwordx4 v166, s[22:23]
	s_add_u32 s100, s28, 0x80
	s_addc_u32 s101, s29, 0
	s_mov_b32 m0, s40
	ds_read_b128 v[212:215], v188 offset:20496
	global_load_lds_dwordx4 v160, s[28:29]
	s_mov_b32 m0, s41
	ds_read_b128 v[208:211], v188 offset:20480
	global_load_lds_dwordx4 v164, s[28:29]
	s_waitcnt vmcnt(8) lgkmcnt(0)
	s_barrier
	s_setprio 1
	v_mfma_scale_f32_16x16x128_f8f6f4 v[92:95], v[16:23], v[192:199], v[92:95], v189, v189 op_sel_hi:[0,0,0]
	v_mfma_scale_f32_16x16x128_f8f6f4 v[88:91], v[24:31], v[192:199], v[88:91], v189, v189 op_sel_hi:[0,0,0]
	v_mfma_scale_f32_16x16x128_f8f6f4 v[76:79], v[16:23], v[200:207], v[76:79], v189, v189 op_sel_hi:[0,0,0]
	v_mfma_scale_f32_16x16x128_f8f6f4 v[72:75], v[24:31], v[200:207], v[72:75], v189, v189 op_sel_hi:[0,0,0]
	v_mfma_scale_f32_16x16x128_f8f6f4 v[224:227], v[16:23], v[208:215], v[60:63], v189, v189 op_sel_hi:[0,0,0]
	v_mfma_scale_f32_16x16x128_f8f6f4 v[228:231], v[24:31], v[208:215], v[56:59], v189, v189 op_sel_hi:[0,0,0]
	v_mfma_scale_f32_16x16x128_f8f6f4 v[232:235], v[16:23], v[216:223], v[44:47], v189, v189 op_sel_hi:[0,0,0]
	v_mfma_scale_f32_16x16x128_f8f6f4 v[236:239], v[24:31], v[216:223], v[40:43], v189, v189 op_sel_hi:[0,0,0]
	s_setprio 0
	s_setprio 1
	v_mfma_scale_f32_16x16x128_f8f6f4 v[84:87], v[0:7], v[192:199], v[84:87], v189, v189 op_sel_hi:[0,0,0]
	v_mfma_scale_f32_16x16x128_f8f6f4 v[80:83], v[8:15], v[192:199], v[80:83], v189, v189 op_sel_hi:[0,0,0]
	v_mfma_scale_f32_16x16x128_f8f6f4 v[68:71], v[0:7], v[200:207], v[68:71], v189, v189 op_sel_hi:[0,0,0]
	v_mfma_scale_f32_16x16x128_f8f6f4 v[64:67], v[8:15], v[200:207], v[64:67], v189, v189 op_sel_hi:[0,0,0]
	v_mfma_scale_f32_16x16x128_f8f6f4 v[240:243], v[0:7], v[208:215], v[52:55], v189, v189 op_sel_hi:[0,0,0]
	v_mfma_scale_f32_16x16x128_f8f6f4 v[208:211], v[8:15], v[208:215], v[48:51], v189, v189 op_sel_hi:[0,0,0]
	v_mfma_scale_f32_16x16x128_f8f6f4 v[212:215], v[0:7], v[216:223], v[36:39], v189, v189 op_sel_hi:[0,0,0]
	v_mfma_scale_f32_16x16x128_f8f6f4 v[216:219], v[8:15], v[216:223], v[32:35], v189, v189 op_sel_hi:[0,0,0]
	s_setprio 0
	s_barrier
; #define PG8_STAGE(bufoff, gbase, voff) do { _Pragma("unroll") for (int _i = 0; _i < 2; ++_i) \
;         __builtin_amdgcn_global_load_lds((const unsigned*)((const char*)(gbase) + (voff)[_i]), (PG8_LAS unsigned*)(lds + (bufoff) + ldsw + _i * 8192), 16, 0, 0); } while (0)
; #define PG8_LDA(dst, b, h) do { if constexpr (DT != 1) { _Pragma("unroll") for (int m = 0; m < 4; ++m) _Pragma("unroll") for (int k = 0; k < 2; ++k) dst[m][k] = *(const PG8_LAS bf16x8*)(lds + PG8_SA(b, h) + aoff + m * 2048 + k * 1024); } \
;         else { _Pragma("unroll") for (int m = 0; m < 4; ++m) dst##8[m] = ld32(lds + PG8_SA(b, h) + aoff + m * 2048); } } while (0)
; #define PG8_LDB(dst, b, h) do { if constexpr (DT != 1) { _Pragma("unroll") for (int n = 0; n < 2; ++n) _Pragma("unroll") for (int k = 0; k < 2; ++k) dst[n][k] = *(const PG8_LAS bf16x8*)(lds + PG8_SB(b, h) + boff + n * 2048 + k * 1024); } \
;         else { _Pragma("unroll") for (int n = 0; n < 2; ++n) dst##8[n] = ld32(lds + PG8_SB(b, h) + boff + n * 2048); } } while (0)
; #define PG8_WAIT_V(n) asm volatile("s_waitcnt vmcnt(" #n ")" ::: "memory")
; #define PG8_WAIT_L(n) asm volatile("s_waitcnt lgkmcnt(" #n ")" ::: "memory")
; #define PG8_BAR __builtin_amdgcn_s_barrier()
; #define PG8_SCHED __builtin_amdgcn_sched_barrier(0)
;     ...
;             PG8_LDB(B0, 1, 0); PG8_LDB(B1, 1, 1); PG8_SCHED; PG8_LDA(At, 1, 0); PG8_STAGE(PG8_SA(0, 1), a2 + hstepA, voffA);
;             PG8_WAIT_V(8); PG8_WAIT_L(0); PG8_BAR; PG8_MMA(0, 0, At, B0); PG8_MMA(0, 1, At, B1); PG8_BAR; PG8_SCHED;
;             PG8_LDA(At, 1, 1); PG8_STAGE(PG8_SB(1, 0), b3, voffB); PG8_STAGE(PG8_SB(1, 1), b3 + hstepB, voffB); PG8_STAGE(PG8_SA(1, 0), a3, voffA);
;             PG8_WAIT_V(8); PG8_WAIT_L(0); PG8_BAR; PG8_MMA(1, 0, At, B0); PG8_MMA(1, 1, At, B1); PG8_BAR; PG8_SCHED;
	ds_read_b128 v[0:3], v190
	ds_read_b128 v[4:7], v190 offset:16
	ds_read_b128 v[8:11], v190 offset:2048
	ds_read_b128 v[12:15], v190 offset:2064
	ds_read_b128 v[16:19], v191
	ds_read_b128 v[20:23], v191 offset:16
	ds_read_b128 v[24:27], v191 offset:2048
	ds_read_b128 v[28:31], v191 offset:2064
	s_add_u32 s22, s28, 0xb0000
	s_addc_u32 s23, s29, 0
	s_mov_b32 m0, s42
	ds_read_b128 v[32:35], v188 offset:32768
	ds_read_b128 v[36:39], v188 offset:32784
	ds_read_b128 v[40:43], v188 offset:34816
	ds_read_b128 v[44:47], v188 offset:34832
	ds_read_b128 v[48:51], v188 offset:36864
	ds_read_b128 v[52:55], v188 offset:36880
	ds_read_b128 v[56:59], v188 offset:38912
	global_load_lds_dwordx4 v160, s[22:23]
	s_mov_b32 m0, s43
	ds_read_b128 v[60:63], v188 offset:38928
	global_load_lds_dwordx4 v164, s[22:23]
	s_waitcnt vmcnt(8) lgkmcnt(0)
	s_barrier
	s_setprio 1
	v_mfma_scale_f32_16x16x128_f8f6f4 v[156:159], v[0:7], v[32:39], v[156:159], v189, v189 op_sel_hi:[0,0,0]
	v_mfma_scale_f32_16x16x128_f8f6f4 v[152:155], v[8:15], v[32:39], v[152:155], v189, v189 op_sel_hi:[0,0,0]
	v_mfma_scale_f32_16x16x128_f8f6f4 v[148:151], v[0:7], v[40:47], v[148:151], v189, v189 op_sel_hi:[0,0,0]
	v_mfma_scale_f32_16x16x128_f8f6f4 v[144:147], v[8:15], v[40:47], v[144:147], v189, v189 op_sel_hi:[0,0,0]
	v_mfma_scale_f32_16x16x128_f8f6f4 v[128:131], v[0:7], v[48:55], v[128:131], v189, v189 op_sel_hi:[0,0,0]
	v_mfma_scale_f32_16x16x128_f8f6f4 v[120:123], v[8:15], v[48:55], v[120:123], v189, v189 op_sel_hi:[0,0,0]
	v_mfma_scale_f32_16x16x128_f8f6f4 v[108:111], v[0:7], v[56:63], v[108:111], v189, v189 op_sel_hi:[0,0,0]
	v_mfma_scale_f32_16x16x128_f8f6f4 v[104:107], v[8:15], v[56:63], v[104:107], v189, v189 op_sel_hi:[0,0,0]
	s_setprio 0
	s_setprio 1
	v_mfma_scale_f32_16x16x128_f8f6f4 v[140:143], v[16:23], v[32:39], v[140:143], v189, v189 op_sel_hi:[0,0,0]
	v_mfma_scale_f32_16x16x128_f8f6f4 v[136:139], v[24:31], v[32:39], v[136:139], v189, v189 op_sel_hi:[0,0,0]
	v_mfma_scale_f32_16x16x128_f8f6f4 v[132:135], v[16:23], v[40:47], v[132:135], v189, v189 op_sel_hi:[0,0,0]
	v_mfma_scale_f32_16x16x128_f8f6f4 v[124:127], v[24:31], v[40:47], v[124:127], v189, v189 op_sel_hi:[0,0,0]
	v_mfma_scale_f32_16x16x128_f8f6f4 v[116:119], v[16:23], v[48:55], v[116:119], v189, v189 op_sel_hi:[0,0,0]
	v_mfma_scale_f32_16x16x128_f8f6f4 v[112:115], v[24:31], v[48:55], v[112:115], v189, v189 op_sel_hi:[0,0,0]
	v_mfma_scale_f32_16x16x128_f8f6f4 v[100:103], v[16:23], v[56:63], v[100:103], v189, v189 op_sel_hi:[0,0,0]
	v_mfma_scale_f32_16x16x128_f8f6f4 v[96:99], v[24:31], v[56:63], v[96:99], v189, v189 op_sel_hi:[0,0,0]
	s_setprio 0
	s_barrier
	s_mov_b32 m0, s46
	s_add_u32 s22, s26, 0xb0080
	ds_read_b128 v[32:35], v188 offset:49152
	ds_read_b128 v[36:39], v188 offset:49168
	ds_read_b128 v[48:51], v188 offset:51200
	ds_read_b128 v[52:55], v188 offset:51216
	global_load_lds_dwordx4 v162, s[98:99]
	s_mov_b32 m0, s47
	s_addc_u32 s23, s27, 0
	global_load_lds_dwordx4 v166, s[98:99]
	s_mov_b32 m0, s50
	ds_read_b128 v[204:207], v188 offset:55312
	global_load_lds_dwordx4 v162, s[22:23]
	s_mov_b32 m0, s51
	ds_read_b128 v[200:203], v188 offset:55296
	global_load_lds_dwordx4 v166, s[22:23]
	s_mov_b32 m0, s48
	ds_read_b128 v[196:199], v188 offset:53264
	global_load_lds_dwordx4 v160, s[100:101]
	s_mov_b32 m0, s49
	ds_read_b128 v[192:195], v188 offset:53248
	global_load_lds_dwordx4 v164, s[100:101]
	s_waitcnt vmcnt(8) lgkmcnt(0)
	s_barrier
	s_setprio 1
	v_mfma_scale_f32_16x16x128_f8f6f4 v[92:95], v[0:7], v[32:39], v[92:95], v189, v189 op_sel_hi:[0,0,0]
	v_mfma_scale_f32_16x16x128_f8f6f4 v[88:91], v[8:15], v[32:39], v[88:91], v189, v189 op_sel_hi:[0,0,0]
	v_mfma_scale_f32_16x16x128_f8f6f4 v[76:79], v[0:7], v[48:55], v[76:79], v189, v189 op_sel_hi:[0,0,0]
	v_mfma_scale_f32_16x16x128_f8f6f4 v[72:75], v[8:15], v[48:55], v[72:75], v189, v189 op_sel_hi:[0,0,0]
	v_mfma_scale_f32_16x16x128_f8f6f4 v[60:63], v[0:7], v[192:199], v[224:227], v189, v189 op_sel_hi:[0,0,0]
	v_mfma_scale_f32_16x16x128_f8f6f4 v[56:59], v[8:15], v[192:199], v[228:231], v189, v189 op_sel_hi:[0,0,0]
	v_mfma_scale_f32_16x16x128_f8f6f4 v[44:47], v[0:7], v[200:207], v[232:235], v189, v189 op_sel_hi:[0,0,0]
	v_mfma_scale_f32_16x16x128_f8f6f4 v[40:43], v[8:15], v[200:207], v[236:239], v189, v189 op_sel_hi:[0,0,0]
	s_setprio 0
	s_setprio 1
	v_mfma_scale_f32_16x16x128_f8f6f4 v[84:87], v[16:23], v[32:39], v[84:87], v189, v189 op_sel_hi:[0,0,0]
	v_mfma_scale_f32_16x16x128_f8f6f4 v[80:83], v[24:31], v[32:39], v[80:83], v189, v189 op_sel_hi:[0,0,0]
	v_mfma_scale_f32_16x16x128_f8f6f4 v[68:71], v[16:23], v[48:55], v[68:71], v189, v189 op_sel_hi:[0,0,0]
	v_mfma_scale_f32_16x16x128_f8f6f4 v[64:67], v[24:31], v[48:55], v[64:67], v189, v189 op_sel_hi:[0,0,0]
	v_mfma_scale_f32_16x16x128_f8f6f4 v[52:55], v[16:23], v[192:199], v[240:243], v189, v189 op_sel_hi:[0,0,0]
	v_mfma_scale_f32_16x16x128_f8f6f4 v[48:51], v[24:31], v[192:199], v[208:211], v189, v189 op_sel_hi:[0,0,0]
	v_mfma_scale_f32_16x16x128_f8f6f4 v[36:39], v[16:23], v[200:207], v[212:215], v189, v189 op_sel_hi:[0,0,0]
	v_mfma_scale_f32_16x16x128_f8f6f4 v[32:35], v[24:31], v[200:207], v[216:219], v189, v189 op_sel_hi:[0,0,0]
	s_setprio 0
	s_barrier
	s_add_u32 s59, s59, 0x100
	s_addc_u32 s60, s60, 0
	s_cmp_ge_i32 s61, s45
	s_mov_b64 s[22:23], s[24:25]
	s_mov_b32 s26, s61
	s_cbranch_scc0 .LBB0_4855
